# fp8 GEMM loops: fused [load+compute] segments per wave half, one barrier per 32 MFMAs/SIMD, staggered epilogues, H1 compute prio 2
# speedup vs baseline: 1.0226x; 1.0148x over previous
; #define PG8_WAIT_V(n) asm volatile("s_waitcnt vmcnt(" #n ")" ::: "memory")
; template <class Epi, class Sched, bool ALIGN_EPI = true, bool F8 = false>
; __device__ __forceinline__ void gemm_phase(PG8_LAS unsigned char* lds, const Sched& S, const Epi& E) {
;     const int tid = threadIdx.x, wid = __builtin_amdgcn_readfirstlane(tid >> 6), lane = tid & 63, wr = wid >> 2, wc = wid & 3, fr = lane & 15, fq = lane >> 4;
;     int Rs[2], Cs[2];
; #pragma unroll
;     for (int i = 0; i < 2; ++i) stage_rc(tid * 16 + i * 8192, Rs[i], Cs[i]);
;     unsigned voffB[2][2], voffA[2][2], voffAn[2][2];
; #pragma unroll
;     for (int h = 0; h < 2; ++h)
; #pragma unroll
;         for (int i = 0; i < 2; ++i) {
;             if constexpr (HasP16<Epi>::v) { const int r = Rs[i]; voffB[h][i] = S.b_off(64 * (r >> 5) + 16 * ((r & 15) >> 2) + 8 * h + 4 * ((r >> 4) & 1) + (r & 3), Cs[i]); }
;             else { const int Rb = Epi::PERM ? ((Rs[i] & ~31) + perm32(Rs[i] & 31)) : Rs[i]; voffB[h][i] = S.b_off(h * HALF + Rb, Cs[i]); } }
;     const size_t kstep = (size_t)SchedKstep<Sched>::v, kstepB = (size_t)SchedKstepB<Sched>::v;
;     const unsigned ldsw = (unsigned)wid * 1024u;
;     const int aoff = lds_byte(wr * 64 + fr, fq * 8), boff = lds_byte(wc * 32 + fr, fq * 8);
;     ...
;     GUnit cur, nxt; int ui = 0;
;     if (!S.next(0, cur)) return;
;     S.a_off(cur, Rs, Cs, voffA);
; #pragma unroll
;     for (int h = 0; h < 2; ++h)
; #pragma unroll
;         for (int i = 0; i < 2; ++i) voffAn[h][i] = voffA[h][i];
;     f32x4 acc[2][2][4][2];
; #pragma unroll
;     for (int a = 0; a < 2; ++a)
; #pragma unroll
;         for (int b = 0; b < 2; ++b)
; #pragma unroll
;             for (int m = 0; m < 4; ++m)
; #pragma unroll
;                 for (int n = 0; n < 2; ++n) acc[a][b][m][n] = (f32x4){0.f, 0.f, 0.f, 0.f};
;     bf16x8 At[4][2], B0[2][2], B1[2][2]; i32x8 At8[4], B08[2], B18[2];
;     const int f8scale = 0x7F7F7F7F;
;     const char* cA = cur.A; const char* cB = cur.B;
;     PG8_STAGE(PG8_SB(0, 0), cB, voffB[0]); PG8_STAGE(PG8_SB(0, 1), cB, voffB[1]); PG8_STAGE(PG8_SA(0, 0), cA, voffA[0]); PG8_STAGE(PG8_SA(0, 1), cA, voffA[1]);
;     if (wr == 1) PG8_BAR;
;     PG8_WAIT_V(2); PG8_BAR;
;     PG8_STAGE(PG8_SB(1, 0), cB + kstepB, voffB[0]); PG8_STAGE(PG8_SA(1, 0), cA + kstep, voffA[0]); PG8_STAGE(PG8_SB(1, 1), cB + kstepB, voffB[1]);
;     PG8_WAIT_V(6); PG8_BAR;
.LBB0_362:
.LBB0_363:
	v_lshlrev_b32_e32 v196, 4, v0
	v_and_b32_e32 v2, 32, v0
	v_lshrrev_b32_e32 v3, 2, v0
	v_and_b32_e32 v162, 48, v0
	v_lshrrev_b32_e32 v6, 5, v0
	v_bitop3_b32 v197, v196, v2, 48 bitop3:0x6c
	v_and_b32_e32 v198, 64, v0
	v_or_b32_e32 v200, 0x2000, v196
	v_and_b32_e32 v6, 4, v6
	v_bfe_u32 v7, v0, 2, 2
	v_and_or_b32 v3, v3, 64, v162
	v_bfe_u32 v199, v0, 2, 4
	v_or_b32_e32 v2, v197, v198
	v_lshrrev_b32_e32 v5, 7, v200
	s_movk_i32 s5, 0x70
	v_or3_b32 v3, v3, v6, v7
	v_and_or_b32 v5, v5, s5, v199
	v_lshl_or_b32 v164, v3, 7, v2
	v_lshrrev_b32_e32 v3, 6, v200
	s_movk_i32 s5, 0xc0
	v_and_or_b32 v3, v3, s5, v162
	v_or3_b32 v3, v3, v6, v7
	v_lshrrev_b32_e32 v4, 3, v0
	v_lshl_or_b32 v166, v3, 7, v2
	v_lshlrev_b32_e32 v3, 6, v0
	v_lshlrev_b32_e32 v6, 2, v0
	v_and_or_b32 v4, v4, 48, v199
	v_and_b32_e32 v3, 0x3c0, v3
	v_and_b32_e32 v6, 32, v6
	v_or_b32_e32 v168, 0x400, v164
	v_or_b32_e32 v172, 0x400, v166
	v_bitop3_b32 v201, v3, v6, v162 bitop3:0x36
	s_andn2_b64 vcc, exec, s[0:1]
	v_lshl_or_b32 v174, v4, 7, v2
	v_lshl_or_b32 v176, v5, 7, v2
	s_cbranch_vccnz .LBB0_411
	s_lshr_b32 s1, s14, 6
	s_lshl_b32 s45, s1, 10
	s_add_i32 s46, s45, 0
	s_add_i32 m0, s46, 0x10000
	v_mov_b32_e32 v165, 0
	v_lshl_add_u64 v[2:3], s[28:29], 0, v[164:165]
	global_load_lds_dwordx4 v164, s[28:29]
	v_mov_b32_e32 v167, v165
	s_add_i32 m0, s46, 0x12000
	s_mov_b64 s[8:9], 0x400
	v_lshl_add_u64 v[4:5], s[28:29], 0, v[166:167]
	global_load_lds_dwordx4 v166, s[28:29]
	s_add_i32 m0, s46, 0x14000
	v_lshl_add_u64 v[2:3], v[2:3], 0, s[8:9]
	global_load_lds_dwordx4 v[2:3], off
	v_lshl_add_u64 v[2:3], v[4:5], 0, s[8:9]
	s_add_i32 m0, s46, 0x16000
	s_add_i32 s47, s46, 0x2000
	global_load_lds_dwordx4 v[2:3], off
	s_mov_b32 m0, s46
	s_add_i32 s48, s46, 0x4000
	global_load_lds_dwordx4 v174, s[26:27]
	s_mov_b32 m0, s47
	v_or_b32_e32 v178, 0x4000, v174
	global_load_lds_dwordx4 v176, s[26:27]
	s_mov_b32 m0, s48
	s_add_i32 s49, s46, 0x6000
	v_or_b32_e32 v180, 0x4000, v176
	global_load_lds_dwordx4 v178, s[26:27]
	s_mov_b32 m0, s49
	s_lshr_b32 s5, s14, 8
	global_load_lds_dwordx4 v180, s[26:27]
	s_cmp_eq_u32 s5, 1
	s_movk_i32 s0, 0x4000
	s_mov_b32 s50, 0
	v_mov_b32_e32 v175, v165
	s_cselect_b64 s[10:11], -1, 0
	s_cmp_lg_u32 s5, 1
	v_mov_b32_e32 v177, v165
	s_cbranch_scc1 .LBB0_366
.LBB0_366:
	s_add_u32 s12, s36, 0x2e000000
	s_addc_u32 s13, s37, 0
	s_add_u32 s18, s36, 0x32000000
	s_addc_u32 s19, s37, 0
	s_and_b32 s1, s1, 3
	s_lshl_b32 s51, s5, 6
	s_lshl_b32 s5, s5, 13
	s_add_u32 s20, s28, 0x8000
	s_addc_u32 s21, s29, 0
	s_add_i32 m0, s46, 0x18000
	v_lshl_add_u64 v[2:3], s[20:21], 0, v[164:165]
	s_waitcnt vmcnt(2)
	s_barrier
	global_load_lds_dwordx4 v[2:3], off
	s_add_i32 m0, s46, 0x1a000
	s_add_u32 s22, s26, 0x8000
	v_lshl_add_u64 v[2:3], s[20:21], 0, v[166:167]
	s_addc_u32 s23, s27, 0
	s_add_i32 s52, s46, 0x8000
	global_load_lds_dwordx4 v[2:3], off
	v_lshl_add_u64 v[2:3], s[22:23], 0, v[174:175]
	s_mov_b32 m0, s52
	s_add_i32 s53, s46, 0xa000
	global_load_lds_dwordx4 v[2:3], off
	v_lshl_add_u64 v[2:3], s[22:23], 0, v[176:177]
	s_mov_b32 m0, s53
	v_or_b32_e32 v203, 16, v163
	global_load_lds_dwordx4 v[2:3], off
	s_add_i32 m0, s46, 0x1c000
	v_lshlrev_b32_e32 v3, 2, v163
	global_load_lds_dwordx4 v168, s[20:21]
	s_add_i32 m0, s46, 0x1e000
	v_lshl_or_b32 v2, v163, 6, v162
	global_load_lds_dwordx4 v172, s[20:21]
	v_and_b32_e32 v3, 32, v3
	v_bitop3_b32 v4, v2, s5, v3 bitop3:0xde
	v_lshlrev_b32_e32 v2, 5, v163
	v_mov_b32_e32 v3, v165
	v_lshl_add_u64 v[182:183], s[18:19], 0, v[2:3]
	v_lshlrev_b32_e32 v2, 5, v203
	v_or_b32_e32 v205, 48, v163
	v_lshl_add_u64 v[184:185], s[18:19], 0, v[2:3]
	v_lshlrev_b32_e32 v2, 5, v205
	v_and_b32_e32 v2, 0x3e0, v2
	v_lshl_add_u64 v[186:187], s[18:19], 0, v[2:3]
	v_and_b32_e32 v2, 0x3800, v200
	v_lshlrev_b32_e32 v3, 7, v199
	v_or3_b32 v2, v197, v2, v3
	v_add3_u32 v188, v2, v198, s0
	v_and_b32_e32 v2, 0x1800, v196
	s_waitcnt vmcnt(6)
	s_cmpk_lt_u32 s14, 0x100
	v_or3_b32 v2, v197, v2, v3
	v_lshl_or_b32 v202, s1, 12, v201
	s_cselect_b64 s[14:15], -1, 0
	v_add_u32_e32 v2, v2, v198
	s_add_i32 s62, 0, 0x10000
	s_add_i32 s63, 0, 0x14000
	v_mov_b32_e32 v179, v165
	v_mov_b32_e32 v181, v165
	v_mov_b32_e32 v169, v165
	v_mov_b32_e32 v173, v165
	v_or_b32_e32 v204, 32, v163
	s_ashr_i32 s59, s33, 31
	s_ashr_i32 s60, s2, 31
	v_lshl_or_b32 v206, s1, 6, v162
	v_mov_b32_e32 v189, v165
	v_or_b32_e32 v190, 0x4000, v2
	v_mov_b32_e32 v191, v165
	v_mov_b64_e32 v[192:193], 0x300
	v_mov_b64_e32 v[194:195], 0x2ff
	s_movk_i32 s61, 0x61
	v_add_u32_e32 v207, s62, v202
	v_add_u32_e32 v208, s63, v202
	v_add_u32_e32 v209, 0, v4
	v_mov_b32_e32 v210, 0x7f7f7f7f
	s_movk_i32 s64, 0x108
	s_movk_i32 s65, 0x600
	s_mov_b32 s16, 0x3c800000
	s_mov_b64 s[24:25], s[28:29]
	s_mov_b64 s[22:23], s[26:27]
	s_barrier
	s_branch .LBB0_369

; #define PG8_STAGE(bufoff, gbase, voff) do { _Pragma("unroll") for (int _i = 0; _i < 2; ++_i) \
;         __builtin_amdgcn_global_load_lds((const unsigned*)((const char*)(gbase) + (voff)[_i]), (PG8_LAS unsigned*)(lds + (bufoff) + ldsw + _i * 8192), 16, 0, 0); } while (0)
; #define PG8_WAIT_V(n) asm volatile("s_waitcnt vmcnt(" #n ")" ::: "memory")
; #define PG8_WAIT_L(n) asm volatile("s_waitcnt lgkmcnt(" #n ")" ::: "memory")
; #define PG8_BAR __builtin_amdgcn_s_barrier()
; #define PG8_SCHED __builtin_amdgcn_sched_barrier(0)
; template <class Epi, class Sched, bool ALIGN_EPI = true, bool F8 = false>
; __device__ __forceinline__ void gemm_phase(PG8_LAS unsigned char* lds, const Sched& S, const Epi& E) {
;     ...
;             PG8_LDB(B0, 0, 0); PG8_LDB(B1, 0, 1); PG8_SCHED; PG8_LDA(At, 0, 0); PG8_STAGE(PG8_SA(1, 1), a1, voffA[1]);
;             PG8_WAIT_V(8); PG8_WAIT_L(0); PG8_BAR; PG8_MMA(0, 0, At, B0); PG8_MMA(0, 1, At, B1); PG8_BAR; PG8_SCHED;
;             PG8_LDA(At, 0, 1); PG8_STAGE(PG8_SB(0, 0), b2, voffB[0]); PG8_STAGE(PG8_SB(0, 1), b2, voffB[1]); PG8_STAGE(PG8_SA(0, 0), a2, vA2[0]);
;             PG8_WAIT_V(8); PG8_WAIT_L(0); PG8_BAR; PG8_MMA(1, 0, At, B0); PG8_MMA(1, 1, At, B1); PG8_BAR; PG8_SCHED;
;     ...
;         for (int a = 0; a < 2; ++a)
; #pragma unroll
;             for (int b = 0; b < 2; ++b)
; #pragma unroll
;                 for (int m = 0; m < 4; ++m)
; #pragma unroll
;                     for (int n = 0; n < 2; ++n) acc[a][b][m][n] = (f32x4){0.f, 0.f, 0.f, 0.f};
.LBB0_371:
	s_add_u32 s5, s28, 0x10000
	s_addc_u32 s19, s29, 0
	s_add_u32 s26, s26, 0x8000
	v_mov_b32_e32 v34, 0
	s_addc_u32 s27, s27, 0
	s_mov_b32 s21, -2
	v_mov_b32_e32 v35, v34
	v_mov_b32_e32 v36, v34
	v_mov_b32_e32 v37, v34
	v_mov_b32_e32 v38, v34
	v_mov_b32_e32 v39, v34
	v_mov_b32_e32 v40, v34
	v_mov_b32_e32 v41, v34
	v_mov_b32_e32 v50, v34
	v_mov_b32_e32 v51, v34
	v_mov_b32_e32 v52, v34
	v_mov_b32_e32 v53, v34
	v_mov_b32_e32 v54, v34
	v_mov_b32_e32 v55, v34
	v_mov_b32_e32 v56, v34
	v_mov_b32_e32 v57, v34
	v_mov_b32_e32 v66, v34
	v_mov_b32_e32 v67, v34
	v_mov_b32_e32 v68, v34
	v_mov_b32_e32 v69, v34
	v_mov_b32_e32 v70, v34
	v_mov_b32_e32 v71, v34
	v_mov_b32_e32 v72, v34
	v_mov_b32_e32 v73, v34
	v_mov_b32_e32 v82, v34
	v_mov_b32_e32 v83, v34
	v_mov_b32_e32 v84, v34
	v_mov_b32_e32 v85, v34
	v_mov_b32_e32 v86, v34
	v_mov_b32_e32 v87, v34
	v_mov_b32_e32 v88, v34
	v_mov_b32_e32 v89, v34
	v_mov_b32_e32 v42, v34
	v_mov_b32_e32 v43, v34
	v_mov_b32_e32 v44, v34
	v_mov_b32_e32 v45, v34
	v_mov_b32_e32 v46, v34
	v_mov_b32_e32 v47, v34
	v_mov_b32_e32 v48, v34
	v_mov_b32_e32 v49, v34
	v_mov_b32_e32 v58, v34
	v_mov_b32_e32 v59, v34
	v_mov_b32_e32 v60, v34
	v_mov_b32_e32 v61, v34
	v_mov_b32_e32 v62, v34
	v_mov_b32_e32 v63, v34
	v_mov_b32_e32 v64, v34
	v_mov_b32_e32 v65, v34
	v_mov_b32_e32 v74, v34
	v_mov_b32_e32 v75, v34
	v_mov_b32_e32 v76, v34
	v_mov_b32_e32 v77, v34
	v_mov_b32_e32 v78, v34
	v_mov_b32_e32 v79, v34
	v_mov_b32_e32 v80, v34
	v_mov_b32_e32 v81, v34
	v_mov_b32_e32 v90, v34
	v_mov_b32_e32 v91, v34
	v_mov_b32_e32 v92, v34
	v_mov_b32_e32 v93, v34
	v_mov_b32_e32 v94, v34
	v_mov_b32_e32 v95, v34
	v_mov_b32_e32 v96, v34
	v_mov_b32_e32 v97, v34
	v_mov_b32_e32 v98, v34
	v_mov_b32_e32 v99, v34
	v_mov_b32_e32 v100, v34
	v_mov_b32_e32 v101, v34
	v_mov_b32_e32 v102, v34
	v_mov_b32_e32 v103, v34
	v_mov_b32_e32 v104, v34
	v_mov_b32_e32 v105, v34
	v_mov_b32_e32 v114, v34
	v_mov_b32_e32 v115, v34
	v_mov_b32_e32 v116, v34
	v_mov_b32_e32 v117, v34
	v_mov_b32_e32 v118, v34
	v_mov_b32_e32 v119, v34
	v_mov_b32_e32 v120, v34
	v_mov_b32_e32 v121, v34
	v_mov_b32_e32 v130, v34
	v_mov_b32_e32 v131, v34
	v_mov_b32_e32 v132, v34
	v_mov_b32_e32 v133, v34
	v_mov_b32_e32 v134, v34
	v_mov_b32_e32 v135, v34
	v_mov_b32_e32 v136, v34
	v_mov_b32_e32 v137, v34
	v_mov_b32_e32 v146, v34
	v_mov_b32_e32 v147, v34
	v_mov_b32_e32 v148, v34
	v_mov_b32_e32 v149, v34
	v_mov_b32_e32 v150, v34
	v_mov_b32_e32 v151, v34
	v_mov_b32_e32 v152, v34
	v_mov_b32_e32 v153, v34
	v_mov_b32_e32 v106, v34
	v_mov_b32_e32 v107, v34
	v_mov_b32_e32 v108, v34
	v_mov_b32_e32 v109, v34
	v_mov_b32_e32 v110, v34
	v_mov_b32_e32 v111, v34
	v_mov_b32_e32 v112, v34
	v_mov_b32_e32 v113, v34
	v_mov_b32_e32 v122, v34
	v_mov_b32_e32 v123, v34
	v_mov_b32_e32 v124, v34
	v_mov_b32_e32 v125, v34
	v_mov_b32_e32 v126, v34
	v_mov_b32_e32 v127, v34
	v_mov_b32_e32 v128, v34
	v_mov_b32_e32 v129, v34
	v_mov_b32_e32 v138, v34
	v_mov_b32_e32 v139, v34
	v_mov_b32_e32 v140, v34
	v_mov_b32_e32 v141, v34
	v_mov_b32_e32 v142, v34
	v_mov_b32_e32 v143, v34
	v_mov_b32_e32 v144, v34
	v_mov_b32_e32 v145, v34
	v_mov_b32_e32 v154, v34
	v_mov_b32_e32 v155, v34
	v_mov_b32_e32 v156, v34
	v_mov_b32_e32 v157, v34
	v_mov_b32_e32 v158, v34
	v_mov_b32_e32 v159, v34
	v_mov_b32_e32 v160, v34
	v_mov_b32_e32 v161, v34
	s_bitcmp1_b32 s3, 2
	s_cbranch_scc1 .Lh1_372
.LBB0_372:
	ds_read_b128 v[18:21], v207
	ds_read_b128 v[22:25], v207 offset:1024
	ds_read_b128 v[26:29], v207 offset:2048
	ds_read_b128 v[30:33], v207 offset:3072
	ds_read_b128 v[2:5], v208
	ds_read_b128 v[6:9], v208 offset:1024
	ds_read_b128 v[10:13], v208 offset:2048
	ds_read_b128 v[14:17], v208 offset:3072
	s_add_u32 s28, s26, 0x8000
	s_addc_u32 s29, s27, 0
	s_cmp_eq_u32 s21, 12
	s_cselect_b32 s40, s22, s28
	s_cselect_b32 s41, s23, s29
	s_cselect_b32 s30, s24, s5
	s_cselect_b32 s31, s25, s19
	s_add_u32 s28, s40, 0x8000
	s_addc_u32 s29, s41, 0
	v_lshl_add_u64 v[244:245], s[26:27], 0, v[190:191]
	s_add_i32 m0, s46, 0xc000
	ds_read_b128 v[212:215], v209
	ds_read_b128 v[216:219], v209 offset:1024
	ds_read_b128 v[220:223], v209 offset:2048
	ds_read_b128 v[224:227], v209 offset:3072
	ds_read_b128 v[228:231], v209 offset:4096
	ds_read_b128 v[232:235], v209 offset:5120
	ds_read_b128 v[236:239], v209 offset:6144
	ds_read_b128 v[240:243], v209 offset:7168
	global_load_lds_dwordx4 v[244:245], off
	v_lshl_add_u64 v[244:245], s[26:27], 0, v[188:189]
	s_add_i32 m0, s46, 0xe000
	s_nop 0
	global_load_lds_dwordx4 v[244:245], off
	s_waitcnt vmcnt(8)
	s_waitcnt lgkmcnt(0)
	s_setprio 1
	s_waitcnt lgkmcnt(0)
	v_mfma_scale_f32_16x16x128_f8f6f4 v[158:161], v[18:25], v[212:219], v[158:161], v210, v210 op_sel_hi:[0,0,0]
	v_mfma_scale_f32_16x16x128_f8f6f4 v[154:157], v[26:33], v[212:219], v[154:157], v210, v210 op_sel_hi:[0,0,0]
	v_mfma_scale_f32_16x16x128_f8f6f4 v[142:145], v[18:25], v[220:227], v[142:145], v210, v210 op_sel_hi:[0,0,0]
	v_mfma_scale_f32_16x16x128_f8f6f4 v[138:141], v[26:33], v[220:227], v[138:141], v210, v210 op_sel_hi:[0,0,0]
	v_mfma_scale_f32_16x16x128_f8f6f4 v[126:129], v[18:25], v[228:235], v[126:129], v210, v210 op_sel_hi:[0,0,0]
	v_mfma_scale_f32_16x16x128_f8f6f4 v[122:125], v[26:33], v[228:235], v[122:125], v210, v210 op_sel_hi:[0,0,0]
	v_mfma_scale_f32_16x16x128_f8f6f4 v[110:113], v[18:25], v[236:243], v[110:113], v210, v210 op_sel_hi:[0,0,0]
	v_mfma_scale_f32_16x16x128_f8f6f4 v[106:109], v[26:33], v[236:243], v[106:109], v210, v210 op_sel_hi:[0,0,0]
	s_nop 3
	s_setprio 0
	s_setprio 1
	v_mfma_scale_f32_16x16x128_f8f6f4 v[150:153], v[2:9], v[212:219], v[150:153], v210, v210 op_sel_hi:[0,0,0]
	v_mfma_scale_f32_16x16x128_f8f6f4 v[146:149], v[10:17], v[212:219], v[146:149], v210, v210 op_sel_hi:[0,0,0]
	v_mfma_scale_f32_16x16x128_f8f6f4 v[134:137], v[2:9], v[220:227], v[134:137], v210, v210 op_sel_hi:[0,0,0]
	v_mfma_scale_f32_16x16x128_f8f6f4 v[130:133], v[10:17], v[220:227], v[130:133], v210, v210 op_sel_hi:[0,0,0]
	v_mfma_scale_f32_16x16x128_f8f6f4 v[118:121], v[2:9], v[228:235], v[118:121], v210, v210 op_sel_hi:[0,0,0]
	v_mfma_scale_f32_16x16x128_f8f6f4 v[114:117], v[10:17], v[228:235], v[114:117], v210, v210 op_sel_hi:[0,0,0]
	v_mfma_scale_f32_16x16x128_f8f6f4 v[102:105], v[2:9], v[236:243], v[102:105], v210, v210 op_sel_hi:[0,0,0]
	v_mfma_scale_f32_16x16x128_f8f6f4 v[98:101], v[10:17], v[236:243], v[98:101], v210, v210 op_sel_hi:[0,0,0]
	s_nop 3
	s_setprio 0
	s_barrier
; #define PG8_STAGE(bufoff, gbase, voff) do { _Pragma("unroll") for (int _i = 0; _i < 2; ++_i) \
;         __builtin_amdgcn_global_load_lds((const unsigned*)((const char*)(gbase) + (voff)[_i]), (PG8_LAS unsigned*)(lds + (bufoff) + ldsw + _i * 8192), 16, 0, 0); } while (0)
; #define PG8_WAIT_V(n) asm volatile("s_waitcnt vmcnt(" #n ")" ::: "memory")
; #define PG8_WAIT_L(n) asm volatile("s_waitcnt lgkmcnt(" #n ")" ::: "memory")
; #define PG8_BAR __builtin_amdgcn_s_barrier()
; #define PG8_SCHED __builtin_amdgcn_sched_barrier(0)
; template <class Epi, class Sched, bool ALIGN_EPI = true, bool F8 = false>
; __device__ __forceinline__ void gemm_phase(PG8_LAS unsigned char* lds, const Sched& S, const Epi& E) {
;     ...
;             PG8_LDB(B0, 0, 0); PG8_LDB(B1, 0, 1); PG8_SCHED; PG8_LDA(At, 0, 0); PG8_STAGE(PG8_SA(1, 1), a1, voffA[1]);
;             PG8_WAIT_V(8); PG8_WAIT_L(0); PG8_BAR; PG8_MMA(0, 0, At, B0); PG8_MMA(0, 1, At, B1); PG8_BAR; PG8_SCHED;
;             PG8_LDA(At, 0, 1); PG8_STAGE(PG8_SB(0, 0), b2, voffB[0]); PG8_STAGE(PG8_SB(0, 1), b2, voffB[1]); PG8_STAGE(PG8_SA(0, 0), a2, vA2[0]);
;             PG8_WAIT_V(8); PG8_WAIT_L(0); PG8_BAR; PG8_MMA(1, 0, At, B0); PG8_MMA(1, 1, At, B1); PG8_BAR; PG8_SCHED;
;             PG8_LDB(B0, 1, 0); PG8_LDB(B1, 1, 1); PG8_SCHED; PG8_LDA(At, 1, 0); PG8_STAGE(PG8_SA(0, 1), a2, vA2[1]);
;             PG8_WAIT_V(8); PG8_WAIT_L(0); PG8_BAR; PG8_MMA(0, 0, At, B0); PG8_MMA(0, 1, At, B1); PG8_BAR; PG8_SCHED;
;             PG8_LDA(At, 1, 1); PG8_STAGE(PG8_SB(1, 0), b3, voffB[0]); PG8_STAGE(PG8_SB(1, 1), b3, voffB[1]); PG8_STAGE(PG8_SA(1, 0), a3, vA2[0]);
;             PG8_WAIT_V(8); PG8_WAIT_L(0); PG8_BAR; PG8_MMA(1, 0, At, B0); PG8_MMA(1, 1, At, B1); PG8_BAR; PG8_SCHED;
	s_add_i32 s67, s62, s45
	v_lshl_add_u64 v[244:245], s[30:31], 0, v[164:165]
	s_mov_b32 m0, s67
	ds_read_b128 v[212:215], v209 offset:16384
	ds_read_b128 v[216:219], v209 offset:17408
	ds_read_b128 v[220:223], v209 offset:18432
	ds_read_b128 v[224:227], v209 offset:19456
	ds_read_b128 v[228:231], v209 offset:20480
	ds_read_b128 v[232:235], v209 offset:21504
	ds_read_b128 v[236:239], v209 offset:22528
	ds_read_b128 v[240:243], v209 offset:23552
	global_load_lds_dwordx4 v[244:245], off
	v_lshl_add_u64 v[246:247], s[30:31], 0, v[166:167]
	s_add_i32 m0, s67, 0x2000
	s_add_i32 s67, s63, s45
	global_load_lds_dwordx4 v[246:247], off
	v_lshl_add_u64 v[244:245], v[244:245], 0, s[8:9]
	s_mov_b32 m0, s67
	s_nop 0
	global_load_lds_dwordx4 v[244:245], off
	v_lshl_add_u64 v[244:245], v[246:247], 0, s[8:9]
	s_add_i32 m0, s67, 0x2000
	s_nop 0
	global_load_lds_dwordx4 v[244:245], off
	v_lshl_add_u64 v[244:245], s[40:41], 0, v[174:175]
	s_mov_b32 m0, s46
	s_nop 0
	global_load_lds_dwordx4 v[244:245], off
	v_lshl_add_u64 v[244:245], s[40:41], 0, v[176:177]
	s_mov_b32 m0, s47
	s_nop 0
	global_load_lds_dwordx4 v[244:245], off
	s_waitcnt vmcnt(8)
	s_waitcnt lgkmcnt(0)
	s_setprio 1
	s_waitcnt lgkmcnt(0)
	v_mfma_scale_f32_16x16x128_f8f6f4 v[94:97], v[18:25], v[212:219], v[94:97], v210, v210 op_sel_hi:[0,0,0]
	v_mfma_scale_f32_16x16x128_f8f6f4 v[90:93], v[26:33], v[212:219], v[90:93], v210, v210 op_sel_hi:[0,0,0]
	v_mfma_scale_f32_16x16x128_f8f6f4 v[78:81], v[18:25], v[220:227], v[78:81], v210, v210 op_sel_hi:[0,0,0]
	v_mfma_scale_f32_16x16x128_f8f6f4 v[74:77], v[26:33], v[220:227], v[74:77], v210, v210 op_sel_hi:[0,0,0]
	v_mfma_scale_f32_16x16x128_f8f6f4 v[62:65], v[18:25], v[228:235], v[62:65], v210, v210 op_sel_hi:[0,0,0]
	v_mfma_scale_f32_16x16x128_f8f6f4 v[58:61], v[26:33], v[228:235], v[58:61], v210, v210 op_sel_hi:[0,0,0]
	v_mfma_scale_f32_16x16x128_f8f6f4 v[46:49], v[18:25], v[236:243], v[46:49], v210, v210 op_sel_hi:[0,0,0]
	v_mfma_scale_f32_16x16x128_f8f6f4 v[42:45], v[26:33], v[236:243], v[42:45], v210, v210 op_sel_hi:[0,0,0]
	s_nop 3
	s_setprio 0
	s_setprio 1
	v_mfma_scale_f32_16x16x128_f8f6f4 v[86:89], v[2:9], v[212:219], v[86:89], v210, v210 op_sel_hi:[0,0,0]
	v_mfma_scale_f32_16x16x128_f8f6f4 v[82:85], v[10:17], v[212:219], v[82:85], v210, v210 op_sel_hi:[0,0,0]
	v_mfma_scale_f32_16x16x128_f8f6f4 v[70:73], v[2:9], v[220:227], v[70:73], v210, v210 op_sel_hi:[0,0,0]
	v_mfma_scale_f32_16x16x128_f8f6f4 v[66:69], v[10:17], v[220:227], v[66:69], v210, v210 op_sel_hi:[0,0,0]
	v_mfma_scale_f32_16x16x128_f8f6f4 v[54:57], v[2:9], v[228:235], v[54:57], v210, v210 op_sel_hi:[0,0,0]
	v_mfma_scale_f32_16x16x128_f8f6f4 v[50:53], v[10:17], v[228:235], v[50:53], v210, v210 op_sel_hi:[0,0,0]
	v_mfma_scale_f32_16x16x128_f8f6f4 v[38:41], v[2:9], v[236:243], v[38:41], v210, v210 op_sel_hi:[0,0,0]
	v_mfma_scale_f32_16x16x128_f8f6f4 v[34:37], v[10:17], v[236:243], v[34:37], v210, v210 op_sel_hi:[0,0,0]
	s_nop 3
	s_setprio 0
	s_barrier
	s_add_i32 s67, 0, 0x18000
	s_add_i32 s68, 0, 0x1c000
	v_add_u32_e32 v14, s67, v202
	v_add_u32_e32 v30, s68, v202
	ds_read_b128 v[2:5], v14
	ds_read_b128 v[6:9], v14 offset:1024
	ds_read_b128 v[10:13], v14 offset:2048
	ds_read_b128 v[14:17], v14 offset:3072
	ds_read_b128 v[18:21], v30
	ds_read_b128 v[22:25], v30 offset:1024
	ds_read_b128 v[26:29], v30 offset:2048
	ds_read_b128 v[30:33], v30 offset:3072
	s_mov_b32 m0, s48
	v_lshl_add_u64 v[244:245], s[40:41], 0, v[178:179]
	ds_read_b128 v[212:215], v209 offset:32768
	ds_read_b128 v[216:219], v209 offset:33792
	ds_read_b128 v[220:223], v209 offset:34816
	ds_read_b128 v[224:227], v209 offset:35840
	ds_read_b128 v[228:231], v209 offset:36864
	ds_read_b128 v[232:235], v209 offset:37888
	ds_read_b128 v[236:239], v209 offset:38912
	ds_read_b128 v[240:243], v209 offset:39936
	global_load_lds_dwordx4 v[244:245], off
	v_lshl_add_u64 v[244:245], s[40:41], 0, v[180:181]
	s_mov_b32 m0, s49
	s_nop 0
	global_load_lds_dwordx4 v[244:245], off
	s_waitcnt vmcnt(8)
	s_waitcnt lgkmcnt(0)
	s_setprio 1
	s_waitcnt lgkmcnt(0)
	v_mfma_scale_f32_16x16x128_f8f6f4 v[158:161], v[2:9], v[212:219], v[158:161], v210, v210 op_sel_hi:[0,0,0]
	v_mfma_scale_f32_16x16x128_f8f6f4 v[154:157], v[10:17], v[212:219], v[154:157], v210, v210 op_sel_hi:[0,0,0]
	v_mfma_scale_f32_16x16x128_f8f6f4 v[142:145], v[2:9], v[220:227], v[142:145], v210, v210 op_sel_hi:[0,0,0]
	v_mfma_scale_f32_16x16x128_f8f6f4 v[138:141], v[10:17], v[220:227], v[138:141], v210, v210 op_sel_hi:[0,0,0]
	v_mfma_scale_f32_16x16x128_f8f6f4 v[126:129], v[2:9], v[228:235], v[126:129], v210, v210 op_sel_hi:[0,0,0]
	v_mfma_scale_f32_16x16x128_f8f6f4 v[122:125], v[10:17], v[228:235], v[122:125], v210, v210 op_sel_hi:[0,0,0]
	v_mfma_scale_f32_16x16x128_f8f6f4 v[110:113], v[2:9], v[236:243], v[110:113], v210, v210 op_sel_hi:[0,0,0]
	v_mfma_scale_f32_16x16x128_f8f6f4 v[106:109], v[10:17], v[236:243], v[106:109], v210, v210 op_sel_hi:[0,0,0]
	s_nop 3
	s_setprio 0
	s_setprio 1
	v_mfma_scale_f32_16x16x128_f8f6f4 v[150:153], v[18:25], v[212:219], v[150:153], v210, v210 op_sel_hi:[0,0,0]
	v_mfma_scale_f32_16x16x128_f8f6f4 v[146:149], v[26:33], v[212:219], v[146:149], v210, v210 op_sel_hi:[0,0,0]
	v_mfma_scale_f32_16x16x128_f8f6f4 v[134:137], v[18:25], v[220:227], v[134:137], v210, v210 op_sel_hi:[0,0,0]
	v_mfma_scale_f32_16x16x128_f8f6f4 v[130:133], v[26:33], v[220:227], v[130:133], v210, v210 op_sel_hi:[0,0,0]
	v_mfma_scale_f32_16x16x128_f8f6f4 v[118:121], v[18:25], v[228:235], v[118:121], v210, v210 op_sel_hi:[0,0,0]
	v_mfma_scale_f32_16x16x128_f8f6f4 v[114:117], v[26:33], v[228:235], v[114:117], v210, v210 op_sel_hi:[0,0,0]
	v_mfma_scale_f32_16x16x128_f8f6f4 v[102:105], v[18:25], v[236:243], v[102:105], v210, v210 op_sel_hi:[0,0,0]
	v_mfma_scale_f32_16x16x128_f8f6f4 v[98:101], v[26:33], v[236:243], v[98:101], v210, v210 op_sel_hi:[0,0,0]
	s_nop 3
	s_setprio 0
	s_barrier
; #define PG8_STAGE(bufoff, gbase, voff) do { _Pragma("unroll") for (int _i = 0; _i < 2; ++_i) \
;         __builtin_amdgcn_global_load_lds((const unsigned*)((const char*)(gbase) + (voff)[_i]), (PG8_LAS unsigned*)(lds + (bufoff) + ldsw + _i * 8192), 16, 0, 0); } while (0)
; #define PG8_WAIT_V(n) asm volatile("s_waitcnt vmcnt(" #n ")" ::: "memory")
; #define PG8_WAIT_L(n) asm volatile("s_waitcnt lgkmcnt(" #n ")" ::: "memory")
; #define PG8_BAR __builtin_amdgcn_s_barrier()
; #define PG8_SCHED __builtin_amdgcn_sched_barrier(0)
; template <class Epi, class Sched, bool ALIGN_EPI = true, bool F8 = false>
; __device__ __forceinline__ void gemm_phase(PG8_LAS unsigned char* lds, const Sched& S, const Epi& E) {
;     ...
;         for (int t = 0; t < nt; t += 2) {
;             const bool last = (t == nt - 2);
;             if constexpr (Sched::GATHER) { if (last && has_next) S.a_off(nxt, Rs, Cs, voffAn); }
;             const char* a1 = cA + (size_t)(t + 1) * kstep;
;             const char* a2 = last ? nA : cA + (size_t)(t + 2) * kstep; const char* b2 = last ? nB : cB + (size_t)(t + 2) * kstepB;
;             const char* a3 = a2 + kstep; const char* b3 = b2 + kstepB;
;             unsigned vA2[2][2];
; #pragma unroll
;             for (int h = 0; h < 2; ++h)
; #pragma unroll
;                 for (int i = 0; i < 2; ++i) { if constexpr (Sched::GATHER) vA2[h][i] = (last && has_next) ? voffAn[h][i] : voffA[h][i]; else vA2[h][i] = voffA[h][i]; }
;             PG8_LDB(B0, 0, 0); PG8_LDB(B1, 0, 1); PG8_SCHED; PG8_LDA(At, 0, 0); PG8_STAGE(PG8_SA(1, 1), a1, voffA[1]);
;             PG8_WAIT_V(8); PG8_WAIT_L(0); PG8_BAR; PG8_MMA(0, 0, At, B0); PG8_MMA(0, 1, At, B1); PG8_BAR; PG8_SCHED;
;     ...
;             PG8_LDA(At, 1, 1); PG8_STAGE(PG8_SB(1, 0), b3, voffB[0]); PG8_STAGE(PG8_SB(1, 1), b3, voffB[1]); PG8_STAGE(PG8_SA(1, 0), a3, vA2[0]);
;             PG8_WAIT_V(8); PG8_WAIT_L(0); PG8_BAR; PG8_MMA(1, 0, At, B0); PG8_MMA(1, 1, At, B1); PG8_BAR; PG8_SCHED;
	s_add_u32 s30, s30, 0x8000
	s_addc_u32 s31, s31, 0
	s_add_i32 s40, s67, s45
	v_lshl_add_u64 v[244:245], s[30:31], 0, v[164:165]
	s_mov_b32 m0, s40
	ds_read_b128 v[212:215], v209 offset:49152
	ds_read_b128 v[216:219], v209 offset:50176
	ds_read_b128 v[220:223], v209 offset:51200
	ds_read_b128 v[224:227], v209 offset:52224
	ds_read_b128 v[228:231], v209 offset:53248
	ds_read_b128 v[232:235], v209 offset:54272
	ds_read_b128 v[236:239], v209 offset:55296
	ds_read_b128 v[240:243], v209 offset:56320
	global_load_lds_dwordx4 v[244:245], off
	v_lshl_add_u64 v[244:245], s[30:31], 0, v[166:167]
	s_add_i32 m0, s40, 0x2000
	s_add_i32 s40, s68, s45
	global_load_lds_dwordx4 v[244:245], off
	v_lshl_add_u64 v[244:245], s[30:31], 0, v[168:169]
	s_mov_b32 m0, s40
	s_nop 0
	global_load_lds_dwordx4 v[244:245], off
	v_lshl_add_u64 v[244:245], s[30:31], 0, v[172:173]
	s_add_i32 m0, s40, 0x2000
	s_nop 0
	global_load_lds_dwordx4 v[244:245], off
	v_lshl_add_u64 v[244:245], s[28:29], 0, v[174:175]
	s_mov_b32 m0, s52
	s_nop 0
	global_load_lds_dwordx4 v[244:245], off
	v_lshl_add_u64 v[244:245], s[28:29], 0, v[176:177]
	s_mov_b32 m0, s53
	s_nop 0
	global_load_lds_dwordx4 v[244:245], off
	s_waitcnt vmcnt(8)
	s_waitcnt lgkmcnt(0)
	s_setprio 1
	s_waitcnt lgkmcnt(0)
	v_mfma_scale_f32_16x16x128_f8f6f4 v[94:97], v[2:9], v[212:219], v[94:97], v210, v210 op_sel_hi:[0,0,0]
	v_mfma_scale_f32_16x16x128_f8f6f4 v[90:93], v[10:17], v[212:219], v[90:93], v210, v210 op_sel_hi:[0,0,0]
	v_mfma_scale_f32_16x16x128_f8f6f4 v[78:81], v[2:9], v[220:227], v[78:81], v210, v210 op_sel_hi:[0,0,0]
	v_mfma_scale_f32_16x16x128_f8f6f4 v[74:77], v[10:17], v[220:227], v[74:77], v210, v210 op_sel_hi:[0,0,0]
	v_mfma_scale_f32_16x16x128_f8f6f4 v[62:65], v[2:9], v[228:235], v[62:65], v210, v210 op_sel_hi:[0,0,0]
	v_mfma_scale_f32_16x16x128_f8f6f4 v[58:61], v[10:17], v[228:235], v[58:61], v210, v210 op_sel_hi:[0,0,0]
	v_mfma_scale_f32_16x16x128_f8f6f4 v[46:49], v[2:9], v[236:243], v[46:49], v210, v210 op_sel_hi:[0,0,0]
	v_mfma_scale_f32_16x16x128_f8f6f4 v[42:45], v[10:17], v[236:243], v[42:45], v210, v210 op_sel_hi:[0,0,0]
	s_nop 3
	s_setprio 0
	s_setprio 1
	v_mfma_scale_f32_16x16x128_f8f6f4 v[86:89], v[18:25], v[212:219], v[86:89], v210, v210 op_sel_hi:[0,0,0]
	v_mfma_scale_f32_16x16x128_f8f6f4 v[82:85], v[26:33], v[212:219], v[82:85], v210, v210 op_sel_hi:[0,0,0]
	v_mfma_scale_f32_16x16x128_f8f6f4 v[70:73], v[18:25], v[220:227], v[70:73], v210, v210 op_sel_hi:[0,0,0]
	v_mfma_scale_f32_16x16x128_f8f6f4 v[66:69], v[26:33], v[220:227], v[66:69], v210, v210 op_sel_hi:[0,0,0]
	v_mfma_scale_f32_16x16x128_f8f6f4 v[54:57], v[18:25], v[228:235], v[54:57], v210, v210 op_sel_hi:[0,0,0]
	v_mfma_scale_f32_16x16x128_f8f6f4 v[50:53], v[26:33], v[228:235], v[50:53], v210, v210 op_sel_hi:[0,0,0]
	v_mfma_scale_f32_16x16x128_f8f6f4 v[38:41], v[18:25], v[236:243], v[38:41], v210, v210 op_sel_hi:[0,0,0]
	v_mfma_scale_f32_16x16x128_f8f6f4 v[34:37], v[26:33], v[236:243], v[34:37], v210, v210 op_sel_hi:[0,0,0]
	s_nop 3
	s_setprio 0
	s_barrier
	s_add_i32 s21, s21, 2
	s_add_u32 s5, s5, 0x10000
	s_addc_u32 s19, s19, 0
	s_add_u32 s26, s26, 0x10000
	s_addc_u32 s27, s27, 0
	s_cmp_gt_u32 s21, 13
	s_cbranch_scc0 .LBB0_372
	s_branch .Lfx_372
.Lh1_372:
	ds_read_b128 v[18:21], v207
	ds_read_b128 v[22:25], v207 offset:1024
	ds_read_b128 v[26:29], v207 offset:2048
	ds_read_b128 v[30:33], v207 offset:3072
	ds_read_b128 v[2:5], v208
	ds_read_b128 v[6:9], v208 offset:1024
	ds_read_b128 v[10:13], v208 offset:2048
	ds_read_b128 v[14:17], v208 offset:3072
	s_add_u32 s28, s26, 0x8000
	s_addc_u32 s29, s27, 0
	s_cmp_eq_u32 s21, 12
	s_cselect_b32 s40, s22, s28
	s_cselect_b32 s41, s23, s29
	s_cselect_b32 s30, s24, s5
	s_cselect_b32 s31, s25, s19
	s_add_u32 s28, s40, 0x8000
	s_addc_u32 s29, s41, 0
	v_lshl_add_u64 v[244:245], s[26:27], 0, v[190:191]
	s_add_i32 m0, s46, 0xc000
	ds_read_b128 v[212:215], v209
	ds_read_b128 v[216:219], v209 offset:1024
	ds_read_b128 v[220:223], v209 offset:2048
	ds_read_b128 v[224:227], v209 offset:3072
	ds_read_b128 v[228:231], v209 offset:4096
	ds_read_b128 v[232:235], v209 offset:5120
	ds_read_b128 v[236:239], v209 offset:6144
	ds_read_b128 v[240:243], v209 offset:7168
	global_load_lds_dwordx4 v[244:245], off
	v_lshl_add_u64 v[244:245], s[26:27], 0, v[188:189]
	s_add_i32 m0, s46, 0xe000
	s_nop 0
	global_load_lds_dwordx4 v[244:245], off
	s_waitcnt vmcnt(8)
	s_waitcnt lgkmcnt(0)
	s_barrier
; #define PG8_STAGE(bufoff, gbase, voff) do { _Pragma("unroll") for (int _i = 0; _i < 2; ++_i) \
;         __builtin_amdgcn_global_load_lds((const unsigned*)((const char*)(gbase) + (voff)[_i]), (PG8_LAS unsigned*)(lds + (bufoff) + ldsw + _i * 8192), 16, 0, 0); } while (0)
; #define PG8_WAIT_V(n) asm volatile("s_waitcnt vmcnt(" #n ")" ::: "memory")
; #define PG8_WAIT_L(n) asm volatile("s_waitcnt lgkmcnt(" #n ")" ::: "memory")
; #define PG8_BAR __builtin_amdgcn_s_barrier()
; #define PG8_SCHED __builtin_amdgcn_sched_barrier(0)
; template <class Epi, class Sched, bool ALIGN_EPI = true, bool F8 = false>
; __device__ __forceinline__ void gemm_phase(PG8_LAS unsigned char* lds, const Sched& S, const Epi& E) {
;     ...
;             PG8_LDB(B0, 0, 0); PG8_LDB(B1, 0, 1); PG8_SCHED; PG8_LDA(At, 0, 0); PG8_STAGE(PG8_SA(1, 1), a1, voffA[1]);
;             PG8_WAIT_V(8); PG8_WAIT_L(0); PG8_BAR; PG8_MMA(0, 0, At, B0); PG8_MMA(0, 1, At, B1); PG8_BAR; PG8_SCHED;
;             PG8_LDA(At, 0, 1); PG8_STAGE(PG8_SB(0, 0), b2, voffB[0]); PG8_STAGE(PG8_SB(0, 1), b2, voffB[1]); PG8_STAGE(PG8_SA(0, 0), a2, vA2[0]);
;             PG8_WAIT_V(8); PG8_WAIT_L(0); PG8_BAR; PG8_MMA(1, 0, At, B0); PG8_MMA(1, 1, At, B1); PG8_BAR; PG8_SCHED;
;             PG8_LDB(B0, 1, 0); PG8_LDB(B1, 1, 1); PG8_SCHED; PG8_LDA(At, 1, 0); PG8_STAGE(PG8_SA(0, 1), a2, vA2[1]);
;             PG8_WAIT_V(8); PG8_WAIT_L(0); PG8_BAR; PG8_MMA(0, 0, At, B0); PG8_MMA(0, 1, At, B1); PG8_BAR; PG8_SCHED;
	s_setprio 2
	s_waitcnt lgkmcnt(0)
	v_mfma_scale_f32_16x16x128_f8f6f4 v[158:161], v[18:25], v[212:219], v[158:161], v210, v210 op_sel_hi:[0,0,0]
	v_mfma_scale_f32_16x16x128_f8f6f4 v[154:157], v[26:33], v[212:219], v[154:157], v210, v210 op_sel_hi:[0,0,0]
	v_mfma_scale_f32_16x16x128_f8f6f4 v[142:145], v[18:25], v[220:227], v[142:145], v210, v210 op_sel_hi:[0,0,0]
	v_mfma_scale_f32_16x16x128_f8f6f4 v[138:141], v[26:33], v[220:227], v[138:141], v210, v210 op_sel_hi:[0,0,0]
	v_mfma_scale_f32_16x16x128_f8f6f4 v[126:129], v[18:25], v[228:235], v[126:129], v210, v210 op_sel_hi:[0,0,0]
	v_mfma_scale_f32_16x16x128_f8f6f4 v[122:125], v[26:33], v[228:235], v[122:125], v210, v210 op_sel_hi:[0,0,0]
	v_mfma_scale_f32_16x16x128_f8f6f4 v[110:113], v[18:25], v[236:243], v[110:113], v210, v210 op_sel_hi:[0,0,0]
	v_mfma_scale_f32_16x16x128_f8f6f4 v[106:109], v[26:33], v[236:243], v[106:109], v210, v210 op_sel_hi:[0,0,0]
	s_nop 3
	s_setprio 0
	s_setprio 2
	v_mfma_scale_f32_16x16x128_f8f6f4 v[150:153], v[2:9], v[212:219], v[150:153], v210, v210 op_sel_hi:[0,0,0]
	v_mfma_scale_f32_16x16x128_f8f6f4 v[146:149], v[10:17], v[212:219], v[146:149], v210, v210 op_sel_hi:[0,0,0]
	v_mfma_scale_f32_16x16x128_f8f6f4 v[134:137], v[2:9], v[220:227], v[134:137], v210, v210 op_sel_hi:[0,0,0]
	v_mfma_scale_f32_16x16x128_f8f6f4 v[130:133], v[10:17], v[220:227], v[130:133], v210, v210 op_sel_hi:[0,0,0]
	v_mfma_scale_f32_16x16x128_f8f6f4 v[118:121], v[2:9], v[228:235], v[118:121], v210, v210 op_sel_hi:[0,0,0]
	v_mfma_scale_f32_16x16x128_f8f6f4 v[114:117], v[10:17], v[228:235], v[114:117], v210, v210 op_sel_hi:[0,0,0]
	v_mfma_scale_f32_16x16x128_f8f6f4 v[102:105], v[2:9], v[236:243], v[102:105], v210, v210 op_sel_hi:[0,0,0]
	v_mfma_scale_f32_16x16x128_f8f6f4 v[98:101], v[10:17], v[236:243], v[98:101], v210, v210 op_sel_hi:[0,0,0]
	s_nop 3
	s_setprio 0
	s_add_i32 s67, s62, s45
	v_lshl_add_u64 v[244:245], s[30:31], 0, v[164:165]
	s_mov_b32 m0, s67
	ds_read_b128 v[212:215], v209 offset:16384
	ds_read_b128 v[216:219], v209 offset:17408
	ds_read_b128 v[220:223], v209 offset:18432
	ds_read_b128 v[224:227], v209 offset:19456
	ds_read_b128 v[228:231], v209 offset:20480
	ds_read_b128 v[232:235], v209 offset:21504
	ds_read_b128 v[236:239], v209 offset:22528
	ds_read_b128 v[240:243], v209 offset:23552
	global_load_lds_dwordx4 v[244:245], off
	v_lshl_add_u64 v[246:247], s[30:31], 0, v[166:167]
	s_add_i32 m0, s67, 0x2000
	s_add_i32 s67, s63, s45
	global_load_lds_dwordx4 v[246:247], off
	v_lshl_add_u64 v[244:245], v[244:245], 0, s[8:9]
	s_mov_b32 m0, s67
	s_nop 0
	global_load_lds_dwordx4 v[244:245], off
	v_lshl_add_u64 v[244:245], v[246:247], 0, s[8:9]
	s_add_i32 m0, s67, 0x2000
	s_nop 0
	global_load_lds_dwordx4 v[244:245], off
	v_lshl_add_u64 v[244:245], s[40:41], 0, v[174:175]
	s_mov_b32 m0, s46
	s_nop 0
	global_load_lds_dwordx4 v[244:245], off
	v_lshl_add_u64 v[244:245], s[40:41], 0, v[176:177]
	s_mov_b32 m0, s47
	s_nop 0
	global_load_lds_dwordx4 v[244:245], off
	s_waitcnt vmcnt(8)
	s_waitcnt lgkmcnt(0)
	s_barrier
	s_setprio 2
	s_waitcnt lgkmcnt(0)
	v_mfma_scale_f32_16x16x128_f8f6f4 v[94:97], v[18:25], v[212:219], v[94:97], v210, v210 op_sel_hi:[0,0,0]
	v_mfma_scale_f32_16x16x128_f8f6f4 v[90:93], v[26:33], v[212:219], v[90:93], v210, v210 op_sel_hi:[0,0,0]
	v_mfma_scale_f32_16x16x128_f8f6f4 v[78:81], v[18:25], v[220:227], v[78:81], v210, v210 op_sel_hi:[0,0,0]
	v_mfma_scale_f32_16x16x128_f8f6f4 v[74:77], v[26:33], v[220:227], v[74:77], v210, v210 op_sel_hi:[0,0,0]
	v_mfma_scale_f32_16x16x128_f8f6f4 v[62:65], v[18:25], v[228:235], v[62:65], v210, v210 op_sel_hi:[0,0,0]
	v_mfma_scale_f32_16x16x128_f8f6f4 v[58:61], v[26:33], v[228:235], v[58:61], v210, v210 op_sel_hi:[0,0,0]
	v_mfma_scale_f32_16x16x128_f8f6f4 v[46:49], v[18:25], v[236:243], v[46:49], v210, v210 op_sel_hi:[0,0,0]
	v_mfma_scale_f32_16x16x128_f8f6f4 v[42:45], v[26:33], v[236:243], v[42:45], v210, v210 op_sel_hi:[0,0,0]
	s_nop 3
	s_setprio 0
	s_setprio 2
	v_mfma_scale_f32_16x16x128_f8f6f4 v[86:89], v[2:9], v[212:219], v[86:89], v210, v210 op_sel_hi:[0,0,0]
	v_mfma_scale_f32_16x16x128_f8f6f4 v[82:85], v[10:17], v[212:219], v[82:85], v210, v210 op_sel_hi:[0,0,0]
	v_mfma_scale_f32_16x16x128_f8f6f4 v[70:73], v[2:9], v[220:227], v[70:73], v210, v210 op_sel_hi:[0,0,0]
	v_mfma_scale_f32_16x16x128_f8f6f4 v[66:69], v[10:17], v[220:227], v[66:69], v210, v210 op_sel_hi:[0,0,0]
	v_mfma_scale_f32_16x16x128_f8f6f4 v[54:57], v[2:9], v[228:235], v[54:57], v210, v210 op_sel_hi:[0,0,0]
	v_mfma_scale_f32_16x16x128_f8f6f4 v[50:53], v[10:17], v[228:235], v[50:53], v210, v210 op_sel_hi:[0,0,0]
	v_mfma_scale_f32_16x16x128_f8f6f4 v[38:41], v[2:9], v[236:243], v[38:41], v210, v210 op_sel_hi:[0,0,0]
	v_mfma_scale_f32_16x16x128_f8f6f4 v[34:37], v[10:17], v[236:243], v[34:37], v210, v210 op_sel_hi:[0,0,0]
	s_nop 3
	s_setprio 0
	s_add_i32 s67, 0, 0x18000
	s_add_i32 s68, 0, 0x1c000
	v_add_u32_e32 v14, s67, v202
	v_add_u32_e32 v30, s68, v202
	ds_read_b128 v[2:5], v14
	ds_read_b128 v[6:9], v14 offset:1024
	ds_read_b128 v[10:13], v14 offset:2048
	ds_read_b128 v[14:17], v14 offset:3072
	ds_read_b128 v[18:21], v30
	ds_read_b128 v[22:25], v30 offset:1024
	ds_read_b128 v[26:29], v30 offset:2048
	ds_read_b128 v[30:33], v30 offset:3072
	s_mov_b32 m0, s48
	v_lshl_add_u64 v[244:245], s[40:41], 0, v[178:179]
	ds_read_b128 v[212:215], v209 offset:32768
	ds_read_b128 v[216:219], v209 offset:33792
	ds_read_b128 v[220:223], v209 offset:34816
	ds_read_b128 v[224:227], v209 offset:35840
	ds_read_b128 v[228:231], v209 offset:36864
	ds_read_b128 v[232:235], v209 offset:37888
	ds_read_b128 v[236:239], v209 offset:38912
	ds_read_b128 v[240:243], v209 offset:39936
	global_load_lds_dwordx4 v[244:245], off
	v_lshl_add_u64 v[244:245], s[40:41], 0, v[180:181]
	s_mov_b32 m0, s49
	s_nop 0
	global_load_lds_dwordx4 v[244:245], off
	s_waitcnt vmcnt(8)
	s_waitcnt lgkmcnt(0)
	s_barrier
; #define PG8_STAGE(bufoff, gbase, voff) do { _Pragma("unroll") for (int _i = 0; _i < 2; ++_i) \
;         __builtin_amdgcn_global_load_lds((const unsigned*)((const char*)(gbase) + (voff)[_i]), (PG8_LAS unsigned*)(lds + (bufoff) + ldsw + _i * 8192), 16, 0, 0); } while (0)
; #define PG8_WAIT_V(n) asm volatile("s_waitcnt vmcnt(" #n ")" ::: "memory")
; #define PG8_WAIT_L(n) asm volatile("s_waitcnt lgkmcnt(" #n ")" ::: "memory")
; #define PG8_BAR __builtin_amdgcn_s_barrier()
; #define PG8_SCHED __builtin_amdgcn_sched_barrier(0)
; template <class Epi, class Sched, bool ALIGN_EPI = true, bool F8 = false>
; __device__ __forceinline__ void gemm_phase(PG8_LAS unsigned char* lds, const Sched& S, const Epi& E) {
;     ...
;             PG8_LDA(At, 1, 1); PG8_STAGE(PG8_SB(1, 0), b3, voffB[0]); PG8_STAGE(PG8_SB(1, 1), b3, voffB[1]); PG8_STAGE(PG8_SA(1, 0), a3, vA2[0]);
;             PG8_WAIT_V(8); PG8_WAIT_L(0); PG8_BAR; PG8_MMA(1, 0, At, B0); PG8_MMA(1, 1, At, B1); PG8_BAR; PG8_SCHED;
;         }
;         if constexpr (ALIGN_EPI) { if (wr == 0) PG8_BAR; }
	s_setprio 2
	s_waitcnt lgkmcnt(0)
	v_mfma_scale_f32_16x16x128_f8f6f4 v[158:161], v[2:9], v[212:219], v[158:161], v210, v210 op_sel_hi:[0,0,0]
	v_mfma_scale_f32_16x16x128_f8f6f4 v[154:157], v[10:17], v[212:219], v[154:157], v210, v210 op_sel_hi:[0,0,0]
	v_mfma_scale_f32_16x16x128_f8f6f4 v[142:145], v[2:9], v[220:227], v[142:145], v210, v210 op_sel_hi:[0,0,0]
	v_mfma_scale_f32_16x16x128_f8f6f4 v[138:141], v[10:17], v[220:227], v[138:141], v210, v210 op_sel_hi:[0,0,0]
	v_mfma_scale_f32_16x16x128_f8f6f4 v[126:129], v[2:9], v[228:235], v[126:129], v210, v210 op_sel_hi:[0,0,0]
	v_mfma_scale_f32_16x16x128_f8f6f4 v[122:125], v[10:17], v[228:235], v[122:125], v210, v210 op_sel_hi:[0,0,0]
	v_mfma_scale_f32_16x16x128_f8f6f4 v[110:113], v[2:9], v[236:243], v[110:113], v210, v210 op_sel_hi:[0,0,0]
	v_mfma_scale_f32_16x16x128_f8f6f4 v[106:109], v[10:17], v[236:243], v[106:109], v210, v210 op_sel_hi:[0,0,0]
	s_nop 3
	s_setprio 0
	s_setprio 2
	v_mfma_scale_f32_16x16x128_f8f6f4 v[150:153], v[18:25], v[212:219], v[150:153], v210, v210 op_sel_hi:[0,0,0]
	v_mfma_scale_f32_16x16x128_f8f6f4 v[146:149], v[26:33], v[212:219], v[146:149], v210, v210 op_sel_hi:[0,0,0]
	v_mfma_scale_f32_16x16x128_f8f6f4 v[134:137], v[18:25], v[220:227], v[134:137], v210, v210 op_sel_hi:[0,0,0]
	v_mfma_scale_f32_16x16x128_f8f6f4 v[130:133], v[26:33], v[220:227], v[130:133], v210, v210 op_sel_hi:[0,0,0]
	v_mfma_scale_f32_16x16x128_f8f6f4 v[118:121], v[18:25], v[228:235], v[118:121], v210, v210 op_sel_hi:[0,0,0]
	v_mfma_scale_f32_16x16x128_f8f6f4 v[114:117], v[26:33], v[228:235], v[114:117], v210, v210 op_sel_hi:[0,0,0]
	v_mfma_scale_f32_16x16x128_f8f6f4 v[102:105], v[18:25], v[236:243], v[102:105], v210, v210 op_sel_hi:[0,0,0]
	v_mfma_scale_f32_16x16x128_f8f6f4 v[98:101], v[26:33], v[236:243], v[98:101], v210, v210 op_sel_hi:[0,0,0]
	s_nop 3
	s_setprio 0
	s_add_u32 s30, s30, 0x8000
	s_addc_u32 s31, s31, 0
	s_add_i32 s40, s67, s45
	v_lshl_add_u64 v[244:245], s[30:31], 0, v[164:165]
	s_mov_b32 m0, s40
	ds_read_b128 v[212:215], v209 offset:49152
	ds_read_b128 v[216:219], v209 offset:50176
	ds_read_b128 v[220:223], v209 offset:51200
	ds_read_b128 v[224:227], v209 offset:52224
	ds_read_b128 v[228:231], v209 offset:53248
	ds_read_b128 v[232:235], v209 offset:54272
	ds_read_b128 v[236:239], v209 offset:55296
	ds_read_b128 v[240:243], v209 offset:56320
	global_load_lds_dwordx4 v[244:245], off
	v_lshl_add_u64 v[244:245], s[30:31], 0, v[166:167]
	s_add_i32 m0, s40, 0x2000
	s_add_i32 s40, s68, s45
	global_load_lds_dwordx4 v[244:245], off
	v_lshl_add_u64 v[244:245], s[30:31], 0, v[168:169]
	s_mov_b32 m0, s40
	s_nop 0
	global_load_lds_dwordx4 v[244:245], off
	v_lshl_add_u64 v[244:245], s[30:31], 0, v[172:173]
	s_add_i32 m0, s40, 0x2000
	s_nop 0
	global_load_lds_dwordx4 v[244:245], off
	v_lshl_add_u64 v[244:245], s[28:29], 0, v[174:175]
	s_mov_b32 m0, s52
	s_nop 0
	global_load_lds_dwordx4 v[244:245], off
	v_lshl_add_u64 v[244:245], s[28:29], 0, v[176:177]
	s_mov_b32 m0, s53
	s_nop 0
	global_load_lds_dwordx4 v[244:245], off
	s_waitcnt vmcnt(8)
	s_waitcnt lgkmcnt(0)
	s_barrier
	s_setprio 2
	s_waitcnt lgkmcnt(0)
	v_mfma_scale_f32_16x16x128_f8f6f4 v[94:97], v[2:9], v[212:219], v[94:97], v210, v210 op_sel_hi:[0,0,0]
	v_mfma_scale_f32_16x16x128_f8f6f4 v[90:93], v[10:17], v[212:219], v[90:93], v210, v210 op_sel_hi:[0,0,0]
	v_mfma_scale_f32_16x16x128_f8f6f4 v[78:81], v[2:9], v[220:227], v[78:81], v210, v210 op_sel_hi:[0,0,0]
	v_mfma_scale_f32_16x16x128_f8f6f4 v[74:77], v[10:17], v[220:227], v[74:77], v210, v210 op_sel_hi:[0,0,0]
	v_mfma_scale_f32_16x16x128_f8f6f4 v[62:65], v[2:9], v[228:235], v[62:65], v210, v210 op_sel_hi:[0,0,0]
	v_mfma_scale_f32_16x16x128_f8f6f4 v[58:61], v[10:17], v[228:235], v[58:61], v210, v210 op_sel_hi:[0,0,0]
	v_mfma_scale_f32_16x16x128_f8f6f4 v[46:49], v[2:9], v[236:243], v[46:49], v210, v210 op_sel_hi:[0,0,0]
	v_mfma_scale_f32_16x16x128_f8f6f4 v[42:45], v[10:17], v[236:243], v[42:45], v210, v210 op_sel_hi:[0,0,0]
	s_nop 3
	s_setprio 0
	s_setprio 2
	v_mfma_scale_f32_16x16x128_f8f6f4 v[86:89], v[18:25], v[212:219], v[86:89], v210, v210 op_sel_hi:[0,0,0]
	v_mfma_scale_f32_16x16x128_f8f6f4 v[82:85], v[26:33], v[212:219], v[82:85], v210, v210 op_sel_hi:[0,0,0]
	v_mfma_scale_f32_16x16x128_f8f6f4 v[70:73], v[18:25], v[220:227], v[70:73], v210, v210 op_sel_hi:[0,0,0]
	v_mfma_scale_f32_16x16x128_f8f6f4 v[66:69], v[26:33], v[220:227], v[66:69], v210, v210 op_sel_hi:[0,0,0]
	v_mfma_scale_f32_16x16x128_f8f6f4 v[54:57], v[18:25], v[228:235], v[54:57], v210, v210 op_sel_hi:[0,0,0]
	v_mfma_scale_f32_16x16x128_f8f6f4 v[50:53], v[26:33], v[228:235], v[50:53], v210, v210 op_sel_hi:[0,0,0]
	v_mfma_scale_f32_16x16x128_f8f6f4 v[38:41], v[18:25], v[236:243], v[38:41], v210, v210 op_sel_hi:[0,0,0]
	v_mfma_scale_f32_16x16x128_f8f6f4 v[34:37], v[26:33], v[236:243], v[34:37], v210, v210 op_sel_hi:[0,0,0]
	s_nop 3
	s_setprio 0
	s_add_i32 s21, s21, 2
	s_add_u32 s5, s5, 0x10000
	s_addc_u32 s19, s19, 0
	s_add_u32 s26, s26, 0x10000
	s_addc_u32 s27, s27, 0
	s_cmp_gt_u32 s21, 13
	s_cbranch_scc0 .Lh1_372
.Lfx_372:
	s_and_b64 vcc, exec, s[14:15]
	s_cbranch_vccz .LBB0_375

; #define PG8_BAR __builtin_amdgcn_s_barrier()
; template <class Epi, class Sched, bool ALIGN_EPI = true, bool F8 = false>
; __device__ __forceinline__ void gemm_phase(PG8_LAS unsigned char* lds, const Sched& S, const Epi& E) {
;     ...
;         cur = nxt; cA = nA; cB = nB; ++ui;
; #pragma unroll
;         for (int h = 0; h < 2; ++h)
; #pragma unroll
;             for (int i = 0; i < 2; ++i) voffA[h][i] = voffAn[h][i];
;         if constexpr (ALIGN_EPI) { if (wr == 1) PG8_BAR; }
;     __device__ __forceinline__ void operator()(AccRef acc, const GUnit& u, int wr, int wc, int fr, int fq) const {
;     ...
;                 constexpr float SC = S8 ? W8_INV : 1.0f; st16_bf16(dst, acc[ai][0][m][0] * SC, acc[ai][0][m][1] * SC, acc[ai][1][m][0] * SC, acc[ai][1][m][1] * SC); }
.LBB0_407:
	v_pk_mul_f32 v[4:5], v[48:49], s[16:17] op_sel_hi:[1,0]
	v_pk_mul_f32 v[2:3], v[46:47], s[16:17] op_sel_hi:[1,0]
	v_pk_mul_f32 v[8:9], v[44:45], s[16:17] op_sel_hi:[1,0]
	v_pk_mul_f32 v[10:11], v[42:43], s[16:17] op_sel_hi:[1,0]
	v_pk_mul_f32 v[12:13], v[40:41], s[16:17] op_sel_hi:[1,0]
	v_pk_mul_f32 v[14:15], v[38:39], s[16:17] op_sel_hi:[1,0]
	v_pk_mul_f32 v[16:17], v[36:37], s[16:17] op_sel_hi:[1,0]
	v_pk_mul_f32 v[18:19], v[34:35], s[16:17] op_sel_hi:[1,0]
	v_cvt_pk_bf16_f32 v2, v2, v3
	v_cvt_pk_bf16_f32 v3, v4, v5
	v_cvt_pk_bf16_f32 v4, v10, v11
	v_cvt_pk_bf16_f32 v5, v8, v9
	s_andn2_b64 vcc, exec, s[0:1]
	s_mov_b64 s[0:1], -1
	v_cvt_pk_bf16_f32 v8, v14, v15
	v_cvt_pk_bf16_f32 v9, v12, v13
	v_cvt_pk_bf16_f32 v10, v18, v19
	v_cvt_pk_bf16_f32 v11, v16, v17
	flat_store_dwordx4 v[6:7], v[2:5]
	flat_store_dwordx4 v[6:7], v[8:11] offset:16
	s_cbranch_vccnz .LBB0_368
	s_andn2_b64 vcc, exec, s[10:11]
	s_cbranch_vccnz .LBB0_367
	s_branch .LBB0_367

; #define PG8_STAGE(bufoff, gbase, voff) do { _Pragma("unroll") for (int _i = 0; _i < 2; ++_i) \
;         __builtin_amdgcn_global_load_lds((const unsigned*)((const char*)(gbase) + (voff)[_i]), (PG8_LAS unsigned*)(lds + (bufoff) + ldsw + _i * 8192), 16, 0, 0); } while (0)
; #define PG8_WAIT_V(n) asm volatile("s_waitcnt vmcnt(" #n ")" ::: "memory")
; #define PG8_BAR __builtin_amdgcn_s_barrier()
;     __device__ __forceinline__ bool get(int i, int& pm, int& pn) const {
;         const long L = (long)i * G + c; if (L >= nwg) return false;
;         int wgid = (int)L; { const int q = nwg / NXCD, r = nwg % NXCD, xcd = wgid % NXCD, off = wgid / NXCD; wgid = (xcd < r ? xcd * (q + 1) : r * (q + 1) + (xcd - r) * q) + off; }
;         const int nig = WGM * nN, gid = wgid / nig, fm = gid * WGM, gsz = (nM - fm) < WGM ? (nM - fm) : WGM;
;         pm = fm + ((wgid % nig) % gsz); pn = (wgid % nig) / gsz; return true;
; template <class Epi, class Sched, bool ALIGN_EPI = true, bool F8 = false>
; __device__ __forceinline__ void gemm_phase(PG8_LAS unsigned char* lds, const Sched& S, const Epi& E) {
;     ...
;     if (!S.next(0, cur)) return;
;     S.a_off(cur, Rs, Cs, voffA);
; #pragma unroll
;     for (int h = 0; h < 2; ++h)
; #pragma unroll
;         for (int i = 0; i < 2; ++i) voffAn[h][i] = voffA[h][i];
;     f32x4 acc[2][2][4][2];
; #pragma unroll
;     for (int a = 0; a < 2; ++a)
; #pragma unroll
;         for (int b = 0; b < 2; ++b)
; #pragma unroll
;             for (int m = 0; m < 4; ++m)
; #pragma unroll
;                 for (int n = 0; n < 2; ++n) acc[a][b][m][n] = (f32x4){0.f, 0.f, 0.f, 0.f};
;     bf16x8 At[4][2], B0[2][2], B1[2][2]; i32x8 At8[4], B08[2], B18[2];
;     const int f8scale = 0x7F7F7F7F;
;     const char* cA = cur.A; const char* cB = cur.B;
;     PG8_STAGE(PG8_SB(0, 0), cB, voffB[0]); PG8_STAGE(PG8_SB(0, 1), cB, voffB[1]); PG8_STAGE(PG8_SA(0, 0), cA, voffA[0]); PG8_STAGE(PG8_SA(0, 1), cA, voffA[1]);
;     if (wr == 1) PG8_BAR;
;     PG8_WAIT_V(2); PG8_BAR;
;     PG8_STAGE(PG8_SB(1, 0), cB + kstepB, voffB[0]); PG8_STAGE(PG8_SA(1, 0), cA + kstep, voffA[0]); PG8_STAGE(PG8_SB(1, 1), cB + kstepB, voffB[1]);
;     PG8_WAIT_V(6); PG8_BAR;
.LBB0_416:
	s_ashr_i32 s0, s4, 3
	s_add_u32 s45, s36, 0x2300000
	s_addc_u32 s46, s37, 0
	s_add_i32 s0, s5, s0
	s_ashr_i32 s4, s0, 31
	s_lshr_b32 s4, s4, 25
	s_add_i32 s4, s0, s4
	s_ashr_i32 s5, s4, 7
	s_and_b32 s4, s4, 0xffffff80
	s_sub_i32 s4, s0, s4
	s_bfe_i32 s0, s4, 0x80000
	s_bfe_u32 s0, s0, 0x3000c
	s_add_i32 s8, s4, s0
	s_bfe_i32 s0, s8, 0x80000
	s_and_b32 s8, s8, 0xf8
	s_sub_i32 s4, s4, s8
	s_lshl_b32 s5, s5, 3
	s_sext_i32_i8 s4, s4
	s_add_i32 s8, s5, s4
	s_lshr_b32 s15, s12, 6
	s_sext_i32_i16 s0, s0
	s_ashr_i32 s9, s8, 31
	s_lshr_b32 s1, s12, 8
	s_lshl_b32 s47, s15, 10
	s_lshr_b32 s0, s0, 3
	s_lshl_b64 s[4:5], s[8:9], 19
	s_add_u32 s24, s42, s4
	s_addc_u32 s25, s43, s5
	s_bfe_i64 s[4:5], s[0:1], 0x100000
	s_lshl_b64 s[4:5], s[4:5], 19
	s_add_u32 s26, s45, s4
	s_addc_u32 s27, s46, s5
	s_add_i32 s48, s47, 0
	s_add_i32 m0, s48, 0x10000
	v_mov_b32_e32 v165, 0
	v_lshl_add_u64 v[2:3], s[26:27], 0, v[164:165]
	global_load_lds_dwordx4 v164, s[26:27]
	v_mov_b32_e32 v167, v165
	s_add_i32 m0, s48, 0x12000
	s_mov_b64 s[4:5], 0x400
	v_lshl_add_u64 v[4:5], s[26:27], 0, v[166:167]
	global_load_lds_dwordx4 v166, s[26:27]
	s_add_i32 m0, s48, 0x14000
	v_lshl_add_u64 v[2:3], v[2:3], 0, s[4:5]
	global_load_lds_dwordx4 v[2:3], off
	v_lshl_add_u64 v[2:3], v[4:5], 0, s[4:5]
	s_add_i32 m0, s48, 0x16000
	s_add_i32 s49, s48, 0x2000
	global_load_lds_dwordx4 v[2:3], off
	s_mov_b32 m0, s48
	s_add_i32 s50, s48, 0x4000
	global_load_lds_dwordx4 v174, s[24:25]
	s_mov_b32 m0, s49
	v_or_b32_e32 v178, 0x4000, v174
	global_load_lds_dwordx4 v176, s[24:25]
	s_mov_b32 m0, s50
	s_add_i32 s51, s48, 0x6000
	v_or_b32_e32 v180, 0x4000, v176
	global_load_lds_dwordx4 v178, s[24:25]
	s_mov_b32 m0, s51
	s_cmp_eq_u32 s1, 1
	global_load_lds_dwordx4 v180, s[24:25]
	s_movk_i32 s16, 0x4000
	s_mov_b32 s9, 0
	s_mov_b32 s52, 0x10000
	v_mov_b32_e32 v175, v165
	s_cselect_b64 s[10:11], -1, 0
	s_cmp_lg_u32 s1, 1
	v_mov_b32_e32 v177, v165
	s_cbranch_scc1 .LBB0_418
.LBB0_418:
	s_add_u32 s53, s13, 0x4000000
	s_addc_u32 s59, s14, 0
	s_and_b32 s17, s15, 3
	s_lshl_b32 s13, s1, 13
	s_add_u32 s14, s26, 0x8000
	s_addc_u32 s15, s27, 0
	s_add_i32 m0, s48, 0x18000
	v_lshl_add_u64 v[2:3], s[14:15], 0, v[164:165]
	s_waitcnt vmcnt(2)
	s_barrier
	global_load_lds_dwordx4 v[2:3], off
	s_add_i32 m0, s48, 0x1a000
	s_add_u32 s18, s24, 0x8000
	v_lshl_add_u64 v[2:3], s[14:15], 0, v[166:167]
	s_addc_u32 s19, s25, 0
	s_add_i32 s60, s48, 0x8000
	global_load_lds_dwordx4 v[2:3], off
	v_lshl_add_u64 v[2:3], s[18:19], 0, v[174:175]
	s_mov_b32 m0, s60
	s_add_i32 s61, s48, 0xa000
	global_load_lds_dwordx4 v[2:3], off
	v_lshl_add_u64 v[2:3], s[18:19], 0, v[176:177]
	s_mov_b32 m0, s61
	v_lshlrev_b32_e32 v4, 7, v199
	global_load_lds_dwordx4 v[2:3], off
	s_add_i32 m0, s48, 0x1c000
	v_lshlrev_b32_e32 v3, 2, v163
	global_load_lds_dwordx4 v168, s[14:15]
	s_add_i32 m0, s48, 0x1e000
	v_lshl_or_b32 v2, v163, 6, v162
	global_load_lds_dwordx4 v172, s[14:15]
	v_and_b32_e32 v3, 32, v3
	v_bitop3_b32 v2, v2, s13, v3 bitop3:0xde
	v_and_b32_e32 v3, 0x3800, v200
	v_or3_b32 v3, v197, v3, v4
	v_add3_u32 v182, v3, v198, s16
	v_and_b32_e32 v3, 0x1800, v196
	s_waitcnt vmcnt(6)
	s_cmpk_lt_u32 s12, 0x100
	v_or3_b32 v3, v197, v3, v4
	v_lshl_or_b32 v191, s17, 12, v201
	s_cselect_b64 s[12:13], -1, 0
	v_add_u32_e32 v3, v3, v198
	s_add_i32 s65, 0, 0x10000
	s_add_i32 s66, 0, 0x14000
	v_mov_b32_e32 v179, v165
	v_mov_b32_e32 v181, v165
	s_sext_i32_i8 s73, s0
	v_mov_b32_e32 v169, v165
	v_mov_b32_e32 v173, v165
	v_lshl_or_b32 v190, s1, 6, v163
	s_mov_b32 s62, 0x18000
	s_mov_b32 s63, 0x8000
	s_lshl_b32 s14, s17, 6
	s_mov_b32 s15, s9
	v_mov_b32_e32 v163, v165
	s_ashr_i32 s64, s33, 31
	v_mov_b32_e32 v183, v165
	v_or_b32_e32 v184, 0x4000, v3
	v_mov_b32_e32 v185, v165
	v_mov_b64_e32 v[186:187], 0x800
	v_mov_b64_e32 v[188:189], 0x7ff
	v_add_u32_e32 v192, s65, v191
	v_add_u32_e32 v193, s66, v191
	v_add_u32_e32 v194, 0, v2
	v_mov_b32_e32 v195, 0x7f7f7f7f
	v_mov_b32_e32 v196, 0x4b000000
	s_mov_b32 s67, 0xc0c0400
	s_mov_b32 s68, 0x5040100
	s_mov_b32 s69, 0x40000
	s_mov_b32 s70, 0x48000
	s_mov_b32 s71, 0x50000
	s_mov_b32 s72, 0
	s_mov_b64 s[20:21], s[24:25]
	s_mov_b64 s[22:23], s[26:27]
	s_barrier
	s_branch .LBB0_421

; #define PG8_STAGE(bufoff, gbase, voff) do { _Pragma("unroll") for (int _i = 0; _i < 2; ++_i) \
;         __builtin_amdgcn_global_load_lds((const unsigned*)((const char*)(gbase) + (voff)[_i]), (PG8_LAS unsigned*)(lds + (bufoff) + ldsw + _i * 8192), 16, 0, 0); } while (0)
; #define PG8_WAIT_V(n) asm volatile("s_waitcnt vmcnt(" #n ")" ::: "memory")
; #define PG8_WAIT_L(n) asm volatile("s_waitcnt lgkmcnt(" #n ")" ::: "memory")
; #define PG8_BAR __builtin_amdgcn_s_barrier()
; #define PG8_SCHED __builtin_amdgcn_sched_barrier(0)
; template <class Epi, class Sched, bool ALIGN_EPI = true, bool F8 = false>
; __device__ __forceinline__ void gemm_phase(PG8_LAS unsigned char* lds, const Sched& S, const Epi& E) {
;     ...
;             PG8_LDB(B0, 0, 0); PG8_LDB(B1, 0, 1); PG8_SCHED; PG8_LDA(At, 0, 0); PG8_STAGE(PG8_SA(1, 1), a1, voffA[1]);
;             PG8_WAIT_V(8); PG8_WAIT_L(0); PG8_BAR; PG8_MMA(0, 0, At, B0); PG8_MMA(0, 1, At, B1); PG8_BAR; PG8_SCHED;
;             PG8_LDA(At, 0, 1); PG8_STAGE(PG8_SB(0, 0), b2, voffB[0]); PG8_STAGE(PG8_SB(0, 1), b2, voffB[1]); PG8_STAGE(PG8_SA(0, 0), a2, vA2[0]);
;             PG8_WAIT_V(8); PG8_WAIT_L(0); PG8_BAR; PG8_MMA(1, 0, At, B0); PG8_MMA(1, 1, At, B1); PG8_BAR; PG8_SCHED;
;     ...
;         for (int a = 0; a < 2; ++a)
; #pragma unroll
;             for (int b = 0; b < 2; ++b)
; #pragma unroll
;                 for (int m = 0; m < 4; ++m)
; #pragma unroll
;                     for (int n = 0; n < 2; ++n) acc[a][b][m][n] = (f32x4){0.f, 0.f, 0.f, 0.f};
.LBB0_427:
	s_add_u32 s17, s26, 0x10000
	s_addc_u32 s19, s27, 0
	s_add_u32 s24, s24, 0x8000
	v_mov_b32_e32 v34, 0
	s_addc_u32 s25, s25, 0
	s_mov_b32 s74, -2
	v_mov_b32_e32 v35, v34
	v_mov_b32_e32 v36, v34
	v_mov_b32_e32 v37, v34
	v_mov_b32_e32 v38, v34
	v_mov_b32_e32 v39, v34
	v_mov_b32_e32 v40, v34
	v_mov_b32_e32 v41, v34
	v_mov_b32_e32 v50, v34
	v_mov_b32_e32 v51, v34
	v_mov_b32_e32 v52, v34
	v_mov_b32_e32 v53, v34
	v_mov_b32_e32 v54, v34
	v_mov_b32_e32 v55, v34
	v_mov_b32_e32 v56, v34
	v_mov_b32_e32 v57, v34
	v_mov_b32_e32 v66, v34
	v_mov_b32_e32 v67, v34
	v_mov_b32_e32 v68, v34
	v_mov_b32_e32 v69, v34
	v_mov_b32_e32 v70, v34
	v_mov_b32_e32 v71, v34
	v_mov_b32_e32 v72, v34
	v_mov_b32_e32 v73, v34
	v_mov_b32_e32 v82, v34
	v_mov_b32_e32 v83, v34
	v_mov_b32_e32 v84, v34
	v_mov_b32_e32 v85, v34
	v_mov_b32_e32 v86, v34
	v_mov_b32_e32 v87, v34
	v_mov_b32_e32 v88, v34
	v_mov_b32_e32 v89, v34
	v_mov_b32_e32 v42, v34
	v_mov_b32_e32 v43, v34
	v_mov_b32_e32 v44, v34
	v_mov_b32_e32 v45, v34
	v_mov_b32_e32 v46, v34
	v_mov_b32_e32 v47, v34
	v_mov_b32_e32 v48, v34
	v_mov_b32_e32 v49, v34
	v_mov_b32_e32 v58, v34
	v_mov_b32_e32 v59, v34
	v_mov_b32_e32 v60, v34
	v_mov_b32_e32 v61, v34
	v_mov_b32_e32 v62, v34
	v_mov_b32_e32 v63, v34
	v_mov_b32_e32 v64, v34
	v_mov_b32_e32 v65, v34
	v_mov_b32_e32 v74, v34
	v_mov_b32_e32 v75, v34
	v_mov_b32_e32 v76, v34
	v_mov_b32_e32 v77, v34
	v_mov_b32_e32 v78, v34
	v_mov_b32_e32 v79, v34
	v_mov_b32_e32 v80, v34
	v_mov_b32_e32 v81, v34
	v_mov_b32_e32 v90, v34
	v_mov_b32_e32 v91, v34
	v_mov_b32_e32 v92, v34
	v_mov_b32_e32 v93, v34
	v_mov_b32_e32 v94, v34
	v_mov_b32_e32 v95, v34
	v_mov_b32_e32 v96, v34
	v_mov_b32_e32 v97, v34
	v_mov_b32_e32 v98, v34
	v_mov_b32_e32 v99, v34
	v_mov_b32_e32 v100, v34
	v_mov_b32_e32 v101, v34
	v_mov_b32_e32 v102, v34
	v_mov_b32_e32 v103, v34
	v_mov_b32_e32 v104, v34
	v_mov_b32_e32 v105, v34
	v_mov_b32_e32 v114, v34
	v_mov_b32_e32 v115, v34
	v_mov_b32_e32 v116, v34
	v_mov_b32_e32 v117, v34
	v_mov_b32_e32 v118, v34
	v_mov_b32_e32 v119, v34
	v_mov_b32_e32 v120, v34
	v_mov_b32_e32 v121, v34
	v_mov_b32_e32 v130, v34
	v_mov_b32_e32 v131, v34
	v_mov_b32_e32 v132, v34
	v_mov_b32_e32 v133, v34
	v_mov_b32_e32 v134, v34
	v_mov_b32_e32 v135, v34
	v_mov_b32_e32 v136, v34
	v_mov_b32_e32 v137, v34
	v_mov_b32_e32 v146, v34
	v_mov_b32_e32 v147, v34
	v_mov_b32_e32 v148, v34
	v_mov_b32_e32 v149, v34
	v_mov_b32_e32 v150, v34
	v_mov_b32_e32 v151, v34
	v_mov_b32_e32 v152, v34
	v_mov_b32_e32 v153, v34
	v_mov_b32_e32 v106, v34
	v_mov_b32_e32 v107, v34
	v_mov_b32_e32 v108, v34
	v_mov_b32_e32 v109, v34
	v_mov_b32_e32 v110, v34
	v_mov_b32_e32 v111, v34
	v_mov_b32_e32 v112, v34
	v_mov_b32_e32 v113, v34
	v_mov_b32_e32 v122, v34
	v_mov_b32_e32 v123, v34
	v_mov_b32_e32 v124, v34
	v_mov_b32_e32 v125, v34
	v_mov_b32_e32 v126, v34
	v_mov_b32_e32 v127, v34
	v_mov_b32_e32 v128, v34
	v_mov_b32_e32 v129, v34
	v_mov_b32_e32 v138, v34
	v_mov_b32_e32 v139, v34
	v_mov_b32_e32 v140, v34
	v_mov_b32_e32 v141, v34
	v_mov_b32_e32 v142, v34
	v_mov_b32_e32 v143, v34
	v_mov_b32_e32 v144, v34
	v_mov_b32_e32 v145, v34
	v_mov_b32_e32 v154, v34
	v_mov_b32_e32 v155, v34
	v_mov_b32_e32 v156, v34
	v_mov_b32_e32 v157, v34
	v_mov_b32_e32 v158, v34
	v_mov_b32_e32 v159, v34
	v_mov_b32_e32 v160, v34
	v_mov_b32_e32 v161, v34
	s_bitcmp1_b32 s3, 2
	s_cbranch_scc1 .Lh1_428
.LBB0_428:
	ds_read_b128 v[18:21], v192
	ds_read_b128 v[22:25], v192 offset:1024
	ds_read_b128 v[26:29], v192 offset:2048
	ds_read_b128 v[30:33], v192 offset:3072
	ds_read_b128 v[2:5], v193
	ds_read_b128 v[6:9], v193 offset:1024
	ds_read_b128 v[10:13], v193 offset:2048
	ds_read_b128 v[14:17], v193 offset:3072
	s_add_u32 s26, s24, 0x8000
	s_addc_u32 s27, s25, 0
	s_cmp_eq_u32 s74, 12
	s_cselect_b32 s30, s20, s26
	s_cselect_b32 s31, s21, s27
	s_cselect_b32 s28, s22, s17
	s_cselect_b32 s29, s23, s19
	s_add_u32 s26, s30, 0x8000
	s_addc_u32 s27, s31, 0
	v_lshl_add_u64 v[230:231], s[24:25], 0, v[184:185]
	s_add_i32 m0, s48, 0xc000
	ds_read_b128 v[198:201], v194
	ds_read_b128 v[202:205], v194 offset:1024
	ds_read_b128 v[206:209], v194 offset:2048
	ds_read_b128 v[210:213], v194 offset:3072
	ds_read_b128 v[214:217], v194 offset:4096
	ds_read_b128 v[218:221], v194 offset:5120
	ds_read_b128 v[222:225], v194 offset:6144
	ds_read_b128 v[226:229], v194 offset:7168
	global_load_lds_dwordx4 v[230:231], off
	v_lshl_add_u64 v[230:231], s[24:25], 0, v[182:183]
	s_add_i32 m0, s48, 0xe000
	s_nop 0
	global_load_lds_dwordx4 v[230:231], off
	s_waitcnt vmcnt(8)
	s_waitcnt lgkmcnt(0)
	s_setprio 1
	s_waitcnt lgkmcnt(0)
	v_mfma_scale_f32_16x16x128_f8f6f4 v[158:161], v[18:25], v[198:205], v[158:161], v195, v195 op_sel_hi:[0,0,0]
	v_mfma_scale_f32_16x16x128_f8f6f4 v[154:157], v[26:33], v[198:205], v[154:157], v195, v195 op_sel_hi:[0,0,0]
	v_mfma_scale_f32_16x16x128_f8f6f4 v[142:145], v[18:25], v[206:213], v[142:145], v195, v195 op_sel_hi:[0,0,0]
	v_mfma_scale_f32_16x16x128_f8f6f4 v[138:141], v[26:33], v[206:213], v[138:141], v195, v195 op_sel_hi:[0,0,0]
	v_mfma_scale_f32_16x16x128_f8f6f4 v[126:129], v[18:25], v[214:221], v[126:129], v195, v195 op_sel_hi:[0,0,0]
	v_mfma_scale_f32_16x16x128_f8f6f4 v[122:125], v[26:33], v[214:221], v[122:125], v195, v195 op_sel_hi:[0,0,0]
	v_mfma_scale_f32_16x16x128_f8f6f4 v[110:113], v[18:25], v[222:229], v[110:113], v195, v195 op_sel_hi:[0,0,0]
	v_mfma_scale_f32_16x16x128_f8f6f4 v[106:109], v[26:33], v[222:229], v[106:109], v195, v195 op_sel_hi:[0,0,0]
	s_nop 3
	s_setprio 0
	s_setprio 1
	v_mfma_scale_f32_16x16x128_f8f6f4 v[150:153], v[2:9], v[198:205], v[150:153], v195, v195 op_sel_hi:[0,0,0]
	v_mfma_scale_f32_16x16x128_f8f6f4 v[146:149], v[10:17], v[198:205], v[146:149], v195, v195 op_sel_hi:[0,0,0]
	v_mfma_scale_f32_16x16x128_f8f6f4 v[134:137], v[2:9], v[206:213], v[134:137], v195, v195 op_sel_hi:[0,0,0]
	v_mfma_scale_f32_16x16x128_f8f6f4 v[130:133], v[10:17], v[206:213], v[130:133], v195, v195 op_sel_hi:[0,0,0]
	v_mfma_scale_f32_16x16x128_f8f6f4 v[118:121], v[2:9], v[214:221], v[118:121], v195, v195 op_sel_hi:[0,0,0]
	v_mfma_scale_f32_16x16x128_f8f6f4 v[114:117], v[10:17], v[214:221], v[114:117], v195, v195 op_sel_hi:[0,0,0]
	v_mfma_scale_f32_16x16x128_f8f6f4 v[102:105], v[2:9], v[222:229], v[102:105], v195, v195 op_sel_hi:[0,0,0]
	v_mfma_scale_f32_16x16x128_f8f6f4 v[98:101], v[10:17], v[222:229], v[98:101], v195, v195 op_sel_hi:[0,0,0]
	s_nop 3
	s_setprio 0
	s_barrier
; #define PG8_STAGE(bufoff, gbase, voff) do { _Pragma("unroll") for (int _i = 0; _i < 2; ++_i) \
;         __builtin_amdgcn_global_load_lds((const unsigned*)((const char*)(gbase) + (voff)[_i]), (PG8_LAS unsigned*)(lds + (bufoff) + ldsw + _i * 8192), 16, 0, 0); } while (0)
; #define PG8_WAIT_V(n) asm volatile("s_waitcnt vmcnt(" #n ")" ::: "memory")
; #define PG8_WAIT_L(n) asm volatile("s_waitcnt lgkmcnt(" #n ")" ::: "memory")
; #define PG8_BAR __builtin_amdgcn_s_barrier()
; #define PG8_SCHED __builtin_amdgcn_sched_barrier(0)
; template <class Epi, class Sched, bool ALIGN_EPI = true, bool F8 = false>
; __device__ __forceinline__ void gemm_phase(PG8_LAS unsigned char* lds, const Sched& S, const Epi& E) {
;     ...
;             PG8_LDA(At, 0, 1); PG8_STAGE(PG8_SB(0, 0), b2, voffB[0]); PG8_STAGE(PG8_SB(0, 1), b2, voffB[1]); PG8_STAGE(PG8_SA(0, 0), a2, vA2[0]);
;             PG8_WAIT_V(8); PG8_WAIT_L(0); PG8_BAR; PG8_MMA(1, 0, At, B0); PG8_MMA(1, 1, At, B1); PG8_BAR; PG8_SCHED;
;             PG8_LDB(B0, 1, 0); PG8_LDB(B1, 1, 1); PG8_SCHED; PG8_LDA(At, 1, 0); PG8_STAGE(PG8_SA(0, 1), a2, vA2[1]);
;             PG8_WAIT_V(8); PG8_WAIT_L(0); PG8_BAR; PG8_MMA(0, 0, At, B0); PG8_MMA(0, 1, At, B1); PG8_BAR; PG8_SCHED;
	s_add_i32 s75, s65, s47
	v_lshl_add_u64 v[230:231], s[28:29], 0, v[164:165]
	s_mov_b32 m0, s75
	ds_read_b128 v[198:201], v194 offset:16384
	ds_read_b128 v[202:205], v194 offset:17408
	ds_read_b128 v[206:209], v194 offset:18432
	ds_read_b128 v[210:213], v194 offset:19456
	ds_read_b128 v[214:217], v194 offset:20480
	ds_read_b128 v[218:221], v194 offset:21504
	ds_read_b128 v[222:225], v194 offset:22528
	ds_read_b128 v[226:229], v194 offset:23552
	global_load_lds_dwordx4 v[230:231], off
	v_lshl_add_u64 v[232:233], s[28:29], 0, v[166:167]
	s_add_i32 m0, s75, 0x2000
	s_add_i32 s75, s66, s47
	global_load_lds_dwordx4 v[232:233], off
	v_lshl_add_u64 v[230:231], v[230:231], 0, s[4:5]
	s_mov_b32 m0, s75
	s_nop 0
	global_load_lds_dwordx4 v[230:231], off
	v_lshl_add_u64 v[230:231], v[232:233], 0, s[4:5]
	s_add_i32 m0, s75, 0x2000
	s_nop 0
	global_load_lds_dwordx4 v[230:231], off
	v_lshl_add_u64 v[230:231], s[30:31], 0, v[174:175]
	s_mov_b32 m0, s48
	s_nop 0
	global_load_lds_dwordx4 v[230:231], off
	v_lshl_add_u64 v[230:231], s[30:31], 0, v[176:177]
	s_mov_b32 m0, s49
	s_nop 0
	global_load_lds_dwordx4 v[230:231], off
	s_waitcnt vmcnt(8)
	s_waitcnt lgkmcnt(0)
	s_setprio 1
	s_waitcnt lgkmcnt(0)
	v_mfma_scale_f32_16x16x128_f8f6f4 v[94:97], v[18:25], v[198:205], v[94:97], v195, v195 op_sel_hi:[0,0,0]
	v_mfma_scale_f32_16x16x128_f8f6f4 v[90:93], v[26:33], v[198:205], v[90:93], v195, v195 op_sel_hi:[0,0,0]
	v_mfma_scale_f32_16x16x128_f8f6f4 v[78:81], v[18:25], v[206:213], v[78:81], v195, v195 op_sel_hi:[0,0,0]
	v_mfma_scale_f32_16x16x128_f8f6f4 v[74:77], v[26:33], v[206:213], v[74:77], v195, v195 op_sel_hi:[0,0,0]
	v_mfma_scale_f32_16x16x128_f8f6f4 v[62:65], v[18:25], v[214:221], v[62:65], v195, v195 op_sel_hi:[0,0,0]
	v_mfma_scale_f32_16x16x128_f8f6f4 v[58:61], v[26:33], v[214:221], v[58:61], v195, v195 op_sel_hi:[0,0,0]
	v_mfma_scale_f32_16x16x128_f8f6f4 v[46:49], v[18:25], v[222:229], v[46:49], v195, v195 op_sel_hi:[0,0,0]
	v_mfma_scale_f32_16x16x128_f8f6f4 v[42:45], v[26:33], v[222:229], v[42:45], v195, v195 op_sel_hi:[0,0,0]
	s_nop 3
	s_setprio 0
	s_setprio 1
	v_mfma_scale_f32_16x16x128_f8f6f4 v[86:89], v[2:9], v[198:205], v[86:89], v195, v195 op_sel_hi:[0,0,0]
	v_mfma_scale_f32_16x16x128_f8f6f4 v[82:85], v[10:17], v[198:205], v[82:85], v195, v195 op_sel_hi:[0,0,0]
	v_mfma_scale_f32_16x16x128_f8f6f4 v[70:73], v[2:9], v[206:213], v[70:73], v195, v195 op_sel_hi:[0,0,0]
	v_mfma_scale_f32_16x16x128_f8f6f4 v[66:69], v[10:17], v[206:213], v[66:69], v195, v195 op_sel_hi:[0,0,0]
	v_mfma_scale_f32_16x16x128_f8f6f4 v[54:57], v[2:9], v[214:221], v[54:57], v195, v195 op_sel_hi:[0,0,0]
	v_mfma_scale_f32_16x16x128_f8f6f4 v[50:53], v[10:17], v[214:221], v[50:53], v195, v195 op_sel_hi:[0,0,0]
	v_mfma_scale_f32_16x16x128_f8f6f4 v[38:41], v[2:9], v[222:229], v[38:41], v195, v195 op_sel_hi:[0,0,0]
	v_mfma_scale_f32_16x16x128_f8f6f4 v[34:37], v[10:17], v[222:229], v[34:37], v195, v195 op_sel_hi:[0,0,0]
	s_nop 3
	s_setprio 0
	s_barrier
	s_add_i32 s75, 0, 0x18000
	s_add_i32 s76, 0, 0x1c000
	v_add_u32_e32 v14, s75, v191
	v_add_u32_e32 v30, s76, v191
	ds_read_b128 v[2:5], v14
	ds_read_b128 v[6:9], v14 offset:1024
	ds_read_b128 v[10:13], v14 offset:2048
	ds_read_b128 v[14:17], v14 offset:3072
	ds_read_b128 v[18:21], v30
	ds_read_b128 v[22:25], v30 offset:1024
	ds_read_b128 v[26:29], v30 offset:2048
	ds_read_b128 v[30:33], v30 offset:3072
	s_mov_b32 m0, s50
	v_lshl_add_u64 v[230:231], s[30:31], 0, v[178:179]
	ds_read_b128 v[198:201], v194 offset:32768
	ds_read_b128 v[202:205], v194 offset:33792
	ds_read_b128 v[206:209], v194 offset:34816
	ds_read_b128 v[210:213], v194 offset:35840
	ds_read_b128 v[214:217], v194 offset:36864
	ds_read_b128 v[218:221], v194 offset:37888
	ds_read_b128 v[222:225], v194 offset:38912
	ds_read_b128 v[226:229], v194 offset:39936
	global_load_lds_dwordx4 v[230:231], off
	v_lshl_add_u64 v[230:231], s[30:31], 0, v[180:181]
	s_mov_b32 m0, s51
	s_nop 0
	global_load_lds_dwordx4 v[230:231], off
	s_waitcnt vmcnt(8)
	s_waitcnt lgkmcnt(0)
	s_setprio 1
	s_waitcnt lgkmcnt(0)
	v_mfma_scale_f32_16x16x128_f8f6f4 v[158:161], v[2:9], v[198:205], v[158:161], v195, v195 op_sel_hi:[0,0,0]
	v_mfma_scale_f32_16x16x128_f8f6f4 v[154:157], v[10:17], v[198:205], v[154:157], v195, v195 op_sel_hi:[0,0,0]
	v_mfma_scale_f32_16x16x128_f8f6f4 v[142:145], v[2:9], v[206:213], v[142:145], v195, v195 op_sel_hi:[0,0,0]
	v_mfma_scale_f32_16x16x128_f8f6f4 v[138:141], v[10:17], v[206:213], v[138:141], v195, v195 op_sel_hi:[0,0,0]
	v_mfma_scale_f32_16x16x128_f8f6f4 v[126:129], v[2:9], v[214:221], v[126:129], v195, v195 op_sel_hi:[0,0,0]
	v_mfma_scale_f32_16x16x128_f8f6f4 v[122:125], v[10:17], v[214:221], v[122:125], v195, v195 op_sel_hi:[0,0,0]
	v_mfma_scale_f32_16x16x128_f8f6f4 v[110:113], v[2:9], v[222:229], v[110:113], v195, v195 op_sel_hi:[0,0,0]
	v_mfma_scale_f32_16x16x128_f8f6f4 v[106:109], v[10:17], v[222:229], v[106:109], v195, v195 op_sel_hi:[0,0,0]
	s_nop 3
	s_setprio 0
	s_setprio 1
	v_mfma_scale_f32_16x16x128_f8f6f4 v[150:153], v[18:25], v[198:205], v[150:153], v195, v195 op_sel_hi:[0,0,0]
	v_mfma_scale_f32_16x16x128_f8f6f4 v[146:149], v[26:33], v[198:205], v[146:149], v195, v195 op_sel_hi:[0,0,0]
	v_mfma_scale_f32_16x16x128_f8f6f4 v[134:137], v[18:25], v[206:213], v[134:137], v195, v195 op_sel_hi:[0,0,0]
	v_mfma_scale_f32_16x16x128_f8f6f4 v[130:133], v[26:33], v[206:213], v[130:133], v195, v195 op_sel_hi:[0,0,0]
	v_mfma_scale_f32_16x16x128_f8f6f4 v[118:121], v[18:25], v[214:221], v[118:121], v195, v195 op_sel_hi:[0,0,0]
	v_mfma_scale_f32_16x16x128_f8f6f4 v[114:117], v[26:33], v[214:221], v[114:117], v195, v195 op_sel_hi:[0,0,0]
	v_mfma_scale_f32_16x16x128_f8f6f4 v[102:105], v[18:25], v[222:229], v[102:105], v195, v195 op_sel_hi:[0,0,0]
	v_mfma_scale_f32_16x16x128_f8f6f4 v[98:101], v[26:33], v[222:229], v[98:101], v195, v195 op_sel_hi:[0,0,0]
	s_nop 3
	s_setprio 0
	s_barrier
; #define PG8_STAGE(bufoff, gbase, voff) do { _Pragma("unroll") for (int _i = 0; _i < 2; ++_i) \
;         __builtin_amdgcn_global_load_lds((const unsigned*)((const char*)(gbase) + (voff)[_i]), (PG8_LAS unsigned*)(lds + (bufoff) + ldsw + _i * 8192), 16, 0, 0); } while (0)
; #define PG8_WAIT_V(n) asm volatile("s_waitcnt vmcnt(" #n ")" ::: "memory")
; #define PG8_WAIT_L(n) asm volatile("s_waitcnt lgkmcnt(" #n ")" ::: "memory")
; #define PG8_BAR __builtin_amdgcn_s_barrier()
; #define PG8_SCHED __builtin_amdgcn_sched_barrier(0)
; template <class Epi, class Sched, bool ALIGN_EPI = true, bool F8 = false>
; __device__ __forceinline__ void gemm_phase(PG8_LAS unsigned char* lds, const Sched& S, const Epi& E) {
;     ...
;         for (int t = 0; t < nt; t += 2) {
;             const bool last = (t == nt - 2);
;             if constexpr (Sched::GATHER) { if (last && has_next) S.a_off(nxt, Rs, Cs, voffAn); }
;             const char* a1 = cA + (size_t)(t + 1) * kstep;
;             const char* a2 = last ? nA : cA + (size_t)(t + 2) * kstep; const char* b2 = last ? nB : cB + (size_t)(t + 2) * kstepB;
;             const char* a3 = a2 + kstep; const char* b3 = b2 + kstepB;
;             unsigned vA2[2][2];
; #pragma unroll
;             for (int h = 0; h < 2; ++h)
; #pragma unroll
;                 for (int i = 0; i < 2; ++i) { if constexpr (Sched::GATHER) vA2[h][i] = (last && has_next) ? voffAn[h][i] : voffA[h][i]; else vA2[h][i] = voffA[h][i]; }
;             PG8_LDB(B0, 0, 0); PG8_LDB(B1, 0, 1); PG8_SCHED; PG8_LDA(At, 0, 0); PG8_STAGE(PG8_SA(1, 1), a1, voffA[1]);
;             PG8_WAIT_V(8); PG8_WAIT_L(0); PG8_BAR; PG8_MMA(0, 0, At, B0); PG8_MMA(0, 1, At, B1); PG8_BAR; PG8_SCHED;
;     ...
;             PG8_LDA(At, 1, 1); PG8_STAGE(PG8_SB(1, 0), b3, voffB[0]); PG8_STAGE(PG8_SB(1, 1), b3, voffB[1]); PG8_STAGE(PG8_SA(1, 0), a3, vA2[0]);
;             PG8_WAIT_V(8); PG8_WAIT_L(0); PG8_BAR; PG8_MMA(1, 0, At, B0); PG8_MMA(1, 1, At, B1); PG8_BAR; PG8_SCHED;
	s_add_u32 s28, s28, 0x8000
	s_addc_u32 s29, s29, 0
	s_add_i32 s30, s75, s47
	v_lshl_add_u64 v[230:231], s[28:29], 0, v[164:165]
	s_mov_b32 m0, s30
	ds_read_b128 v[198:201], v194 offset:49152
	ds_read_b128 v[202:205], v194 offset:50176
	ds_read_b128 v[206:209], v194 offset:51200
	ds_read_b128 v[210:213], v194 offset:52224
	ds_read_b128 v[214:217], v194 offset:53248
	ds_read_b128 v[218:221], v194 offset:54272
	ds_read_b128 v[222:225], v194 offset:55296
	ds_read_b128 v[226:229], v194 offset:56320
	global_load_lds_dwordx4 v[230:231], off
	v_lshl_add_u64 v[230:231], s[28:29], 0, v[166:167]
	s_add_i32 m0, s30, 0x2000
	s_add_i32 s30, s76, s47
	global_load_lds_dwordx4 v[230:231], off
	v_lshl_add_u64 v[230:231], s[28:29], 0, v[168:169]
	s_mov_b32 m0, s30
	s_nop 0
	global_load_lds_dwordx4 v[230:231], off
	v_lshl_add_u64 v[230:231], s[28:29], 0, v[172:173]
	s_add_i32 m0, s30, 0x2000
	s_nop 0
	global_load_lds_dwordx4 v[230:231], off
	v_lshl_add_u64 v[230:231], s[26:27], 0, v[174:175]
	s_mov_b32 m0, s60
	s_nop 0
	global_load_lds_dwordx4 v[230:231], off
	v_lshl_add_u64 v[230:231], s[26:27], 0, v[176:177]
	s_mov_b32 m0, s61
	s_nop 0
	global_load_lds_dwordx4 v[230:231], off
	s_waitcnt vmcnt(8)
	s_waitcnt lgkmcnt(0)
	s_setprio 1
	s_waitcnt lgkmcnt(0)
	v_mfma_scale_f32_16x16x128_f8f6f4 v[94:97], v[2:9], v[198:205], v[94:97], v195, v195 op_sel_hi:[0,0,0]
	v_mfma_scale_f32_16x16x128_f8f6f4 v[90:93], v[10:17], v[198:205], v[90:93], v195, v195 op_sel_hi:[0,0,0]
	v_mfma_scale_f32_16x16x128_f8f6f4 v[78:81], v[2:9], v[206:213], v[78:81], v195, v195 op_sel_hi:[0,0,0]
	v_mfma_scale_f32_16x16x128_f8f6f4 v[74:77], v[10:17], v[206:213], v[74:77], v195, v195 op_sel_hi:[0,0,0]
	v_mfma_scale_f32_16x16x128_f8f6f4 v[62:65], v[2:9], v[214:221], v[62:65], v195, v195 op_sel_hi:[0,0,0]
	v_mfma_scale_f32_16x16x128_f8f6f4 v[58:61], v[10:17], v[214:221], v[58:61], v195, v195 op_sel_hi:[0,0,0]
	v_mfma_scale_f32_16x16x128_f8f6f4 v[46:49], v[2:9], v[222:229], v[46:49], v195, v195 op_sel_hi:[0,0,0]
	v_mfma_scale_f32_16x16x128_f8f6f4 v[42:45], v[10:17], v[222:229], v[42:45], v195, v195 op_sel_hi:[0,0,0]
	s_nop 3
	s_setprio 0
	s_setprio 1
	v_mfma_scale_f32_16x16x128_f8f6f4 v[86:89], v[18:25], v[198:205], v[86:89], v195, v195 op_sel_hi:[0,0,0]
	v_mfma_scale_f32_16x16x128_f8f6f4 v[82:85], v[26:33], v[198:205], v[82:85], v195, v195 op_sel_hi:[0,0,0]
	v_mfma_scale_f32_16x16x128_f8f6f4 v[70:73], v[18:25], v[206:213], v[70:73], v195, v195 op_sel_hi:[0,0,0]
	v_mfma_scale_f32_16x16x128_f8f6f4 v[66:69], v[26:33], v[206:213], v[66:69], v195, v195 op_sel_hi:[0,0,0]
	v_mfma_scale_f32_16x16x128_f8f6f4 v[54:57], v[18:25], v[214:221], v[54:57], v195, v195 op_sel_hi:[0,0,0]
	v_mfma_scale_f32_16x16x128_f8f6f4 v[50:53], v[26:33], v[214:221], v[50:53], v195, v195 op_sel_hi:[0,0,0]
	v_mfma_scale_f32_16x16x128_f8f6f4 v[38:41], v[18:25], v[222:229], v[38:41], v195, v195 op_sel_hi:[0,0,0]
	v_mfma_scale_f32_16x16x128_f8f6f4 v[34:37], v[26:33], v[222:229], v[34:37], v195, v195 op_sel_hi:[0,0,0]
	s_nop 3
	s_setprio 0
	s_barrier
	s_add_i32 s74, s74, 2
	s_add_u32 s17, s17, 0x10000
	s_addc_u32 s19, s19, 0
	s_add_u32 s24, s24, 0x10000
	s_addc_u32 s25, s25, 0
	s_cmp_gt_u32 s74, 13
	s_cbranch_scc0 .LBB0_428
	s_branch .Lfx_428
.Lh1_428:
	ds_read_b128 v[18:21], v192
	ds_read_b128 v[22:25], v192 offset:1024
	ds_read_b128 v[26:29], v192 offset:2048
	ds_read_b128 v[30:33], v192 offset:3072
	ds_read_b128 v[2:5], v193
	ds_read_b128 v[6:9], v193 offset:1024
	ds_read_b128 v[10:13], v193 offset:2048
	ds_read_b128 v[14:17], v193 offset:3072
	s_add_u32 s26, s24, 0x8000
	s_addc_u32 s27, s25, 0
	s_cmp_eq_u32 s74, 12
	s_cselect_b32 s30, s20, s26
	s_cselect_b32 s31, s21, s27
	s_cselect_b32 s28, s22, s17
	s_cselect_b32 s29, s23, s19
	s_add_u32 s26, s30, 0x8000
	s_addc_u32 s27, s31, 0
	v_lshl_add_u64 v[230:231], s[24:25], 0, v[184:185]
	s_add_i32 m0, s48, 0xc000
	ds_read_b128 v[198:201], v194
	ds_read_b128 v[202:205], v194 offset:1024
	ds_read_b128 v[206:209], v194 offset:2048
	ds_read_b128 v[210:213], v194 offset:3072
	ds_read_b128 v[214:217], v194 offset:4096
	ds_read_b128 v[218:221], v194 offset:5120
	ds_read_b128 v[222:225], v194 offset:6144
	ds_read_b128 v[226:229], v194 offset:7168
	global_load_lds_dwordx4 v[230:231], off
	v_lshl_add_u64 v[230:231], s[24:25], 0, v[182:183]
	s_add_i32 m0, s48, 0xe000
	s_nop 0
	global_load_lds_dwordx4 v[230:231], off
	s_waitcnt vmcnt(8)
	s_waitcnt lgkmcnt(0)
	s_barrier
; #define PG8_STAGE(bufoff, gbase, voff) do { _Pragma("unroll") for (int _i = 0; _i < 2; ++_i) \
;         __builtin_amdgcn_global_load_lds((const unsigned*)((const char*)(gbase) + (voff)[_i]), (PG8_LAS unsigned*)(lds + (bufoff) + ldsw + _i * 8192), 16, 0, 0); } while (0)
; #define PG8_WAIT_V(n) asm volatile("s_waitcnt vmcnt(" #n ")" ::: "memory")
; #define PG8_WAIT_L(n) asm volatile("s_waitcnt lgkmcnt(" #n ")" ::: "memory")
; #define PG8_BAR __builtin_amdgcn_s_barrier()
; #define PG8_SCHED __builtin_amdgcn_sched_barrier(0)
; template <class Epi, class Sched, bool ALIGN_EPI = true, bool F8 = false>
; __device__ __forceinline__ void gemm_phase(PG8_LAS unsigned char* lds, const Sched& S, const Epi& E) {
;     ...
;             PG8_LDB(B0, 0, 0); PG8_LDB(B1, 0, 1); PG8_SCHED; PG8_LDA(At, 0, 0); PG8_STAGE(PG8_SA(1, 1), a1, voffA[1]);
;             PG8_WAIT_V(8); PG8_WAIT_L(0); PG8_BAR; PG8_MMA(0, 0, At, B0); PG8_MMA(0, 1, At, B1); PG8_BAR; PG8_SCHED;
;             PG8_LDA(At, 0, 1); PG8_STAGE(PG8_SB(0, 0), b2, voffB[0]); PG8_STAGE(PG8_SB(0, 1), b2, voffB[1]); PG8_STAGE(PG8_SA(0, 0), a2, vA2[0]);
;             PG8_WAIT_V(8); PG8_WAIT_L(0); PG8_BAR; PG8_MMA(1, 0, At, B0); PG8_MMA(1, 1, At, B1); PG8_BAR; PG8_SCHED;
;             PG8_LDB(B0, 1, 0); PG8_LDB(B1, 1, 1); PG8_SCHED; PG8_LDA(At, 1, 0); PG8_STAGE(PG8_SA(0, 1), a2, vA2[1]);
;             PG8_WAIT_V(8); PG8_WAIT_L(0); PG8_BAR; PG8_MMA(0, 0, At, B0); PG8_MMA(0, 1, At, B1); PG8_BAR; PG8_SCHED;
	s_setprio 2
	s_waitcnt lgkmcnt(0)
	v_mfma_scale_f32_16x16x128_f8f6f4 v[158:161], v[18:25], v[198:205], v[158:161], v195, v195 op_sel_hi:[0,0,0]
	v_mfma_scale_f32_16x16x128_f8f6f4 v[154:157], v[26:33], v[198:205], v[154:157], v195, v195 op_sel_hi:[0,0,0]
	v_mfma_scale_f32_16x16x128_f8f6f4 v[142:145], v[18:25], v[206:213], v[142:145], v195, v195 op_sel_hi:[0,0,0]
	v_mfma_scale_f32_16x16x128_f8f6f4 v[138:141], v[26:33], v[206:213], v[138:141], v195, v195 op_sel_hi:[0,0,0]
	v_mfma_scale_f32_16x16x128_f8f6f4 v[126:129], v[18:25], v[214:221], v[126:129], v195, v195 op_sel_hi:[0,0,0]
	v_mfma_scale_f32_16x16x128_f8f6f4 v[122:125], v[26:33], v[214:221], v[122:125], v195, v195 op_sel_hi:[0,0,0]
	v_mfma_scale_f32_16x16x128_f8f6f4 v[110:113], v[18:25], v[222:229], v[110:113], v195, v195 op_sel_hi:[0,0,0]
	v_mfma_scale_f32_16x16x128_f8f6f4 v[106:109], v[26:33], v[222:229], v[106:109], v195, v195 op_sel_hi:[0,0,0]
	s_nop 3
	s_setprio 0
	s_setprio 2
	v_mfma_scale_f32_16x16x128_f8f6f4 v[150:153], v[2:9], v[198:205], v[150:153], v195, v195 op_sel_hi:[0,0,0]
	v_mfma_scale_f32_16x16x128_f8f6f4 v[146:149], v[10:17], v[198:205], v[146:149], v195, v195 op_sel_hi:[0,0,0]
	v_mfma_scale_f32_16x16x128_f8f6f4 v[134:137], v[2:9], v[206:213], v[134:137], v195, v195 op_sel_hi:[0,0,0]
	v_mfma_scale_f32_16x16x128_f8f6f4 v[130:133], v[10:17], v[206:213], v[130:133], v195, v195 op_sel_hi:[0,0,0]
	v_mfma_scale_f32_16x16x128_f8f6f4 v[118:121], v[2:9], v[214:221], v[118:121], v195, v195 op_sel_hi:[0,0,0]
	v_mfma_scale_f32_16x16x128_f8f6f4 v[114:117], v[10:17], v[214:221], v[114:117], v195, v195 op_sel_hi:[0,0,0]
	v_mfma_scale_f32_16x16x128_f8f6f4 v[102:105], v[2:9], v[222:229], v[102:105], v195, v195 op_sel_hi:[0,0,0]
	v_mfma_scale_f32_16x16x128_f8f6f4 v[98:101], v[10:17], v[222:229], v[98:101], v195, v195 op_sel_hi:[0,0,0]
	s_nop 3
	s_setprio 0
	s_add_i32 s75, s65, s47
	v_lshl_add_u64 v[230:231], s[28:29], 0, v[164:165]
	s_mov_b32 m0, s75
	ds_read_b128 v[198:201], v194 offset:16384
	ds_read_b128 v[202:205], v194 offset:17408
	ds_read_b128 v[206:209], v194 offset:18432
	ds_read_b128 v[210:213], v194 offset:19456
	ds_read_b128 v[214:217], v194 offset:20480
	ds_read_b128 v[218:221], v194 offset:21504
	ds_read_b128 v[222:225], v194 offset:22528
	ds_read_b128 v[226:229], v194 offset:23552
	global_load_lds_dwordx4 v[230:231], off
	v_lshl_add_u64 v[232:233], s[28:29], 0, v[166:167]
	s_add_i32 m0, s75, 0x2000
	s_add_i32 s75, s66, s47
	global_load_lds_dwordx4 v[232:233], off
	v_lshl_add_u64 v[230:231], v[230:231], 0, s[4:5]
	s_mov_b32 m0, s75
	s_nop 0
	global_load_lds_dwordx4 v[230:231], off
	v_lshl_add_u64 v[230:231], v[232:233], 0, s[4:5]
	s_add_i32 m0, s75, 0x2000
	s_nop 0
	global_load_lds_dwordx4 v[230:231], off
	v_lshl_add_u64 v[230:231], s[30:31], 0, v[174:175]
	s_mov_b32 m0, s48
	s_nop 0
	global_load_lds_dwordx4 v[230:231], off
	v_lshl_add_u64 v[230:231], s[30:31], 0, v[176:177]
	s_mov_b32 m0, s49
	s_nop 0
	global_load_lds_dwordx4 v[230:231], off
	s_waitcnt vmcnt(8)
	s_waitcnt lgkmcnt(0)
	s_barrier
	s_setprio 2
	s_waitcnt lgkmcnt(0)
	v_mfma_scale_f32_16x16x128_f8f6f4 v[94:97], v[18:25], v[198:205], v[94:97], v195, v195 op_sel_hi:[0,0,0]
	v_mfma_scale_f32_16x16x128_f8f6f4 v[90:93], v[26:33], v[198:205], v[90:93], v195, v195 op_sel_hi:[0,0,0]
	v_mfma_scale_f32_16x16x128_f8f6f4 v[78:81], v[18:25], v[206:213], v[78:81], v195, v195 op_sel_hi:[0,0,0]
	v_mfma_scale_f32_16x16x128_f8f6f4 v[74:77], v[26:33], v[206:213], v[74:77], v195, v195 op_sel_hi:[0,0,0]
	v_mfma_scale_f32_16x16x128_f8f6f4 v[62:65], v[18:25], v[214:221], v[62:65], v195, v195 op_sel_hi:[0,0,0]
	v_mfma_scale_f32_16x16x128_f8f6f4 v[58:61], v[26:33], v[214:221], v[58:61], v195, v195 op_sel_hi:[0,0,0]
	v_mfma_scale_f32_16x16x128_f8f6f4 v[46:49], v[18:25], v[222:229], v[46:49], v195, v195 op_sel_hi:[0,0,0]
	v_mfma_scale_f32_16x16x128_f8f6f4 v[42:45], v[26:33], v[222:229], v[42:45], v195, v195 op_sel_hi:[0,0,0]
	s_nop 3
	s_setprio 0
	s_setprio 2
	v_mfma_scale_f32_16x16x128_f8f6f4 v[86:89], v[2:9], v[198:205], v[86:89], v195, v195 op_sel_hi:[0,0,0]
	v_mfma_scale_f32_16x16x128_f8f6f4 v[82:85], v[10:17], v[198:205], v[82:85], v195, v195 op_sel_hi:[0,0,0]
	v_mfma_scale_f32_16x16x128_f8f6f4 v[70:73], v[2:9], v[206:213], v[70:73], v195, v195 op_sel_hi:[0,0,0]
	v_mfma_scale_f32_16x16x128_f8f6f4 v[66:69], v[10:17], v[206:213], v[66:69], v195, v195 op_sel_hi:[0,0,0]
	v_mfma_scale_f32_16x16x128_f8f6f4 v[54:57], v[2:9], v[214:221], v[54:57], v195, v195 op_sel_hi:[0,0,0]
	v_mfma_scale_f32_16x16x128_f8f6f4 v[50:53], v[10:17], v[214:221], v[50:53], v195, v195 op_sel_hi:[0,0,0]
	v_mfma_scale_f32_16x16x128_f8f6f4 v[38:41], v[2:9], v[222:229], v[38:41], v195, v195 op_sel_hi:[0,0,0]
	v_mfma_scale_f32_16x16x128_f8f6f4 v[34:37], v[10:17], v[222:229], v[34:37], v195, v195 op_sel_hi:[0,0,0]
	s_nop 3
	s_setprio 0
	s_add_i32 s75, 0, 0x18000
	s_add_i32 s76, 0, 0x1c000
	v_add_u32_e32 v14, s75, v191
	v_add_u32_e32 v30, s76, v191
	ds_read_b128 v[2:5], v14
	ds_read_b128 v[6:9], v14 offset:1024
	ds_read_b128 v[10:13], v14 offset:2048
	ds_read_b128 v[14:17], v14 offset:3072
	ds_read_b128 v[18:21], v30
	ds_read_b128 v[22:25], v30 offset:1024
	ds_read_b128 v[26:29], v30 offset:2048
	ds_read_b128 v[30:33], v30 offset:3072
	s_mov_b32 m0, s50
	v_lshl_add_u64 v[230:231], s[30:31], 0, v[178:179]
	ds_read_b128 v[198:201], v194 offset:32768
	ds_read_b128 v[202:205], v194 offset:33792
	ds_read_b128 v[206:209], v194 offset:34816
	ds_read_b128 v[210:213], v194 offset:35840
	ds_read_b128 v[214:217], v194 offset:36864
	ds_read_b128 v[218:221], v194 offset:37888
	ds_read_b128 v[222:225], v194 offset:38912
	ds_read_b128 v[226:229], v194 offset:39936
	global_load_lds_dwordx4 v[230:231], off
	v_lshl_add_u64 v[230:231], s[30:31], 0, v[180:181]
	s_mov_b32 m0, s51
	s_nop 0
	global_load_lds_dwordx4 v[230:231], off
	s_waitcnt vmcnt(8)
	s_waitcnt lgkmcnt(0)
	s_barrier
; #define PG8_STAGE(bufoff, gbase, voff) do { _Pragma("unroll") for (int _i = 0; _i < 2; ++_i) \
;         __builtin_amdgcn_global_load_lds((const unsigned*)((const char*)(gbase) + (voff)[_i]), (PG8_LAS unsigned*)(lds + (bufoff) + ldsw + _i * 8192), 16, 0, 0); } while (0)
; #define PG8_WAIT_V(n) asm volatile("s_waitcnt vmcnt(" #n ")" ::: "memory")
; #define PG8_WAIT_L(n) asm volatile("s_waitcnt lgkmcnt(" #n ")" ::: "memory")
; #define PG8_BAR __builtin_amdgcn_s_barrier()
; #define PG8_SCHED __builtin_amdgcn_sched_barrier(0)
; template <class Epi, class Sched, bool ALIGN_EPI = true, bool F8 = false>
; __device__ __forceinline__ void gemm_phase(PG8_LAS unsigned char* lds, const Sched& S, const Epi& E) {
;     ...
;             PG8_LDA(At, 1, 1); PG8_STAGE(PG8_SB(1, 0), b3, voffB[0]); PG8_STAGE(PG8_SB(1, 1), b3, voffB[1]); PG8_STAGE(PG8_SA(1, 0), a3, vA2[0]);
;             PG8_WAIT_V(8); PG8_WAIT_L(0); PG8_BAR; PG8_MMA(1, 0, At, B0); PG8_MMA(1, 1, At, B1); PG8_BAR; PG8_SCHED;
;         }
;         if constexpr (ALIGN_EPI) { if (wr == 0) PG8_BAR; }
	s_setprio 2
	s_waitcnt lgkmcnt(0)
	v_mfma_scale_f32_16x16x128_f8f6f4 v[158:161], v[2:9], v[198:205], v[158:161], v195, v195 op_sel_hi:[0,0,0]
	v_mfma_scale_f32_16x16x128_f8f6f4 v[154:157], v[10:17], v[198:205], v[154:157], v195, v195 op_sel_hi:[0,0,0]
	v_mfma_scale_f32_16x16x128_f8f6f4 v[142:145], v[2:9], v[206:213], v[142:145], v195, v195 op_sel_hi:[0,0,0]
	v_mfma_scale_f32_16x16x128_f8f6f4 v[138:141], v[10:17], v[206:213], v[138:141], v195, v195 op_sel_hi:[0,0,0]
	v_mfma_scale_f32_16x16x128_f8f6f4 v[126:129], v[2:9], v[214:221], v[126:129], v195, v195 op_sel_hi:[0,0,0]
	v_mfma_scale_f32_16x16x128_f8f6f4 v[122:125], v[10:17], v[214:221], v[122:125], v195, v195 op_sel_hi:[0,0,0]
	v_mfma_scale_f32_16x16x128_f8f6f4 v[110:113], v[2:9], v[222:229], v[110:113], v195, v195 op_sel_hi:[0,0,0]
	v_mfma_scale_f32_16x16x128_f8f6f4 v[106:109], v[10:17], v[222:229], v[106:109], v195, v195 op_sel_hi:[0,0,0]
	s_nop 3
	s_setprio 0
	s_setprio 2
	v_mfma_scale_f32_16x16x128_f8f6f4 v[150:153], v[18:25], v[198:205], v[150:153], v195, v195 op_sel_hi:[0,0,0]
	v_mfma_scale_f32_16x16x128_f8f6f4 v[146:149], v[26:33], v[198:205], v[146:149], v195, v195 op_sel_hi:[0,0,0]
	v_mfma_scale_f32_16x16x128_f8f6f4 v[134:137], v[18:25], v[206:213], v[134:137], v195, v195 op_sel_hi:[0,0,0]
	v_mfma_scale_f32_16x16x128_f8f6f4 v[130:133], v[26:33], v[206:213], v[130:133], v195, v195 op_sel_hi:[0,0,0]
	v_mfma_scale_f32_16x16x128_f8f6f4 v[118:121], v[18:25], v[214:221], v[118:121], v195, v195 op_sel_hi:[0,0,0]
	v_mfma_scale_f32_16x16x128_f8f6f4 v[114:117], v[26:33], v[214:221], v[114:117], v195, v195 op_sel_hi:[0,0,0]
	v_mfma_scale_f32_16x16x128_f8f6f4 v[102:105], v[18:25], v[222:229], v[102:105], v195, v195 op_sel_hi:[0,0,0]
	v_mfma_scale_f32_16x16x128_f8f6f4 v[98:101], v[26:33], v[222:229], v[98:101], v195, v195 op_sel_hi:[0,0,0]
	s_nop 3
	s_setprio 0
	s_add_u32 s28, s28, 0x8000
	s_addc_u32 s29, s29, 0
	s_add_i32 s30, s75, s47
	v_lshl_add_u64 v[230:231], s[28:29], 0, v[164:165]
	s_mov_b32 m0, s30
	ds_read_b128 v[198:201], v194 offset:49152
	ds_read_b128 v[202:205], v194 offset:50176
	ds_read_b128 v[206:209], v194 offset:51200
	ds_read_b128 v[210:213], v194 offset:52224
	ds_read_b128 v[214:217], v194 offset:53248
	ds_read_b128 v[218:221], v194 offset:54272
	ds_read_b128 v[222:225], v194 offset:55296
	ds_read_b128 v[226:229], v194 offset:56320
	global_load_lds_dwordx4 v[230:231], off
	v_lshl_add_u64 v[230:231], s[28:29], 0, v[166:167]
	s_add_i32 m0, s30, 0x2000
	s_add_i32 s30, s76, s47
	global_load_lds_dwordx4 v[230:231], off
	v_lshl_add_u64 v[230:231], s[28:29], 0, v[168:169]
	s_mov_b32 m0, s30
	s_nop 0
	global_load_lds_dwordx4 v[230:231], off
	v_lshl_add_u64 v[230:231], s[28:29], 0, v[172:173]
	s_add_i32 m0, s30, 0x2000
	s_nop 0
	global_load_lds_dwordx4 v[230:231], off
	v_lshl_add_u64 v[230:231], s[26:27], 0, v[174:175]
	s_mov_b32 m0, s60
	s_nop 0
	global_load_lds_dwordx4 v[230:231], off
	v_lshl_add_u64 v[230:231], s[26:27], 0, v[176:177]
	s_mov_b32 m0, s61
	s_nop 0
	global_load_lds_dwordx4 v[230:231], off
	s_waitcnt vmcnt(8)
	s_waitcnt lgkmcnt(0)
	s_barrier
	s_setprio 2
	s_waitcnt lgkmcnt(0)
	v_mfma_scale_f32_16x16x128_f8f6f4 v[94:97], v[2:9], v[198:205], v[94:97], v195, v195 op_sel_hi:[0,0,0]
	v_mfma_scale_f32_16x16x128_f8f6f4 v[90:93], v[10:17], v[198:205], v[90:93], v195, v195 op_sel_hi:[0,0,0]
	v_mfma_scale_f32_16x16x128_f8f6f4 v[78:81], v[2:9], v[206:213], v[78:81], v195, v195 op_sel_hi:[0,0,0]
	v_mfma_scale_f32_16x16x128_f8f6f4 v[74:77], v[10:17], v[206:213], v[74:77], v195, v195 op_sel_hi:[0,0,0]
	v_mfma_scale_f32_16x16x128_f8f6f4 v[62:65], v[2:9], v[214:221], v[62:65], v195, v195 op_sel_hi:[0,0,0]
	v_mfma_scale_f32_16x16x128_f8f6f4 v[58:61], v[10:17], v[214:221], v[58:61], v195, v195 op_sel_hi:[0,0,0]
	v_mfma_scale_f32_16x16x128_f8f6f4 v[46:49], v[2:9], v[222:229], v[46:49], v195, v195 op_sel_hi:[0,0,0]
	v_mfma_scale_f32_16x16x128_f8f6f4 v[42:45], v[10:17], v[222:229], v[42:45], v195, v195 op_sel_hi:[0,0,0]
	s_nop 3
	s_setprio 0
	s_setprio 2
	v_mfma_scale_f32_16x16x128_f8f6f4 v[86:89], v[18:25], v[198:205], v[86:89], v195, v195 op_sel_hi:[0,0,0]
	v_mfma_scale_f32_16x16x128_f8f6f4 v[82:85], v[26:33], v[198:205], v[82:85], v195, v195 op_sel_hi:[0,0,0]
	v_mfma_scale_f32_16x16x128_f8f6f4 v[70:73], v[18:25], v[206:213], v[70:73], v195, v195 op_sel_hi:[0,0,0]
	v_mfma_scale_f32_16x16x128_f8f6f4 v[66:69], v[26:33], v[206:213], v[66:69], v195, v195 op_sel_hi:[0,0,0]
	v_mfma_scale_f32_16x16x128_f8f6f4 v[54:57], v[18:25], v[214:221], v[54:57], v195, v195 op_sel_hi:[0,0,0]
	v_mfma_scale_f32_16x16x128_f8f6f4 v[50:53], v[26:33], v[214:221], v[50:53], v195, v195 op_sel_hi:[0,0,0]
	v_mfma_scale_f32_16x16x128_f8f6f4 v[38:41], v[18:25], v[222:229], v[38:41], v195, v195 op_sel_hi:[0,0,0]
	v_mfma_scale_f32_16x16x128_f8f6f4 v[34:37], v[26:33], v[222:229], v[34:37], v195, v195 op_sel_hi:[0,0,0]
	s_nop 3
	s_setprio 0
	s_add_i32 s74, s74, 2
	s_add_u32 s17, s17, 0x10000
	s_addc_u32 s19, s19, 0
	s_add_u32 s24, s24, 0x10000
	s_addc_u32 s25, s25, 0
	s_cmp_gt_u32 s74, 13
	s_cbranch_scc0 .Lh1_428
.Lfx_428:
	s_and_b64 vcc, exec, s[12:13]
	s_cbranch_vccz .LBB0_431
; __device__ __forceinline__ float fsigmoid(float x) { return __builtin_amdgcn_rcpf(1.0f + __builtin_amdgcn_exp2f(-1.44269504f * x)); }
; template <class Epi, class Sched, bool ALIGN_EPI = true, bool F8 = false>
; __device__ __forceinline__ void gemm_phase(PG8_LAS unsigned char* lds, const Sched& S, const Epi& E) {
;     ...
;         if constexpr (F8) {
; #pragma unroll
;             for (int a = 0; a < 2; ++a)
; #pragma unroll
;                 for (int b = 0; b < 2; ++b)
;                     asm volatile("s_nop 15\n\ts_nop 7" : "+v"(acc[a][b][0][0]), "+v"(acc[a][b][0][1]), "+v"(acc[a][b][1][0]), "+v"(acc[a][b][1][1]), "+v"(acc[a][b][2][0]), "+v"(acc[a][b][2][1]), "+v"(acc[a][b][3][0]), "+v"(acc[a][b][3][1]));
;     __device__ __forceinline__ void operator()(AccRef acc, const GUnit& u, int wr, int wc, int fr, int fq) const {
;         const int pm = u.x0, pn = u.x1; unsigned char* base = (pn < 8 ? GZF : GZS) + (size_t)(pm * 256 + wr * 64 + fr) * D + (pn & 7) * 256 + wc * 64 + 16 * fq;
; #pragma unroll
;         for (int ai = 0; ai < 2; ++ai)
; #pragma unroll
;             for (int m = 0; m < 4; ++m) { u32x4 w;
; #pragma unroll
;                 for (int bj = 0; bj < 2; ++bj)
; #pragma unroll
;                     for (int n = 0; n < 2; ++n) { const f32x4 v = acc[ai][bj][m][n]; w[bj * 2 + n] = pk4_u8(fsigmoid(v[0] * W8_INV), fsigmoid(v[1] * W8_INV), fsigmoid(v[2] * W8_INV), fsigmoid(v[3] * W8_INV)); }
;                 *(u32x4*)(base + (size_t)(ai * 128 + m * 16) * D) = w; }
.LBB0_431:
	s_nop 15
	s_nop 7
	s_nop 15
	s_nop 7
	v_lshl_add_u32 v2, s8, 8, v190
	v_mul_f32_e32 v4, 0x3c800000, v158
	v_mul_f32_e32 v5, 0x3c800000, v159
	v_mul_f32_e32 v6, 0x3c800000, v160
	v_mul_f32_e32 v7, 0x3c800000, v161
	v_mul_f32_e32 v4, 0xbfb8aa3b, v4
	v_mul_f32_e32 v5, 0xbfb8aa3b, v5
	v_mul_f32_e32 v6, 0xbfb8aa3b, v6
	v_mul_f32_e32 v7, 0xbfb8aa3b, v7
	v_exp_f32_e32 v4, v4
	v_exp_f32_e32 v5, v5
	v_exp_f32_e32 v6, v6
	v_exp_f32_e32 v7, v7
	v_add_f32_e32 v4, 1.0, v4
	v_add_f32_e32 v5, 1.0, v5
	v_add_f32_e32 v6, 1.0, v6
	v_add_f32_e32 v7, 1.0, v7
	v_rcp_f32_e32 v4, v4
	v_rcp_f32_e32 v5, v5
	v_rcp_f32_e32 v6, v6
	v_rcp_f32_e32 v7, v7
	v_fmamk_f32 v4, v4, 0x437f0000, v196
	v_fmamk_f32 v5, v5, 0x437f0000, v196
	v_fmamk_f32 v6, v6, 0x437f0000, v196
	v_fmamk_f32 v7, v7, 0x437f0000, v196
	v_perm_b32 v4, v5, v4, s67
	v_perm_b32 v5, v7, v6, s67
	v_mul_f32_e32 v6, 0x3c800000, v154
	v_mul_f32_e32 v7, 0x3c800000, v155
	v_mul_f32_e32 v6, 0xbfb8aa3b, v6
	v_mul_f32_e32 v7, 0xbfb8aa3b, v7
	v_exp_f32_e32 v6, v6
	v_exp_f32_e32 v7, v7
	v_perm_b32 v4, v5, v4, s68
	v_mul_f32_e32 v8, 0x3c800000, v157
	v_add_f32_e32 v5, 1.0, v6
	v_add_f32_e32 v6, 1.0, v7
	v_mul_f32_e32 v7, 0x3c800000, v156
	v_mul_f32_e32 v7, 0xbfb8aa3b, v7
	v_mul_f32_e32 v8, 0xbfb8aa3b, v8
	v_exp_f32_e32 v7, v7
	v_exp_f32_e32 v8, v8
	v_rcp_f32_e32 v5, v5
	v_rcp_f32_e32 v6, v6
	v_add_f32_e32 v7, 1.0, v7
	v_add_f32_e32 v8, 1.0, v8
	v_rcp_f32_e32 v7, v7
	v_rcp_f32_e32 v8, v8
	v_fmamk_f32 v5, v5, 0x437f0000, v196
	v_fmamk_f32 v6, v6, 0x437f0000, v196
	v_fmamk_f32 v7, v7, 0x437f0000, v196
	v_fmamk_f32 v8, v8, 0x437f0000, v196
	v_perm_b32 v5, v6, v5, s67
	v_perm_b32 v6, v8, v7, s67
	v_mul_f32_e32 v7, 0x3c800000, v150
	v_mul_f32_e32 v8, 0x3c800000, v151
	v_mul_f32_e32 v7, 0xbfb8aa3b, v7
	v_mul_f32_e32 v8, 0xbfb8aa3b, v8
	v_exp_f32_e32 v7, v7
	v_exp_f32_e32 v8, v8
	v_perm_b32 v5, v6, v5, s68
	v_mul_f32_e32 v9, 0x3c800000, v153
	v_add_f32_e32 v6, 1.0, v7
	v_add_f32_e32 v7, 1.0, v8
	v_mul_f32_e32 v8, 0x3c800000, v152
	v_mul_f32_e32 v8, 0xbfb8aa3b, v8
	v_mul_f32_e32 v9, 0xbfb8aa3b, v9
	v_exp_f32_e32 v8, v8
	v_exp_f32_e32 v9, v9
	v_rcp_f32_e32 v6, v6
	v_rcp_f32_e32 v7, v7
	v_add_f32_e32 v8, 1.0, v8
	v_add_f32_e32 v9, 1.0, v9
	v_rcp_f32_e32 v8, v8
	v_rcp_f32_e32 v9, v9
	v_fmamk_f32 v6, v6, 0x437f0000, v196
	v_fmamk_f32 v7, v7, 0x437f0000, v196
	v_fmamk_f32 v8, v8, 0x437f0000, v196
	v_fmamk_f32 v9, v9, 0x437f0000, v196
	v_perm_b32 v6, v7, v6, s67
	v_perm_b32 v7, v9, v8, s67
	v_mul_f32_e32 v8, 0x3c800000, v146
	v_mul_f32_e32 v9, 0x3c800000, v147
	v_mul_f32_e32 v8, 0xbfb8aa3b, v8
	v_mul_f32_e32 v9, 0xbfb8aa3b, v9
	v_exp_f32_e32 v8, v8
	v_exp_f32_e32 v9, v9
	v_perm_b32 v6, v7, v6, s68
	v_mul_f32_e32 v10, 0x3c800000, v149
	v_add_f32_e32 v7, 1.0, v8
	v_add_f32_e32 v8, 1.0, v9
	v_mul_f32_e32 v9, 0x3c800000, v148
	v_mul_f32_e32 v9, 0xbfb8aa3b, v9
	v_mul_f32_e32 v10, 0xbfb8aa3b, v10
	v_exp_f32_e32 v9, v9
	v_exp_f32_e32 v10, v10
	v_rcp_f32_e32 v7, v7
	v_rcp_f32_e32 v8, v8
	v_add_f32_e32 v9, 1.0, v9
	v_add_f32_e32 v10, 1.0, v10
	v_rcp_f32_e32 v9, v9
	v_rcp_f32_e32 v10, v10
	s_cmp_lt_i32 s73, 8
	v_ashrrev_i32_e32 v3, 31, v2
	s_cselect_b32 s25, s41, s59
	s_cselect_b32 s24, s40, s53
	v_lshlrev_b64 v[2:3], 11, v[2:3]
	s_lshl_b32 s8, s73, 8
	v_lshl_add_u64 v[2:3], s[24:25], 0, v[2:3]
	s_and_b32 s8, s8, 0x700
	v_lshl_add_u64 v[2:3], v[2:3], 0, s[8:9]
	v_fmamk_f32 v7, v7, 0x437f0000, v196
	v_fmamk_f32 v8, v8, 0x437f0000, v196
	v_fmamk_f32 v9, v9, 0x437f0000, v196
	v_fmamk_f32 v10, v10, 0x437f0000, v196
	v_lshl_add_u64 v[2:3], v[2:3], 0, s[14:15]
	v_perm_b32 v7, v8, v7, s67
	v_perm_b32 v8, v10, v9, s67
	v_lshl_add_u64 v[2:3], v[2:3], 0, v[162:163]
	v_perm_b32 v7, v8, v7, s68
	s_nop 15
	s_nop 7
	s_nop 15
	s_nop 7
	v_mul_f32_e32 v8, 0x3c800000, v142
	v_mul_f32_e32 v9, 0x3c800000, v143
	flat_store_dwordx4 v[2:3], v[4:7]
	v_mul_f32_e32 v8, 0xbfb8aa3b, v8
	v_mul_f32_e32 v9, 0xbfb8aa3b, v9
	v_mul_f32_e32 v6, 0x3c800000, v144
	v_mul_f32_e32 v7, 0x3c800000, v145
	v_mul_f32_e32 v6, 0xbfb8aa3b, v6
	v_mul_f32_e32 v7, 0xbfb8aa3b, v7
	v_exp_f32_e32 v8, v8
	v_exp_f32_e32 v9, v9
	v_exp_f32_e32 v6, v6
	v_exp_f32_e32 v7, v7
	v_add_f32_e32 v4, 1.0, v8
	v_add_f32_e32 v5, 1.0, v9
	v_add_f32_e32 v6, 1.0, v6
	v_add_f32_e32 v7, 1.0, v7
	v_rcp_f32_e32 v4, v4
	v_rcp_f32_e32 v5, v5
	v_rcp_f32_e32 v6, v6
	v_rcp_f32_e32 v7, v7
	v_fmamk_f32 v4, v4, 0x437f0000, v196
	v_fmamk_f32 v5, v5, 0x437f0000, v196
	v_fmamk_f32 v6, v6, 0x437f0000, v196
	v_fmamk_f32 v7, v7, 0x437f0000, v196
	v_perm_b32 v4, v5, v4, s67
	v_perm_b32 v5, v7, v6, s67
	v_mul_f32_e32 v6, 0x3c800000, v138
	v_mul_f32_e32 v7, 0x3c800000, v139
	v_mul_f32_e32 v6, 0xbfb8aa3b, v6
	v_mul_f32_e32 v7, 0xbfb8aa3b, v7
	v_exp_f32_e32 v6, v6
	v_exp_f32_e32 v7, v7
	v_perm_b32 v4, v5, v4, s68
	v_mul_f32_e32 v8, 0x3c800000, v141
	v_add_f32_e32 v5, 1.0, v6
	v_add_f32_e32 v6, 1.0, v7
	v_mul_f32_e32 v7, 0x3c800000, v140
	v_mul_f32_e32 v7, 0xbfb8aa3b, v7
	v_mul_f32_e32 v8, 0xbfb8aa3b, v8
	v_exp_f32_e32 v7, v7
	v_exp_f32_e32 v8, v8
	v_rcp_f32_e32 v5, v5
	v_rcp_f32_e32 v6, v6
	v_add_f32_e32 v7, 1.0, v7
	v_add_f32_e32 v8, 1.0, v8
	v_rcp_f32_e32 v7, v7
	v_rcp_f32_e32 v8, v8
	v_fmamk_f32 v5, v5, 0x437f0000, v196
	v_fmamk_f32 v6, v6, 0x437f0000, v196
	v_fmamk_f32 v7, v7, 0x437f0000, v196
	v_fmamk_f32 v8, v8, 0x437f0000, v196
	v_perm_b32 v5, v6, v5, s67
	v_perm_b32 v6, v8, v7, s67
	v_mul_f32_e32 v7, 0x3c800000, v134
	v_mul_f32_e32 v8, 0x3c800000, v135
	v_mul_f32_e32 v7, 0xbfb8aa3b, v7
	v_mul_f32_e32 v8, 0xbfb8aa3b, v8
	v_exp_f32_e32 v7, v7
	v_exp_f32_e32 v8, v8
	v_perm_b32 v5, v6, v5, s68
	v_mul_f32_e32 v9, 0x3c800000, v137
	v_add_f32_e32 v6, 1.0, v7
	v_add_f32_e32 v7, 1.0, v8
	v_mul_f32_e32 v8, 0x3c800000, v136
; __device__ __forceinline__ float fsigmoid(float x) { return __builtin_amdgcn_rcpf(1.0f + __builtin_amdgcn_exp2f(-1.44269504f * x)); }
;     __device__ __forceinline__ void operator()(AccRef acc, const GUnit& u, int wr, int wc, int fr, int fq) const {
;         const int pm = u.x0, pn = u.x1; unsigned char* base = (pn < 8 ? GZF : GZS) + (size_t)(pm * 256 + wr * 64 + fr) * D + (pn & 7) * 256 + wc * 64 + 16 * fq;
; #pragma unroll
;         for (int ai = 0; ai < 2; ++ai)
; #pragma unroll
;             for (int m = 0; m < 4; ++m) { u32x4 w;
; #pragma unroll
;                 for (int bj = 0; bj < 2; ++bj)
; #pragma unroll
;                     for (int n = 0; n < 2; ++n) { const f32x4 v = acc[ai][bj][m][n]; w[bj * 2 + n] = pk4_u8(fsigmoid(v[0] * W8_INV), fsigmoid(v[1] * W8_INV), fsigmoid(v[2] * W8_INV), fsigmoid(v[3] * W8_INV)); }
;                 *(u32x4*)(base + (size_t)(ai * 128 + m * 16) * D) = w; }
	v_mul_f32_e32 v8, 0xbfb8aa3b, v8
	v_mul_f32_e32 v9, 0xbfb8aa3b, v9
	v_exp_f32_e32 v8, v8
	v_exp_f32_e32 v9, v9
	v_rcp_f32_e32 v6, v6
	v_rcp_f32_e32 v7, v7
	v_add_f32_e32 v8, 1.0, v8
	v_add_f32_e32 v9, 1.0, v9
	v_rcp_f32_e32 v8, v8
	v_rcp_f32_e32 v9, v9
	v_fmamk_f32 v6, v6, 0x437f0000, v196
	v_fmamk_f32 v7, v7, 0x437f0000, v196
	v_fmamk_f32 v8, v8, 0x437f0000, v196
	v_fmamk_f32 v9, v9, 0x437f0000, v196
	v_perm_b32 v6, v7, v6, s67
	v_perm_b32 v7, v9, v8, s67
	v_mul_f32_e32 v8, 0x3c800000, v130
	v_mul_f32_e32 v9, 0x3c800000, v131
	v_mul_f32_e32 v8, 0xbfb8aa3b, v8
	v_mul_f32_e32 v9, 0xbfb8aa3b, v9
	v_exp_f32_e32 v8, v8
	v_exp_f32_e32 v9, v9
	v_perm_b32 v6, v7, v6, s68
	v_mul_f32_e32 v10, 0x3c800000, v133
	v_add_f32_e32 v7, 1.0, v8
	v_add_f32_e32 v8, 1.0, v9
	v_mul_f32_e32 v9, 0x3c800000, v132
	v_mul_f32_e32 v9, 0xbfb8aa3b, v9
	v_mul_f32_e32 v10, 0xbfb8aa3b, v10
	v_exp_f32_e32 v9, v9
	v_exp_f32_e32 v10, v10
	v_rcp_f32_e32 v7, v7
	v_rcp_f32_e32 v8, v8
	v_add_f32_e32 v9, 1.0, v9
	v_add_f32_e32 v10, 1.0, v10
	v_rcp_f32_e32 v9, v9
	v_rcp_f32_e32 v10, v10
	v_fmamk_f32 v7, v7, 0x437f0000, v196
	v_fmamk_f32 v8, v8, 0x437f0000, v196
	v_fmamk_f32 v9, v9, 0x437f0000, v196
	v_fmamk_f32 v10, v10, 0x437f0000, v196
	v_perm_b32 v7, v8, v7, s67
	v_perm_b32 v8, v10, v9, s67
	v_perm_b32 v7, v8, v7, s68
	v_add_co_u32_e32 v8, vcc, s63, v2
	v_mul_f32_e32 v10, 0x3c800000, v126
	s_nop 0
	v_addc_co_u32_e32 v9, vcc, 0, v3, vcc
	v_mul_f32_e32 v11, 0x3c800000, v127
	flat_store_dwordx4 v[8:9], v[4:7]
	v_mul_f32_e32 v10, 0xbfb8aa3b, v10
	v_mul_f32_e32 v11, 0xbfb8aa3b, v11
	v_mul_f32_e32 v6, 0x3c800000, v128
	v_mul_f32_e32 v7, 0x3c800000, v129
	v_mul_f32_e32 v6, 0xbfb8aa3b, v6
	v_mul_f32_e32 v7, 0xbfb8aa3b, v7
	v_exp_f32_e32 v10, v10
	v_exp_f32_e32 v11, v11
	v_exp_f32_e32 v6, v6
	v_exp_f32_e32 v7, v7
	v_add_f32_e32 v4, 1.0, v10
	v_add_f32_e32 v5, 1.0, v11
	v_add_f32_e32 v6, 1.0, v6
	v_add_f32_e32 v7, 1.0, v7
	v_rcp_f32_e32 v4, v4
	v_rcp_f32_e32 v5, v5
	v_rcp_f32_e32 v6, v6
	v_rcp_f32_e32 v7, v7
	v_fmamk_f32 v4, v4, 0x437f0000, v196
	v_fmamk_f32 v5, v5, 0x437f0000, v196
	v_fmamk_f32 v6, v6, 0x437f0000, v196
	v_fmamk_f32 v7, v7, 0x437f0000, v196
	v_perm_b32 v4, v5, v4, s67
	v_perm_b32 v5, v7, v6, s67
	v_mul_f32_e32 v6, 0x3c800000, v122
	v_mul_f32_e32 v7, 0x3c800000, v123
	v_mul_f32_e32 v6, 0xbfb8aa3b, v6
	v_mul_f32_e32 v7, 0xbfb8aa3b, v7
	v_exp_f32_e32 v6, v6
	v_exp_f32_e32 v7, v7
	v_perm_b32 v4, v5, v4, s68
	v_mul_f32_e32 v8, 0x3c800000, v125
	v_add_f32_e32 v5, 1.0, v6
	v_add_f32_e32 v6, 1.0, v7
	v_mul_f32_e32 v7, 0x3c800000, v124
	v_mul_f32_e32 v7, 0xbfb8aa3b, v7
	v_mul_f32_e32 v8, 0xbfb8aa3b, v8
	v_exp_f32_e32 v7, v7
	v_exp_f32_e32 v8, v8
	v_rcp_f32_e32 v5, v5
	v_rcp_f32_e32 v6, v6
	v_add_f32_e32 v7, 1.0, v7
	v_add_f32_e32 v8, 1.0, v8
	v_rcp_f32_e32 v7, v7
	v_rcp_f32_e32 v8, v8
	v_fmamk_f32 v5, v5, 0x437f0000, v196
	v_fmamk_f32 v6, v6, 0x437f0000, v196
	v_fmamk_f32 v7, v7, 0x437f0000, v196
	v_fmamk_f32 v8, v8, 0x437f0000, v196
	v_perm_b32 v5, v6, v5, s67
	v_perm_b32 v6, v8, v7, s67
	v_mul_f32_e32 v7, 0x3c800000, v118
	v_mul_f32_e32 v8, 0x3c800000, v119
	v_mul_f32_e32 v7, 0xbfb8aa3b, v7
	v_mul_f32_e32 v8, 0xbfb8aa3b, v8
	v_exp_f32_e32 v7, v7
	v_exp_f32_e32 v8, v8
	v_perm_b32 v5, v6, v5, s68
	v_mul_f32_e32 v9, 0x3c800000, v121
	v_add_f32_e32 v6, 1.0, v7
	v_add_f32_e32 v7, 1.0, v8
	v_mul_f32_e32 v8, 0x3c800000, v120
	v_mul_f32_e32 v8, 0xbfb8aa3b, v8
	v_mul_f32_e32 v9, 0xbfb8aa3b, v9
	v_exp_f32_e32 v8, v8
	v_exp_f32_e32 v9, v9
	v_rcp_f32_e32 v6, v6
	v_rcp_f32_e32 v7, v7
	v_add_f32_e32 v8, 1.0, v8
	v_add_f32_e32 v9, 1.0, v9
	v_rcp_f32_e32 v8, v8
	v_rcp_f32_e32 v9, v9
	v_fmamk_f32 v6, v6, 0x437f0000, v196
	v_fmamk_f32 v7, v7, 0x437f0000, v196
	v_fmamk_f32 v8, v8, 0x437f0000, v196
	v_fmamk_f32 v9, v9, 0x437f0000, v196
	v_perm_b32 v6, v7, v6, s67
	v_perm_b32 v7, v9, v8, s67
	v_mul_f32_e32 v8, 0x3c800000, v114
	v_mul_f32_e32 v9, 0x3c800000, v115
	v_mul_f32_e32 v8, 0xbfb8aa3b, v8
	v_mul_f32_e32 v9, 0xbfb8aa3b, v9
	v_exp_f32_e32 v8, v8
	v_exp_f32_e32 v9, v9
	v_perm_b32 v6, v7, v6, s68
	v_mul_f32_e32 v10, 0x3c800000, v117
	v_add_f32_e32 v7, 1.0, v8
	v_add_f32_e32 v8, 1.0, v9
	v_mul_f32_e32 v9, 0x3c800000, v116
	v_mul_f32_e32 v9, 0xbfb8aa3b, v9
	v_mul_f32_e32 v10, 0xbfb8aa3b, v10
	v_exp_f32_e32 v9, v9
	v_exp_f32_e32 v10, v10
	v_rcp_f32_e32 v7, v7
	v_rcp_f32_e32 v8, v8
	v_add_f32_e32 v9, 1.0, v9
	v_add_f32_e32 v10, 1.0, v10
	v_rcp_f32_e32 v9, v9
	v_rcp_f32_e32 v10, v10
	v_fmamk_f32 v7, v7, 0x437f0000, v196
	v_fmamk_f32 v8, v8, 0x437f0000, v196
	v_fmamk_f32 v9, v9, 0x437f0000, v196
	v_fmamk_f32 v10, v10, 0x437f0000, v196
	v_perm_b32 v7, v8, v7, s67
	v_perm_b32 v8, v10, v9, s67
	v_perm_b32 v7, v8, v7, s68
	v_add_co_u32_e32 v8, vcc, s52, v2
	v_mul_f32_e32 v10, 0x3c800000, v110
	s_nop 0
	v_addc_co_u32_e32 v9, vcc, 0, v3, vcc
	v_mul_f32_e32 v11, 0x3c800000, v111
	flat_store_dwordx4 v[8:9], v[4:7]
	v_mul_f32_e32 v10, 0xbfb8aa3b, v10
	v_mul_f32_e32 v11, 0xbfb8aa3b, v11
	v_mul_f32_e32 v6, 0x3c800000, v112
	v_mul_f32_e32 v7, 0x3c800000, v113
	v_mul_f32_e32 v6, 0xbfb8aa3b, v6
	v_mul_f32_e32 v7, 0xbfb8aa3b, v7
	v_exp_f32_e32 v10, v10
	v_exp_f32_e32 v11, v11
	v_exp_f32_e32 v6, v6
	v_exp_f32_e32 v7, v7
	v_add_f32_e32 v4, 1.0, v10
	v_add_f32_e32 v5, 1.0, v11
	v_add_f32_e32 v6, 1.0, v6
	v_add_f32_e32 v7, 1.0, v7
	v_rcp_f32_e32 v4, v4
	v_rcp_f32_e32 v5, v5
	v_rcp_f32_e32 v6, v6
	v_rcp_f32_e32 v7, v7
	v_fmamk_f32 v4, v4, 0x437f0000, v196
	v_fmamk_f32 v5, v5, 0x437f0000, v196
	v_fmamk_f32 v6, v6, 0x437f0000, v196
	v_fmamk_f32 v7, v7, 0x437f0000, v196
	v_perm_b32 v4, v5, v4, s67
	v_perm_b32 v5, v7, v6, s67
	v_mul_f32_e32 v6, 0x3c800000, v106
	v_mul_f32_e32 v7, 0x3c800000, v107
	v_mul_f32_e32 v6, 0xbfb8aa3b, v6
; __device__ __forceinline__ float fsigmoid(float x) { return __builtin_amdgcn_rcpf(1.0f + __builtin_amdgcn_exp2f(-1.44269504f * x)); }
;     __device__ __forceinline__ void operator()(AccRef acc, const GUnit& u, int wr, int wc, int fr, int fq) const {
;         const int pm = u.x0, pn = u.x1; unsigned char* base = (pn < 8 ? GZF : GZS) + (size_t)(pm * 256 + wr * 64 + fr) * D + (pn & 7) * 256 + wc * 64 + 16 * fq;
; #pragma unroll
;         for (int ai = 0; ai < 2; ++ai)
; #pragma unroll
;             for (int m = 0; m < 4; ++m) { u32x4 w;
; #pragma unroll
;                 for (int bj = 0; bj < 2; ++bj)
; #pragma unroll
;                     for (int n = 0; n < 2; ++n) { const f32x4 v = acc[ai][bj][m][n]; w[bj * 2 + n] = pk4_u8(fsigmoid(v[0] * W8_INV), fsigmoid(v[1] * W8_INV), fsigmoid(v[2] * W8_INV), fsigmoid(v[3] * W8_INV)); }
;                 *(u32x4*)(base + (size_t)(ai * 128 + m * 16) * D) = w; }
	v_mul_f32_e32 v7, 0xbfb8aa3b, v7
	v_exp_f32_e32 v6, v6
	v_exp_f32_e32 v7, v7
	v_perm_b32 v4, v5, v4, s68
	v_mul_f32_e32 v8, 0x3c800000, v109
	v_add_f32_e32 v5, 1.0, v6
	v_add_f32_e32 v6, 1.0, v7
	v_mul_f32_e32 v7, 0x3c800000, v108
	v_mul_f32_e32 v7, 0xbfb8aa3b, v7
	v_mul_f32_e32 v8, 0xbfb8aa3b, v8
	v_exp_f32_e32 v7, v7
	v_exp_f32_e32 v8, v8
	v_rcp_f32_e32 v5, v5
	v_rcp_f32_e32 v6, v6
	v_add_f32_e32 v7, 1.0, v7
	v_add_f32_e32 v8, 1.0, v8
	v_rcp_f32_e32 v7, v7
	v_rcp_f32_e32 v8, v8
	v_fmamk_f32 v5, v5, 0x437f0000, v196
	v_fmamk_f32 v6, v6, 0x437f0000, v196
	v_fmamk_f32 v7, v7, 0x437f0000, v196
	v_fmamk_f32 v8, v8, 0x437f0000, v196
	v_perm_b32 v5, v6, v5, s67
	v_perm_b32 v6, v8, v7, s67
	v_mul_f32_e32 v7, 0x3c800000, v102
	v_mul_f32_e32 v8, 0x3c800000, v103
	v_mul_f32_e32 v7, 0xbfb8aa3b, v7
	v_mul_f32_e32 v8, 0xbfb8aa3b, v8
	v_exp_f32_e32 v7, v7
	v_exp_f32_e32 v8, v8
	v_perm_b32 v5, v6, v5, s68
	v_mul_f32_e32 v9, 0x3c800000, v105
	v_add_f32_e32 v6, 1.0, v7
	v_add_f32_e32 v7, 1.0, v8
	v_mul_f32_e32 v8, 0x3c800000, v104
	v_mul_f32_e32 v8, 0xbfb8aa3b, v8
	v_mul_f32_e32 v9, 0xbfb8aa3b, v9
	v_exp_f32_e32 v8, v8
	v_exp_f32_e32 v9, v9
	v_rcp_f32_e32 v6, v6
	v_rcp_f32_e32 v7, v7
	v_add_f32_e32 v8, 1.0, v8
	v_add_f32_e32 v9, 1.0, v9
	v_rcp_f32_e32 v8, v8
	v_rcp_f32_e32 v9, v9
	v_fmamk_f32 v6, v6, 0x437f0000, v196
	v_fmamk_f32 v7, v7, 0x437f0000, v196
	v_fmamk_f32 v8, v8, 0x437f0000, v196
	v_fmamk_f32 v9, v9, 0x437f0000, v196
	v_perm_b32 v6, v7, v6, s67
	v_perm_b32 v7, v9, v8, s67
	v_mul_f32_e32 v8, 0x3c800000, v98
	v_mul_f32_e32 v9, 0x3c800000, v99
	v_mul_f32_e32 v8, 0xbfb8aa3b, v8
	v_mul_f32_e32 v9, 0xbfb8aa3b, v9
	v_exp_f32_e32 v8, v8
	v_exp_f32_e32 v9, v9
	v_perm_b32 v6, v7, v6, s68
	v_mul_f32_e32 v10, 0x3c800000, v101
	v_add_f32_e32 v7, 1.0, v8
	v_add_f32_e32 v8, 1.0, v9
	v_mul_f32_e32 v9, 0x3c800000, v100
	v_mul_f32_e32 v9, 0xbfb8aa3b, v9
	v_mul_f32_e32 v10, 0xbfb8aa3b, v10
	v_exp_f32_e32 v9, v9
	v_exp_f32_e32 v10, v10
	v_rcp_f32_e32 v7, v7
	v_rcp_f32_e32 v8, v8
	v_add_f32_e32 v9, 1.0, v9
	v_add_f32_e32 v10, 1.0, v10
	v_rcp_f32_e32 v9, v9
	v_rcp_f32_e32 v10, v10
	v_fmamk_f32 v7, v7, 0x437f0000, v196
	v_fmamk_f32 v8, v8, 0x437f0000, v196
	v_fmamk_f32 v9, v9, 0x437f0000, v196
	v_fmamk_f32 v10, v10, 0x437f0000, v196
	v_perm_b32 v7, v8, v7, s67
	v_perm_b32 v8, v10, v9, s67
	v_perm_b32 v7, v8, v7, s68
	v_add_co_u32_e32 v8, vcc, s62, v2
	v_mul_f32_e32 v10, 0x3c800000, v94
	s_nop 0
	v_addc_co_u32_e32 v9, vcc, 0, v3, vcc
	v_mul_f32_e32 v11, 0x3c800000, v95
	flat_store_dwordx4 v[8:9], v[4:7]
	v_mul_f32_e32 v10, 0xbfb8aa3b, v10
	v_mul_f32_e32 v11, 0xbfb8aa3b, v11
	v_mul_f32_e32 v6, 0x3c800000, v96
	v_mul_f32_e32 v7, 0x3c800000, v97
	v_mul_f32_e32 v6, 0xbfb8aa3b, v6
	v_mul_f32_e32 v7, 0xbfb8aa3b, v7
	v_exp_f32_e32 v10, v10
	v_exp_f32_e32 v11, v11
	v_exp_f32_e32 v6, v6
	v_exp_f32_e32 v7, v7
	v_add_f32_e32 v4, 1.0, v10
	v_add_f32_e32 v5, 1.0, v11
	v_add_f32_e32 v6, 1.0, v6
	v_add_f32_e32 v7, 1.0, v7
	v_rcp_f32_e32 v4, v4
	v_rcp_f32_e32 v5, v5
	v_rcp_f32_e32 v6, v6
	v_rcp_f32_e32 v7, v7
	v_fmamk_f32 v4, v4, 0x437f0000, v196
	v_fmamk_f32 v5, v5, 0x437f0000, v196
	v_fmamk_f32 v6, v6, 0x437f0000, v196
	v_fmamk_f32 v7, v7, 0x437f0000, v196
	v_perm_b32 v4, v5, v4, s67
	v_perm_b32 v5, v7, v6, s67
	v_mul_f32_e32 v6, 0x3c800000, v90
	v_mul_f32_e32 v7, 0x3c800000, v91
	v_mul_f32_e32 v6, 0xbfb8aa3b, v6
	v_mul_f32_e32 v7, 0xbfb8aa3b, v7
	v_exp_f32_e32 v6, v6
	v_exp_f32_e32 v7, v7
	v_perm_b32 v4, v5, v4, s68
	v_mul_f32_e32 v8, 0x3c800000, v93
	v_add_f32_e32 v5, 1.0, v6
	v_add_f32_e32 v6, 1.0, v7
	v_mul_f32_e32 v7, 0x3c800000, v92
	v_mul_f32_e32 v7, 0xbfb8aa3b, v7
	v_mul_f32_e32 v8, 0xbfb8aa3b, v8
	v_exp_f32_e32 v7, v7
	v_exp_f32_e32 v8, v8
	v_rcp_f32_e32 v5, v5
	v_rcp_f32_e32 v6, v6
	v_add_f32_e32 v7, 1.0, v7
	v_add_f32_e32 v8, 1.0, v8
	v_rcp_f32_e32 v7, v7
	v_rcp_f32_e32 v8, v8
	v_fmamk_f32 v5, v5, 0x437f0000, v196
	v_fmamk_f32 v6, v6, 0x437f0000, v196
	v_fmamk_f32 v7, v7, 0x437f0000, v196
	v_fmamk_f32 v8, v8, 0x437f0000, v196
	v_perm_b32 v5, v6, v5, s67
	v_perm_b32 v6, v8, v7, s67
	v_mul_f32_e32 v7, 0x3c800000, v86
	v_mul_f32_e32 v8, 0x3c800000, v87
	v_mul_f32_e32 v7, 0xbfb8aa3b, v7
	v_mul_f32_e32 v8, 0xbfb8aa3b, v8
	v_exp_f32_e32 v7, v7
	v_exp_f32_e32 v8, v8
	v_perm_b32 v5, v6, v5, s68
	v_mul_f32_e32 v9, 0x3c800000, v89
	v_add_f32_e32 v6, 1.0, v7
	v_add_f32_e32 v7, 1.0, v8
	v_mul_f32_e32 v8, 0x3c800000, v88
	v_mul_f32_e32 v8, 0xbfb8aa3b, v8
	v_mul_f32_e32 v9, 0xbfb8aa3b, v9
	v_exp_f32_e32 v8, v8
	v_exp_f32_e32 v9, v9
	v_rcp_f32_e32 v6, v6
	v_rcp_f32_e32 v7, v7
	v_add_f32_e32 v8, 1.0, v8
	v_add_f32_e32 v9, 1.0, v9
	v_rcp_f32_e32 v8, v8
	v_rcp_f32_e32 v9, v9
	v_fmamk_f32 v6, v6, 0x437f0000, v196
	v_fmamk_f32 v7, v7, 0x437f0000, v196
	v_fmamk_f32 v8, v8, 0x437f0000, v196
	v_fmamk_f32 v9, v9, 0x437f0000, v196
	v_perm_b32 v6, v7, v6, s67
	v_perm_b32 v7, v9, v8, s67
	v_mul_f32_e32 v8, 0x3c800000, v82
	v_mul_f32_e32 v9, 0x3c800000, v83
	v_mul_f32_e32 v8, 0xbfb8aa3b, v8
	v_mul_f32_e32 v9, 0xbfb8aa3b, v9
	v_exp_f32_e32 v8, v8
	v_exp_f32_e32 v9, v9
	v_perm_b32 v6, v7, v6, s68
	v_mul_f32_e32 v10, 0x3c800000, v85
	v_add_f32_e32 v7, 1.0, v8
	v_add_f32_e32 v8, 1.0, v9
	v_mul_f32_e32 v9, 0x3c800000, v84
	v_mul_f32_e32 v9, 0xbfb8aa3b, v9
	v_mul_f32_e32 v10, 0xbfb8aa3b, v10
	v_exp_f32_e32 v9, v9
	v_exp_f32_e32 v10, v10
	v_rcp_f32_e32 v7, v7
	v_rcp_f32_e32 v8, v8
	v_add_f32_e32 v9, 1.0, v9
	v_add_f32_e32 v10, 1.0, v10
	v_rcp_f32_e32 v9, v9
	v_rcp_f32_e32 v10, v10
	v_fmamk_f32 v7, v7, 0x437f0000, v196
	v_fmamk_f32 v8, v8, 0x437f0000, v196
	v_fmamk_f32 v9, v9, 0x437f0000, v196
	v_fmamk_f32 v10, v10, 0x437f0000, v196
	v_perm_b32 v7, v8, v7, s67
	v_perm_b32 v8, v10, v9, s67
; __device__ __forceinline__ float fsigmoid(float x) { return __builtin_amdgcn_rcpf(1.0f + __builtin_amdgcn_exp2f(-1.44269504f * x)); }
;     __device__ __forceinline__ void operator()(AccRef acc, const GUnit& u, int wr, int wc, int fr, int fq) const {
;         const int pm = u.x0, pn = u.x1; unsigned char* base = (pn < 8 ? GZF : GZS) + (size_t)(pm * 256 + wr * 64 + fr) * D + (pn & 7) * 256 + wc * 64 + 16 * fq;
; #pragma unroll
;         for (int ai = 0; ai < 2; ++ai)
; #pragma unroll
;             for (int m = 0; m < 4; ++m) { u32x4 w;
; #pragma unroll
;                 for (int bj = 0; bj < 2; ++bj)
; #pragma unroll
;                     for (int n = 0; n < 2; ++n) { const f32x4 v = acc[ai][bj][m][n]; w[bj * 2 + n] = pk4_u8(fsigmoid(v[0] * W8_INV), fsigmoid(v[1] * W8_INV), fsigmoid(v[2] * W8_INV), fsigmoid(v[3] * W8_INV)); }
;                 *(u32x4*)(base + (size_t)(ai * 128 + m * 16) * D) = w; }
	v_perm_b32 v7, v8, v7, s68
	v_add_co_u32_e32 v8, vcc, s69, v2
	v_mul_f32_e32 v10, 0x3c800000, v78
	s_nop 0
	v_addc_co_u32_e32 v9, vcc, 0, v3, vcc
	v_mul_f32_e32 v11, 0x3c800000, v79
	flat_store_dwordx4 v[8:9], v[4:7]
	v_mul_f32_e32 v10, 0xbfb8aa3b, v10
	v_mul_f32_e32 v11, 0xbfb8aa3b, v11
	v_mul_f32_e32 v6, 0x3c800000, v80
	v_mul_f32_e32 v7, 0x3c800000, v81
	v_mul_f32_e32 v6, 0xbfb8aa3b, v6
	v_mul_f32_e32 v7, 0xbfb8aa3b, v7
	v_exp_f32_e32 v10, v10
	v_exp_f32_e32 v11, v11
	v_exp_f32_e32 v6, v6
	v_exp_f32_e32 v7, v7
	v_add_f32_e32 v4, 1.0, v10
	v_add_f32_e32 v5, 1.0, v11
	v_add_f32_e32 v6, 1.0, v6
	v_add_f32_e32 v7, 1.0, v7
	v_rcp_f32_e32 v4, v4
	v_rcp_f32_e32 v5, v5
	v_rcp_f32_e32 v6, v6
	v_rcp_f32_e32 v7, v7
	v_fmamk_f32 v4, v4, 0x437f0000, v196
	v_fmamk_f32 v5, v5, 0x437f0000, v196
	v_fmamk_f32 v6, v6, 0x437f0000, v196
	v_fmamk_f32 v7, v7, 0x437f0000, v196
	v_perm_b32 v4, v5, v4, s67
	v_perm_b32 v5, v7, v6, s67
	v_mul_f32_e32 v6, 0x3c800000, v74
	v_mul_f32_e32 v7, 0x3c800000, v75
	v_mul_f32_e32 v6, 0xbfb8aa3b, v6
	v_mul_f32_e32 v7, 0xbfb8aa3b, v7
	v_exp_f32_e32 v6, v6
	v_exp_f32_e32 v7, v7
	v_perm_b32 v4, v5, v4, s68
	v_mul_f32_e32 v8, 0x3c800000, v77
	v_add_f32_e32 v5, 1.0, v6
	v_add_f32_e32 v6, 1.0, v7
	v_mul_f32_e32 v7, 0x3c800000, v76
	v_mul_f32_e32 v7, 0xbfb8aa3b, v7
	v_mul_f32_e32 v8, 0xbfb8aa3b, v8
	v_exp_f32_e32 v7, v7
	v_exp_f32_e32 v8, v8
	v_rcp_f32_e32 v5, v5
	v_rcp_f32_e32 v6, v6
	v_add_f32_e32 v7, 1.0, v7
	v_add_f32_e32 v8, 1.0, v8
	v_rcp_f32_e32 v7, v7
	v_rcp_f32_e32 v8, v8
	v_fmamk_f32 v5, v5, 0x437f0000, v196
	v_fmamk_f32 v6, v6, 0x437f0000, v196
	v_fmamk_f32 v7, v7, 0x437f0000, v196
	v_fmamk_f32 v8, v8, 0x437f0000, v196
	v_perm_b32 v5, v6, v5, s67
	v_perm_b32 v6, v8, v7, s67
	v_mul_f32_e32 v7, 0x3c800000, v70
	v_mul_f32_e32 v8, 0x3c800000, v71
	v_mul_f32_e32 v7, 0xbfb8aa3b, v7
	v_mul_f32_e32 v8, 0xbfb8aa3b, v8
	v_exp_f32_e32 v7, v7
	v_exp_f32_e32 v8, v8
	v_perm_b32 v5, v6, v5, s68
	v_mul_f32_e32 v9, 0x3c800000, v73
	v_add_f32_e32 v6, 1.0, v7
	v_add_f32_e32 v7, 1.0, v8
	v_mul_f32_e32 v8, 0x3c800000, v72
	v_mul_f32_e32 v8, 0xbfb8aa3b, v8
	v_mul_f32_e32 v9, 0xbfb8aa3b, v9
	v_exp_f32_e32 v8, v8
	v_exp_f32_e32 v9, v9
	v_rcp_f32_e32 v6, v6
	v_rcp_f32_e32 v7, v7
	v_add_f32_e32 v8, 1.0, v8
	v_add_f32_e32 v9, 1.0, v9
	v_rcp_f32_e32 v8, v8
	v_rcp_f32_e32 v9, v9
	v_fmamk_f32 v6, v6, 0x437f0000, v196
	v_fmamk_f32 v7, v7, 0x437f0000, v196
	v_fmamk_f32 v8, v8, 0x437f0000, v196
	v_fmamk_f32 v9, v9, 0x437f0000, v196
	v_perm_b32 v6, v7, v6, s67
	v_perm_b32 v7, v9, v8, s67
	v_mul_f32_e32 v8, 0x3c800000, v66
	v_mul_f32_e32 v9, 0x3c800000, v67
	v_mul_f32_e32 v8, 0xbfb8aa3b, v8
	v_mul_f32_e32 v9, 0xbfb8aa3b, v9
	v_exp_f32_e32 v8, v8
	v_exp_f32_e32 v9, v9
	v_perm_b32 v6, v7, v6, s68
	v_mul_f32_e32 v10, 0x3c800000, v69
	v_add_f32_e32 v7, 1.0, v8
	v_add_f32_e32 v8, 1.0, v9
	v_mul_f32_e32 v9, 0x3c800000, v68
	v_mul_f32_e32 v9, 0xbfb8aa3b, v9
	v_mul_f32_e32 v10, 0xbfb8aa3b, v10
	v_exp_f32_e32 v9, v9
	v_exp_f32_e32 v10, v10
	v_rcp_f32_e32 v7, v7
	v_rcp_f32_e32 v8, v8
	v_add_f32_e32 v9, 1.0, v9
	v_add_f32_e32 v10, 1.0, v10
	v_rcp_f32_e32 v9, v9
	v_rcp_f32_e32 v10, v10
	v_fmamk_f32 v7, v7, 0x437f0000, v196
	v_fmamk_f32 v8, v8, 0x437f0000, v196
	v_fmamk_f32 v9, v9, 0x437f0000, v196
	v_fmamk_f32 v10, v10, 0x437f0000, v196
	v_perm_b32 v7, v8, v7, s67
	v_perm_b32 v8, v10, v9, s67
	v_perm_b32 v7, v8, v7, s68
	v_add_co_u32_e32 v8, vcc, s70, v2
	v_mul_f32_e32 v10, 0x3c800000, v62
	s_nop 0
	v_addc_co_u32_e32 v9, vcc, 0, v3, vcc
	v_mul_f32_e32 v11, 0x3c800000, v63
	flat_store_dwordx4 v[8:9], v[4:7]
	v_mul_f32_e32 v10, 0xbfb8aa3b, v10
	v_mul_f32_e32 v11, 0xbfb8aa3b, v11
	v_mul_f32_e32 v6, 0x3c800000, v64
	v_mul_f32_e32 v7, 0x3c800000, v65
	v_mul_f32_e32 v6, 0xbfb8aa3b, v6
	v_mul_f32_e32 v7, 0xbfb8aa3b, v7
	v_exp_f32_e32 v10, v10
	v_exp_f32_e32 v11, v11
	v_exp_f32_e32 v6, v6
	v_exp_f32_e32 v7, v7
	v_add_f32_e32 v4, 1.0, v10
	v_add_f32_e32 v5, 1.0, v11
	v_add_f32_e32 v6, 1.0, v6
	v_add_f32_e32 v7, 1.0, v7
	v_rcp_f32_e32 v4, v4
	v_rcp_f32_e32 v5, v5
	v_rcp_f32_e32 v6, v6
	v_rcp_f32_e32 v7, v7
	v_fmamk_f32 v4, v4, 0x437f0000, v196
	v_fmamk_f32 v5, v5, 0x437f0000, v196
	v_fmamk_f32 v6, v6, 0x437f0000, v196
	v_fmamk_f32 v7, v7, 0x437f0000, v196
	v_perm_b32 v4, v5, v4, s67
	v_perm_b32 v5, v7, v6, s67
	v_mul_f32_e32 v6, 0x3c800000, v58
	v_mul_f32_e32 v7, 0x3c800000, v59
	v_mul_f32_e32 v6, 0xbfb8aa3b, v6
	v_mul_f32_e32 v7, 0xbfb8aa3b, v7
	v_exp_f32_e32 v6, v6
	v_exp_f32_e32 v7, v7
	v_perm_b32 v4, v5, v4, s68
	v_mul_f32_e32 v8, 0x3c800000, v61
	v_add_f32_e32 v5, 1.0, v6
	v_add_f32_e32 v6, 1.0, v7
	v_mul_f32_e32 v7, 0x3c800000, v60
	v_mul_f32_e32 v7, 0xbfb8aa3b, v7
	v_mul_f32_e32 v8, 0xbfb8aa3b, v8
	v_exp_f32_e32 v7, v7
	v_exp_f32_e32 v8, v8
	v_rcp_f32_e32 v5, v5
	v_rcp_f32_e32 v6, v6
	v_add_f32_e32 v7, 1.0, v7
	v_add_f32_e32 v8, 1.0, v8
	v_rcp_f32_e32 v7, v7
	v_rcp_f32_e32 v8, v8
	v_fmamk_f32 v5, v5, 0x437f0000, v196
	v_fmamk_f32 v6, v6, 0x437f0000, v196
	v_fmamk_f32 v7, v7, 0x437f0000, v196
	v_fmamk_f32 v8, v8, 0x437f0000, v196
	v_perm_b32 v5, v6, v5, s67
	v_perm_b32 v6, v8, v7, s67
	v_mul_f32_e32 v7, 0x3c800000, v54
	v_mul_f32_e32 v8, 0x3c800000, v55
	v_mul_f32_e32 v7, 0xbfb8aa3b, v7
; __device__ __forceinline__ float fsigmoid(float x) { return __builtin_amdgcn_rcpf(1.0f + __builtin_amdgcn_exp2f(-1.44269504f * x)); }
; #define PG8_BAR __builtin_amdgcn_s_barrier()
; template <class Epi, class Sched, bool ALIGN_EPI = true, bool F8 = false>
; __device__ __forceinline__ void gemm_phase(PG8_LAS unsigned char* lds, const Sched& S, const Epi& E) {
;     ...
;         cur = nxt; cA = nA; cB = nB; ++ui;
; #pragma unroll
;         for (int h = 0; h < 2; ++h)
; #pragma unroll
;             for (int i = 0; i < 2; ++i) voffA[h][i] = voffAn[h][i];
;         if constexpr (ALIGN_EPI) { if (wr == 1) PG8_BAR; }
;     __device__ __forceinline__ void operator()(AccRef acc, const GUnit& u, int wr, int wc, int fr, int fq) const {
;         const int pm = u.x0, pn = u.x1; unsigned char* base = (pn < 8 ? GZF : GZS) + (size_t)(pm * 256 + wr * 64 + fr) * D + (pn & 7) * 256 + wc * 64 + 16 * fq;
; #pragma unroll
;         for (int ai = 0; ai < 2; ++ai)
; #pragma unroll
;             for (int m = 0; m < 4; ++m) { u32x4 w;
; #pragma unroll
;                 for (int bj = 0; bj < 2; ++bj)
; #pragma unroll
;                     for (int n = 0; n < 2; ++n) { const f32x4 v = acc[ai][bj][m][n]; w[bj * 2 + n] = pk4_u8(fsigmoid(v[0] * W8_INV), fsigmoid(v[1] * W8_INV), fsigmoid(v[2] * W8_INV), fsigmoid(v[3] * W8_INV)); }
;                 *(u32x4*)(base + (size_t)(ai * 128 + m * 16) * D) = w; }
	v_mul_f32_e32 v8, 0xbfb8aa3b, v8
	v_exp_f32_e32 v7, v7
	v_exp_f32_e32 v8, v8
	v_perm_b32 v5, v6, v5, s68
	v_mul_f32_e32 v9, 0x3c800000, v57
	v_add_f32_e32 v6, 1.0, v7
	v_add_f32_e32 v7, 1.0, v8
	v_mul_f32_e32 v8, 0x3c800000, v56
	v_mul_f32_e32 v8, 0xbfb8aa3b, v8
	v_mul_f32_e32 v9, 0xbfb8aa3b, v9
	v_exp_f32_e32 v8, v8
	v_exp_f32_e32 v9, v9
	v_rcp_f32_e32 v6, v6
	v_rcp_f32_e32 v7, v7
	v_add_f32_e32 v8, 1.0, v8
	v_add_f32_e32 v9, 1.0, v9
	v_rcp_f32_e32 v8, v8
	v_rcp_f32_e32 v9, v9
	v_fmamk_f32 v6, v6, 0x437f0000, v196
	v_fmamk_f32 v7, v7, 0x437f0000, v196
	v_fmamk_f32 v8, v8, 0x437f0000, v196
	v_fmamk_f32 v9, v9, 0x437f0000, v196
	v_perm_b32 v6, v7, v6, s67
	v_perm_b32 v7, v9, v8, s67
	v_mul_f32_e32 v8, 0x3c800000, v50
	v_mul_f32_e32 v9, 0x3c800000, v51
	v_mul_f32_e32 v8, 0xbfb8aa3b, v8
	v_mul_f32_e32 v9, 0xbfb8aa3b, v9
	v_exp_f32_e32 v8, v8
	v_exp_f32_e32 v9, v9
	v_perm_b32 v6, v7, v6, s68
	v_mul_f32_e32 v10, 0x3c800000, v53
	v_add_f32_e32 v7, 1.0, v8
	v_add_f32_e32 v8, 1.0, v9
	v_mul_f32_e32 v9, 0x3c800000, v52
	v_mul_f32_e32 v9, 0xbfb8aa3b, v9
	v_mul_f32_e32 v10, 0xbfb8aa3b, v10
	v_exp_f32_e32 v9, v9
	v_exp_f32_e32 v10, v10
	v_rcp_f32_e32 v7, v7
	v_rcp_f32_e32 v8, v8
	v_add_f32_e32 v9, 1.0, v9
	v_add_f32_e32 v10, 1.0, v10
	v_rcp_f32_e32 v9, v9
	v_rcp_f32_e32 v10, v10
	v_fmamk_f32 v7, v7, 0x437f0000, v196
	v_fmamk_f32 v8, v8, 0x437f0000, v196
	v_fmamk_f32 v9, v9, 0x437f0000, v196
	v_fmamk_f32 v10, v10, 0x437f0000, v196
	v_perm_b32 v7, v8, v7, s67
	v_perm_b32 v8, v10, v9, s67
	v_perm_b32 v7, v8, v7, s68
	v_add_co_u32_e32 v8, vcc, s71, v2
	v_mul_f32_e32 v10, 0x3c800000, v46
	s_nop 0
	v_addc_co_u32_e32 v9, vcc, 0, v3, vcc
	v_mul_f32_e32 v11, 0x3c800000, v47
	flat_store_dwordx4 v[8:9], v[4:7]
	v_mul_f32_e32 v10, 0xbfb8aa3b, v10
	v_mul_f32_e32 v11, 0xbfb8aa3b, v11
	v_mul_f32_e32 v6, 0x3c800000, v48
	v_mul_f32_e32 v7, 0x3c800000, v49
	v_mul_f32_e32 v6, 0xbfb8aa3b, v6
	v_mul_f32_e32 v7, 0xbfb8aa3b, v7
	v_exp_f32_e32 v10, v10
	v_exp_f32_e32 v11, v11
	v_exp_f32_e32 v6, v6
	v_exp_f32_e32 v7, v7
	v_add_f32_e32 v4, 1.0, v10
	v_add_f32_e32 v5, 1.0, v11
	v_add_f32_e32 v6, 1.0, v6
	v_add_f32_e32 v7, 1.0, v7
	v_rcp_f32_e32 v4, v4
	v_rcp_f32_e32 v5, v5
	v_rcp_f32_e32 v6, v6
	v_rcp_f32_e32 v7, v7
	v_fmamk_f32 v4, v4, 0x437f0000, v196
	v_fmamk_f32 v5, v5, 0x437f0000, v196
	v_fmamk_f32 v6, v6, 0x437f0000, v196
	v_fmamk_f32 v7, v7, 0x437f0000, v196
	v_perm_b32 v4, v5, v4, s67
	v_perm_b32 v5, v7, v6, s67
	v_mul_f32_e32 v6, 0x3c800000, v42
	v_mul_f32_e32 v7, 0x3c800000, v43
	v_mul_f32_e32 v6, 0xbfb8aa3b, v6
	v_mul_f32_e32 v7, 0xbfb8aa3b, v7
	v_exp_f32_e32 v6, v6
	v_exp_f32_e32 v7, v7
	v_perm_b32 v4, v5, v4, s68
	v_mul_f32_e32 v8, 0x3c800000, v45
	v_add_f32_e32 v5, 1.0, v6
	v_add_f32_e32 v6, 1.0, v7
	v_mul_f32_e32 v7, 0x3c800000, v44
	v_mul_f32_e32 v7, 0xbfb8aa3b, v7
	v_mul_f32_e32 v8, 0xbfb8aa3b, v8
	v_exp_f32_e32 v7, v7
	v_exp_f32_e32 v8, v8
	v_rcp_f32_e32 v5, v5
	v_rcp_f32_e32 v6, v6
	v_add_f32_e32 v7, 1.0, v7
	v_add_f32_e32 v8, 1.0, v8
	v_rcp_f32_e32 v7, v7
	v_rcp_f32_e32 v8, v8
	v_fmamk_f32 v5, v5, 0x437f0000, v196
	v_fmamk_f32 v6, v6, 0x437f0000, v196
	v_fmamk_f32 v7, v7, 0x437f0000, v196
	v_fmamk_f32 v8, v8, 0x437f0000, v196
	v_perm_b32 v5, v6, v5, s67
	v_perm_b32 v6, v8, v7, s67
	v_mul_f32_e32 v7, 0x3c800000, v38
	v_mul_f32_e32 v8, 0x3c800000, v39
	v_mul_f32_e32 v7, 0xbfb8aa3b, v7
	v_mul_f32_e32 v8, 0xbfb8aa3b, v8
	v_exp_f32_e32 v7, v7
	v_exp_f32_e32 v8, v8
	v_perm_b32 v5, v6, v5, s68
	v_mul_f32_e32 v9, 0x3c800000, v41
	v_add_f32_e32 v6, 1.0, v7
	v_add_f32_e32 v7, 1.0, v8
	v_mul_f32_e32 v8, 0x3c800000, v40
	v_mul_f32_e32 v8, 0xbfb8aa3b, v8
	v_mul_f32_e32 v9, 0xbfb8aa3b, v9
	v_exp_f32_e32 v8, v8
	v_exp_f32_e32 v9, v9
	v_rcp_f32_e32 v6, v6
	v_rcp_f32_e32 v7, v7
	v_add_f32_e32 v8, 1.0, v8
	v_add_f32_e32 v9, 1.0, v9
	v_rcp_f32_e32 v8, v8
	v_rcp_f32_e32 v9, v9
	v_fmamk_f32 v6, v6, 0x437f0000, v196
	v_fmamk_f32 v7, v7, 0x437f0000, v196
	v_fmamk_f32 v8, v8, 0x437f0000, v196
	v_fmamk_f32 v9, v9, 0x437f0000, v196
	v_perm_b32 v6, v7, v6, s67
	v_perm_b32 v7, v9, v8, s67
	v_mul_f32_e32 v8, 0x3c800000, v34
	v_mul_f32_e32 v9, 0x3c800000, v35
	v_mul_f32_e32 v8, 0xbfb8aa3b, v8
	v_mul_f32_e32 v9, 0xbfb8aa3b, v9
	v_exp_f32_e32 v8, v8
	v_exp_f32_e32 v9, v9
	v_perm_b32 v6, v7, v6, s68
	v_mul_f32_e32 v10, 0x3c800000, v37
	v_add_f32_e32 v7, 1.0, v8
	v_add_f32_e32 v8, 1.0, v9
	v_mul_f32_e32 v9, 0x3c800000, v36
	v_mul_f32_e32 v9, 0xbfb8aa3b, v9
	v_mul_f32_e32 v10, 0xbfb8aa3b, v10
	v_exp_f32_e32 v9, v9
	v_exp_f32_e32 v10, v10
	v_rcp_f32_e32 v7, v7
	v_rcp_f32_e32 v8, v8
	v_add_f32_e32 v9, 1.0, v9
	v_add_f32_e32 v10, 1.0, v10
	v_rcp_f32_e32 v9, v9
	v_rcp_f32_e32 v10, v10
	v_fmamk_f32 v7, v7, 0x437f0000, v196
	v_fmamk_f32 v8, v8, 0x437f0000, v196
	v_fmamk_f32 v9, v9, 0x437f0000, v196
	v_fmamk_f32 v10, v10, 0x437f0000, v196
	v_add_co_u32_e32 v2, vcc, 0x58000, v2
	v_perm_b32 v7, v8, v7, s67
	v_perm_b32 v8, v10, v9, s67
	v_addc_co_u32_e32 v3, vcc, 0, v3, vcc
	v_perm_b32 v7, v8, v7, s68
	s_andn2_b64 vcc, exec, s[0:1]
	s_mov_b64 s[0:1], -1
	flat_store_dwordx4 v[2:3], v[4:7]
	s_cbranch_vccnz .LBB0_420
	s_andn2_b64 vcc, exec, s[10:11]
	s_cbranch_vccnz .LBB0_419
	s_branch .LBB0_419

; #define PG8_STAGE(bufoff, gbase, voff) do { _Pragma("unroll") for (int _i = 0; _i < 2; ++_i) \
;         __builtin_amdgcn_global_load_lds((const unsigned*)((const char*)(gbase) + (voff)[_i]), (PG8_LAS unsigned*)(lds + (bufoff) + ldsw + _i * 8192), 16, 0, 0); } while (0)
; #define PG8_BAR __builtin_amdgcn_s_barrier()
; template <class Epi, class Sched, bool ALIGN_EPI = true, bool F8 = false>
; __device__ __forceinline__ void gemm_phase(PG8_LAS unsigned char* lds, const Sched& S, const Epi& E) {
;     ...
;     PG8_STAGE(PG8_SB(0, 0), cB, voffB[0]); PG8_STAGE(PG8_SB(0, 1), cB, voffB[1]); PG8_STAGE(PG8_SA(0, 0), cA, voffA[0]); PG8_STAGE(PG8_SA(0, 1), cA, voffA[1]);
;     if (wr == 1) PG8_BAR;
;     __device__ __forceinline__ bool next(int i, GUnit& u) const { int pm, pn; if (!o.get(i >> 1, pm, pn)) return false; const int seg = i & 1;
;         u.A = A + ((size_t)(pm * KT + seg * (SW / 128)) << 15); u.B = B + ((size_t)(pn * KT + seg * (SW / 128)) << 15); u.nt = seg ? FW / 128 : SW / 128; u.x0 = pm; u.x1 = pn; u.x2 = seg; u.x3 = 0; return true; }
.LBB0_822:
	s_ashr_i32 s9, s9, 3
	s_add_u32 s40, s36, 0x1e000000
	s_addc_u32 s41, s37, 0
	s_add_u32 s42, s36, 0x2e00000
	s_addc_u32 s43, s37, 0
	s_add_i32 s8, s8, s9
	s_ashr_i32 s9, s8, 31
	s_lshr_b32 s9, s9, 26
	s_add_i32 s9, s8, s9
	s_ashr_i32 s10, s9, 6
	s_andn2_b32 s9, s9, 63
	s_sub_i32 s8, s8, s9
	s_lshl_b32 s9, s10, 3
	s_bfe_i32 s10, s8, 0x80000
	s_bfe_u32 s10, s10, 0x3000c
	v_lshlrev_b32_e32 v2, 4, v0
	v_bfe_u32 v5, v0, 2, 4
	v_lshrrev_b32_e32 v6, 3, v0
	s_add_i32 s10, s8, s10
	v_and_or_b32 v10, v6, 48, v5
	v_or_b32_e32 v6, 0x2000, v2
	s_bfe_i32 s11, s10, 0x80000
	s_and_b32 s10, s10, 0xf8
	v_lshrrev_b32_e32 v7, 7, v6
	s_movk_i32 s1, 0x70
	s_sub_i32 s8, s8, s10
	v_and_b32_e32 v3, 32, v0
	v_lshrrev_b32_e32 v8, 2, v0
	v_and_or_b32 v11, v7, s1, v5
	v_and_b32_e32 v7, 48, v0
	v_lshrrev_b32_e32 v12, 5, v0
	s_sext_i32_i8 s8, s8
	v_bitop3_b32 v3, v2, v3, 48 bitop3:0x6c
	v_and_b32_e32 v4, 64, v0
	v_and_b32_e32 v12, 4, v12
	v_bfe_u32 v13, v0, 2, 2
	v_and_or_b32 v8, v8, 64, v7
	s_add_i32 s71, s9, s8
	v_or_b32_e32 v9, v3, v4
	v_or3_b32 v8, v8, v12, v13
	s_mul_i32 s8, s71, 12
	s_lshr_b32 s0, s16, 6
	v_lshl_or_b32 v158, v8, 7, v9
	v_lshrrev_b32_e32 v8, 6, v6
	s_movk_i32 s1, 0xc0
	s_sext_i32_i16 s11, s11
	s_ashr_i32 s9, s8, 31
	v_and_or_b32 v8, v8, s1, v7
	s_lshr_b32 s1, s16, 8
	s_lshl_b32 s44, s0, 10
	s_ashr_i32 s70, s11, 3
	s_lshl_b64 s[8:9], s[8:9], 15
	s_add_u32 s24, s40, s8
	s_mul_i32 s8, s70, 12
	s_addc_u32 s25, s41, s9
	s_ashr_i32 s9, s8, 31
	s_lshl_b64 s[8:9], s[8:9], 15
	s_add_u32 s26, s42, s8
	s_addc_u32 s27, s43, s9
	v_lshl_or_b32 v164, v11, 7, v9
	s_add_i32 s45, s44, 0
	v_mov_b32_e32 v11, 0
	v_or3_b32 v8, v8, v12, v13
	s_add_i32 m0, s45, 0x10000
	v_mov_b32_e32 v159, v11
	v_lshl_or_b32 v160, v8, 7, v9
	v_lshl_or_b32 v162, v10, 7, v9
	v_lshl_add_u64 v[8:9], s[26:27], 0, v[158:159]
	global_load_lds_dwordx4 v158, s[26:27]
	v_mov_b32_e32 v161, v11
	s_add_i32 m0, s45, 0x12000
	s_mov_b64 s[8:9], 0x400
	v_lshl_add_u64 v[12:13], s[26:27], 0, v[160:161]
	global_load_lds_dwordx4 v160, s[26:27]
	s_add_i32 m0, s45, 0x14000
	v_lshl_add_u64 v[8:9], v[8:9], 0, s[8:9]
	global_load_lds_dwordx4 v[8:9], off
	v_lshl_add_u64 v[8:9], v[12:13], 0, s[8:9]
	s_add_i32 m0, s45, 0x16000
	s_add_i32 s46, s45, 0x2000
	global_load_lds_dwordx4 v[8:9], off
	s_mov_b32 m0, s45
	s_add_i32 s47, s45, 0x4000
	global_load_lds_dwordx4 v162, s[24:25]
	s_mov_b32 m0, s46
	v_or_b32_e32 v166, 0x4000, v162
	global_load_lds_dwordx4 v164, s[24:25]
	s_mov_b32 m0, s47
	s_add_i32 s48, s45, 0x6000
	v_or_b32_e32 v168, 0x4000, v164
	global_load_lds_dwordx4 v166, s[24:25]
	s_mov_b32 m0, s48
	s_cmp_eq_u32 s1, 1
	global_load_lds_dwordx4 v168, s[24:25]
	s_mov_b32 s72, 4
	s_movk_i32 s18, 0x4000
	s_mov_b32 s49, 0x10000
	v_mov_b32_e32 v163, v11
	s_cselect_b64 s[10:11], -1, 0
	s_cmp_lg_u32 s1, 1
	v_mov_b32_e32 v165, v11
	s_cbranch_scc1 .LBB0_824
; #define PG8_STAGE(bufoff, gbase, voff) do { _Pragma("unroll") for (int _i = 0; _i < 2; ++_i) \
;         __builtin_amdgcn_global_load_lds((const unsigned*)((const char*)(gbase) + (voff)[_i]), (PG8_LAS unsigned*)(lds + (bufoff) + ldsw + _i * 8192), 16, 0, 0); } while (0)
; #define PG8_WAIT_V(n) asm volatile("s_waitcnt vmcnt(" #n ")" ::: "memory")
; #define PG8_BAR __builtin_amdgcn_s_barrier()
; template <class Epi, class Sched, bool ALIGN_EPI = true, bool F8 = false>
; __device__ __forceinline__ void gemm_phase(PG8_LAS unsigned char* lds, const Sched& S, const Epi& E) {
;     ...
;     f32x4 acc[2][2][4][2];
; #pragma unroll
;     for (int a = 0; a < 2; ++a)
; #pragma unroll
;         for (int b = 0; b < 2; ++b)
; #pragma unroll
;             for (int m = 0; m < 4; ++m)
; #pragma unroll
;                 for (int n = 0; n < 2; ++n) acc[a][b][m][n] = (f32x4){0.f, 0.f, 0.f, 0.f};
;     ...
;     if (wr == 1) PG8_BAR;
;     PG8_WAIT_V(2); PG8_BAR;
;     PG8_STAGE(PG8_SB(1, 0), cB + kstepB, voffB[0]); PG8_STAGE(PG8_SA(1, 0), cA + kstep, voffA[0]); PG8_STAGE(PG8_SB(1, 1), cB + kstepB, voffB[1]);
;     PG8_WAIT_V(6); PG8_BAR;
.LBB0_824:
	s_add_u32 s12, s36, 0x26000000
	s_addc_u32 s13, s37, 0
	s_add_u32 s14, s14, 0x4000000
	v_and_b32_e32 v8, 15, v0
	v_lshlrev_b32_e32 v9, 2, v0
	s_addc_u32 s15, s15, 0
	s_and_b32 s22, s0, 3
	v_lshl_or_b32 v177, s1, 6, v8
	v_lshl_or_b32 v8, v8, 6, v7
	s_lshl_b32 s0, s1, 13
	v_and_b32_e32 v10, 32, v9
	v_bitop3_b32 v14, v8, s0, v10 bitop3:0xde
	v_lshlrev_b32_e32 v8, 6, v0
	s_movk_i32 s0, 0x3c0
	s_lshl_b32 s17, s22, 12
	v_and_or_b32 v12, v8, s0, v7
	s_add_u32 s0, s26, 0x8000
	s_addc_u32 s1, s27, 0
	s_add_i32 m0, s45, 0x18000
	v_lshl_add_u64 v[8:9], s[0:1], 0, v[158:159]
	s_waitcnt vmcnt(2)
	s_barrier
	global_load_lds_dwordx4 v[8:9], off
	s_add_i32 m0, s45, 0x1a000
	s_add_u32 s20, s24, 0x8000
	v_lshl_add_u64 v[8:9], s[0:1], 0, v[160:161]
	s_addc_u32 s21, s25, 0
	s_add_i32 s50, s45, 0x8000
	global_load_lds_dwordx4 v[8:9], off
	v_lshl_add_u64 v[8:9], s[20:21], 0, v[162:163]
	s_mov_b32 m0, s50
	s_add_i32 s51, s45, 0xa000
	global_load_lds_dwordx4 v[8:9], off
	v_lshl_add_u64 v[8:9], s[20:21], 0, v[164:165]
	s_mov_b32 m0, s51
	v_or_b32_e32 v172, 0x400, v158
	global_load_lds_dwordx4 v[8:9], off
	s_add_i32 m0, s45, 0x1c000
	v_or_b32_e32 v174, 0x400, v160
	global_load_lds_dwordx4 v172, s[0:1]
	s_add_i32 m0, s45, 0x1e000
	v_lshlrev_b32_e32 v5, 7, v5
	global_load_lds_dwordx4 v174, s[0:1]
	v_and_b32_e32 v2, 0x1800, v2
	v_bitop3_b32 v190, s17, v12, v10 bitop3:0xf6
	s_waitcnt vmcnt(6)
	s_cmpk_lt_u32 s16, 0x100
	v_and_b32_e32 v6, 0x3800, v6
	v_or3_b32 v2, v3, v2, v5
	v_mov_b32_e32 v12, v11
	v_mov_b32_e32 v13, v11
	s_cselect_b64 s[16:17], -1, 0
	s_lshl_b32 s53, s22, 6
	v_or3_b32 v6, v3, v6, v5
	v_add_u32_e32 v2, v2, v4
	v_mov_b32_e32 v10, v11
	v_add_u32_e32 v198, 0, v14
	v_mov_b64_e32 v[16:17], v[12:13]
	v_mov_b64_e32 v[20:21], v[12:13]
	v_mov_b64_e32 v[24:25], v[12:13]
	v_mov_b64_e32 v[28:29], v[12:13]
	v_mov_b64_e32 v[32:33], v[12:13]
	v_mov_b64_e32 v[36:37], v[12:13]
	v_mov_b64_e32 v[40:41], v[12:13]
	v_mov_b64_e32 v[44:45], v[12:13]
	v_mov_b64_e32 v[48:49], v[12:13]
	v_mov_b64_e32 v[52:53], v[12:13]
	v_mov_b64_e32 v[56:57], v[12:13]
	v_mov_b64_e32 v[60:61], v[12:13]
	v_mov_b64_e32 v[64:65], v[12:13]
	v_mov_b64_e32 v[68:69], v[12:13]
	v_mov_b64_e32 v[72:73], v[12:13]
	v_mov_b64_e32 v[76:77], v[12:13]
	v_mov_b64_e32 v[80:81], v[12:13]
	v_mov_b64_e32 v[84:85], v[12:13]
	v_mov_b64_e32 v[88:89], v[12:13]
	v_mov_b64_e32 v[92:93], v[12:13]
	v_mov_b64_e32 v[96:97], v[12:13]
	v_mov_b64_e32 v[100:101], v[12:13]
	v_mov_b64_e32 v[104:105], v[12:13]
	v_mov_b64_e32 v[108:109], v[12:13]
	v_mov_b64_e32 v[112:113], v[12:13]
	v_mov_b64_e32 v[116:117], v[12:13]
	v_mov_b64_e32 v[120:121], v[12:13]
	v_mov_b64_e32 v[124:125], v[12:13]
	v_mov_b64_e32 v[128:129], v[12:13]
	v_mov_b64_e32 v[132:133], v[12:13]
	v_mov_b64_e32 v[136:137], v[12:13]
	v_mov_b64_e32 v[140:141], v[12:13]
	v_mov_b32_e32 v167, v11
	v_mov_b32_e32 v169, v11
	v_mov_b32_e32 v173, v11
	v_mov_b32_e32 v175, v11
	s_mov_b32 s52, 0x18000
	v_or_b32_e32 v176, s53, v7
	v_and_or_b32 v178, s53, 64, v7
	v_mov_b32_e32 v179, v11
	v_or_b32_e32 v191, 16, v177
	v_or_b32_e32 v192, 32, v177
	v_or_b32_e32 v193, 48, v177
	v_add_u32_e32 v194, 0x80, v177
	v_add_u32_e32 v195, 0x90, v177
	v_add_u32_e32 v196, 0xa0, v177
	v_add_u32_e32 v197, 0xb0, v177
	v_add3_u32 v180, v6, v4, s18
	v_mov_b32_e32 v181, v11
	v_or_b32_e32 v182, 0x4000, v2
	v_mov_b32_e32 v183, v11
	s_mov_b32 s73, 0
	v_mov_b64_e32 v[184:185], 0x400
	v_mov_b64_e32 v[186:187], 0x3ff
	s_add_i32 s58, 0, 0x10000
	s_add_i32 s59, 0, 0x14000
	v_mov_b32_e32 v199, 0x7f7f7f7f
	s_mov_b32 s60, 0xc3e00000
	s_mov_b32 s61, 0x40000
	s_mov_b32 s62, 0x48000
	s_mov_b32 s63, 0x50000
	s_mov_b32 s64, 0x58000
	s_mov_b32 s18, 0x3d800000
	v_mov_b32_e32 v200, 0x43e00000
	v_mov_b64_e32 v[14:15], v[10:11]
	v_mov_b64_e32 v[18:19], v[10:11]
	v_mov_b64_e32 v[22:23], v[10:11]
	v_mov_b64_e32 v[26:27], v[10:11]
	v_mov_b64_e32 v[30:31], v[10:11]
	v_mov_b64_e32 v[34:35], v[10:11]
	v_mov_b64_e32 v[38:39], v[10:11]
	v_mov_b64_e32 v[42:43], v[10:11]
	v_mov_b64_e32 v[46:47], v[10:11]
	v_mov_b64_e32 v[50:51], v[10:11]
	v_mov_b64_e32 v[54:55], v[10:11]
	v_mov_b64_e32 v[58:59], v[10:11]
	v_mov_b64_e32 v[62:63], v[10:11]
	v_mov_b64_e32 v[66:67], v[10:11]
	v_mov_b64_e32 v[70:71], v[10:11]
	v_mov_b64_e32 v[74:75], v[10:11]
	v_mov_b64_e32 v[78:79], v[10:11]
	v_mov_b64_e32 v[82:83], v[10:11]
	v_mov_b64_e32 v[86:87], v[10:11]
	v_mov_b64_e32 v[90:91], v[10:11]
	v_mov_b64_e32 v[94:95], v[10:11]
	v_mov_b64_e32 v[98:99], v[10:11]
	v_mov_b64_e32 v[102:103], v[10:11]
	v_mov_b64_e32 v[106:107], v[10:11]
	v_mov_b64_e32 v[110:111], v[10:11]
	v_mov_b64_e32 v[114:115], v[10:11]
	v_mov_b64_e32 v[118:119], v[10:11]
	v_mov_b64_e32 v[122:123], v[10:11]
	v_mov_b64_e32 v[126:127], v[10:11]
	v_mov_b64_e32 v[130:131], v[10:11]
	v_mov_b64_e32 v[134:135], v[10:11]
	v_mov_b64_e32 v[138:139], v[10:11]
	s_mov_b32 s65, 0
	s_mov_b64 s[20:21], s[24:25]
	s_mov_b64 s[22:23], s[26:27]
	s_barrier
	s_branch .LBB0_827

; #define PG8_STAGE(bufoff, gbase, voff) do { _Pragma("unroll") for (int _i = 0; _i < 2; ++_i) \
;         __builtin_amdgcn_global_load_lds((const unsigned*)((const char*)(gbase) + (voff)[_i]), (PG8_LAS unsigned*)(lds + (bufoff) + ldsw + _i * 8192), 16, 0, 0); } while (0)
; #define PG8_WAIT_V(n) asm volatile("s_waitcnt vmcnt(" #n ")" ::: "memory")
; #define PG8_WAIT_L(n) asm volatile("s_waitcnt lgkmcnt(" #n ")" ::: "memory")
; #define PG8_BAR __builtin_amdgcn_s_barrier()
; #define PG8_SCHED __builtin_amdgcn_sched_barrier(0)
; template <class Epi, class Sched, bool ALIGN_EPI = true, bool F8 = false>
; __device__ __forceinline__ void gemm_phase(PG8_LAS unsigned char* lds, const Sched& S, const Epi& E) {
;     ...
;         for (int t = 0; t < nt; t += 2) {
;             const bool last = (t == nt - 2);
;             if constexpr (Sched::GATHER) { if (last && has_next) S.a_off(nxt, Rs, Cs, voffAn); }
;             const char* a1 = cA + (size_t)(t + 1) * kstep;
;             const char* a2 = last ? nA : cA + (size_t)(t + 2) * kstep; const char* b2 = last ? nB : cB + (size_t)(t + 2) * kstepB;
;             const char* a3 = a2 + kstep; const char* b3 = b2 + kstepB;
;             unsigned vA2[2][2];
; #pragma unroll
;             for (int h = 0; h < 2; ++h)
; #pragma unroll
;                 for (int i = 0; i < 2; ++i) { if constexpr (Sched::GATHER) vA2[h][i] = (last && has_next) ? voffAn[h][i] : voffA[h][i]; else vA2[h][i] = voffA[h][i]; }
;             PG8_LDB(B0, 0, 0); PG8_LDB(B1, 0, 1); PG8_SCHED; PG8_LDA(At, 0, 0); PG8_STAGE(PG8_SA(1, 1), a1, voffA[1]);
;             PG8_WAIT_V(8); PG8_WAIT_L(0); PG8_BAR; PG8_MMA(0, 0, At, B0); PG8_MMA(0, 1, At, B1); PG8_BAR; PG8_SCHED;
;             PG8_LDA(At, 0, 1); PG8_STAGE(PG8_SB(0, 0), b2, voffB[0]); PG8_STAGE(PG8_SB(0, 1), b2, voffB[1]); PG8_STAGE(PG8_SA(0, 0), a2, vA2[0]);
;             PG8_WAIT_V(8); PG8_WAIT_L(0); PG8_BAR; PG8_MMA(1, 0, At, B0); PG8_MMA(1, 1, At, B1); PG8_BAR; PG8_SCHED;
.LBB0_833:
	s_add_i32 s74, s72, -2
	s_add_u32 s75, s26, 0x10000
	s_addc_u32 s76, s27, 0
	s_add_u32 s24, s24, 0x8000
	s_addc_u32 s25, s25, 0
	s_mov_b32 s26, 0
	s_bitcmp1_b32 s3, 2
	s_cbranch_scc1 .Lh1_834
.LBB0_834:
	v_add_u32_e32 v10, s58, v190
	ds_read_b128 v[2:5], v10
	ds_read_b128 v[6:9], v10 offset:1024
	ds_read_b128 v[142:145], v10 offset:2048
	ds_read_b128 v[146:149], v10 offset:3072
	v_add_u32_e32 v10, s59, v190
	ds_read_b128 v[150:153], v10
	ds_read_b128 v[154:157], v10 offset:1024
	ds_read_b128 v[202:205], v10 offset:2048
	ds_read_b128 v[206:209], v10 offset:3072
	s_add_i32 s77, s26, 2
	s_add_u32 s27, s24, 0x8000
	s_addc_u32 s28, s25, 0
	s_cmp_eq_u32 s74, s26
	s_cselect_b32 s30, s20, s27
	s_cselect_b32 s31, s21, s28
	s_cselect_b32 s28, s22, s75
	s_cselect_b32 s29, s23, s76
	s_add_u32 s26, s30, 0x8000
	s_addc_u32 s27, s31, 0
	v_lshl_add_u64 v[12:13], s[24:25], 0, v[182:183]
	s_add_i32 m0, s45, 0xc000
	ds_read_b128 v[210:213], v198
	ds_read_b128 v[214:217], v198 offset:1024
	ds_read_b128 v[218:221], v198 offset:2048
	ds_read_b128 v[222:225], v198 offset:3072
	ds_read_b128 v[226:229], v198 offset:4096
	ds_read_b128 v[230:233], v198 offset:5120
	ds_read_b128 v[234:237], v198 offset:6144
	ds_read_b128 v[238:241], v198 offset:7168
	global_load_lds_dwordx4 v[12:13], off
	v_lshl_add_u64 v[12:13], s[24:25], 0, v[180:181]
	s_add_i32 m0, s45, 0xe000
	s_nop 0
	global_load_lds_dwordx4 v[12:13], off
	s_waitcnt vmcnt(8)
	s_waitcnt lgkmcnt(0)
	s_setprio 1
	s_waitcnt lgkmcnt(0)
	v_mfma_scale_f32_16x16x128_f8f6f4 v[138:141], v[2:9], v[210:217], v[138:141], v199, v199 op_sel_hi:[0,0,0]
	v_mfma_scale_f32_16x16x128_f8f6f4 v[134:137], v[142:149], v[210:217], v[134:137], v199, v199 op_sel_hi:[0,0,0]
	v_mfma_scale_f32_16x16x128_f8f6f4 v[130:133], v[2:9], v[218:225], v[130:133], v199, v199 op_sel_hi:[0,0,0]
	v_mfma_scale_f32_16x16x128_f8f6f4 v[126:129], v[142:149], v[218:225], v[126:129], v199, v199 op_sel_hi:[0,0,0]
	v_mfma_scale_f32_16x16x128_f8f6f4 v[122:125], v[2:9], v[226:233], v[122:125], v199, v199 op_sel_hi:[0,0,0]
	v_mfma_scale_f32_16x16x128_f8f6f4 v[118:121], v[142:149], v[226:233], v[118:121], v199, v199 op_sel_hi:[0,0,0]
	v_mfma_scale_f32_16x16x128_f8f6f4 v[114:117], v[2:9], v[234:241], v[114:117], v199, v199 op_sel_hi:[0,0,0]
	v_mfma_scale_f32_16x16x128_f8f6f4 v[110:113], v[142:149], v[234:241], v[110:113], v199, v199 op_sel_hi:[0,0,0]
	s_nop 3
	s_setprio 0
	s_setprio 1
	v_mfma_scale_f32_16x16x128_f8f6f4 v[106:109], v[150:157], v[210:217], v[106:109], v199, v199 op_sel_hi:[0,0,0]
	v_mfma_scale_f32_16x16x128_f8f6f4 v[102:105], v[202:209], v[210:217], v[102:105], v199, v199 op_sel_hi:[0,0,0]
	v_mfma_scale_f32_16x16x128_f8f6f4 v[98:101], v[150:157], v[218:225], v[98:101], v199, v199 op_sel_hi:[0,0,0]
	v_mfma_scale_f32_16x16x128_f8f6f4 v[94:97], v[202:209], v[218:225], v[94:97], v199, v199 op_sel_hi:[0,0,0]
	v_mfma_scale_f32_16x16x128_f8f6f4 v[90:93], v[150:157], v[226:233], v[90:93], v199, v199 op_sel_hi:[0,0,0]
	v_mfma_scale_f32_16x16x128_f8f6f4 v[86:89], v[202:209], v[226:233], v[86:89], v199, v199 op_sel_hi:[0,0,0]
	v_mfma_scale_f32_16x16x128_f8f6f4 v[82:85], v[150:157], v[234:241], v[82:85], v199, v199 op_sel_hi:[0,0,0]
	v_mfma_scale_f32_16x16x128_f8f6f4 v[78:81], v[202:209], v[234:241], v[78:81], v199, v199 op_sel_hi:[0,0,0]
	s_nop 3
	s_setprio 0
	s_barrier
	s_add_i32 s78, s58, s44
	v_lshl_add_u64 v[12:13], s[28:29], 0, v[158:159]
	s_mov_b32 m0, s78
	ds_read_b128 v[210:213], v198 offset:16384
	ds_read_b128 v[214:217], v198 offset:17408
	ds_read_b128 v[218:221], v198 offset:18432
	ds_read_b128 v[222:225], v198 offset:19456
	ds_read_b128 v[226:229], v198 offset:20480
	ds_read_b128 v[230:233], v198 offset:21504
	ds_read_b128 v[234:237], v198 offset:22528
	ds_read_b128 v[238:241], v198 offset:23552
	global_load_lds_dwordx4 v[12:13], off
	v_lshl_add_u64 v[188:189], s[28:29], 0, v[160:161]
	s_add_i32 m0, s78, 0x2000
	s_add_i32 s78, s59, s44
	global_load_lds_dwordx4 v[188:189], off
	v_lshl_add_u64 v[12:13], v[12:13], 0, s[8:9]
	s_mov_b32 m0, s78
	s_nop 0
	global_load_lds_dwordx4 v[12:13], off
	v_lshl_add_u64 v[12:13], v[188:189], 0, s[8:9]
	s_add_i32 m0, s78, 0x2000
	s_nop 0
	global_load_lds_dwordx4 v[12:13], off
	v_lshl_add_u64 v[12:13], s[30:31], 0, v[162:163]
	s_mov_b32 m0, s45
	s_nop 0
	global_load_lds_dwordx4 v[12:13], off
	v_lshl_add_u64 v[12:13], s[30:31], 0, v[164:165]
	s_mov_b32 m0, s46
	s_nop 0
	global_load_lds_dwordx4 v[12:13], off
	s_waitcnt vmcnt(8)
	s_waitcnt lgkmcnt(0)
	s_setprio 1
	s_waitcnt lgkmcnt(0)
	v_mfma_scale_f32_16x16x128_f8f6f4 v[74:77], v[2:9], v[210:217], v[74:77], v199, v199 op_sel_hi:[0,0,0]
	v_mfma_scale_f32_16x16x128_f8f6f4 v[70:73], v[142:149], v[210:217], v[70:73], v199, v199 op_sel_hi:[0,0,0]
	v_mfma_scale_f32_16x16x128_f8f6f4 v[66:69], v[2:9], v[218:225], v[66:69], v199, v199 op_sel_hi:[0,0,0]
	v_mfma_scale_f32_16x16x128_f8f6f4 v[62:65], v[142:149], v[218:225], v[62:65], v199, v199 op_sel_hi:[0,0,0]
	v_mfma_scale_f32_16x16x128_f8f6f4 v[58:61], v[2:9], v[226:233], v[58:61], v199, v199 op_sel_hi:[0,0,0]
	v_mfma_scale_f32_16x16x128_f8f6f4 v[54:57], v[142:149], v[226:233], v[54:57], v199, v199 op_sel_hi:[0,0,0]
	v_mfma_scale_f32_16x16x128_f8f6f4 v[50:53], v[2:9], v[234:241], v[50:53], v199, v199 op_sel_hi:[0,0,0]
	v_mfma_scale_f32_16x16x128_f8f6f4 v[46:49], v[142:149], v[234:241], v[46:49], v199, v199 op_sel_hi:[0,0,0]
	s_nop 3
	s_setprio 0
	s_setprio 1
	v_mfma_scale_f32_16x16x128_f8f6f4 v[42:45], v[150:157], v[210:217], v[42:45], v199, v199 op_sel_hi:[0,0,0]
	v_mfma_scale_f32_16x16x128_f8f6f4 v[38:41], v[202:209], v[210:217], v[38:41], v199, v199 op_sel_hi:[0,0,0]
	v_mfma_scale_f32_16x16x128_f8f6f4 v[34:37], v[150:157], v[218:225], v[34:37], v199, v199 op_sel_hi:[0,0,0]
	v_mfma_scale_f32_16x16x128_f8f6f4 v[30:33], v[202:209], v[218:225], v[30:33], v199, v199 op_sel_hi:[0,0,0]
	v_mfma_scale_f32_16x16x128_f8f6f4 v[26:29], v[150:157], v[226:233], v[26:29], v199, v199 op_sel_hi:[0,0,0]
	v_mfma_scale_f32_16x16x128_f8f6f4 v[22:25], v[202:209], v[226:233], v[22:25], v199, v199 op_sel_hi:[0,0,0]
	v_mfma_scale_f32_16x16x128_f8f6f4 v[18:21], v[150:157], v[234:241], v[18:21], v199, v199 op_sel_hi:[0,0,0]
	v_mfma_scale_f32_16x16x128_f8f6f4 v[14:17], v[202:209], v[234:241], v[14:17], v199, v199 op_sel_hi:[0,0,0]
	s_nop 3
	s_setprio 0
	s_barrier
; #define PG8_STAGE(bufoff, gbase, voff) do { _Pragma("unroll") for (int _i = 0; _i < 2; ++_i) \
;         __builtin_amdgcn_global_load_lds((const unsigned*)((const char*)(gbase) + (voff)[_i]), (PG8_LAS unsigned*)(lds + (bufoff) + ldsw + _i * 8192), 16, 0, 0); } while (0)
; #define PG8_WAIT_V(n) asm volatile("s_waitcnt vmcnt(" #n ")" ::: "memory")
; #define PG8_WAIT_L(n) asm volatile("s_waitcnt lgkmcnt(" #n ")" ::: "memory")
; #define PG8_BAR __builtin_amdgcn_s_barrier()
; #define PG8_SCHED __builtin_amdgcn_sched_barrier(0)
; template <class Epi, class Sched, bool ALIGN_EPI = true, bool F8 = false>
; __device__ __forceinline__ void gemm_phase(PG8_LAS unsigned char* lds, const Sched& S, const Epi& E) {
;     ...
;             PG8_LDB(B0, 1, 0); PG8_LDB(B1, 1, 1); PG8_SCHED; PG8_LDA(At, 1, 0); PG8_STAGE(PG8_SA(0, 1), a2, vA2[1]);
;             PG8_WAIT_V(8); PG8_WAIT_L(0); PG8_BAR; PG8_MMA(0, 0, At, B0); PG8_MMA(0, 1, At, B1); PG8_BAR; PG8_SCHED;
;             PG8_LDA(At, 1, 1); PG8_STAGE(PG8_SB(1, 0), b3, voffB[0]); PG8_STAGE(PG8_SB(1, 1), b3, voffB[1]); PG8_STAGE(PG8_SA(1, 0), a3, vA2[0]);
;             PG8_WAIT_V(8); PG8_WAIT_L(0); PG8_BAR; PG8_MMA(1, 0, At, B0); PG8_MMA(1, 1, At, B1); PG8_BAR; PG8_SCHED;
	s_add_i32 s78, 0, 0x18000
	s_add_i32 s79, 0, 0x1c000
	v_add_u32_e32 v2, s78, v190
	v_add_u32_e32 v10, s79, v190
	ds_read_b128 v[142:145], v2
	ds_read_b128 v[146:149], v2 offset:1024
	ds_read_b128 v[150:153], v2 offset:2048
	ds_read_b128 v[154:157], v2 offset:3072
	ds_read_b128 v[2:5], v10
	ds_read_b128 v[6:9], v10 offset:1024
	ds_read_b128 v[202:205], v10 offset:2048
	ds_read_b128 v[206:209], v10 offset:3072
	s_mov_b32 m0, s47
	v_lshl_add_u64 v[12:13], s[30:31], 0, v[166:167]
	ds_read_b128 v[210:213], v198 offset:32768
	ds_read_b128 v[214:217], v198 offset:33792
	ds_read_b128 v[218:221], v198 offset:34816
	ds_read_b128 v[222:225], v198 offset:35840
	ds_read_b128 v[226:229], v198 offset:36864
	ds_read_b128 v[230:233], v198 offset:37888
	ds_read_b128 v[234:237], v198 offset:38912
	ds_read_b128 v[238:241], v198 offset:39936
	global_load_lds_dwordx4 v[12:13], off
	v_lshl_add_u64 v[12:13], s[30:31], 0, v[168:169]
	s_mov_b32 m0, s48
	s_nop 0
	global_load_lds_dwordx4 v[12:13], off
	s_waitcnt vmcnt(8)
	s_waitcnt lgkmcnt(0)
	s_setprio 1
	s_waitcnt lgkmcnt(0)
	v_mfma_scale_f32_16x16x128_f8f6f4 v[138:141], v[142:149], v[210:217], v[138:141], v199, v199 op_sel_hi:[0,0,0]
	v_mfma_scale_f32_16x16x128_f8f6f4 v[134:137], v[150:157], v[210:217], v[134:137], v199, v199 op_sel_hi:[0,0,0]
	v_mfma_scale_f32_16x16x128_f8f6f4 v[130:133], v[142:149], v[218:225], v[130:133], v199, v199 op_sel_hi:[0,0,0]
	v_mfma_scale_f32_16x16x128_f8f6f4 v[126:129], v[150:157], v[218:225], v[126:129], v199, v199 op_sel_hi:[0,0,0]
	v_mfma_scale_f32_16x16x128_f8f6f4 v[122:125], v[142:149], v[226:233], v[122:125], v199, v199 op_sel_hi:[0,0,0]
	v_mfma_scale_f32_16x16x128_f8f6f4 v[118:121], v[150:157], v[226:233], v[118:121], v199, v199 op_sel_hi:[0,0,0]
	v_mfma_scale_f32_16x16x128_f8f6f4 v[114:117], v[142:149], v[234:241], v[114:117], v199, v199 op_sel_hi:[0,0,0]
	v_mfma_scale_f32_16x16x128_f8f6f4 v[110:113], v[150:157], v[234:241], v[110:113], v199, v199 op_sel_hi:[0,0,0]
	s_nop 3
	s_setprio 0
	s_setprio 1
	v_mfma_scale_f32_16x16x128_f8f6f4 v[106:109], v[2:9], v[210:217], v[106:109], v199, v199 op_sel_hi:[0,0,0]
	v_mfma_scale_f32_16x16x128_f8f6f4 v[102:105], v[202:209], v[210:217], v[102:105], v199, v199 op_sel_hi:[0,0,0]
	v_mfma_scale_f32_16x16x128_f8f6f4 v[98:101], v[2:9], v[218:225], v[98:101], v199, v199 op_sel_hi:[0,0,0]
	v_mfma_scale_f32_16x16x128_f8f6f4 v[94:97], v[202:209], v[218:225], v[94:97], v199, v199 op_sel_hi:[0,0,0]
	v_mfma_scale_f32_16x16x128_f8f6f4 v[90:93], v[2:9], v[226:233], v[90:93], v199, v199 op_sel_hi:[0,0,0]
	v_mfma_scale_f32_16x16x128_f8f6f4 v[86:89], v[202:209], v[226:233], v[86:89], v199, v199 op_sel_hi:[0,0,0]
	v_mfma_scale_f32_16x16x128_f8f6f4 v[82:85], v[2:9], v[234:241], v[82:85], v199, v199 op_sel_hi:[0,0,0]
	v_mfma_scale_f32_16x16x128_f8f6f4 v[78:81], v[202:209], v[234:241], v[78:81], v199, v199 op_sel_hi:[0,0,0]
	s_nop 3
	s_setprio 0
	s_barrier
	s_add_u32 s28, s28, 0x8000
	s_addc_u32 s29, s29, 0
	s_add_i32 s30, s78, s44
	v_lshl_add_u64 v[12:13], s[28:29], 0, v[158:159]
	s_mov_b32 m0, s30
	ds_read_b128 v[210:213], v198 offset:49152
	ds_read_b128 v[214:217], v198 offset:50176
	ds_read_b128 v[218:221], v198 offset:51200
	ds_read_b128 v[222:225], v198 offset:52224
	ds_read_b128 v[226:229], v198 offset:53248
	ds_read_b128 v[230:233], v198 offset:54272
	ds_read_b128 v[234:237], v198 offset:55296
	ds_read_b128 v[238:241], v198 offset:56320
	global_load_lds_dwordx4 v[12:13], off
	v_lshl_add_u64 v[12:13], s[28:29], 0, v[160:161]
	s_add_i32 m0, s30, 0x2000
	s_add_i32 s30, s79, s44
	global_load_lds_dwordx4 v[12:13], off
	v_lshl_add_u64 v[12:13], s[28:29], 0, v[172:173]
	s_mov_b32 m0, s30
	s_nop 0
	global_load_lds_dwordx4 v[12:13], off
	v_lshl_add_u64 v[12:13], s[28:29], 0, v[174:175]
	s_add_i32 m0, s30, 0x2000
	s_nop 0
	global_load_lds_dwordx4 v[12:13], off
	v_lshl_add_u64 v[12:13], s[26:27], 0, v[162:163]
	s_mov_b32 m0, s50
	s_nop 0
	global_load_lds_dwordx4 v[12:13], off
	v_lshl_add_u64 v[12:13], s[26:27], 0, v[164:165]
	s_mov_b32 m0, s51
	s_nop 0
	global_load_lds_dwordx4 v[12:13], off
	s_waitcnt vmcnt(8)
	s_waitcnt lgkmcnt(0)
	s_setprio 1
	s_waitcnt lgkmcnt(0)
	v_mfma_scale_f32_16x16x128_f8f6f4 v[74:77], v[142:149], v[210:217], v[74:77], v199, v199 op_sel_hi:[0,0,0]
	v_mfma_scale_f32_16x16x128_f8f6f4 v[70:73], v[150:157], v[210:217], v[70:73], v199, v199 op_sel_hi:[0,0,0]
	v_mfma_scale_f32_16x16x128_f8f6f4 v[66:69], v[142:149], v[218:225], v[66:69], v199, v199 op_sel_hi:[0,0,0]
	v_mfma_scale_f32_16x16x128_f8f6f4 v[62:65], v[150:157], v[218:225], v[62:65], v199, v199 op_sel_hi:[0,0,0]
	v_mfma_scale_f32_16x16x128_f8f6f4 v[58:61], v[142:149], v[226:233], v[58:61], v199, v199 op_sel_hi:[0,0,0]
	v_mfma_scale_f32_16x16x128_f8f6f4 v[54:57], v[150:157], v[226:233], v[54:57], v199, v199 op_sel_hi:[0,0,0]
	v_mfma_scale_f32_16x16x128_f8f6f4 v[50:53], v[142:149], v[234:241], v[50:53], v199, v199 op_sel_hi:[0,0,0]
	v_mfma_scale_f32_16x16x128_f8f6f4 v[46:49], v[150:157], v[234:241], v[46:49], v199, v199 op_sel_hi:[0,0,0]
	s_nop 3
	s_setprio 0
	s_setprio 1
	v_mfma_scale_f32_16x16x128_f8f6f4 v[42:45], v[2:9], v[210:217], v[42:45], v199, v199 op_sel_hi:[0,0,0]
	v_mfma_scale_f32_16x16x128_f8f6f4 v[38:41], v[202:209], v[210:217], v[38:41], v199, v199 op_sel_hi:[0,0,0]
	v_mfma_scale_f32_16x16x128_f8f6f4 v[34:37], v[2:9], v[218:225], v[34:37], v199, v199 op_sel_hi:[0,0,0]
	v_mfma_scale_f32_16x16x128_f8f6f4 v[30:33], v[202:209], v[218:225], v[30:33], v199, v199 op_sel_hi:[0,0,0]
	v_mfma_scale_f32_16x16x128_f8f6f4 v[26:29], v[2:9], v[226:233], v[26:29], v199, v199 op_sel_hi:[0,0,0]
	v_mfma_scale_f32_16x16x128_f8f6f4 v[22:25], v[202:209], v[226:233], v[22:25], v199, v199 op_sel_hi:[0,0,0]
	v_mfma_scale_f32_16x16x128_f8f6f4 v[18:21], v[2:9], v[234:241], v[18:21], v199, v199 op_sel_hi:[0,0,0]
	v_mfma_scale_f32_16x16x128_f8f6f4 v[14:17], v[202:209], v[234:241], v[14:17], v199, v199 op_sel_hi:[0,0,0]
	s_nop 3
	s_setprio 0
	s_barrier
	s_add_u32 s75, s75, 0x10000
	s_addc_u32 s76, s76, 0
	s_add_u32 s24, s24, 0x10000
	s_addc_u32 s25, s25, 0
	s_cmp_ge_i32 s77, s72
	s_mov_b32 s26, s77
	s_cbranch_scc0 .LBB0_834
	s_branch .Lfx_834
; #define PG8_STAGE(bufoff, gbase, voff) do { _Pragma("unroll") for (int _i = 0; _i < 2; ++_i) \
;         __builtin_amdgcn_global_load_lds((const unsigned*)((const char*)(gbase) + (voff)[_i]), (PG8_LAS unsigned*)(lds + (bufoff) + ldsw + _i * 8192), 16, 0, 0); } while (0)
; #define PG8_WAIT_V(n) asm volatile("s_waitcnt vmcnt(" #n ")" ::: "memory")
; #define PG8_WAIT_L(n) asm volatile("s_waitcnt lgkmcnt(" #n ")" ::: "memory")
; #define PG8_BAR __builtin_amdgcn_s_barrier()
; #define PG8_SCHED __builtin_amdgcn_sched_barrier(0)
; template <class Epi, class Sched, bool ALIGN_EPI = true, bool F8 = false>
; __device__ __forceinline__ void gemm_phase(PG8_LAS unsigned char* lds, const Sched& S, const Epi& E) {
;     ...
;             PG8_LDB(B0, 0, 0); PG8_LDB(B1, 0, 1); PG8_SCHED; PG8_LDA(At, 0, 0); PG8_STAGE(PG8_SA(1, 1), a1, voffA[1]);
;             PG8_WAIT_V(8); PG8_WAIT_L(0); PG8_BAR; PG8_MMA(0, 0, At, B0); PG8_MMA(0, 1, At, B1); PG8_BAR; PG8_SCHED;
;             PG8_LDA(At, 0, 1); PG8_STAGE(PG8_SB(0, 0), b2, voffB[0]); PG8_STAGE(PG8_SB(0, 1), b2, voffB[1]); PG8_STAGE(PG8_SA(0, 0), a2, vA2[0]);
;             PG8_WAIT_V(8); PG8_WAIT_L(0); PG8_BAR; PG8_MMA(1, 0, At, B0); PG8_MMA(1, 1, At, B1); PG8_BAR; PG8_SCHED;
.Lh1_834:
	v_add_u32_e32 v10, s58, v190
	ds_read_b128 v[2:5], v10
	ds_read_b128 v[6:9], v10 offset:1024
	ds_read_b128 v[142:145], v10 offset:2048
	ds_read_b128 v[146:149], v10 offset:3072
	v_add_u32_e32 v10, s59, v190
	ds_read_b128 v[150:153], v10
	ds_read_b128 v[154:157], v10 offset:1024
	ds_read_b128 v[202:205], v10 offset:2048
	ds_read_b128 v[206:209], v10 offset:3072
	s_add_i32 s77, s26, 2
	s_add_u32 s27, s24, 0x8000
	s_addc_u32 s28, s25, 0
	s_cmp_eq_u32 s74, s26
	s_cselect_b32 s30, s20, s27
	s_cselect_b32 s31, s21, s28
	s_cselect_b32 s28, s22, s75
	s_cselect_b32 s29, s23, s76
	s_add_u32 s26, s30, 0x8000
	s_addc_u32 s27, s31, 0
	v_lshl_add_u64 v[12:13], s[24:25], 0, v[182:183]
	s_add_i32 m0, s45, 0xc000
	ds_read_b128 v[210:213], v198
	ds_read_b128 v[214:217], v198 offset:1024
	ds_read_b128 v[218:221], v198 offset:2048
	ds_read_b128 v[222:225], v198 offset:3072
	ds_read_b128 v[226:229], v198 offset:4096
	ds_read_b128 v[230:233], v198 offset:5120
	ds_read_b128 v[234:237], v198 offset:6144
	ds_read_b128 v[238:241], v198 offset:7168
	global_load_lds_dwordx4 v[12:13], off
	v_lshl_add_u64 v[12:13], s[24:25], 0, v[180:181]
	s_add_i32 m0, s45, 0xe000
	s_nop 0
	global_load_lds_dwordx4 v[12:13], off
	s_waitcnt vmcnt(8)
	s_waitcnt lgkmcnt(0)
	s_barrier
	s_setprio 2
	s_waitcnt lgkmcnt(0)
	v_mfma_scale_f32_16x16x128_f8f6f4 v[138:141], v[2:9], v[210:217], v[138:141], v199, v199 op_sel_hi:[0,0,0]
	v_mfma_scale_f32_16x16x128_f8f6f4 v[134:137], v[142:149], v[210:217], v[134:137], v199, v199 op_sel_hi:[0,0,0]
	v_mfma_scale_f32_16x16x128_f8f6f4 v[130:133], v[2:9], v[218:225], v[130:133], v199, v199 op_sel_hi:[0,0,0]
	v_mfma_scale_f32_16x16x128_f8f6f4 v[126:129], v[142:149], v[218:225], v[126:129], v199, v199 op_sel_hi:[0,0,0]
	v_mfma_scale_f32_16x16x128_f8f6f4 v[122:125], v[2:9], v[226:233], v[122:125], v199, v199 op_sel_hi:[0,0,0]
	v_mfma_scale_f32_16x16x128_f8f6f4 v[118:121], v[142:149], v[226:233], v[118:121], v199, v199 op_sel_hi:[0,0,0]
	v_mfma_scale_f32_16x16x128_f8f6f4 v[114:117], v[2:9], v[234:241], v[114:117], v199, v199 op_sel_hi:[0,0,0]
	v_mfma_scale_f32_16x16x128_f8f6f4 v[110:113], v[142:149], v[234:241], v[110:113], v199, v199 op_sel_hi:[0,0,0]
	s_nop 3
	s_setprio 0
	s_setprio 2
	v_mfma_scale_f32_16x16x128_f8f6f4 v[106:109], v[150:157], v[210:217], v[106:109], v199, v199 op_sel_hi:[0,0,0]
	v_mfma_scale_f32_16x16x128_f8f6f4 v[102:105], v[202:209], v[210:217], v[102:105], v199, v199 op_sel_hi:[0,0,0]
	v_mfma_scale_f32_16x16x128_f8f6f4 v[98:101], v[150:157], v[218:225], v[98:101], v199, v199 op_sel_hi:[0,0,0]
	v_mfma_scale_f32_16x16x128_f8f6f4 v[94:97], v[202:209], v[218:225], v[94:97], v199, v199 op_sel_hi:[0,0,0]
	v_mfma_scale_f32_16x16x128_f8f6f4 v[90:93], v[150:157], v[226:233], v[90:93], v199, v199 op_sel_hi:[0,0,0]
	v_mfma_scale_f32_16x16x128_f8f6f4 v[86:89], v[202:209], v[226:233], v[86:89], v199, v199 op_sel_hi:[0,0,0]
	v_mfma_scale_f32_16x16x128_f8f6f4 v[82:85], v[150:157], v[234:241], v[82:85], v199, v199 op_sel_hi:[0,0,0]
	v_mfma_scale_f32_16x16x128_f8f6f4 v[78:81], v[202:209], v[234:241], v[78:81], v199, v199 op_sel_hi:[0,0,0]
	s_nop 3
	s_setprio 0
	s_add_i32 s78, s58, s44
	v_lshl_add_u64 v[12:13], s[28:29], 0, v[158:159]
	s_mov_b32 m0, s78
	ds_read_b128 v[210:213], v198 offset:16384
	ds_read_b128 v[214:217], v198 offset:17408
	ds_read_b128 v[218:221], v198 offset:18432
	ds_read_b128 v[222:225], v198 offset:19456
	ds_read_b128 v[226:229], v198 offset:20480
	ds_read_b128 v[230:233], v198 offset:21504
	ds_read_b128 v[234:237], v198 offset:22528
	ds_read_b128 v[238:241], v198 offset:23552
	global_load_lds_dwordx4 v[12:13], off
	v_lshl_add_u64 v[188:189], s[28:29], 0, v[160:161]
	s_add_i32 m0, s78, 0x2000
	s_add_i32 s78, s59, s44
	global_load_lds_dwordx4 v[188:189], off
	v_lshl_add_u64 v[12:13], v[12:13], 0, s[8:9]
	s_mov_b32 m0, s78
	s_nop 0
	global_load_lds_dwordx4 v[12:13], off
	v_lshl_add_u64 v[12:13], v[188:189], 0, s[8:9]
	s_add_i32 m0, s78, 0x2000
	s_nop 0
	global_load_lds_dwordx4 v[12:13], off
	v_lshl_add_u64 v[12:13], s[30:31], 0, v[162:163]
	s_mov_b32 m0, s45
	s_nop 0
	global_load_lds_dwordx4 v[12:13], off
	v_lshl_add_u64 v[12:13], s[30:31], 0, v[164:165]
	s_mov_b32 m0, s46
	s_nop 0
	global_load_lds_dwordx4 v[12:13], off
	s_waitcnt vmcnt(8)
	s_waitcnt lgkmcnt(0)
	s_barrier
; #define PG8_STAGE(bufoff, gbase, voff) do { _Pragma("unroll") for (int _i = 0; _i < 2; ++_i) \
;         __builtin_amdgcn_global_load_lds((const unsigned*)((const char*)(gbase) + (voff)[_i]), (PG8_LAS unsigned*)(lds + (bufoff) + ldsw + _i * 8192), 16, 0, 0); } while (0)
; #define PG8_WAIT_V(n) asm volatile("s_waitcnt vmcnt(" #n ")" ::: "memory")
; #define PG8_WAIT_L(n) asm volatile("s_waitcnt lgkmcnt(" #n ")" ::: "memory")
; #define PG8_BAR __builtin_amdgcn_s_barrier()
; #define PG8_SCHED __builtin_amdgcn_sched_barrier(0)
; template <class Epi, class Sched, bool ALIGN_EPI = true, bool F8 = false>
; __device__ __forceinline__ void gemm_phase(PG8_LAS unsigned char* lds, const Sched& S, const Epi& E) {
;     ...
;             PG8_LDA(At, 0, 1); PG8_STAGE(PG8_SB(0, 0), b2, voffB[0]); PG8_STAGE(PG8_SB(0, 1), b2, voffB[1]); PG8_STAGE(PG8_SA(0, 0), a2, vA2[0]);
;             PG8_WAIT_V(8); PG8_WAIT_L(0); PG8_BAR; PG8_MMA(1, 0, At, B0); PG8_MMA(1, 1, At, B1); PG8_BAR; PG8_SCHED;
;             PG8_LDB(B0, 1, 0); PG8_LDB(B1, 1, 1); PG8_SCHED; PG8_LDA(At, 1, 0); PG8_STAGE(PG8_SA(0, 1), a2, vA2[1]);
;             PG8_WAIT_V(8); PG8_WAIT_L(0); PG8_BAR; PG8_MMA(0, 0, At, B0); PG8_MMA(0, 1, At, B1); PG8_BAR; PG8_SCHED;
;             PG8_LDA(At, 1, 1); PG8_STAGE(PG8_SB(1, 0), b3, voffB[0]); PG8_STAGE(PG8_SB(1, 1), b3, voffB[1]); PG8_STAGE(PG8_SA(1, 0), a3, vA2[0]);
	s_setprio 2
	s_waitcnt lgkmcnt(0)
	v_mfma_scale_f32_16x16x128_f8f6f4 v[74:77], v[2:9], v[210:217], v[74:77], v199, v199 op_sel_hi:[0,0,0]
	v_mfma_scale_f32_16x16x128_f8f6f4 v[70:73], v[142:149], v[210:217], v[70:73], v199, v199 op_sel_hi:[0,0,0]
	v_mfma_scale_f32_16x16x128_f8f6f4 v[66:69], v[2:9], v[218:225], v[66:69], v199, v199 op_sel_hi:[0,0,0]
	v_mfma_scale_f32_16x16x128_f8f6f4 v[62:65], v[142:149], v[218:225], v[62:65], v199, v199 op_sel_hi:[0,0,0]
	v_mfma_scale_f32_16x16x128_f8f6f4 v[58:61], v[2:9], v[226:233], v[58:61], v199, v199 op_sel_hi:[0,0,0]
	v_mfma_scale_f32_16x16x128_f8f6f4 v[54:57], v[142:149], v[226:233], v[54:57], v199, v199 op_sel_hi:[0,0,0]
	v_mfma_scale_f32_16x16x128_f8f6f4 v[50:53], v[2:9], v[234:241], v[50:53], v199, v199 op_sel_hi:[0,0,0]
	v_mfma_scale_f32_16x16x128_f8f6f4 v[46:49], v[142:149], v[234:241], v[46:49], v199, v199 op_sel_hi:[0,0,0]
	s_nop 3
	s_setprio 0
	s_setprio 2
	v_mfma_scale_f32_16x16x128_f8f6f4 v[42:45], v[150:157], v[210:217], v[42:45], v199, v199 op_sel_hi:[0,0,0]
	v_mfma_scale_f32_16x16x128_f8f6f4 v[38:41], v[202:209], v[210:217], v[38:41], v199, v199 op_sel_hi:[0,0,0]
	v_mfma_scale_f32_16x16x128_f8f6f4 v[34:37], v[150:157], v[218:225], v[34:37], v199, v199 op_sel_hi:[0,0,0]
	v_mfma_scale_f32_16x16x128_f8f6f4 v[30:33], v[202:209], v[218:225], v[30:33], v199, v199 op_sel_hi:[0,0,0]
	v_mfma_scale_f32_16x16x128_f8f6f4 v[26:29], v[150:157], v[226:233], v[26:29], v199, v199 op_sel_hi:[0,0,0]
	v_mfma_scale_f32_16x16x128_f8f6f4 v[22:25], v[202:209], v[226:233], v[22:25], v199, v199 op_sel_hi:[0,0,0]
	v_mfma_scale_f32_16x16x128_f8f6f4 v[18:21], v[150:157], v[234:241], v[18:21], v199, v199 op_sel_hi:[0,0,0]
	v_mfma_scale_f32_16x16x128_f8f6f4 v[14:17], v[202:209], v[234:241], v[14:17], v199, v199 op_sel_hi:[0,0,0]
	s_nop 3
	s_setprio 0
	s_add_i32 s78, 0, 0x18000
	s_add_i32 s79, 0, 0x1c000
	v_add_u32_e32 v2, s78, v190
	v_add_u32_e32 v10, s79, v190
	ds_read_b128 v[142:145], v2
	ds_read_b128 v[146:149], v2 offset:1024
	ds_read_b128 v[150:153], v2 offset:2048
	ds_read_b128 v[154:157], v2 offset:3072
	ds_read_b128 v[2:5], v10
	ds_read_b128 v[6:9], v10 offset:1024
	ds_read_b128 v[202:205], v10 offset:2048
	ds_read_b128 v[206:209], v10 offset:3072
	s_mov_b32 m0, s47
	v_lshl_add_u64 v[12:13], s[30:31], 0, v[166:167]
	ds_read_b128 v[210:213], v198 offset:32768
	ds_read_b128 v[214:217], v198 offset:33792
	ds_read_b128 v[218:221], v198 offset:34816
	ds_read_b128 v[222:225], v198 offset:35840
	ds_read_b128 v[226:229], v198 offset:36864
	ds_read_b128 v[230:233], v198 offset:37888
	ds_read_b128 v[234:237], v198 offset:38912
	ds_read_b128 v[238:241], v198 offset:39936
	global_load_lds_dwordx4 v[12:13], off
	v_lshl_add_u64 v[12:13], s[30:31], 0, v[168:169]
	s_mov_b32 m0, s48
	s_nop 0
	global_load_lds_dwordx4 v[12:13], off
	s_waitcnt vmcnt(8)
	s_waitcnt lgkmcnt(0)
	s_barrier
	s_setprio 2
	s_waitcnt lgkmcnt(0)
	v_mfma_scale_f32_16x16x128_f8f6f4 v[138:141], v[142:149], v[210:217], v[138:141], v199, v199 op_sel_hi:[0,0,0]
	v_mfma_scale_f32_16x16x128_f8f6f4 v[134:137], v[150:157], v[210:217], v[134:137], v199, v199 op_sel_hi:[0,0,0]
	v_mfma_scale_f32_16x16x128_f8f6f4 v[130:133], v[142:149], v[218:225], v[130:133], v199, v199 op_sel_hi:[0,0,0]
	v_mfma_scale_f32_16x16x128_f8f6f4 v[126:129], v[150:157], v[218:225], v[126:129], v199, v199 op_sel_hi:[0,0,0]
	v_mfma_scale_f32_16x16x128_f8f6f4 v[122:125], v[142:149], v[226:233], v[122:125], v199, v199 op_sel_hi:[0,0,0]
	v_mfma_scale_f32_16x16x128_f8f6f4 v[118:121], v[150:157], v[226:233], v[118:121], v199, v199 op_sel_hi:[0,0,0]
	v_mfma_scale_f32_16x16x128_f8f6f4 v[114:117], v[142:149], v[234:241], v[114:117], v199, v199 op_sel_hi:[0,0,0]
	v_mfma_scale_f32_16x16x128_f8f6f4 v[110:113], v[150:157], v[234:241], v[110:113], v199, v199 op_sel_hi:[0,0,0]
	s_nop 3
	s_setprio 0
	s_setprio 2
	v_mfma_scale_f32_16x16x128_f8f6f4 v[106:109], v[2:9], v[210:217], v[106:109], v199, v199 op_sel_hi:[0,0,0]
	v_mfma_scale_f32_16x16x128_f8f6f4 v[102:105], v[202:209], v[210:217], v[102:105], v199, v199 op_sel_hi:[0,0,0]
	v_mfma_scale_f32_16x16x128_f8f6f4 v[98:101], v[2:9], v[218:225], v[98:101], v199, v199 op_sel_hi:[0,0,0]
	v_mfma_scale_f32_16x16x128_f8f6f4 v[94:97], v[202:209], v[218:225], v[94:97], v199, v199 op_sel_hi:[0,0,0]
	v_mfma_scale_f32_16x16x128_f8f6f4 v[90:93], v[2:9], v[226:233], v[90:93], v199, v199 op_sel_hi:[0,0,0]
	v_mfma_scale_f32_16x16x128_f8f6f4 v[86:89], v[202:209], v[226:233], v[86:89], v199, v199 op_sel_hi:[0,0,0]
	v_mfma_scale_f32_16x16x128_f8f6f4 v[82:85], v[2:9], v[234:241], v[82:85], v199, v199 op_sel_hi:[0,0,0]
	v_mfma_scale_f32_16x16x128_f8f6f4 v[78:81], v[202:209], v[234:241], v[78:81], v199, v199 op_sel_hi:[0,0,0]
	s_nop 3
	s_setprio 0
	s_add_u32 s28, s28, 0x8000
	s_addc_u32 s29, s29, 0
	s_add_i32 s30, s78, s44
	v_lshl_add_u64 v[12:13], s[28:29], 0, v[158:159]
	s_mov_b32 m0, s30
	ds_read_b128 v[210:213], v198 offset:49152
	ds_read_b128 v[214:217], v198 offset:50176
	ds_read_b128 v[218:221], v198 offset:51200
	ds_read_b128 v[222:225], v198 offset:52224
	ds_read_b128 v[226:229], v198 offset:53248
	ds_read_b128 v[230:233], v198 offset:54272
	ds_read_b128 v[234:237], v198 offset:55296
	ds_read_b128 v[238:241], v198 offset:56320
	global_load_lds_dwordx4 v[12:13], off
	v_lshl_add_u64 v[12:13], s[28:29], 0, v[160:161]
	s_add_i32 m0, s30, 0x2000
	s_add_i32 s30, s79, s44
	global_load_lds_dwordx4 v[12:13], off
	v_lshl_add_u64 v[12:13], s[28:29], 0, v[172:173]
	s_mov_b32 m0, s30
	s_nop 0
	global_load_lds_dwordx4 v[12:13], off
	v_lshl_add_u64 v[12:13], s[28:29], 0, v[174:175]
	s_add_i32 m0, s30, 0x2000
	s_nop 0
	global_load_lds_dwordx4 v[12:13], off
	v_lshl_add_u64 v[12:13], s[26:27], 0, v[162:163]
	s_mov_b32 m0, s50
	s_nop 0
	global_load_lds_dwordx4 v[12:13], off
	v_lshl_add_u64 v[12:13], s[26:27], 0, v[164:165]
	s_mov_b32 m0, s51
	s_nop 0
	global_load_lds_dwordx4 v[12:13], off
	s_waitcnt vmcnt(8)
	s_waitcnt lgkmcnt(0)
	s_barrier
; __device__ __forceinline__ f32x4 u8x4_f32(unsigned w) { return (f32x4){(float)(w & 0xffu), (float)((w >> 8) & 0xffu), (float)((w >> 16) & 0xffu), (float)(w >> 24)}; }
; __device__ __forceinline__ unsigned pk4_fp8(float a, float b, float c, float d) { int w = 0; w = __builtin_amdgcn_cvt_pk_fp8_f32(clamp8(a), clamp8(b), w, false); w = __builtin_amdgcn_cvt_pk_fp8_f32(clamp8(c), clamp8(d), w, true); return (unsigned)w; }
; #define PG8_STAGE(bufoff, gbase, voff) do { _Pragma("unroll") for (int _i = 0; _i < 2; ++_i) \
;         __builtin_amdgcn_global_load_lds((const unsigned*)((const char*)(gbase) + (voff)[_i]), (PG8_LAS unsigned*)(lds + (bufoff) + ldsw + _i * 8192), 16, 0, 0); } while (0)
; #define PG8_WAIT_V(n) asm volatile("s_waitcnt vmcnt(" #n ")" ::: "memory")
; #define PG8_WAIT_L(n) asm volatile("s_waitcnt lgkmcnt(" #n ")" ::: "memory")
; #define PG8_BAR __builtin_amdgcn_s_barrier()
; template <class Epi, class Sched, bool ALIGN_EPI = true, bool F8 = false>
; __device__ __forceinline__ void gemm_phase(PG8_LAS unsigned char* lds, const Sched& S, const Epi& E) {
;     ...
;             PG8_LDA(At, 1, 1); PG8_STAGE(PG8_SB(1, 0), b3, voffB[0]); PG8_STAGE(PG8_SB(1, 1), b3, voffB[1]); PG8_STAGE(PG8_SA(1, 0), a3, vA2[0]);
;             PG8_WAIT_V(8); PG8_WAIT_L(0); PG8_BAR; PG8_MMA(1, 0, At, B0); PG8_MMA(1, 1, At, B1); PG8_BAR; PG8_SCHED;
;         }
;         if constexpr (ALIGN_EPI) { if (wr == 0) PG8_BAR; }
;     __device__ __forceinline__ void operator()(f32x4 (&acc)[2][2][4][2], const GUnit& u, int wr, int wc, int fr, int fq) const {
;     ...
; #pragma unroll
;         for (int ai = 0; ai < 2; ++ai) {
;             u32x4 qf[4];
; #pragma unroll
;             for (int m = 0; m < 4; ++m) qf[m] = __builtin_nontemporal_load((const u32x4*)(GZF + off0 + (size_t)(ai * 128 + m * 16) * D));
; #pragma unroll
;             for (int m = 0; m < 4; ++m) { u32x4 w;
; #pragma unroll
;                 for (int q = 0; q < 4; ++q) { const f32x4 f = u8x4_f32(qf[m][q]); const f32x4 a = acc[ai][q >> 1][m][q & 1]; f32x4 v;
; #pragma unroll
;                     for (int j = 0; j < 4; ++j) v[j] = a[j] * (fmaxf(f[j], 0.5f) * (W8_INV / 255.0f));
;                     w[q] = pk4_fp8(v[0], v[1], v[2], v[3]); }
;                 *(u32x4*)(M8 + tiled_off((size_t)(u.x0 * 256 + wr * 64 + fr + ai * 128 + m * 16), u.x1 * 256 + wc * 64 + 16 * fq, D / 128)) = w; }
	s_setprio 2
	s_waitcnt lgkmcnt(0)
	v_mfma_scale_f32_16x16x128_f8f6f4 v[74:77], v[142:149], v[210:217], v[74:77], v199, v199 op_sel_hi:[0,0,0]
	v_mfma_scale_f32_16x16x128_f8f6f4 v[70:73], v[150:157], v[210:217], v[70:73], v199, v199 op_sel_hi:[0,0,0]
	v_mfma_scale_f32_16x16x128_f8f6f4 v[66:69], v[142:149], v[218:225], v[66:69], v199, v199 op_sel_hi:[0,0,0]
	v_mfma_scale_f32_16x16x128_f8f6f4 v[62:65], v[150:157], v[218:225], v[62:65], v199, v199 op_sel_hi:[0,0,0]
	v_mfma_scale_f32_16x16x128_f8f6f4 v[58:61], v[142:149], v[226:233], v[58:61], v199, v199 op_sel_hi:[0,0,0]
	v_mfma_scale_f32_16x16x128_f8f6f4 v[54:57], v[150:157], v[226:233], v[54:57], v199, v199 op_sel_hi:[0,0,0]
	v_mfma_scale_f32_16x16x128_f8f6f4 v[50:53], v[142:149], v[234:241], v[50:53], v199, v199 op_sel_hi:[0,0,0]
	v_mfma_scale_f32_16x16x128_f8f6f4 v[46:49], v[150:157], v[234:241], v[46:49], v199, v199 op_sel_hi:[0,0,0]
	s_nop 3
	s_setprio 0
	s_setprio 2
	v_mfma_scale_f32_16x16x128_f8f6f4 v[42:45], v[2:9], v[210:217], v[42:45], v199, v199 op_sel_hi:[0,0,0]
	v_mfma_scale_f32_16x16x128_f8f6f4 v[38:41], v[202:209], v[210:217], v[38:41], v199, v199 op_sel_hi:[0,0,0]
	v_mfma_scale_f32_16x16x128_f8f6f4 v[34:37], v[2:9], v[218:225], v[34:37], v199, v199 op_sel_hi:[0,0,0]
	v_mfma_scale_f32_16x16x128_f8f6f4 v[30:33], v[202:209], v[218:225], v[30:33], v199, v199 op_sel_hi:[0,0,0]
	v_mfma_scale_f32_16x16x128_f8f6f4 v[26:29], v[2:9], v[226:233], v[26:29], v199, v199 op_sel_hi:[0,0,0]
	v_mfma_scale_f32_16x16x128_f8f6f4 v[22:25], v[202:209], v[226:233], v[22:25], v199, v199 op_sel_hi:[0,0,0]
	v_mfma_scale_f32_16x16x128_f8f6f4 v[18:21], v[2:9], v[234:241], v[18:21], v199, v199 op_sel_hi:[0,0,0]
	v_mfma_scale_f32_16x16x128_f8f6f4 v[14:17], v[202:209], v[234:241], v[14:17], v199, v199 op_sel_hi:[0,0,0]
	s_nop 3
	s_setprio 0
	s_add_u32 s75, s75, 0x10000
	s_addc_u32 s76, s76, 0
	s_add_u32 s24, s24, 0x10000
	s_addc_u32 s25, s25, 0
	s_cmp_ge_i32 s77, s72
	s_mov_b32 s26, s77
	s_cbranch_scc0 .Lh1_834
.Lfx_834:
	s_and_b64 vcc, exec, s[16:17]
	s_cbranch_vccz .LBB0_837
.LBB0_837:
	s_lshl_b32 s28, s71, 8
	v_add_u32_e32 v144, s28, v177
	v_ashrrev_i32_e32 v145, 31, v144
	s_lshl_b32 s26, s70, 8
	v_lshlrev_b64 v[2:3], 11, v[144:145]
	s_ashr_i32 s27, s26, 31
	v_lshl_add_u64 v[142:143], v[2:3], 0, s[26:27]
	v_or_b32_e32 v142, v142, v176
	s_cmp_lg_u32 s73, 0
	s_cselect_b64 s[24:25], -1, 0
	s_cmp_eq_u32 s73, 0
	v_lshl_add_u64 v[12:13], s[6:7], 0, v[142:143]
	s_nop 15
	s_nop 7
	s_nop 15
	s_nop 7
	s_nop 15
	s_nop 7
	s_nop 15
	s_nop 7
	s_cbranch_scc1 .LBB0_845
	flat_load_dwordx4 v[146:149], v[12:13] nt
	v_add_co_u32_e32 v2, vcc, 0x8000, v12
	v_mov_b32_e32 v151, 0
	s_nop 0
	v_addc_co_u32_e32 v3, vcc, 0, v13, vcc
	v_add_co_u32_e32 v4, vcc, 0x10000, v12
	v_mov_b32_e32 v150, 0
	s_nop 0
	v_addc_co_u32_e32 v5, vcc, 0, v13, vcc
	flat_load_dwordx4 v[154:157], v[2:3] nt
	flat_load_dwordx4 v[6:9], v[4:5] nt
	v_add_co_u32_e32 v188, vcc, 0x18000, v12
	v_mov_b32_e32 v152, 0
	s_nop 0
	v_addc_co_u32_e32 v189, vcc, 0, v13, vcc
	flat_load_dwordx4 v[2:5], v[188:189] nt
	s_or_b32 s26, s26, s53
	s_ashr_i32 s26, s26, 7
	s_ashr_i32 s27, s26, 31
	s_waitcnt vmcnt(0) lgkmcnt(0)
	v_cvt_f32_ubyte0_e32 v189, v147
	v_cvt_f32_ubyte1_e32 v201, v147
	v_max_f32_e32 v189, 0.5, v189
	v_max_f32_e32 v201, 0.5, v201
	v_mul_f32_e32 v189, 0x38808081, v189
	v_mul_f32_e32 v201, 0x38808081, v201
	v_cvt_f32_ubyte0_e32 v10, v146
	v_cvt_f32_ubyte1_e32 v153, v146
	v_cvt_f32_ubyte0_e32 v203, v148
	v_cvt_f32_ubyte1_e32 v204, v148
	v_mul_f32_e32 v189, v134, v189
	v_mul_f32_e32 v201, v135, v201
	v_cvt_f32_ubyte2_e32 v202, v147
	v_cvt_f32_ubyte3_e32 v147, v147
	v_max_f32_e32 v10, 0.5, v10
	v_max_f32_e32 v153, 0.5, v153
	v_max_f32_e32 v203, 0.5, v203
	v_max_f32_e32 v204, 0.5, v204
	v_med3_f32 v189, v189, s60, v200
	v_med3_f32 v201, v201, s60, v200
	v_cvt_f32_ubyte2_e32 v205, v148
	v_cvt_f32_ubyte3_e32 v148, v148
	v_max_f32_e32 v202, 0.5, v202
	v_max_f32_e32 v147, 0.5, v147
	v_mul_f32_e32 v10, 0x38808081, v10
	v_mul_f32_e32 v153, 0x38808081, v153
	v_mul_f32_e32 v203, 0x38808081, v203
	v_mul_f32_e32 v204, 0x38808081, v204
	v_cvt_pk_fp8_f32 v151, v189, v201
	v_max_f32_e32 v148, 0.5, v148
	v_mul_f32_e32 v202, 0x38808081, v202
	v_mul_f32_e32 v147, 0x38808081, v147
	v_mul_f32_e32 v10, v138, v10
	v_mul_f32_e32 v153, v139, v153
	v_mul_f32_e32 v203, v106, v203
	v_mul_f32_e32 v204, v107, v204
	v_cvt_f32_ubyte2_e32 v188, v146
	v_cvt_f32_ubyte3_e32 v146, v146
	v_mul_f32_e32 v148, 0x38808081, v148
	v_mul_f32_e32 v202, v136, v202
	v_mul_f32_e32 v147, v137, v147
	v_med3_f32 v10, v10, s60, v200
	v_med3_f32 v153, v153, s60, v200
	v_med3_f32 v203, v203, s60, v200
	v_med3_f32 v204, v204, s60, v200
	v_cvt_f32_ubyte0_e32 v206, v149
	v_cvt_f32_ubyte1_e32 v207, v149
	v_max_f32_e32 v188, 0.5, v188
	v_max_f32_e32 v146, 0.5, v146
	v_max_f32_e32 v205, 0.5, v205
	v_mul_f32_e32 v148, v109, v148
	v_med3_f32 v202, v202, s60, v200
	v_med3_f32 v147, v147, s60, v200
	v_cvt_pk_fp8_f32 v150, v10, v153
	v_cvt_pk_fp8_f32 v152, v203, v204
	v_mul_f32_e32 v188, 0x38808081, v188
	v_mul_f32_e32 v146, 0x38808081, v146
	v_mul_f32_e32 v205, 0x38808081, v205
	v_med3_f32 v10, v148, s60, v200
	v_cvt_pk_fp8_f32 v151, v202, v147 op_sel:[0,0,1]
	v_max_f32_e32 v147, 0.5, v206
	v_max_f32_e32 v148, 0.5, v207
	v_mul_f32_e32 v188, v140, v188
	v_mul_f32_e32 v146, v141, v146
	v_mul_f32_e32 v205, v108, v205
	v_mul_f32_e32 v147, 0x38808081, v147
	v_mul_f32_e32 v148, 0x38808081, v148
	v_med3_f32 v188, v188, s60, v200
	v_med3_f32 v146, v146, s60, v200
	v_med3_f32 v205, v205, s60, v200
	v_mul_f32_e32 v147, v102, v147
	v_mul_f32_e32 v148, v103, v148
	v_cvt_pk_fp8_f32 v150, v188, v146 op_sel:[0,0,1]
; __device__ __forceinline__ f32x4 u8x4_f32(unsigned w) { return (f32x4){(float)(w & 0xffu), (float)((w >> 8) & 0xffu), (float)((w >> 16) & 0xffu), (float)(w >> 24)}; }
; __device__ __forceinline__ unsigned pk4_fp8(float a, float b, float c, float d) { int w = 0; w = __builtin_amdgcn_cvt_pk_fp8_f32(clamp8(a), clamp8(b), w, false); w = __builtin_amdgcn_cvt_pk_fp8_f32(clamp8(c), clamp8(d), w, true); return (unsigned)w; }
; __host__ __device__ __forceinline__ size_t tiled_off(size_t r, int kb, int ktiles) { return (((r >> 8) * ktiles + (kb >> 7)) << 15) + ((r & 255) << 7) + (kb & 127); }
;     __device__ __forceinline__ void operator()(f32x4 (&acc)[2][2][4][2], const GUnit& u, int wr, int wc, int fr, int fq) const {
;     ...
;             for (int m = 0; m < 4; ++m) { u32x4 w;
; #pragma unroll
;                 for (int q = 0; q < 4; ++q) { const f32x4 f = u8x4_f32(qf[m][q]); const f32x4 a = acc[ai][q >> 1][m][q & 1]; f32x4 v;
; #pragma unroll
;                     for (int j = 0; j < 4; ++j) v[j] = a[j] * (fmaxf(f[j], 0.5f) * (W8_INV / 255.0f));
;                     w[q] = pk4_fp8(v[0], v[1], v[2], v[3]); }
;                 *(u32x4*)(M8 + tiled_off((size_t)(u.x0 * 256 + wr * 64 + fr + ai * 128 + m * 16), u.x1 * 256 + wc * 64 + 16 * fq, D / 128)) = w; }
	v_cvt_pk_fp8_f32 v152, v205, v10 op_sel:[0,0,1]
	v_cvt_f32_ubyte2_e32 v10, v149
	v_cvt_f32_ubyte3_e32 v146, v149
	v_med3_f32 v147, v147, s60, v200
	v_med3_f32 v148, v148, s60, v200
	v_mov_b32_e32 v153, 0
	v_max_f32_e32 v10, 0.5, v10
	v_max_f32_e32 v146, 0.5, v146
	v_cvt_pk_fp8_f32 v153, v147, v148
	v_mul_f32_e32 v10, 0x38808081, v10
	v_mul_f32_e32 v146, 0x38808081, v146
	v_mul_f32_e32 v10, v104, v10
	v_mul_f32_e32 v146, v105, v146
	v_med3_f32 v10, v10, s60, v200
	v_med3_f32 v146, v146, s60, v200
	v_cvt_pk_fp8_f32 v153, v10, v146 op_sel:[0,0,1]
	v_lshrrev_b64 v[146:147], 4, v[144:145]
	v_and_b32_e32 v147, 0x1ffff, v147
	v_and_b32_e32 v146, -16, v146
	v_lshl_add_u64 v[146:147], v[146:147], 0, s[26:27]
	v_lshlrev_b64 v[146:147], 15, v[146:147]
	v_lshlrev_b32_e32 v10, 7, v144
	v_and_b32_e32 v10, 0x6780, v10
	v_lshl_add_u64 v[144:145], s[12:13], 0, v[146:147]
	v_lshl_add_u64 v[144:145], v[144:145], 0, v[10:11]
	v_lshl_add_u64 v[144:145], v[144:145], 0, v[178:179]
	flat_store_dwordx4 v[144:145], v[150:153]
	v_cvt_f32_ubyte0_e32 v10, v154
	v_cvt_f32_ubyte1_e32 v144, v154
	v_max_f32_e32 v10, 0.5, v10
	v_max_f32_e32 v144, 0.5, v144
	v_mul_f32_e32 v10, 0x38808081, v10
	v_mul_f32_e32 v144, 0x38808081, v144
	v_mul_f32_e32 v10, v130, v10
	v_mul_f32_e32 v144, v131, v144
	v_cvt_f32_ubyte2_e32 v145, v154
	v_cvt_f32_ubyte3_e32 v146, v154
	v_med3_f32 v10, v10, s60, v200
	v_med3_f32 v147, v144, s60, v200
	v_mov_b32_e32 v144, v11
	v_max_f32_e32 v145, 0.5, v145
	v_max_f32_e32 v146, 0.5, v146
	v_cvt_pk_fp8_f32 v144, v10, v147
	v_mul_f32_e32 v145, 0x38808081, v145
	v_mul_f32_e32 v146, 0x38808081, v146
	v_mul_f32_e32 v145, v132, v145
	v_mul_f32_e32 v10, v133, v146
	v_med3_f32 v145, v145, s60, v200
	v_med3_f32 v10, v10, s60, v200
	v_cvt_pk_fp8_f32 v144, v145, v10 op_sel:[0,0,1]
	v_cvt_f32_ubyte0_e32 v10, v155
	v_cvt_f32_ubyte1_e32 v145, v155
	v_max_f32_e32 v10, 0.5, v10
	v_max_f32_e32 v145, 0.5, v145
	v_mul_f32_e32 v10, 0x38808081, v10
	v_mul_f32_e32 v145, 0x38808081, v145
	v_mul_f32_e32 v10, v126, v10
	v_mul_f32_e32 v145, v127, v145
	v_cvt_f32_ubyte2_e32 v146, v155
	v_cvt_f32_ubyte3_e32 v147, v155
	v_med3_f32 v10, v10, s60, v200
	v_med3_f32 v148, v145, s60, v200
	v_mov_b32_e32 v145, v11
	v_max_f32_e32 v146, 0.5, v146
	v_max_f32_e32 v147, 0.5, v147
	v_cvt_pk_fp8_f32 v145, v10, v148
	v_mul_f32_e32 v146, 0x38808081, v146
	v_mul_f32_e32 v147, 0x38808081, v147
	v_mul_f32_e32 v146, v128, v146
	v_mul_f32_e32 v10, v129, v147
	v_med3_f32 v146, v146, s60, v200
	v_med3_f32 v10, v10, s60, v200
	v_cvt_pk_fp8_f32 v145, v146, v10 op_sel:[0,0,1]
	v_cvt_f32_ubyte0_e32 v10, v156
	v_cvt_f32_ubyte1_e32 v146, v156
	v_max_f32_e32 v10, 0.5, v10
	v_max_f32_e32 v146, 0.5, v146
	v_mul_f32_e32 v10, 0x38808081, v10
	v_mul_f32_e32 v146, 0x38808081, v146
	v_mul_f32_e32 v10, v98, v10
	v_mul_f32_e32 v146, v99, v146
	v_cvt_f32_ubyte2_e32 v147, v156
	v_cvt_f32_ubyte3_e32 v148, v156
	v_med3_f32 v10, v10, s60, v200
	v_med3_f32 v149, v146, s60, v200
	v_mov_b32_e32 v146, v11
	v_max_f32_e32 v147, 0.5, v147
	v_max_f32_e32 v148, 0.5, v148
	v_cvt_pk_fp8_f32 v146, v10, v149
	v_mul_f32_e32 v147, 0x38808081, v147
	v_mul_f32_e32 v148, 0x38808081, v148
	v_mul_f32_e32 v147, v100, v147
	v_mul_f32_e32 v10, v101, v148
	v_med3_f32 v147, v147, s60, v200
	v_med3_f32 v10, v10, s60, v200
	v_cvt_pk_fp8_f32 v146, v147, v10 op_sel:[0,0,1]
	v_cvt_f32_ubyte0_e32 v10, v157
	v_cvt_f32_ubyte1_e32 v147, v157
	v_max_f32_e32 v10, 0.5, v10
	v_max_f32_e32 v147, 0.5, v147
	v_mul_f32_e32 v10, 0x38808081, v10
	v_mul_f32_e32 v147, 0x38808081, v147
	v_mul_f32_e32 v10, v94, v10
	v_mul_f32_e32 v147, v95, v147
	v_cvt_f32_ubyte2_e32 v148, v157
	v_cvt_f32_ubyte3_e32 v149, v157
	v_med3_f32 v10, v10, s60, v200
	v_med3_f32 v150, v147, s60, v200
	v_mov_b32_e32 v147, v11
	v_max_f32_e32 v148, 0.5, v148
	v_max_f32_e32 v149, 0.5, v149
	v_cvt_pk_fp8_f32 v147, v10, v150
	v_mul_f32_e32 v148, 0x38808081, v148
	v_mul_f32_e32 v149, 0x38808081, v149
	v_mul_f32_e32 v148, v96, v148
	v_mul_f32_e32 v10, v97, v149
	v_med3_f32 v148, v148, s60, v200
	v_med3_f32 v10, v10, s60, v200
	v_cvt_pk_fp8_f32 v147, v148, v10 op_sel:[0,0,1]
	v_add_u32_e32 v148, s28, v191
	v_ashrrev_i32_e32 v149, 31, v148
	v_lshrrev_b64 v[150:151], 4, v[148:149]
	v_and_b32_e32 v151, 0x1ffff, v151
	v_and_b32_e32 v150, -16, v150
	v_lshl_add_u64 v[150:151], v[150:151], 0, s[26:27]
	v_lshlrev_b64 v[150:151], 15, v[150:151]
	v_lshlrev_b32_e32 v10, 7, v148
	v_and_b32_e32 v10, 0x7f80, v10
	v_lshl_add_u64 v[148:149], s[12:13], 0, v[150:151]
	v_lshl_add_u64 v[148:149], v[148:149], 0, v[10:11]
	v_lshl_add_u64 v[148:149], v[148:149], 0, v[178:179]
	flat_store_dwordx4 v[148:149], v[144:147]
	v_cvt_f32_ubyte0_e32 v10, v6
	v_max_f32_e32 v10, 0.5, v10
	v_cvt_f32_ubyte1_e32 v144, v6
	v_max_f32_e32 v144, 0.5, v144
	v_cvt_f32_ubyte2_e32 v145, v6
	v_cvt_f32_ubyte3_e32 v6, v6
	v_mul_f32_e32 v10, 0x38808081, v10
	v_mul_f32_e32 v144, 0x38808081, v144
	v_mul_f32_e32 v10, v122, v10
	v_mul_f32_e32 v144, v123, v144
	v_max_f32_e32 v6, 0.5, v6
	v_mul_f32_e32 v146, 0x38808081, v6
	v_med3_f32 v10, v10, s60, v200
	v_med3_f32 v144, v144, s60, v200
	v_mov_b32_e32 v6, v11
	v_max_f32_e32 v145, 0.5, v145
	v_cvt_pk_fp8_f32 v6, v10, v144
	v_mul_f32_e32 v145, 0x38808081, v145
	v_mul_f32_e32 v145, v124, v145
	v_mul_f32_e32 v10, v125, v146
	v_med3_f32 v144, v145, s60, v200
	v_med3_f32 v10, v10, s60, v200
	v_cvt_pk_fp8_f32 v6, v144, v10 op_sel:[0,0,1]
	v_cvt_f32_ubyte0_e32 v10, v7
	v_cvt_f32_ubyte1_e32 v144, v7
	v_max_f32_e32 v10, 0.5, v10
	v_max_f32_e32 v144, 0.5, v144
	v_cvt_f32_ubyte2_e32 v145, v7
	v_cvt_f32_ubyte3_e32 v7, v7
	v_mul_f32_e32 v10, 0x38808081, v10
	v_mul_f32_e32 v144, 0x38808081, v144
	v_mul_f32_e32 v10, v118, v10
; __device__ __forceinline__ f32x4 u8x4_f32(unsigned w) { return (f32x4){(float)(w & 0xffu), (float)((w >> 8) & 0xffu), (float)((w >> 16) & 0xffu), (float)(w >> 24)}; }
; __device__ __forceinline__ unsigned pk4_fp8(float a, float b, float c, float d) { int w = 0; w = __builtin_amdgcn_cvt_pk_fp8_f32(clamp8(a), clamp8(b), w, false); w = __builtin_amdgcn_cvt_pk_fp8_f32(clamp8(c), clamp8(d), w, true); return (unsigned)w; }
; __host__ __device__ __forceinline__ size_t tiled_off(size_t r, int kb, int ktiles) { return (((r >> 8) * ktiles + (kb >> 7)) << 15) + ((r & 255) << 7) + (kb & 127); }
;     __device__ __forceinline__ void operator()(f32x4 (&acc)[2][2][4][2], const GUnit& u, int wr, int wc, int fr, int fq) const {
;     ...
;         for (int ai = 0; ai < 2; ++ai) {
;             u32x4 qf[4];
; #pragma unroll
;             for (int m = 0; m < 4; ++m) qf[m] = __builtin_nontemporal_load((const u32x4*)(GZF + off0 + (size_t)(ai * 128 + m * 16) * D));
; #pragma unroll
;             for (int m = 0; m < 4; ++m) { u32x4 w;
; #pragma unroll
;                 for (int q = 0; q < 4; ++q) { const f32x4 f = u8x4_f32(qf[m][q]); const f32x4 a = acc[ai][q >> 1][m][q & 1]; f32x4 v;
; #pragma unroll
;                     for (int j = 0; j < 4; ++j) v[j] = a[j] * (fmaxf(f[j], 0.5f) * (W8_INV / 255.0f));
;                     w[q] = pk4_fp8(v[0], v[1], v[2], v[3]); }
;                 *(u32x4*)(M8 + tiled_off((size_t)(u.x0 * 256 + wr * 64 + fr + ai * 128 + m * 16), u.x1 * 256 + wc * 64 + 16 * fq, D / 128)) = w; }
	v_mul_f32_e32 v144, v119, v144
	v_max_f32_e32 v7, 0.5, v7
	v_mul_f32_e32 v146, 0x38808081, v7
	v_med3_f32 v10, v10, s60, v200
	v_med3_f32 v144, v144, s60, v200
	v_mov_b32_e32 v7, v11
	v_max_f32_e32 v145, 0.5, v145
	v_cvt_pk_fp8_f32 v7, v10, v144
	v_mul_f32_e32 v145, 0x38808081, v145
	v_mul_f32_e32 v145, v120, v145
	v_mul_f32_e32 v10, v121, v146
	v_med3_f32 v144, v145, s60, v200
	v_med3_f32 v10, v10, s60, v200
	v_cvt_pk_fp8_f32 v7, v144, v10 op_sel:[0,0,1]
	v_cvt_f32_ubyte0_e32 v10, v8
	v_cvt_f32_ubyte1_e32 v144, v8
	v_max_f32_e32 v10, 0.5, v10
	v_max_f32_e32 v144, 0.5, v144
	v_cvt_f32_ubyte2_e32 v145, v8
	v_cvt_f32_ubyte3_e32 v8, v8
	v_mul_f32_e32 v10, 0x38808081, v10
	v_mul_f32_e32 v144, 0x38808081, v144
	v_mul_f32_e32 v10, v90, v10
	v_mul_f32_e32 v144, v91, v144
	v_max_f32_e32 v8, 0.5, v8
	v_mul_f32_e32 v146, 0x38808081, v8
	v_med3_f32 v10, v10, s60, v200
	v_med3_f32 v144, v144, s60, v200
	v_mov_b32_e32 v8, v11
	v_max_f32_e32 v145, 0.5, v145
	v_cvt_pk_fp8_f32 v8, v10, v144
	v_mul_f32_e32 v145, 0x38808081, v145
	v_mul_f32_e32 v145, v92, v145
	v_mul_f32_e32 v10, v93, v146
	v_med3_f32 v144, v145, s60, v200
	v_med3_f32 v10, v10, s60, v200
	v_cvt_pk_fp8_f32 v8, v144, v10 op_sel:[0,0,1]
	v_cvt_f32_ubyte0_e32 v10, v9
	v_cvt_f32_ubyte1_e32 v144, v9
	v_max_f32_e32 v10, 0.5, v10
	v_max_f32_e32 v144, 0.5, v144
	v_cvt_f32_ubyte2_e32 v145, v9
	v_cvt_f32_ubyte3_e32 v9, v9
	v_mul_f32_e32 v10, 0x38808081, v10
	v_mul_f32_e32 v144, 0x38808081, v144
	v_mul_f32_e32 v10, v86, v10
	v_mul_f32_e32 v144, v87, v144
	v_max_f32_e32 v9, 0.5, v9
	v_mul_f32_e32 v146, 0x38808081, v9
	v_med3_f32 v10, v10, s60, v200
	v_med3_f32 v144, v144, s60, v200
	v_mov_b32_e32 v9, v11
	v_max_f32_e32 v145, 0.5, v145
	v_cvt_pk_fp8_f32 v9, v10, v144
	v_mul_f32_e32 v145, 0x38808081, v145
	v_mul_f32_e32 v145, v88, v145
	v_mul_f32_e32 v10, v89, v146
	v_med3_f32 v144, v145, s60, v200
	v_med3_f32 v10, v10, s60, v200
	v_cvt_pk_fp8_f32 v9, v144, v10 op_sel:[0,0,1]
	v_add_u32_e32 v144, s28, v192
	v_ashrrev_i32_e32 v145, 31, v144
	v_lshrrev_b64 v[146:147], 4, v[144:145]
	v_and_b32_e32 v147, 0x1ffff, v147
	v_and_b32_e32 v146, -16, v146
	v_lshl_add_u64 v[146:147], v[146:147], 0, s[26:27]
	v_lshlrev_b64 v[146:147], 15, v[146:147]
	v_lshlrev_b32_e32 v10, 7, v144
	v_and_b32_e32 v10, 0x7f80, v10
	v_lshl_add_u64 v[144:145], s[12:13], 0, v[146:147]
	v_lshl_add_u64 v[144:145], v[144:145], 0, v[10:11]
	v_lshl_add_u64 v[144:145], v[144:145], 0, v[178:179]
	flat_store_dwordx4 v[144:145], v[6:9]
	s_nop 1
	v_cvt_f32_ubyte0_e32 v6, v2
	v_cvt_f32_ubyte1_e32 v7, v2
	v_max_f32_e32 v6, 0.5, v6
	v_max_f32_e32 v7, 0.5, v7
	v_cvt_f32_ubyte2_e32 v8, v2
	v_cvt_f32_ubyte3_e32 v2, v2
	v_mul_f32_e32 v6, 0x38808081, v6
	v_mul_f32_e32 v7, 0x38808081, v7
	v_mul_f32_e32 v6, v114, v6
	v_mul_f32_e32 v7, v115, v7
	v_max_f32_e32 v2, 0.5, v2
	v_mul_f32_e32 v9, 0x38808081, v2
	v_med3_f32 v6, v6, s60, v200
	v_med3_f32 v7, v7, s60, v200
	v_mov_b32_e32 v2, v11
	v_max_f32_e32 v8, 0.5, v8
	v_cvt_pk_fp8_f32 v2, v6, v7
	v_mul_f32_e32 v8, 0x38808081, v8
	v_mul_f32_e32 v8, v116, v8
	v_mul_f32_e32 v6, v117, v9
	v_med3_f32 v7, v8, s60, v200
	v_med3_f32 v6, v6, s60, v200
	v_cvt_pk_fp8_f32 v2, v7, v6 op_sel:[0,0,1]
	v_cvt_f32_ubyte0_e32 v6, v3
	v_cvt_f32_ubyte1_e32 v7, v3
	v_max_f32_e32 v6, 0.5, v6
	v_max_f32_e32 v7, 0.5, v7
	v_cvt_f32_ubyte2_e32 v8, v3
	v_cvt_f32_ubyte3_e32 v3, v3
	v_mul_f32_e32 v6, 0x38808081, v6
	v_mul_f32_e32 v7, 0x38808081, v7
	v_mul_f32_e32 v6, v110, v6
	v_mul_f32_e32 v7, v111, v7
	v_max_f32_e32 v3, 0.5, v3
	v_mul_f32_e32 v9, 0x38808081, v3
	v_med3_f32 v6, v6, s60, v200
	v_med3_f32 v7, v7, s60, v200
	v_mov_b32_e32 v3, v11
	v_max_f32_e32 v8, 0.5, v8
	v_cvt_pk_fp8_f32 v3, v6, v7
	v_mul_f32_e32 v8, 0x38808081, v8
	v_mul_f32_e32 v8, v112, v8
	v_mul_f32_e32 v6, v113, v9
	v_med3_f32 v7, v8, s60, v200
	v_med3_f32 v6, v6, s60, v200
	v_cvt_pk_fp8_f32 v3, v7, v6 op_sel:[0,0,1]
	v_cvt_f32_ubyte0_e32 v6, v4
	v_cvt_f32_ubyte1_e32 v7, v4
	v_max_f32_e32 v6, 0.5, v6
	v_max_f32_e32 v7, 0.5, v7
	v_cvt_f32_ubyte2_e32 v8, v4
	v_cvt_f32_ubyte3_e32 v4, v4
	v_mul_f32_e32 v6, 0x38808081, v6
	v_mul_f32_e32 v7, 0x38808081, v7
	v_mul_f32_e32 v6, v82, v6
	v_mul_f32_e32 v7, v83, v7
	v_max_f32_e32 v4, 0.5, v4
	v_mul_f32_e32 v9, 0x38808081, v4
	v_med3_f32 v6, v6, s60, v200
	v_med3_f32 v7, v7, s60, v200
	v_mov_b32_e32 v4, v11
	v_max_f32_e32 v8, 0.5, v8
	v_cvt_pk_fp8_f32 v4, v6, v7
	v_mul_f32_e32 v8, 0x38808081, v8
	v_mul_f32_e32 v8, v84, v8
	v_mul_f32_e32 v6, v85, v9
	v_med3_f32 v7, v8, s60, v200
	v_med3_f32 v6, v6, s60, v200
	v_cvt_pk_fp8_f32 v4, v7, v6 op_sel:[0,0,1]
	v_cvt_f32_ubyte0_e32 v6, v5
	v_cvt_f32_ubyte1_e32 v7, v5
	v_max_f32_e32 v6, 0.5, v6
	v_max_f32_e32 v7, 0.5, v7
	v_cvt_f32_ubyte2_e32 v8, v5
	v_cvt_f32_ubyte3_e32 v5, v5
	v_mul_f32_e32 v6, 0x38808081, v6
	v_mul_f32_e32 v7, 0x38808081, v7
	v_mul_f32_e32 v6, v78, v6
	v_mul_f32_e32 v7, v79, v7
	v_max_f32_e32 v5, 0.5, v5
	v_mul_f32_e32 v9, 0x38808081, v5
	v_med3_f32 v6, v6, s60, v200
	v_med3_f32 v7, v7, s60, v200
	v_mov_b32_e32 v5, v11
	v_max_f32_e32 v8, 0.5, v8
	v_cvt_pk_fp8_f32 v5, v6, v7
	v_mul_f32_e32 v8, 0x38808081, v8
	v_mul_f32_e32 v8, v80, v8
	v_mul_f32_e32 v6, v81, v9
	v_med3_f32 v7, v8, s60, v200
	v_med3_f32 v6, v6, s60, v200
	v_cvt_pk_fp8_f32 v5, v7, v6 op_sel:[0,0,1]
	v_add_u32_e32 v6, s28, v193
	v_ashrrev_i32_e32 v7, 31, v6
	v_lshrrev_b64 v[8:9], 4, v[6:7]
	v_and_b32_e32 v9, 0x1ffff, v9
	v_and_b32_e32 v8, -16, v8
	v_lshl_add_u64 v[8:9], v[8:9], 0, s[26:27]
	v_lshlrev_b64 v[8:9], 15, v[8:9]
	v_lshlrev_b32_e32 v6, 7, v6
	v_and_b32_e32 v10, 0x7f80, v6
	v_lshl_add_u64 v[6:7], s[12:13], 0, v[8:9]
	v_lshl_add_u64 v[6:7], v[6:7], 0, v[10:11]
	v_lshl_add_u64 v[6:7], v[6:7], 0, v[178:179]
	flat_store_dwordx4 v[6:7], v[2:5]
	s_nop 1
	v_add_co_u32_e32 v2, vcc, s61, v12
	s_nop 1
	v_addc_co_u32_e32 v3, vcc, 0, v13, vcc
	flat_load_dwordx4 v[144:147], v[2:3] nt
	v_add_co_u32_e32 v2, vcc, s62, v12
	s_waitcnt vmcnt(0) lgkmcnt(0)
; __device__ __forceinline__ f32x4 u8x4_f32(unsigned w) { return (f32x4){(float)(w & 0xffu), (float)((w >> 8) & 0xffu), (float)((w >> 16) & 0xffu), (float)(w >> 24)}; }
; __device__ __forceinline__ unsigned pk4_fp8(float a, float b, float c, float d) { int w = 0; w = __builtin_amdgcn_cvt_pk_fp8_f32(clamp8(a), clamp8(b), w, false); w = __builtin_amdgcn_cvt_pk_fp8_f32(clamp8(c), clamp8(d), w, true); return (unsigned)w; }
; __host__ __device__ __forceinline__ size_t tiled_off(size_t r, int kb, int ktiles) { return (((r >> 8) * ktiles + (kb >> 7)) << 15) + ((r & 255) << 7) + (kb & 127); }
;     __device__ __forceinline__ void operator()(f32x4 (&acc)[2][2][4][2], const GUnit& u, int wr, int wc, int fr, int fq) const {
;     ...
;             for (int m = 0; m < 4; ++m) qf[m] = __builtin_nontemporal_load((const u32x4*)(GZF + off0 + (size_t)(ai * 128 + m * 16) * D));
; #pragma unroll
;             for (int m = 0; m < 4; ++m) { u32x4 w;
; #pragma unroll
;                 for (int q = 0; q < 4; ++q) { const f32x4 f = u8x4_f32(qf[m][q]); const f32x4 a = acc[ai][q >> 1][m][q & 1]; f32x4 v;
; #pragma unroll
;                     for (int j = 0; j < 4; ++j) v[j] = a[j] * (fmaxf(f[j], 0.5f) * (W8_INV / 255.0f));
;                     w[q] = pk4_fp8(v[0], v[1], v[2], v[3]); }
;                 *(u32x4*)(M8 + tiled_off((size_t)(u.x0 * 256 + wr * 64 + fr + ai * 128 + m * 16), u.x1 * 256 + wc * 64 + 16 * fq, D / 128)) = w; }
	v_cvt_f32_ubyte0_e32 v10, v144
	v_addc_co_u32_e32 v3, vcc, 0, v13, vcc
	flat_load_dwordx4 v[148:151], v[2:3] nt
	v_cvt_f32_ubyte1_e32 v152, v144
	v_max_f32_e32 v10, 0.5, v10
	v_max_f32_e32 v152, 0.5, v152
	v_cvt_f32_ubyte2_e32 v153, v144
	v_cvt_f32_ubyte3_e32 v144, v144
	v_mul_f32_e32 v10, 0x38808081, v10
	v_mul_f32_e32 v152, 0x38808081, v152
	v_mul_f32_e32 v10, v74, v10
	v_mul_f32_e32 v152, v75, v152
	v_max_f32_e32 v144, 0.5, v144
	v_mul_f32_e32 v154, 0x38808081, v144
	v_med3_f32 v10, v10, s60, v200
	v_med3_f32 v152, v152, s60, v200
	v_mov_b32_e32 v144, v11
	v_max_f32_e32 v153, 0.5, v153
	v_cvt_pk_fp8_f32 v144, v10, v152
	v_mul_f32_e32 v153, 0x38808081, v153
	v_add_co_u32_e32 v2, vcc, s63, v12
	v_mul_f32_e32 v153, v76, v153
	v_mul_f32_e32 v10, v77, v154
	v_addc_co_u32_e32 v3, vcc, 0, v13, vcc
	v_med3_f32 v152, v153, s60, v200
	v_med3_f32 v10, v10, s60, v200
	v_add_co_u32_e32 v4, vcc, s64, v12
	v_cvt_pk_fp8_f32 v144, v152, v10 op_sel:[0,0,1]
	v_cvt_f32_ubyte0_e32 v10, v145
	v_cvt_f32_ubyte1_e32 v152, v145
	v_addc_co_u32_e32 v5, vcc, 0, v13, vcc
	v_max_f32_e32 v10, 0.5, v10
	v_max_f32_e32 v152, 0.5, v152
	flat_load_dwordx4 v[6:9], v[2:3] nt
	s_nop 0
	flat_load_dwordx4 v[2:5], v[4:5] nt
	v_cvt_f32_ubyte2_e32 v153, v145
	v_cvt_f32_ubyte3_e32 v145, v145
	v_mul_f32_e32 v10, 0x38808081, v10
	v_mul_f32_e32 v152, 0x38808081, v152
	v_mul_f32_e32 v10, v70, v10
	v_mul_f32_e32 v152, v71, v152
	v_max_f32_e32 v145, 0.5, v145
	v_mul_f32_e32 v154, 0x38808081, v145
	v_med3_f32 v10, v10, s60, v200
	v_med3_f32 v152, v152, s60, v200
	v_mov_b32_e32 v145, v11
	v_max_f32_e32 v153, 0.5, v153
	v_cvt_pk_fp8_f32 v145, v10, v152
	v_mul_f32_e32 v153, 0x38808081, v153
	v_mul_f32_e32 v153, v72, v153
	v_mul_f32_e32 v10, v73, v154
	v_med3_f32 v152, v153, s60, v200
	v_med3_f32 v10, v10, s60, v200
	v_cvt_pk_fp8_f32 v145, v152, v10 op_sel:[0,0,1]
	v_cvt_f32_ubyte0_e32 v10, v146
	v_cvt_f32_ubyte1_e32 v152, v146
	v_max_f32_e32 v10, 0.5, v10
	v_max_f32_e32 v152, 0.5, v152
	v_cvt_f32_ubyte2_e32 v153, v146
	v_cvt_f32_ubyte3_e32 v146, v146
	v_mul_f32_e32 v10, 0x38808081, v10
	v_mul_f32_e32 v152, 0x38808081, v152
	v_mul_f32_e32 v10, v42, v10
	v_mul_f32_e32 v152, v43, v152
	v_max_f32_e32 v146, 0.5, v146
	v_mul_f32_e32 v154, 0x38808081, v146
	v_med3_f32 v10, v10, s60, v200
	v_med3_f32 v152, v152, s60, v200
	v_mov_b32_e32 v146, v11
	v_max_f32_e32 v153, 0.5, v153
	v_cvt_pk_fp8_f32 v146, v10, v152
	v_mul_f32_e32 v153, 0x38808081, v153
	v_mul_f32_e32 v153, v44, v153
	v_mul_f32_e32 v10, v45, v154
	v_med3_f32 v152, v153, s60, v200
	v_med3_f32 v10, v10, s60, v200
	v_cvt_pk_fp8_f32 v146, v152, v10 op_sel:[0,0,1]
	v_cvt_f32_ubyte0_e32 v10, v147
	v_cvt_f32_ubyte1_e32 v152, v147
	v_max_f32_e32 v10, 0.5, v10
	v_max_f32_e32 v152, 0.5, v152
	v_cvt_f32_ubyte2_e32 v153, v147
	v_cvt_f32_ubyte3_e32 v147, v147
	v_mul_f32_e32 v10, 0x38808081, v10
	v_mul_f32_e32 v152, 0x38808081, v152
	v_mul_f32_e32 v10, v38, v10
	v_mul_f32_e32 v152, v39, v152
	v_max_f32_e32 v147, 0.5, v147
	v_mul_f32_e32 v154, 0x38808081, v147
	v_med3_f32 v10, v10, s60, v200
	v_med3_f32 v152, v152, s60, v200
	v_mov_b32_e32 v147, v11
	v_max_f32_e32 v153, 0.5, v153
	v_cvt_pk_fp8_f32 v147, v10, v152
	v_mul_f32_e32 v153, 0x38808081, v153
	v_mul_f32_e32 v153, v40, v153
	v_mul_f32_e32 v10, v41, v154
	v_med3_f32 v152, v153, s60, v200
	v_med3_f32 v10, v10, s60, v200
	v_cvt_pk_fp8_f32 v147, v152, v10 op_sel:[0,0,1]
	v_add_u32_e32 v152, s28, v194
	v_ashrrev_i32_e32 v153, 31, v152
	v_lshrrev_b64 v[154:155], 4, v[152:153]
	v_and_b32_e32 v155, 0x1ffff, v155
	v_and_b32_e32 v154, -16, v154
	v_lshl_add_u64 v[154:155], v[154:155], 0, s[26:27]
	v_lshlrev_b64 v[154:155], 15, v[154:155]
	v_lshlrev_b32_e32 v10, 7, v152
	v_and_b32_e32 v10, 0x7f80, v10
	v_lshl_add_u64 v[152:153], s[12:13], 0, v[154:155]
	v_lshl_add_u64 v[152:153], v[152:153], 0, v[10:11]
	v_lshl_add_u64 v[152:153], v[152:153], 0, v[178:179]
	flat_store_dwordx4 v[152:153], v[144:147]
	s_waitcnt vmcnt(0) lgkmcnt(0)
	v_cvt_f32_ubyte0_e32 v10, v148
	v_max_f32_e32 v10, 0.5, v10
	v_cvt_f32_ubyte1_e32 v144, v148
	v_max_f32_e32 v144, 0.5, v144
	v_mul_f32_e32 v10, 0x38808081, v10
	v_mul_f32_e32 v144, 0x38808081, v144
	v_mul_f32_e32 v10, v66, v10
	v_mul_f32_e32 v144, v67, v144
	v_cvt_f32_ubyte2_e32 v145, v148
	v_cvt_f32_ubyte3_e32 v146, v148
	v_med3_f32 v10, v10, s60, v200
	v_med3_f32 v147, v144, s60, v200
	v_mov_b32_e32 v144, v11
	v_max_f32_e32 v145, 0.5, v145
	v_max_f32_e32 v146, 0.5, v146
	v_cvt_pk_fp8_f32 v144, v10, v147
	v_mul_f32_e32 v145, 0x38808081, v145
	v_mul_f32_e32 v146, 0x38808081, v146
	v_mul_f32_e32 v145, v68, v145
	v_mul_f32_e32 v10, v69, v146
	v_med3_f32 v145, v145, s60, v200
	v_med3_f32 v10, v10, s60, v200
	v_cvt_pk_fp8_f32 v144, v145, v10 op_sel:[0,0,1]
	v_cvt_f32_ubyte0_e32 v10, v149
	v_cvt_f32_ubyte1_e32 v145, v149
	v_max_f32_e32 v10, 0.5, v10
	v_max_f32_e32 v145, 0.5, v145
	v_mul_f32_e32 v10, 0x38808081, v10
	v_mul_f32_e32 v145, 0x38808081, v145
	v_mul_f32_e32 v10, v62, v10
	v_mul_f32_e32 v145, v63, v145
	v_cvt_f32_ubyte2_e32 v146, v149
	v_cvt_f32_ubyte3_e32 v147, v149
	v_med3_f32 v10, v10, s60, v200
	v_med3_f32 v148, v145, s60, v200
	v_mov_b32_e32 v145, v11
	v_max_f32_e32 v146, 0.5, v146
	v_max_f32_e32 v147, 0.5, v147
	v_cvt_pk_fp8_f32 v145, v10, v148
	v_mul_f32_e32 v146, 0x38808081, v146
	v_mul_f32_e32 v147, 0x38808081, v147
	v_mul_f32_e32 v146, v64, v146
	v_mul_f32_e32 v10, v65, v147
	v_med3_f32 v146, v146, s60, v200
	v_med3_f32 v10, v10, s60, v200
	v_cvt_pk_fp8_f32 v145, v146, v10 op_sel:[0,0,1]
	v_cvt_f32_ubyte0_e32 v10, v150
	v_cvt_f32_ubyte1_e32 v146, v150
	v_max_f32_e32 v10, 0.5, v10
	v_max_f32_e32 v146, 0.5, v146
	v_mul_f32_e32 v10, 0x38808081, v10
; __device__ __forceinline__ f32x4 u8x4_f32(unsigned w) { return (f32x4){(float)(w & 0xffu), (float)((w >> 8) & 0xffu), (float)((w >> 16) & 0xffu), (float)(w >> 24)}; }
; __device__ __forceinline__ unsigned pk4_fp8(float a, float b, float c, float d) { int w = 0; w = __builtin_amdgcn_cvt_pk_fp8_f32(clamp8(a), clamp8(b), w, false); w = __builtin_amdgcn_cvt_pk_fp8_f32(clamp8(c), clamp8(d), w, true); return (unsigned)w; }
; __host__ __device__ __forceinline__ size_t tiled_off(size_t r, int kb, int ktiles) { return (((r >> 8) * ktiles + (kb >> 7)) << 15) + ((r & 255) << 7) + (kb & 127); }
;     __device__ __forceinline__ void operator()(f32x4 (&acc)[2][2][4][2], const GUnit& u, int wr, int wc, int fr, int fq) const {
;     ...
;             for (int m = 0; m < 4; ++m) { u32x4 w;
; #pragma unroll
;                 for (int q = 0; q < 4; ++q) { const f32x4 f = u8x4_f32(qf[m][q]); const f32x4 a = acc[ai][q >> 1][m][q & 1]; f32x4 v;
; #pragma unroll
;                     for (int j = 0; j < 4; ++j) v[j] = a[j] * (fmaxf(f[j], 0.5f) * (W8_INV / 255.0f));
;                     w[q] = pk4_fp8(v[0], v[1], v[2], v[3]); }
;                 *(u32x4*)(M8 + tiled_off((size_t)(u.x0 * 256 + wr * 64 + fr + ai * 128 + m * 16), u.x1 * 256 + wc * 64 + 16 * fq, D / 128)) = w; }
	v_mul_f32_e32 v146, 0x38808081, v146
	v_mul_f32_e32 v10, v34, v10
	v_mul_f32_e32 v146, v35, v146
	v_cvt_f32_ubyte2_e32 v147, v150
	v_cvt_f32_ubyte3_e32 v148, v150
	v_med3_f32 v10, v10, s60, v200
	v_med3_f32 v149, v146, s60, v200
	v_mov_b32_e32 v146, v11
	v_max_f32_e32 v147, 0.5, v147
	v_max_f32_e32 v148, 0.5, v148
	v_cvt_pk_fp8_f32 v146, v10, v149
	v_mul_f32_e32 v147, 0x38808081, v147
	v_mul_f32_e32 v148, 0x38808081, v148
	v_mul_f32_e32 v147, v36, v147
	v_mul_f32_e32 v10, v37, v148
	v_med3_f32 v147, v147, s60, v200
	v_med3_f32 v10, v10, s60, v200
	v_cvt_pk_fp8_f32 v146, v147, v10 op_sel:[0,0,1]
	v_cvt_f32_ubyte0_e32 v10, v151
	v_cvt_f32_ubyte1_e32 v147, v151
	v_max_f32_e32 v10, 0.5, v10
	v_max_f32_e32 v147, 0.5, v147
	v_mul_f32_e32 v10, 0x38808081, v10
	v_mul_f32_e32 v147, 0x38808081, v147
	v_mul_f32_e32 v10, v30, v10
	v_mul_f32_e32 v147, v31, v147
	v_cvt_f32_ubyte2_e32 v148, v151
	v_cvt_f32_ubyte3_e32 v149, v151
	v_med3_f32 v10, v10, s60, v200
	v_med3_f32 v150, v147, s60, v200
	v_mov_b32_e32 v147, v11
	v_max_f32_e32 v148, 0.5, v148
	v_max_f32_e32 v149, 0.5, v149
	v_cvt_pk_fp8_f32 v147, v10, v150
	v_mul_f32_e32 v148, 0x38808081, v148
	v_mul_f32_e32 v149, 0x38808081, v149
	v_mul_f32_e32 v148, v32, v148
	v_mul_f32_e32 v10, v33, v149
	v_med3_f32 v148, v148, s60, v200
	v_med3_f32 v10, v10, s60, v200
	v_cvt_pk_fp8_f32 v147, v148, v10 op_sel:[0,0,1]
	v_add_u32_e32 v148, s28, v195
	v_ashrrev_i32_e32 v149, 31, v148
	v_lshrrev_b64 v[150:151], 4, v[148:149]
	v_and_b32_e32 v151, 0x1ffff, v151
	v_and_b32_e32 v150, -16, v150
	v_lshl_add_u64 v[150:151], v[150:151], 0, s[26:27]
	v_lshlrev_b64 v[150:151], 15, v[150:151]
	v_lshlrev_b32_e32 v10, 7, v148
	v_and_b32_e32 v10, 0x7f80, v10
	v_lshl_add_u64 v[148:149], s[12:13], 0, v[150:151]
	v_lshl_add_u64 v[148:149], v[148:149], 0, v[10:11]
	v_lshl_add_u64 v[148:149], v[148:149], 0, v[178:179]
	flat_store_dwordx4 v[148:149], v[144:147]
	v_cvt_f32_ubyte0_e32 v10, v6
	v_max_f32_e32 v10, 0.5, v10
	v_cvt_f32_ubyte1_e32 v144, v6
	v_max_f32_e32 v144, 0.5, v144
	v_cvt_f32_ubyte2_e32 v145, v6
	v_cvt_f32_ubyte3_e32 v6, v6
	v_mul_f32_e32 v10, 0x38808081, v10
	v_mul_f32_e32 v144, 0x38808081, v144
	v_mul_f32_e32 v10, v58, v10
	v_mul_f32_e32 v144, v59, v144
	v_max_f32_e32 v6, 0.5, v6
	v_mul_f32_e32 v146, 0x38808081, v6
	v_med3_f32 v10, v10, s60, v200
	v_med3_f32 v144, v144, s60, v200
	v_mov_b32_e32 v6, v11
	v_max_f32_e32 v145, 0.5, v145
	v_cvt_pk_fp8_f32 v6, v10, v144
	v_mul_f32_e32 v145, 0x38808081, v145
	v_mul_f32_e32 v145, v60, v145
	v_mul_f32_e32 v10, v61, v146
	v_med3_f32 v144, v145, s60, v200
	v_med3_f32 v10, v10, s60, v200
	v_cvt_pk_fp8_f32 v6, v144, v10 op_sel:[0,0,1]
	v_cvt_f32_ubyte0_e32 v10, v7
	v_cvt_f32_ubyte1_e32 v144, v7
	v_max_f32_e32 v10, 0.5, v10
	v_max_f32_e32 v144, 0.5, v144
	v_cvt_f32_ubyte2_e32 v145, v7
	v_cvt_f32_ubyte3_e32 v7, v7
	v_mul_f32_e32 v10, 0x38808081, v10
	v_mul_f32_e32 v144, 0x38808081, v144
	v_mul_f32_e32 v10, v54, v10
	v_mul_f32_e32 v144, v55, v144
	v_max_f32_e32 v7, 0.5, v7
	v_mul_f32_e32 v146, 0x38808081, v7
	v_med3_f32 v10, v10, s60, v200
	v_med3_f32 v144, v144, s60, v200
	v_mov_b32_e32 v7, v11
	v_max_f32_e32 v145, 0.5, v145
	v_cvt_pk_fp8_f32 v7, v10, v144
	v_mul_f32_e32 v145, 0x38808081, v145
	v_mul_f32_e32 v145, v56, v145
	v_mul_f32_e32 v10, v57, v146
	v_med3_f32 v144, v145, s60, v200
	v_med3_f32 v10, v10, s60, v200
	v_cvt_pk_fp8_f32 v7, v144, v10 op_sel:[0,0,1]
	v_cvt_f32_ubyte0_e32 v10, v8
	v_cvt_f32_ubyte1_e32 v144, v8
	v_max_f32_e32 v10, 0.5, v10
	v_max_f32_e32 v144, 0.5, v144
	v_cvt_f32_ubyte2_e32 v145, v8
	v_cvt_f32_ubyte3_e32 v8, v8
	v_mul_f32_e32 v10, 0x38808081, v10
	v_mul_f32_e32 v144, 0x38808081, v144
	v_mul_f32_e32 v10, v26, v10
	v_mul_f32_e32 v144, v27, v144
	v_max_f32_e32 v8, 0.5, v8
	v_mul_f32_e32 v146, 0x38808081, v8
	v_med3_f32 v10, v10, s60, v200
	v_med3_f32 v144, v144, s60, v200
	v_mov_b32_e32 v8, v11
	v_max_f32_e32 v145, 0.5, v145
	v_cvt_pk_fp8_f32 v8, v10, v144
	v_mul_f32_e32 v145, 0x38808081, v145
	v_mul_f32_e32 v145, v28, v145
	v_mul_f32_e32 v10, v29, v146
	v_med3_f32 v144, v145, s60, v200
	v_med3_f32 v10, v10, s60, v200
	v_cvt_pk_fp8_f32 v8, v144, v10 op_sel:[0,0,1]
	v_cvt_f32_ubyte0_e32 v10, v9
	v_cvt_f32_ubyte1_e32 v144, v9
	v_max_f32_e32 v10, 0.5, v10
	v_max_f32_e32 v144, 0.5, v144
	v_cvt_f32_ubyte2_e32 v145, v9
	v_cvt_f32_ubyte3_e32 v9, v9
; __device__ __forceinline__ f32x4 u8x4_f32(unsigned w) { return (f32x4){(float)(w & 0xffu), (float)((w >> 8) & 0xffu), (float)((w >> 16) & 0xffu), (float)(w >> 24)}; }
; __device__ __forceinline__ unsigned pk4_fp8(float a, float b, float c, float d) { int w = 0; w = __builtin_amdgcn_cvt_pk_fp8_f32(clamp8(a), clamp8(b), w, false); w = __builtin_amdgcn_cvt_pk_fp8_f32(clamp8(c), clamp8(d), w, true); return (unsigned)w; }
; __host__ __device__ __forceinline__ size_t tiled_off(size_t r, int kb, int ktiles) { return (((r >> 8) * ktiles + (kb >> 7)) << 15) + ((r & 255) << 7) + (kb & 127); }
;     __device__ __forceinline__ void operator()(f32x4 (&acc)[2][2][4][2], const GUnit& u, int wr, int wc, int fr, int fq) const {
;     ...
;             for (int m = 0; m < 4; ++m) { u32x4 w;
; #pragma unroll
;                 for (int q = 0; q < 4; ++q) { const f32x4 f = u8x4_f32(qf[m][q]); const f32x4 a = acc[ai][q >> 1][m][q & 1]; f32x4 v;
; #pragma unroll
;                     for (int j = 0; j < 4; ++j) v[j] = a[j] * (fmaxf(f[j], 0.5f) * (W8_INV / 255.0f));
;                     w[q] = pk4_fp8(v[0], v[1], v[2], v[3]); }
;                 *(u32x4*)(M8 + tiled_off((size_t)(u.x0 * 256 + wr * 64 + fr + ai * 128 + m * 16), u.x1 * 256 + wc * 64 + 16 * fq, D / 128)) = w; }
	v_mul_f32_e32 v10, 0x38808081, v10
	v_mul_f32_e32 v144, 0x38808081, v144
	v_mul_f32_e32 v10, v22, v10
	v_mul_f32_e32 v144, v23, v144
	v_max_f32_e32 v9, 0.5, v9
	v_mul_f32_e32 v146, 0x38808081, v9
	v_med3_f32 v10, v10, s60, v200
	v_med3_f32 v144, v144, s60, v200
	v_mov_b32_e32 v9, v11
	v_max_f32_e32 v145, 0.5, v145
	v_cvt_pk_fp8_f32 v9, v10, v144
	v_mul_f32_e32 v145, 0x38808081, v145
	v_mul_f32_e32 v145, v24, v145
	v_mul_f32_e32 v10, v25, v146
	v_med3_f32 v144, v145, s60, v200
	v_med3_f32 v10, v10, s60, v200
	v_cvt_pk_fp8_f32 v9, v144, v10 op_sel:[0,0,1]
	v_add_u32_e32 v144, s28, v196
	v_ashrrev_i32_e32 v145, 31, v144
	v_lshrrev_b64 v[146:147], 4, v[144:145]
	v_and_b32_e32 v147, 0x1ffff, v147
	v_and_b32_e32 v146, -16, v146
	v_lshl_add_u64 v[146:147], v[146:147], 0, s[26:27]
	v_lshlrev_b64 v[146:147], 15, v[146:147]
	v_lshlrev_b32_e32 v10, 7, v144
	v_and_b32_e32 v10, 0x7f80, v10
	v_lshl_add_u64 v[144:145], s[12:13], 0, v[146:147]
	v_lshl_add_u64 v[144:145], v[144:145], 0, v[10:11]
	v_lshl_add_u64 v[144:145], v[144:145], 0, v[178:179]
	flat_store_dwordx4 v[144:145], v[6:9]
	s_nop 1
	v_cvt_f32_ubyte0_e32 v6, v2
	v_cvt_f32_ubyte1_e32 v7, v2
	v_max_f32_e32 v6, 0.5, v6
	v_max_f32_e32 v7, 0.5, v7
	v_cvt_f32_ubyte2_e32 v8, v2
	v_cvt_f32_ubyte3_e32 v2, v2
	v_mul_f32_e32 v6, 0x38808081, v6
	v_mul_f32_e32 v7, 0x38808081, v7
	v_mul_f32_e32 v6, v50, v6
	v_mul_f32_e32 v7, v51, v7
	v_max_f32_e32 v2, 0.5, v2
	v_mul_f32_e32 v9, 0x38808081, v2
	v_med3_f32 v6, v6, s60, v200
	v_med3_f32 v7, v7, s60, v200
	v_mov_b32_e32 v2, v11
	v_max_f32_e32 v8, 0.5, v8
	v_cvt_pk_fp8_f32 v2, v6, v7
	v_mul_f32_e32 v8, 0x38808081, v8
	v_mul_f32_e32 v8, v52, v8
	v_mul_f32_e32 v6, v53, v9
	v_med3_f32 v7, v8, s60, v200
	v_med3_f32 v6, v6, s60, v200
	v_cvt_pk_fp8_f32 v2, v7, v6 op_sel:[0,0,1]
	v_cvt_f32_ubyte0_e32 v6, v3
	v_cvt_f32_ubyte1_e32 v7, v3
	v_max_f32_e32 v6, 0.5, v6
	v_max_f32_e32 v7, 0.5, v7
	v_cvt_f32_ubyte2_e32 v8, v3
	v_cvt_f32_ubyte3_e32 v3, v3
	v_mul_f32_e32 v6, 0x38808081, v6
	v_mul_f32_e32 v7, 0x38808081, v7
	v_mul_f32_e32 v6, v46, v6
	v_mul_f32_e32 v7, v47, v7
	v_max_f32_e32 v3, 0.5, v3
	v_mul_f32_e32 v9, 0x38808081, v3
	v_med3_f32 v6, v6, s60, v200
	v_med3_f32 v7, v7, s60, v200
	v_mov_b32_e32 v3, v11
	v_max_f32_e32 v8, 0.5, v8
	v_cvt_pk_fp8_f32 v3, v6, v7
	v_mul_f32_e32 v8, 0x38808081, v8
	v_mul_f32_e32 v8, v48, v8
	v_mul_f32_e32 v6, v49, v9
	v_med3_f32 v7, v8, s60, v200
	v_med3_f32 v6, v6, s60, v200
	v_cvt_pk_fp8_f32 v3, v7, v6 op_sel:[0,0,1]
	v_cvt_f32_ubyte0_e32 v6, v4
	v_cvt_f32_ubyte1_e32 v7, v4
	v_max_f32_e32 v6, 0.5, v6
	v_max_f32_e32 v7, 0.5, v7
	v_cvt_f32_ubyte2_e32 v8, v4
	v_cvt_f32_ubyte3_e32 v4, v4
	v_mul_f32_e32 v6, 0x38808081, v6
	v_mul_f32_e32 v7, 0x38808081, v7
	v_mul_f32_e32 v6, v18, v6
	v_mul_f32_e32 v7, v19, v7
	v_max_f32_e32 v4, 0.5, v4
	v_mul_f32_e32 v9, 0x38808081, v4
	v_med3_f32 v6, v6, s60, v200
	v_med3_f32 v7, v7, s60, v200
	v_mov_b32_e32 v4, v11
	v_max_f32_e32 v8, 0.5, v8
	v_cvt_pk_fp8_f32 v4, v6, v7
	v_mul_f32_e32 v8, 0x38808081, v8
	v_mul_f32_e32 v8, v20, v8
	v_mul_f32_e32 v6, v21, v9
	v_med3_f32 v7, v8, s60, v200
	v_med3_f32 v6, v6, s60, v200
	v_cvt_pk_fp8_f32 v4, v7, v6 op_sel:[0,0,1]
	v_cvt_f32_ubyte0_e32 v6, v5
	v_cvt_f32_ubyte1_e32 v7, v5
	v_max_f32_e32 v6, 0.5, v6
	v_max_f32_e32 v7, 0.5, v7
	v_cvt_f32_ubyte2_e32 v8, v5
	v_cvt_f32_ubyte3_e32 v5, v5
	v_mul_f32_e32 v6, 0x38808081, v6
	v_mul_f32_e32 v7, 0x38808081, v7
	v_mul_f32_e32 v6, v14, v6
	v_mul_f32_e32 v7, v15, v7
	v_max_f32_e32 v5, 0.5, v5
	v_mul_f32_e32 v9, 0x38808081, v5
	v_med3_f32 v6, v6, s60, v200
	v_med3_f32 v7, v7, s60, v200
	v_mov_b32_e32 v5, v11
	v_max_f32_e32 v8, 0.5, v8
	v_cvt_pk_fp8_f32 v5, v6, v7
	v_mul_f32_e32 v8, 0x38808081, v8
	v_mul_f32_e32 v8, v16, v8
	v_mul_f32_e32 v6, v17, v9
	v_med3_f32 v7, v8, s60, v200
	v_med3_f32 v6, v6, s60, v200
	v_cvt_pk_fp8_f32 v5, v7, v6 op_sel:[0,0,1]
	v_add_u32_e32 v6, s28, v197
	v_ashrrev_i32_e32 v7, 31, v6
	v_lshrrev_b64 v[8:9], 4, v[6:7]
	v_and_b32_e32 v9, 0x1ffff, v9
	v_and_b32_e32 v8, -16, v8
	v_lshl_add_u64 v[8:9], v[8:9], 0, s[26:27]
	v_lshlrev_b64 v[8:9], 15, v[8:9]
	v_lshlrev_b32_e32 v6, 7, v6
	v_and_b32_e32 v10, 0x7f80, v6
	v_lshl_add_u64 v[6:7], s[12:13], 0, v[8:9]
	v_lshl_add_u64 v[6:7], v[6:7], 0, v[10:11]
	v_lshl_add_u64 v[6:7], v[6:7], 0, v[178:179]
	flat_store_dwordx4 v[6:7], v[2:5]
	s_cbranch_execnz .LBB0_840

; #define PG8_BAR __builtin_amdgcn_s_barrier()
; template <class Epi, class Sched, bool ALIGN_EPI = true, bool F8 = false>
; __device__ __forceinline__ void gemm_phase(PG8_LAS unsigned char* lds, const Sched& S, const Epi& E) {
;     ...
;         cur = nxt; cA = nA; cB = nB; ++ui;
; #pragma unroll
;         for (int h = 0; h < 2; ++h)
; #pragma unroll
;             for (int i = 0; i < 2; ++i) voffA[h][i] = voffAn[h][i];
;         if constexpr (ALIGN_EPI) { if (wr == 1) PG8_BAR; }
;     }
.LBB0_843:
	s_andn2_b64 vcc, exec, s[10:11]
	s_cbranch_vccnz .LBB0_825
	s_branch .LBB0_825

; #define PG8_STAGE(bufoff, gbase, voff) do { _Pragma("unroll") for (int _i = 0; _i < 2; ++_i) \
;         __builtin_amdgcn_global_load_lds((const unsigned*)((const char*)(gbase) + (voff)[_i]), (PG8_LAS unsigned*)(lds + (bufoff) + ldsw + _i * 8192), 16, 0, 0); } while (0)
; #define PG8_WAIT_V(n) asm volatile("s_waitcnt vmcnt(" #n ")" ::: "memory")
; #define PG8_BAR __builtin_amdgcn_s_barrier()
;     __device__ __forceinline__ unsigned b_off(int R, int C) const { return (unsigned)(R * ldb + C) * 2u; }
;     __device__ __forceinline__ unsigned b_off(int R, int C) const { return (unsigned)(R * 128 + C * 2); }
;     __device__ __forceinline__ unsigned b_off(int R, int C) const { return (unsigned)(R * ldb + C) * 2u; }
;     __device__ __forceinline__ unsigned b_off(int R, int C) const { return (unsigned)(R * 128 + C * 2); }
;     __device__ __forceinline__ unsigned b_off(int R, int C) const { return (unsigned)(R * 512 + C) * 2u; }
; template <class Epi, class Sched, bool ALIGN_EPI = true, bool F8 = false>
; __device__ __forceinline__ void gemm_phase(PG8_LAS unsigned char* lds, const Sched& S, const Epi& E) {
;     ...
;     for (int i = 0; i < 2; ++i) stage_rc(tid * 16 + i * 8192, Rs[i], Cs[i]);
;     unsigned voffB[2][2], voffA[2][2], voffAn[2][2];
; #pragma unroll
;     for (int h = 0; h < 2; ++h)
; #pragma unroll
;         for (int i = 0; i < 2; ++i) {
;             if constexpr (HasP16<Epi>::v) { const int r = Rs[i]; voffB[h][i] = S.b_off(64 * (r >> 5) + 16 * ((r & 15) >> 2) + 8 * h + 4 * ((r >> 4) & 1) + (r & 3), Cs[i]); }
;             else { const int Rb = Epi::PERM ? ((Rs[i] & ~31) + perm32(Rs[i] & 31)) : Rs[i]; voffB[h][i] = S.b_off(h * HALF + Rb, Cs[i]); } }
;     const size_t kstep = (size_t)SchedKstep<Sched>::v, kstepB = (size_t)SchedKstepB<Sched>::v;
;     const unsigned ldsw = (unsigned)wid * 1024u;
;     const int aoff = lds_byte(wr * 64 + fr, fq * 8), boff = lds_byte(wc * 32 + fr, fq * 8);
;     ...
;     const char* cA = cur.A; const char* cB = cur.B;
;     PG8_STAGE(PG8_SB(0, 0), cB, voffB[0]); PG8_STAGE(PG8_SB(0, 1), cB, voffB[1]); PG8_STAGE(PG8_SA(0, 0), cA, voffA[0]); PG8_STAGE(PG8_SA(0, 1), cA, voffA[1]);
;     if (wr == 1) PG8_BAR;
;     PG8_WAIT_V(2); PG8_BAR;
;     PG8_STAGE(PG8_SB(1, 0), cB + kstepB, voffB[0]); PG8_STAGE(PG8_SA(1, 0), cA + kstep, voffA[0]); PG8_STAGE(PG8_SB(1, 1), cB + kstepB, voffB[1]);
;     PG8_WAIT_V(6); PG8_BAR;
.LBB0_899:
	s_add_u32 s44, s36, 0x26000000
	s_addc_u32 s45, s37, 0
	s_add_u32 s46, s36, 0x3400000
	s_addc_u32 s47, s37, 0
	s_add_i32 s0, s6, s0
	s_ashr_i32 s6, s0, 31
	s_lshr_b32 s6, s6, 26
	s_add_i32 s6, s0, s6
	s_ashr_i32 s7, s6, 6
	s_and_b32 s6, s6, 0xffc0
	s_sub_i32 s6, s0, s6
	s_bfe_i32 s0, s6, 0x80000
	v_lshlrev_b32_e32 v2, 4, v0
	v_bfe_u32 v5, v0, 2, 4
	v_lshrrev_b32_e32 v6, 3, v0
	s_bfe_u32 s0, s0, 0x3000c
	v_and_or_b32 v10, v6, 48, v5
	v_or_b32_e32 v6, 0x2000, v2
	s_add_i32 s8, s6, s0
	v_lshrrev_b32_e32 v7, 7, v6
	s_movk_i32 s1, 0x70
	s_bfe_i32 s0, s8, 0x80000
	s_and_b32 s8, s8, 0xf8
	v_and_b32_e32 v3, 32, v0
	v_lshrrev_b32_e32 v8, 2, v0
	v_and_or_b32 v11, v7, s1, v5
	v_and_b32_e32 v7, 48, v0
	v_lshrrev_b32_e32 v12, 5, v0
	s_sub_i32 s6, s6, s8
	v_bitop3_b32 v3, v2, v3, 48 bitop3:0x6c
	v_and_b32_e32 v4, 64, v0
	v_and_b32_e32 v12, 4, v12
	v_bfe_u32 v13, v0, 2, 2
	v_and_or_b32 v8, v8, 64, v7
	s_lshl_b32 s7, s7, 3
	s_sext_i32_i8 s6, s6
	v_or_b32_e32 v9, v3, v4
	v_or3_b32 v8, v8, v12, v13
	s_add_i32 s26, s7, s6
	s_lshr_b32 s13, s12, 6
	v_lshl_or_b32 v162, v8, 7, v9
	v_lshrrev_b32_e32 v8, 6, v6
	s_movk_i32 s1, 0xc0
	s_sext_i32_i16 s0, s0
	s_ashr_i32 s27, s26, 31
	v_and_or_b32 v8, v8, s1, v7
	s_lshr_b32 s1, s12, 8
	s_lshl_b32 s48, s13, 10
	s_lshr_b32 s0, s0, 3
	s_lshl_b64 s[6:7], s[26:27], 19
	s_add_u32 s28, s44, s6
	s_addc_u32 s29, s45, s7
	s_bfe_i64 s[6:7], s[0:1], 0x100000
	s_lshl_b64 s[6:7], s[6:7], 19
	s_add_u32 s30, s46, s6
	s_addc_u32 s31, s47, s7
	s_add_i32 s27, s48, 0
	v_or3_b32 v8, v8, v12, v13
	s_add_i32 m0, s27, 0x10000
	v_mov_b32_e32 v163, 0
	v_lshl_or_b32 v164, v8, 7, v9
	v_lshl_or_b32 v166, v10, 7, v9
	v_lshl_or_b32 v168, v11, 7, v9
	v_lshl_add_u64 v[8:9], s[30:31], 0, v[162:163]
	global_load_lds_dwordx4 v162, s[30:31]
	v_mov_b32_e32 v165, v163
	s_add_i32 m0, s27, 0x12000
	s_mov_b64 s[6:7], 0x400
	v_lshl_add_u64 v[10:11], s[30:31], 0, v[164:165]
	global_load_lds_dwordx4 v164, s[30:31]
	s_add_i32 m0, s27, 0x14000
	v_lshl_add_u64 v[8:9], v[8:9], 0, s[6:7]
	global_load_lds_dwordx4 v[8:9], off
	v_lshl_add_u64 v[8:9], v[10:11], 0, s[6:7]
	s_add_i32 m0, s27, 0x16000
	s_add_i32 s49, s27, 0x2000
	global_load_lds_dwordx4 v[8:9], off
	s_mov_b32 m0, s27
	s_add_i32 s50, s27, 0x4000
	global_load_lds_dwordx4 v166, s[28:29]
	s_mov_b32 m0, s49
	v_or_b32_e32 v172, 0x4000, v166
	global_load_lds_dwordx4 v168, s[28:29]
	s_mov_b32 m0, s50
	s_add_i32 s51, s27, 0x6000
	v_or_b32_e32 v174, 0x4000, v168
	global_load_lds_dwordx4 v172, s[28:29]
	s_mov_b32 m0, s51
	s_cmp_eq_u32 s1, 1
	global_load_lds_dwordx4 v174, s[28:29]
	s_movk_i32 s14, 0x4000
	s_mov_b32 s52, 0
	v_mov_b32_e32 v167, v163
	s_cselect_b64 s[8:9], -1, 0
	s_cmp_lg_u32 s1, 1
	v_mov_b32_e32 v169, v163
	s_cbranch_scc1 .LBB0_901
.LBB0_901:
	s_add_u32 s10, s36, 0x1e000000
	s_addc_u32 s11, s37, 0
	s_and_b32 s15, s13, 3
	s_lshl_b32 s13, s1, 13
	s_lshl_b32 s16, s15, 12
	s_add_u32 s18, s30, 0x8000
	s_addc_u32 s19, s31, 0
	s_add_i32 m0, s27, 0x18000
	v_lshl_add_u64 v[8:9], s[18:19], 0, v[162:163]
	s_waitcnt vmcnt(2)
	s_barrier
	global_load_lds_dwordx4 v[8:9], off
	s_add_i32 m0, s27, 0x1a000
	s_add_u32 s20, s28, 0x8000
	v_lshl_add_u64 v[8:9], s[18:19], 0, v[164:165]
	s_addc_u32 s21, s29, 0
	s_add_i32 s53, s27, 0x8000
	global_load_lds_dwordx4 v[8:9], off
	v_lshl_add_u64 v[8:9], s[20:21], 0, v[166:167]
	s_mov_b32 m0, s53
	s_add_i32 s58, s27, 0xa000
	global_load_lds_dwordx4 v[8:9], off
	v_lshl_add_u64 v[8:9], s[20:21], 0, v[168:169]
	s_mov_b32 m0, s58
	v_or_b32_e32 v176, 0x400, v162
	global_load_lds_dwordx4 v[8:9], off
	s_add_i32 m0, s27, 0x1c000
	v_or_b32_e32 v178, 0x400, v164
	global_load_lds_dwordx4 v176, s[18:19]
	s_add_i32 m0, s27, 0x1e000
	s_sext_i32_i8 s64, s0
	global_load_lds_dwordx4 v178, s[18:19]
	v_and_b32_e32 v8, 15, v0
	v_lshlrev_b32_e32 v9, 2, v0
	v_lshlrev_b32_e32 v10, 6, v0
	s_movk_i32 s0, 0x3c0
	v_lshlrev_b32_e32 v5, 7, v5
	v_and_b32_e32 v2, 0x1800, v2
	v_lshl_or_b32 v188, s1, 6, v8
	v_lshl_or_b32 v8, v8, 6, v7
	v_and_b32_e32 v9, 32, v9
	v_and_or_b32 v10, v10, s0, v7
	s_waitcnt vmcnt(6)
	s_cmpk_lt_u32 s12, 0x100
	v_and_b32_e32 v6, 0x3800, v6
	v_or3_b32 v2, v3, v2, v5
	v_bitop3_b32 v8, v8, s13, v9 bitop3:0xde
	v_bitop3_b32 v189, s16, v10, v9 bitop3:0xf6
	s_cselect_b64 s[12:13], -1, 0
	v_or3_b32 v6, v3, v6, v5
	v_add_u32_e32 v2, v2, v4
	s_add_i32 s60, 0, 0x10000
	s_add_i32 s61, 0, 0x14000
	v_mov_b32_e32 v173, v163
	v_mov_b32_e32 v175, v163
	v_mov_b32_e32 v177, v163
	v_mov_b32_e32 v179, v163
	s_ashr_i32 s59, s33, 31
	v_lshl_or_b32 v190, s15, 6, v7
	v_add3_u32 v180, v6, v4, s14
	v_mov_b32_e32 v181, v163
	v_or_b32_e32 v182, 0x4000, v2
	v_mov_b32_e32 v183, v163
	v_mov_b64_e32 v[184:185], 0x400
	v_mov_b64_e32 v[186:187], 0x3ff
	v_add_u32_e32 v191, s60, v189
	v_add_u32_e32 v192, s61, v189
	v_add_u32_e32 v193, 0, v8
	v_mov_b32_e32 v194, 0x7f7f7f7f
	s_mov_b64 s[14:15], 0x504000
	s_mov_b32 s62, 0x504000
	s_mov_b32 s16, 0x3e800000
	s_mov_b32 s63, 0xc3e00000
	v_mov_b32_e32 v195, 0x43e00000
	s_mov_b64 s[22:23], s[28:29]
	s_mov_b64 s[24:25], s[30:31]
	s_barrier
	s_branch .LBB0_904

; #define PG8_STAGE(bufoff, gbase, voff) do { _Pragma("unroll") for (int _i = 0; _i < 2; ++_i) \
;         __builtin_amdgcn_global_load_lds((const unsigned*)((const char*)(gbase) + (voff)[_i]), (PG8_LAS unsigned*)(lds + (bufoff) + ldsw + _i * 8192), 16, 0, 0); } while (0)
; #define PG8_WAIT_V(n) asm volatile("s_waitcnt vmcnt(" #n ")" ::: "memory")
; #define PG8_WAIT_L(n) asm volatile("s_waitcnt lgkmcnt(" #n ")" ::: "memory")
; #define PG8_BAR __builtin_amdgcn_s_barrier()
; #define PG8_SCHED __builtin_amdgcn_sched_barrier(0)
; template <class Epi, class Sched, bool ALIGN_EPI = true, bool F8 = false>
; __device__ __forceinline__ void gemm_phase(PG8_LAS unsigned char* lds, const Sched& S, const Epi& E) {
;     ...
;             PG8_LDB(B0, 0, 0); PG8_LDB(B1, 0, 1); PG8_SCHED; PG8_LDA(At, 0, 0); PG8_STAGE(PG8_SA(1, 1), a1, voffA[1]);
;             PG8_WAIT_V(8); PG8_WAIT_L(0); PG8_BAR; PG8_MMA(0, 0, At, B0); PG8_MMA(0, 1, At, B1); PG8_BAR; PG8_SCHED;
;     ...
;                     for (int n = 0; n < 2; ++n) acc[a][b][m][n] = (f32x4){0.f, 0.f, 0.f, 0.f};
;         }
;         cur = nxt; cA = nA; cB = nB; ++ui;
.LBB0_910:
	s_add_u32 s19, s30, 0x10000
	s_addc_u32 s21, s31, 0
	s_add_u32 s28, s28, 0x8000
	v_mov_b32_e32 v34, 0
	s_addc_u32 s29, s29, 0
	s_mov_b32 s65, -2
	v_mov_b32_e32 v35, v34
	v_mov_b32_e32 v36, v34
	v_mov_b32_e32 v37, v34
	v_mov_b32_e32 v38, v34
	v_mov_b32_e32 v39, v34
	v_mov_b32_e32 v40, v34
	v_mov_b32_e32 v41, v34
	v_mov_b32_e32 v46, v34
	v_mov_b32_e32 v47, v34
	v_mov_b32_e32 v48, v34
	v_mov_b32_e32 v49, v34
	v_mov_b32_e32 v54, v34
	v_mov_b32_e32 v55, v34
	v_mov_b32_e32 v56, v34
	v_mov_b32_e32 v57, v34
	v_mov_b32_e32 v62, v34
	v_mov_b32_e32 v63, v34
	v_mov_b32_e32 v64, v34
	v_mov_b32_e32 v65, v34
	v_mov_b32_e32 v70, v34
	v_mov_b32_e32 v71, v34
	v_mov_b32_e32 v72, v34
	v_mov_b32_e32 v73, v34
	v_mov_b32_e32 v78, v34
	v_mov_b32_e32 v79, v34
	v_mov_b32_e32 v80, v34
	v_mov_b32_e32 v81, v34
	v_mov_b32_e32 v86, v34
	v_mov_b32_e32 v87, v34
	v_mov_b32_e32 v88, v34
	v_mov_b32_e32 v89, v34
	v_mov_b32_e32 v42, v34
	v_mov_b32_e32 v43, v34
	v_mov_b32_e32 v44, v34
	v_mov_b32_e32 v45, v34
	v_mov_b32_e32 v50, v34
	v_mov_b32_e32 v51, v34
	v_mov_b32_e32 v52, v34
	v_mov_b32_e32 v53, v34
	v_mov_b32_e32 v58, v34
	v_mov_b32_e32 v59, v34
	v_mov_b32_e32 v60, v34
	v_mov_b32_e32 v61, v34
	v_mov_b32_e32 v66, v34
	v_mov_b32_e32 v67, v34
	v_mov_b32_e32 v68, v34
	v_mov_b32_e32 v69, v34
	v_mov_b32_e32 v74, v34
	v_mov_b32_e32 v75, v34
	v_mov_b32_e32 v76, v34
	v_mov_b32_e32 v77, v34
	v_mov_b32_e32 v82, v34
	v_mov_b32_e32 v83, v34
	v_mov_b32_e32 v84, v34
	v_mov_b32_e32 v85, v34
	v_mov_b32_e32 v90, v34
	v_mov_b32_e32 v91, v34
	v_mov_b32_e32 v92, v34
	v_mov_b32_e32 v93, v34
	v_mov_b32_e32 v94, v34
	v_mov_b32_e32 v95, v34
	v_mov_b32_e32 v96, v34
	v_mov_b32_e32 v97, v34
	v_mov_b32_e32 v98, v34
	v_mov_b32_e32 v99, v34
	v_mov_b32_e32 v100, v34
	v_mov_b32_e32 v101, v34
	v_mov_b32_e32 v102, v34
	v_mov_b32_e32 v103, v34
	v_mov_b32_e32 v104, v34
	v_mov_b32_e32 v105, v34
	v_mov_b32_e32 v110, v34
	v_mov_b32_e32 v111, v34
	v_mov_b32_e32 v112, v34
	v_mov_b32_e32 v113, v34
	v_mov_b32_e32 v118, v34
	v_mov_b32_e32 v119, v34
	v_mov_b32_e32 v120, v34
	v_mov_b32_e32 v121, v34
	v_mov_b32_e32 v126, v34
	v_mov_b32_e32 v127, v34
	v_mov_b32_e32 v128, v34
	v_mov_b32_e32 v129, v34
	v_mov_b32_e32 v134, v34
	v_mov_b32_e32 v135, v34
	v_mov_b32_e32 v136, v34
	v_mov_b32_e32 v137, v34
	v_mov_b32_e32 v138, v34
	v_mov_b32_e32 v139, v34
	v_mov_b32_e32 v140, v34
	v_mov_b32_e32 v141, v34
	v_mov_b32_e32 v142, v34
	v_mov_b32_e32 v143, v34
	v_mov_b32_e32 v144, v34
	v_mov_b32_e32 v145, v34
	v_mov_b32_e32 v106, v34
	v_mov_b32_e32 v107, v34
	v_mov_b32_e32 v108, v34
	v_mov_b32_e32 v109, v34
	v_mov_b32_e32 v114, v34
	v_mov_b32_e32 v115, v34
	v_mov_b32_e32 v116, v34
	v_mov_b32_e32 v117, v34
	v_mov_b32_e32 v122, v34
	v_mov_b32_e32 v123, v34
	v_mov_b32_e32 v124, v34
	v_mov_b32_e32 v125, v34
	v_mov_b32_e32 v130, v34
	v_mov_b32_e32 v131, v34
	v_mov_b32_e32 v132, v34
	v_mov_b32_e32 v133, v34
	v_mov_b32_e32 v146, v34
	v_mov_b32_e32 v147, v34
	v_mov_b32_e32 v148, v34
	v_mov_b32_e32 v149, v34
	v_mov_b32_e32 v150, v34
	v_mov_b32_e32 v151, v34
	v_mov_b32_e32 v152, v34
	v_mov_b32_e32 v153, v34
	v_mov_b32_e32 v154, v34
	v_mov_b32_e32 v155, v34
	v_mov_b32_e32 v156, v34
	v_mov_b32_e32 v157, v34
	v_mov_b32_e32 v158, v34
	v_mov_b32_e32 v159, v34
	v_mov_b32_e32 v160, v34
	v_mov_b32_e32 v161, v34
	s_bitcmp1_b32 s3, 2
	s_cbranch_scc1 .Lh1_911
.LBB0_911:
	ds_read_b128 v[18:21], v191
	ds_read_b128 v[22:25], v191 offset:1024
	ds_read_b128 v[26:29], v191 offset:2048
	ds_read_b128 v[30:33], v191 offset:3072
	ds_read_b128 v[2:5], v192
	ds_read_b128 v[6:9], v192 offset:1024
	ds_read_b128 v[10:13], v192 offset:2048
	ds_read_b128 v[14:17], v192 offset:3072
	s_add_u32 s30, s28, 0x8000
	s_addc_u32 s31, s29, 0
	s_cmp_eq_u32 s65, 12
	s_cselect_b32 s42, s22, s30
	s_cselect_b32 s43, s23, s31
	s_cselect_b32 s40, s24, s19
	s_cselect_b32 s41, s25, s21
	s_add_u32 s30, s42, 0x8000
	s_addc_u32 s31, s43, 0
	v_lshl_add_u64 v[228:229], s[28:29], 0, v[182:183]
	s_add_i32 m0, s27, 0xc000
	ds_read_b128 v[196:199], v193
	ds_read_b128 v[200:203], v193 offset:1024
	ds_read_b128 v[204:207], v193 offset:2048
	ds_read_b128 v[208:211], v193 offset:3072
	ds_read_b128 v[212:215], v193 offset:4096
	ds_read_b128 v[216:219], v193 offset:5120
	ds_read_b128 v[220:223], v193 offset:6144
	ds_read_b128 v[224:227], v193 offset:7168
	global_load_lds_dwordx4 v[228:229], off
	v_lshl_add_u64 v[228:229], s[28:29], 0, v[180:181]
	s_add_i32 m0, s27, 0xe000
	s_nop 0
	global_load_lds_dwordx4 v[228:229], off
	s_waitcnt vmcnt(8)
	s_waitcnt lgkmcnt(0)
	s_setprio 1
	s_waitcnt lgkmcnt(0)
	v_mfma_scale_f32_16x16x128_f8f6f4 v[158:161], v[18:25], v[196:203], v[158:161], v194, v194 op_sel_hi:[0,0,0]
	v_mfma_scale_f32_16x16x128_f8f6f4 v[154:157], v[26:33], v[196:203], v[154:157], v194, v194 op_sel_hi:[0,0,0]
	v_mfma_scale_f32_16x16x128_f8f6f4 v[150:153], v[18:25], v[204:211], v[150:153], v194, v194 op_sel_hi:[0,0,0]
	v_mfma_scale_f32_16x16x128_f8f6f4 v[146:149], v[26:33], v[204:211], v[146:149], v194, v194 op_sel_hi:[0,0,0]
	v_mfma_scale_f32_16x16x128_f8f6f4 v[130:133], v[18:25], v[212:219], v[130:133], v194, v194 op_sel_hi:[0,0,0]
	v_mfma_scale_f32_16x16x128_f8f6f4 v[122:125], v[26:33], v[212:219], v[122:125], v194, v194 op_sel_hi:[0,0,0]
	v_mfma_scale_f32_16x16x128_f8f6f4 v[114:117], v[18:25], v[220:227], v[114:117], v194, v194 op_sel_hi:[0,0,0]
	v_mfma_scale_f32_16x16x128_f8f6f4 v[106:109], v[26:33], v[220:227], v[106:109], v194, v194 op_sel_hi:[0,0,0]
	s_nop 3
	s_setprio 0
	s_setprio 1
	v_mfma_scale_f32_16x16x128_f8f6f4 v[142:145], v[2:9], v[196:203], v[142:145], v194, v194 op_sel_hi:[0,0,0]
	v_mfma_scale_f32_16x16x128_f8f6f4 v[138:141], v[10:17], v[196:203], v[138:141], v194, v194 op_sel_hi:[0,0,0]
	v_mfma_scale_f32_16x16x128_f8f6f4 v[134:137], v[2:9], v[204:211], v[134:137], v194, v194 op_sel_hi:[0,0,0]
	v_mfma_scale_f32_16x16x128_f8f6f4 v[126:129], v[10:17], v[204:211], v[126:129], v194, v194 op_sel_hi:[0,0,0]
	v_mfma_scale_f32_16x16x128_f8f6f4 v[118:121], v[2:9], v[212:219], v[118:121], v194, v194 op_sel_hi:[0,0,0]
	v_mfma_scale_f32_16x16x128_f8f6f4 v[110:113], v[10:17], v[212:219], v[110:113], v194, v194 op_sel_hi:[0,0,0]
	v_mfma_scale_f32_16x16x128_f8f6f4 v[102:105], v[2:9], v[220:227], v[102:105], v194, v194 op_sel_hi:[0,0,0]
	v_mfma_scale_f32_16x16x128_f8f6f4 v[98:101], v[10:17], v[220:227], v[98:101], v194, v194 op_sel_hi:[0,0,0]
	s_nop 3
	s_setprio 0
	s_barrier
; #define PG8_STAGE(bufoff, gbase, voff) do { _Pragma("unroll") for (int _i = 0; _i < 2; ++_i) \
;         __builtin_amdgcn_global_load_lds((const unsigned*)((const char*)(gbase) + (voff)[_i]), (PG8_LAS unsigned*)(lds + (bufoff) + ldsw + _i * 8192), 16, 0, 0); } while (0)
; #define PG8_WAIT_V(n) asm volatile("s_waitcnt vmcnt(" #n ")" ::: "memory")
; #define PG8_WAIT_L(n) asm volatile("s_waitcnt lgkmcnt(" #n ")" ::: "memory")
; #define PG8_BAR __builtin_amdgcn_s_barrier()
; #define PG8_SCHED __builtin_amdgcn_sched_barrier(0)
; template <class Epi, class Sched, bool ALIGN_EPI = true, bool F8 = false>
; __device__ __forceinline__ void gemm_phase(PG8_LAS unsigned char* lds, const Sched& S, const Epi& E) {
;     ...
;             PG8_LDA(At, 0, 1); PG8_STAGE(PG8_SB(0, 0), b2, voffB[0]); PG8_STAGE(PG8_SB(0, 1), b2, voffB[1]); PG8_STAGE(PG8_SA(0, 0), a2, vA2[0]);
;             PG8_WAIT_V(8); PG8_WAIT_L(0); PG8_BAR; PG8_MMA(1, 0, At, B0); PG8_MMA(1, 1, At, B1); PG8_BAR; PG8_SCHED;
;             PG8_LDB(B0, 1, 0); PG8_LDB(B1, 1, 1); PG8_SCHED; PG8_LDA(At, 1, 0); PG8_STAGE(PG8_SA(0, 1), a2, vA2[1]);
;             PG8_WAIT_V(8); PG8_WAIT_L(0); PG8_BAR; PG8_MMA(0, 0, At, B0); PG8_MMA(0, 1, At, B1); PG8_BAR; PG8_SCHED;
	s_add_i32 s66, s60, s48
	v_lshl_add_u64 v[228:229], s[40:41], 0, v[162:163]
	s_mov_b32 m0, s66
	ds_read_b128 v[196:199], v193 offset:16384
	ds_read_b128 v[200:203], v193 offset:17408
	ds_read_b128 v[204:207], v193 offset:18432
	ds_read_b128 v[208:211], v193 offset:19456
	ds_read_b128 v[212:215], v193 offset:20480
	ds_read_b128 v[216:219], v193 offset:21504
	ds_read_b128 v[220:223], v193 offset:22528
	ds_read_b128 v[224:227], v193 offset:23552
	global_load_lds_dwordx4 v[228:229], off
	v_lshl_add_u64 v[230:231], s[40:41], 0, v[164:165]
	s_add_i32 m0, s66, 0x2000
	s_add_i32 s66, s61, s48
	global_load_lds_dwordx4 v[230:231], off
	v_lshl_add_u64 v[228:229], v[228:229], 0, s[6:7]
	s_mov_b32 m0, s66
	s_nop 0
	global_load_lds_dwordx4 v[228:229], off
	v_lshl_add_u64 v[228:229], v[230:231], 0, s[6:7]
	s_add_i32 m0, s66, 0x2000
	s_nop 0
	global_load_lds_dwordx4 v[228:229], off
	v_lshl_add_u64 v[228:229], s[42:43], 0, v[166:167]
	s_mov_b32 m0, s27
	s_nop 0
	global_load_lds_dwordx4 v[228:229], off
	v_lshl_add_u64 v[228:229], s[42:43], 0, v[168:169]
	s_mov_b32 m0, s49
	s_nop 0
	global_load_lds_dwordx4 v[228:229], off
	s_waitcnt vmcnt(8)
	s_waitcnt lgkmcnt(0)
	s_setprio 1
	s_waitcnt lgkmcnt(0)
	v_mfma_scale_f32_16x16x128_f8f6f4 v[94:97], v[18:25], v[196:203], v[94:97], v194, v194 op_sel_hi:[0,0,0]
	v_mfma_scale_f32_16x16x128_f8f6f4 v[90:93], v[26:33], v[196:203], v[90:93], v194, v194 op_sel_hi:[0,0,0]
	v_mfma_scale_f32_16x16x128_f8f6f4 v[82:85], v[18:25], v[204:211], v[82:85], v194, v194 op_sel_hi:[0,0,0]
	v_mfma_scale_f32_16x16x128_f8f6f4 v[74:77], v[26:33], v[204:211], v[74:77], v194, v194 op_sel_hi:[0,0,0]
	v_mfma_scale_f32_16x16x128_f8f6f4 v[66:69], v[18:25], v[212:219], v[66:69], v194, v194 op_sel_hi:[0,0,0]
	v_mfma_scale_f32_16x16x128_f8f6f4 v[58:61], v[26:33], v[212:219], v[58:61], v194, v194 op_sel_hi:[0,0,0]
	v_mfma_scale_f32_16x16x128_f8f6f4 v[50:53], v[18:25], v[220:227], v[50:53], v194, v194 op_sel_hi:[0,0,0]
	v_mfma_scale_f32_16x16x128_f8f6f4 v[42:45], v[26:33], v[220:227], v[42:45], v194, v194 op_sel_hi:[0,0,0]
	s_nop 3
	s_setprio 0
	s_setprio 1
	v_mfma_scale_f32_16x16x128_f8f6f4 v[86:89], v[2:9], v[196:203], v[86:89], v194, v194 op_sel_hi:[0,0,0]
	v_mfma_scale_f32_16x16x128_f8f6f4 v[78:81], v[10:17], v[196:203], v[78:81], v194, v194 op_sel_hi:[0,0,0]
	v_mfma_scale_f32_16x16x128_f8f6f4 v[70:73], v[2:9], v[204:211], v[70:73], v194, v194 op_sel_hi:[0,0,0]
	v_mfma_scale_f32_16x16x128_f8f6f4 v[62:65], v[10:17], v[204:211], v[62:65], v194, v194 op_sel_hi:[0,0,0]
	v_mfma_scale_f32_16x16x128_f8f6f4 v[54:57], v[2:9], v[212:219], v[54:57], v194, v194 op_sel_hi:[0,0,0]
	v_mfma_scale_f32_16x16x128_f8f6f4 v[46:49], v[10:17], v[212:219], v[46:49], v194, v194 op_sel_hi:[0,0,0]
	v_mfma_scale_f32_16x16x128_f8f6f4 v[38:41], v[2:9], v[220:227], v[38:41], v194, v194 op_sel_hi:[0,0,0]
	v_mfma_scale_f32_16x16x128_f8f6f4 v[34:37], v[10:17], v[220:227], v[34:37], v194, v194 op_sel_hi:[0,0,0]
	s_nop 3
	s_setprio 0
	s_barrier
	s_add_i32 s66, 0, 0x18000
	s_add_i32 s67, 0, 0x1c000
	v_add_u32_e32 v14, s66, v189
	v_add_u32_e32 v30, s67, v189
	ds_read_b128 v[2:5], v14
	ds_read_b128 v[6:9], v14 offset:1024
	ds_read_b128 v[10:13], v14 offset:2048
	ds_read_b128 v[14:17], v14 offset:3072
	ds_read_b128 v[18:21], v30
	ds_read_b128 v[22:25], v30 offset:1024
	ds_read_b128 v[26:29], v30 offset:2048
	ds_read_b128 v[30:33], v30 offset:3072
	s_mov_b32 m0, s50
	v_lshl_add_u64 v[228:229], s[42:43], 0, v[172:173]
	ds_read_b128 v[196:199], v193 offset:32768
	ds_read_b128 v[200:203], v193 offset:33792
	ds_read_b128 v[204:207], v193 offset:34816
	ds_read_b128 v[208:211], v193 offset:35840
	ds_read_b128 v[212:215], v193 offset:36864
	ds_read_b128 v[216:219], v193 offset:37888
	ds_read_b128 v[220:223], v193 offset:38912
	ds_read_b128 v[224:227], v193 offset:39936
	global_load_lds_dwordx4 v[228:229], off
	v_lshl_add_u64 v[228:229], s[42:43], 0, v[174:175]
	s_mov_b32 m0, s51
	s_nop 0
	global_load_lds_dwordx4 v[228:229], off
	s_waitcnt vmcnt(8)
	s_waitcnt lgkmcnt(0)
	s_setprio 1
	s_waitcnt lgkmcnt(0)
	v_mfma_scale_f32_16x16x128_f8f6f4 v[158:161], v[2:9], v[196:203], v[158:161], v194, v194 op_sel_hi:[0,0,0]
	v_mfma_scale_f32_16x16x128_f8f6f4 v[154:157], v[10:17], v[196:203], v[154:157], v194, v194 op_sel_hi:[0,0,0]
	v_mfma_scale_f32_16x16x128_f8f6f4 v[150:153], v[2:9], v[204:211], v[150:153], v194, v194 op_sel_hi:[0,0,0]
	v_mfma_scale_f32_16x16x128_f8f6f4 v[146:149], v[10:17], v[204:211], v[146:149], v194, v194 op_sel_hi:[0,0,0]
	v_mfma_scale_f32_16x16x128_f8f6f4 v[130:133], v[2:9], v[212:219], v[130:133], v194, v194 op_sel_hi:[0,0,0]
	v_mfma_scale_f32_16x16x128_f8f6f4 v[122:125], v[10:17], v[212:219], v[122:125], v194, v194 op_sel_hi:[0,0,0]
	v_mfma_scale_f32_16x16x128_f8f6f4 v[114:117], v[2:9], v[220:227], v[114:117], v194, v194 op_sel_hi:[0,0,0]
	v_mfma_scale_f32_16x16x128_f8f6f4 v[106:109], v[10:17], v[220:227], v[106:109], v194, v194 op_sel_hi:[0,0,0]
	s_nop 3
	s_setprio 0
	s_setprio 1
	v_mfma_scale_f32_16x16x128_f8f6f4 v[142:145], v[18:25], v[196:203], v[142:145], v194, v194 op_sel_hi:[0,0,0]
	v_mfma_scale_f32_16x16x128_f8f6f4 v[138:141], v[26:33], v[196:203], v[138:141], v194, v194 op_sel_hi:[0,0,0]
	v_mfma_scale_f32_16x16x128_f8f6f4 v[134:137], v[18:25], v[204:211], v[134:137], v194, v194 op_sel_hi:[0,0,0]
	v_mfma_scale_f32_16x16x128_f8f6f4 v[126:129], v[26:33], v[204:211], v[126:129], v194, v194 op_sel_hi:[0,0,0]
	v_mfma_scale_f32_16x16x128_f8f6f4 v[118:121], v[18:25], v[212:219], v[118:121], v194, v194 op_sel_hi:[0,0,0]
	v_mfma_scale_f32_16x16x128_f8f6f4 v[110:113], v[26:33], v[212:219], v[110:113], v194, v194 op_sel_hi:[0,0,0]
	v_mfma_scale_f32_16x16x128_f8f6f4 v[102:105], v[18:25], v[220:227], v[102:105], v194, v194 op_sel_hi:[0,0,0]
	v_mfma_scale_f32_16x16x128_f8f6f4 v[98:101], v[26:33], v[220:227], v[98:101], v194, v194 op_sel_hi:[0,0,0]
	s_nop 3
	s_setprio 0
	s_barrier
; #define PG8_STAGE(bufoff, gbase, voff) do { _Pragma("unroll") for (int _i = 0; _i < 2; ++_i) \
;         __builtin_amdgcn_global_load_lds((const unsigned*)((const char*)(gbase) + (voff)[_i]), (PG8_LAS unsigned*)(lds + (bufoff) + ldsw + _i * 8192), 16, 0, 0); } while (0)
; #define PG8_WAIT_V(n) asm volatile("s_waitcnt vmcnt(" #n ")" ::: "memory")
; #define PG8_WAIT_L(n) asm volatile("s_waitcnt lgkmcnt(" #n ")" ::: "memory")
; #define PG8_BAR __builtin_amdgcn_s_barrier()
; #define PG8_SCHED __builtin_amdgcn_sched_barrier(0)
; template <class Epi, class Sched, bool ALIGN_EPI = true, bool F8 = false>
; __device__ __forceinline__ void gemm_phase(PG8_LAS unsigned char* lds, const Sched& S, const Epi& E) {
;     ...
;             PG8_LDB(B0, 0, 0); PG8_LDB(B1, 0, 1); PG8_SCHED; PG8_LDA(At, 0, 0); PG8_STAGE(PG8_SA(1, 1), a1, voffA[1]);
;             PG8_WAIT_V(8); PG8_WAIT_L(0); PG8_BAR; PG8_MMA(0, 0, At, B0); PG8_MMA(0, 1, At, B1); PG8_BAR; PG8_SCHED;
;     ...
;             PG8_LDA(At, 1, 1); PG8_STAGE(PG8_SB(1, 0), b3, voffB[0]); PG8_STAGE(PG8_SB(1, 1), b3, voffB[1]); PG8_STAGE(PG8_SA(1, 0), a3, vA2[0]);
;             PG8_WAIT_V(8); PG8_WAIT_L(0); PG8_BAR; PG8_MMA(1, 0, At, B0); PG8_MMA(1, 1, At, B1); PG8_BAR; PG8_SCHED;
	s_add_u32 s40, s40, 0x8000
	s_addc_u32 s41, s41, 0
	s_add_i32 s42, s66, s48
	v_lshl_add_u64 v[228:229], s[40:41], 0, v[162:163]
	s_mov_b32 m0, s42
	ds_read_b128 v[196:199], v193 offset:49152
	ds_read_b128 v[200:203], v193 offset:50176
	ds_read_b128 v[204:207], v193 offset:51200
	ds_read_b128 v[208:211], v193 offset:52224
	ds_read_b128 v[212:215], v193 offset:53248
	ds_read_b128 v[216:219], v193 offset:54272
	ds_read_b128 v[220:223], v193 offset:55296
	ds_read_b128 v[224:227], v193 offset:56320
	global_load_lds_dwordx4 v[228:229], off
	v_lshl_add_u64 v[228:229], s[40:41], 0, v[164:165]
	s_add_i32 m0, s42, 0x2000
	s_add_i32 s42, s67, s48
	global_load_lds_dwordx4 v[228:229], off
	v_lshl_add_u64 v[228:229], s[40:41], 0, v[176:177]
	s_mov_b32 m0, s42
	s_nop 0
	global_load_lds_dwordx4 v[228:229], off
	v_lshl_add_u64 v[228:229], s[40:41], 0, v[178:179]
	s_add_i32 m0, s42, 0x2000
	s_nop 0
	global_load_lds_dwordx4 v[228:229], off
	v_lshl_add_u64 v[228:229], s[30:31], 0, v[166:167]
	s_mov_b32 m0, s53
	s_nop 0
	global_load_lds_dwordx4 v[228:229], off
	v_lshl_add_u64 v[228:229], s[30:31], 0, v[168:169]
	s_mov_b32 m0, s58
	s_nop 0
	global_load_lds_dwordx4 v[228:229], off
	s_waitcnt vmcnt(8)
	s_waitcnt lgkmcnt(0)
	s_setprio 1
	s_waitcnt lgkmcnt(0)
	v_mfma_scale_f32_16x16x128_f8f6f4 v[94:97], v[2:9], v[196:203], v[94:97], v194, v194 op_sel_hi:[0,0,0]
	v_mfma_scale_f32_16x16x128_f8f6f4 v[90:93], v[10:17], v[196:203], v[90:93], v194, v194 op_sel_hi:[0,0,0]
	v_mfma_scale_f32_16x16x128_f8f6f4 v[82:85], v[2:9], v[204:211], v[82:85], v194, v194 op_sel_hi:[0,0,0]
	v_mfma_scale_f32_16x16x128_f8f6f4 v[74:77], v[10:17], v[204:211], v[74:77], v194, v194 op_sel_hi:[0,0,0]
	v_mfma_scale_f32_16x16x128_f8f6f4 v[66:69], v[2:9], v[212:219], v[66:69], v194, v194 op_sel_hi:[0,0,0]
	v_mfma_scale_f32_16x16x128_f8f6f4 v[58:61], v[10:17], v[212:219], v[58:61], v194, v194 op_sel_hi:[0,0,0]
	v_mfma_scale_f32_16x16x128_f8f6f4 v[50:53], v[2:9], v[220:227], v[50:53], v194, v194 op_sel_hi:[0,0,0]
	v_mfma_scale_f32_16x16x128_f8f6f4 v[42:45], v[10:17], v[220:227], v[42:45], v194, v194 op_sel_hi:[0,0,0]
	s_nop 3
	s_setprio 0
	s_setprio 1
	v_mfma_scale_f32_16x16x128_f8f6f4 v[86:89], v[18:25], v[196:203], v[86:89], v194, v194 op_sel_hi:[0,0,0]
	v_mfma_scale_f32_16x16x128_f8f6f4 v[78:81], v[26:33], v[196:203], v[78:81], v194, v194 op_sel_hi:[0,0,0]
	v_mfma_scale_f32_16x16x128_f8f6f4 v[70:73], v[18:25], v[204:211], v[70:73], v194, v194 op_sel_hi:[0,0,0]
	v_mfma_scale_f32_16x16x128_f8f6f4 v[62:65], v[26:33], v[204:211], v[62:65], v194, v194 op_sel_hi:[0,0,0]
	v_mfma_scale_f32_16x16x128_f8f6f4 v[54:57], v[18:25], v[212:219], v[54:57], v194, v194 op_sel_hi:[0,0,0]
	v_mfma_scale_f32_16x16x128_f8f6f4 v[46:49], v[26:33], v[212:219], v[46:49], v194, v194 op_sel_hi:[0,0,0]
	v_mfma_scale_f32_16x16x128_f8f6f4 v[38:41], v[18:25], v[220:227], v[38:41], v194, v194 op_sel_hi:[0,0,0]
	v_mfma_scale_f32_16x16x128_f8f6f4 v[34:37], v[26:33], v[220:227], v[34:37], v194, v194 op_sel_hi:[0,0,0]
	s_nop 3
	s_setprio 0
	s_barrier
	s_add_i32 s65, s65, 2
	s_add_u32 s19, s19, 0x10000
	s_addc_u32 s21, s21, 0
	s_add_u32 s28, s28, 0x10000
	s_addc_u32 s29, s29, 0
	s_cmp_gt_u32 s65, 13
	s_cbranch_scc0 .LBB0_911
	s_branch .Lfx_911
.Lh1_911:
	ds_read_b128 v[18:21], v191
	ds_read_b128 v[22:25], v191 offset:1024
	ds_read_b128 v[26:29], v191 offset:2048
	ds_read_b128 v[30:33], v191 offset:3072
	ds_read_b128 v[2:5], v192
	ds_read_b128 v[6:9], v192 offset:1024
	ds_read_b128 v[10:13], v192 offset:2048
	ds_read_b128 v[14:17], v192 offset:3072
	s_add_u32 s30, s28, 0x8000
	s_addc_u32 s31, s29, 0
	s_cmp_eq_u32 s65, 12
	s_cselect_b32 s42, s22, s30
	s_cselect_b32 s43, s23, s31
	s_cselect_b32 s40, s24, s19
	s_cselect_b32 s41, s25, s21
	s_add_u32 s30, s42, 0x8000
	s_addc_u32 s31, s43, 0
	v_lshl_add_u64 v[228:229], s[28:29], 0, v[182:183]
	s_add_i32 m0, s27, 0xc000
	ds_read_b128 v[196:199], v193
	ds_read_b128 v[200:203], v193 offset:1024
	ds_read_b128 v[204:207], v193 offset:2048
	ds_read_b128 v[208:211], v193 offset:3072
	ds_read_b128 v[212:215], v193 offset:4096
	ds_read_b128 v[216:219], v193 offset:5120
	ds_read_b128 v[220:223], v193 offset:6144
	ds_read_b128 v[224:227], v193 offset:7168
	global_load_lds_dwordx4 v[228:229], off
	v_lshl_add_u64 v[228:229], s[28:29], 0, v[180:181]
	s_add_i32 m0, s27, 0xe000
	s_nop 0
	global_load_lds_dwordx4 v[228:229], off
	s_waitcnt vmcnt(8)
	s_waitcnt lgkmcnt(0)
	s_barrier
; #define PG8_STAGE(bufoff, gbase, voff) do { _Pragma("unroll") for (int _i = 0; _i < 2; ++_i) \
;         __builtin_amdgcn_global_load_lds((const unsigned*)((const char*)(gbase) + (voff)[_i]), (PG8_LAS unsigned*)(lds + (bufoff) + ldsw + _i * 8192), 16, 0, 0); } while (0)
; #define PG8_WAIT_V(n) asm volatile("s_waitcnt vmcnt(" #n ")" ::: "memory")
; #define PG8_WAIT_L(n) asm volatile("s_waitcnt lgkmcnt(" #n ")" ::: "memory")
; #define PG8_BAR __builtin_amdgcn_s_barrier()
; #define PG8_SCHED __builtin_amdgcn_sched_barrier(0)
; template <class Epi, class Sched, bool ALIGN_EPI = true, bool F8 = false>
; __device__ __forceinline__ void gemm_phase(PG8_LAS unsigned char* lds, const Sched& S, const Epi& E) {
;     ...
;             PG8_WAIT_V(8); PG8_WAIT_L(0); PG8_BAR; PG8_MMA(0, 0, At, B0); PG8_MMA(0, 1, At, B1); PG8_BAR; PG8_SCHED;
;             PG8_LDA(At, 0, 1); PG8_STAGE(PG8_SB(0, 0), b2, voffB[0]); PG8_STAGE(PG8_SB(0, 1), b2, voffB[1]); PG8_STAGE(PG8_SA(0, 0), a2, vA2[0]);
;             PG8_WAIT_V(8); PG8_WAIT_L(0); PG8_BAR; PG8_MMA(1, 0, At, B0); PG8_MMA(1, 1, At, B1); PG8_BAR; PG8_SCHED;
;             PG8_LDB(B0, 1, 0); PG8_LDB(B1, 1, 1); PG8_SCHED; PG8_LDA(At, 1, 0); PG8_STAGE(PG8_SA(0, 1), a2, vA2[1]);
	s_setprio 2
	s_waitcnt lgkmcnt(0)
	v_mfma_scale_f32_16x16x128_f8f6f4 v[158:161], v[18:25], v[196:203], v[158:161], v194, v194 op_sel_hi:[0,0,0]
	v_mfma_scale_f32_16x16x128_f8f6f4 v[154:157], v[26:33], v[196:203], v[154:157], v194, v194 op_sel_hi:[0,0,0]
	v_mfma_scale_f32_16x16x128_f8f6f4 v[150:153], v[18:25], v[204:211], v[150:153], v194, v194 op_sel_hi:[0,0,0]
	v_mfma_scale_f32_16x16x128_f8f6f4 v[146:149], v[26:33], v[204:211], v[146:149], v194, v194 op_sel_hi:[0,0,0]
	v_mfma_scale_f32_16x16x128_f8f6f4 v[130:133], v[18:25], v[212:219], v[130:133], v194, v194 op_sel_hi:[0,0,0]
	v_mfma_scale_f32_16x16x128_f8f6f4 v[122:125], v[26:33], v[212:219], v[122:125], v194, v194 op_sel_hi:[0,0,0]
	v_mfma_scale_f32_16x16x128_f8f6f4 v[114:117], v[18:25], v[220:227], v[114:117], v194, v194 op_sel_hi:[0,0,0]
	v_mfma_scale_f32_16x16x128_f8f6f4 v[106:109], v[26:33], v[220:227], v[106:109], v194, v194 op_sel_hi:[0,0,0]
	s_nop 3
	s_setprio 0
	s_setprio 2
	v_mfma_scale_f32_16x16x128_f8f6f4 v[142:145], v[2:9], v[196:203], v[142:145], v194, v194 op_sel_hi:[0,0,0]
	v_mfma_scale_f32_16x16x128_f8f6f4 v[138:141], v[10:17], v[196:203], v[138:141], v194, v194 op_sel_hi:[0,0,0]
	v_mfma_scale_f32_16x16x128_f8f6f4 v[134:137], v[2:9], v[204:211], v[134:137], v194, v194 op_sel_hi:[0,0,0]
	v_mfma_scale_f32_16x16x128_f8f6f4 v[126:129], v[10:17], v[204:211], v[126:129], v194, v194 op_sel_hi:[0,0,0]
	v_mfma_scale_f32_16x16x128_f8f6f4 v[118:121], v[2:9], v[212:219], v[118:121], v194, v194 op_sel_hi:[0,0,0]
	v_mfma_scale_f32_16x16x128_f8f6f4 v[110:113], v[10:17], v[212:219], v[110:113], v194, v194 op_sel_hi:[0,0,0]
	v_mfma_scale_f32_16x16x128_f8f6f4 v[102:105], v[2:9], v[220:227], v[102:105], v194, v194 op_sel_hi:[0,0,0]
	v_mfma_scale_f32_16x16x128_f8f6f4 v[98:101], v[10:17], v[220:227], v[98:101], v194, v194 op_sel_hi:[0,0,0]
	s_nop 3
	s_setprio 0
	s_add_i32 s66, s60, s48
	v_lshl_add_u64 v[228:229], s[40:41], 0, v[162:163]
	s_mov_b32 m0, s66
	ds_read_b128 v[196:199], v193 offset:16384
	ds_read_b128 v[200:203], v193 offset:17408
	ds_read_b128 v[204:207], v193 offset:18432
	ds_read_b128 v[208:211], v193 offset:19456
	ds_read_b128 v[212:215], v193 offset:20480
	ds_read_b128 v[216:219], v193 offset:21504
	ds_read_b128 v[220:223], v193 offset:22528
	ds_read_b128 v[224:227], v193 offset:23552
	global_load_lds_dwordx4 v[228:229], off
	v_lshl_add_u64 v[230:231], s[40:41], 0, v[164:165]
	s_add_i32 m0, s66, 0x2000
	s_add_i32 s66, s61, s48
	global_load_lds_dwordx4 v[230:231], off
	v_lshl_add_u64 v[228:229], v[228:229], 0, s[6:7]
	s_mov_b32 m0, s66
	s_nop 0
	global_load_lds_dwordx4 v[228:229], off
	v_lshl_add_u64 v[228:229], v[230:231], 0, s[6:7]
	s_add_i32 m0, s66, 0x2000
	s_nop 0
	global_load_lds_dwordx4 v[228:229], off
	v_lshl_add_u64 v[228:229], s[42:43], 0, v[166:167]
	s_mov_b32 m0, s27
	s_nop 0
	global_load_lds_dwordx4 v[228:229], off
	v_lshl_add_u64 v[228:229], s[42:43], 0, v[168:169]
	s_mov_b32 m0, s49
	s_nop 0
	global_load_lds_dwordx4 v[228:229], off
	s_waitcnt vmcnt(8)
	s_waitcnt lgkmcnt(0)
	s_barrier
	s_setprio 2
	s_waitcnt lgkmcnt(0)
	v_mfma_scale_f32_16x16x128_f8f6f4 v[94:97], v[18:25], v[196:203], v[94:97], v194, v194 op_sel_hi:[0,0,0]
	v_mfma_scale_f32_16x16x128_f8f6f4 v[90:93], v[26:33], v[196:203], v[90:93], v194, v194 op_sel_hi:[0,0,0]
	v_mfma_scale_f32_16x16x128_f8f6f4 v[82:85], v[18:25], v[204:211], v[82:85], v194, v194 op_sel_hi:[0,0,0]
	v_mfma_scale_f32_16x16x128_f8f6f4 v[74:77], v[26:33], v[204:211], v[74:77], v194, v194 op_sel_hi:[0,0,0]
	v_mfma_scale_f32_16x16x128_f8f6f4 v[66:69], v[18:25], v[212:219], v[66:69], v194, v194 op_sel_hi:[0,0,0]
	v_mfma_scale_f32_16x16x128_f8f6f4 v[58:61], v[26:33], v[212:219], v[58:61], v194, v194 op_sel_hi:[0,0,0]
	v_mfma_scale_f32_16x16x128_f8f6f4 v[50:53], v[18:25], v[220:227], v[50:53], v194, v194 op_sel_hi:[0,0,0]
	v_mfma_scale_f32_16x16x128_f8f6f4 v[42:45], v[26:33], v[220:227], v[42:45], v194, v194 op_sel_hi:[0,0,0]
	s_nop 3
	s_setprio 0
	s_setprio 2
	v_mfma_scale_f32_16x16x128_f8f6f4 v[86:89], v[2:9], v[196:203], v[86:89], v194, v194 op_sel_hi:[0,0,0]
	v_mfma_scale_f32_16x16x128_f8f6f4 v[78:81], v[10:17], v[196:203], v[78:81], v194, v194 op_sel_hi:[0,0,0]
	v_mfma_scale_f32_16x16x128_f8f6f4 v[70:73], v[2:9], v[204:211], v[70:73], v194, v194 op_sel_hi:[0,0,0]
	v_mfma_scale_f32_16x16x128_f8f6f4 v[62:65], v[10:17], v[204:211], v[62:65], v194, v194 op_sel_hi:[0,0,0]
	v_mfma_scale_f32_16x16x128_f8f6f4 v[54:57], v[2:9], v[212:219], v[54:57], v194, v194 op_sel_hi:[0,0,0]
	v_mfma_scale_f32_16x16x128_f8f6f4 v[46:49], v[10:17], v[212:219], v[46:49], v194, v194 op_sel_hi:[0,0,0]
	v_mfma_scale_f32_16x16x128_f8f6f4 v[38:41], v[2:9], v[220:227], v[38:41], v194, v194 op_sel_hi:[0,0,0]
	v_mfma_scale_f32_16x16x128_f8f6f4 v[34:37], v[10:17], v[220:227], v[34:37], v194, v194 op_sel_hi:[0,0,0]
	s_nop 3
	s_setprio 0
	s_add_i32 s66, 0, 0x18000
	s_add_i32 s67, 0, 0x1c000
	v_add_u32_e32 v14, s66, v189
	v_add_u32_e32 v30, s67, v189
	ds_read_b128 v[2:5], v14
	ds_read_b128 v[6:9], v14 offset:1024
	ds_read_b128 v[10:13], v14 offset:2048
	ds_read_b128 v[14:17], v14 offset:3072
	ds_read_b128 v[18:21], v30
	ds_read_b128 v[22:25], v30 offset:1024
	ds_read_b128 v[26:29], v30 offset:2048
	ds_read_b128 v[30:33], v30 offset:3072
	s_mov_b32 m0, s50
	v_lshl_add_u64 v[228:229], s[42:43], 0, v[172:173]
	ds_read_b128 v[196:199], v193 offset:32768
	ds_read_b128 v[200:203], v193 offset:33792
	ds_read_b128 v[204:207], v193 offset:34816
	ds_read_b128 v[208:211], v193 offset:35840
	ds_read_b128 v[212:215], v193 offset:36864
	ds_read_b128 v[216:219], v193 offset:37888
	ds_read_b128 v[220:223], v193 offset:38912
	ds_read_b128 v[224:227], v193 offset:39936
	global_load_lds_dwordx4 v[228:229], off
	v_lshl_add_u64 v[228:229], s[42:43], 0, v[174:175]
	s_mov_b32 m0, s51
	s_nop 0
	global_load_lds_dwordx4 v[228:229], off
	s_waitcnt vmcnt(8)
	s_waitcnt lgkmcnt(0)
	s_barrier
; #define PG8_STAGE(bufoff, gbase, voff) do { _Pragma("unroll") for (int _i = 0; _i < 2; ++_i) \
;         __builtin_amdgcn_global_load_lds((const unsigned*)((const char*)(gbase) + (voff)[_i]), (PG8_LAS unsigned*)(lds + (bufoff) + ldsw + _i * 8192), 16, 0, 0); } while (0)
; #define PG8_WAIT_V(n) asm volatile("s_waitcnt vmcnt(" #n ")" ::: "memory")
; #define PG8_WAIT_L(n) asm volatile("s_waitcnt lgkmcnt(" #n ")" ::: "memory")
; #define PG8_BAR __builtin_amdgcn_s_barrier()
; #define PG8_SCHED __builtin_amdgcn_sched_barrier(0)
; template <class Epi, class Sched, bool ALIGN_EPI = true, bool F8 = false>
; __device__ __forceinline__ void gemm_phase(PG8_LAS unsigned char* lds, const Sched& S, const Epi& E) {
;     ...
;             PG8_WAIT_V(8); PG8_WAIT_L(0); PG8_BAR; PG8_MMA(0, 0, At, B0); PG8_MMA(0, 1, At, B1); PG8_BAR; PG8_SCHED;
;             PG8_LDA(At, 1, 1); PG8_STAGE(PG8_SB(1, 0), b3, voffB[0]); PG8_STAGE(PG8_SB(1, 1), b3, voffB[1]); PG8_STAGE(PG8_SA(1, 0), a3, vA2[0]);
;             PG8_WAIT_V(8); PG8_WAIT_L(0); PG8_BAR; PG8_MMA(1, 0, At, B0); PG8_MMA(1, 1, At, B1); PG8_BAR; PG8_SCHED;
	s_setprio 2
	s_waitcnt lgkmcnt(0)
	v_mfma_scale_f32_16x16x128_f8f6f4 v[158:161], v[2:9], v[196:203], v[158:161], v194, v194 op_sel_hi:[0,0,0]
	v_mfma_scale_f32_16x16x128_f8f6f4 v[154:157], v[10:17], v[196:203], v[154:157], v194, v194 op_sel_hi:[0,0,0]
	v_mfma_scale_f32_16x16x128_f8f6f4 v[150:153], v[2:9], v[204:211], v[150:153], v194, v194 op_sel_hi:[0,0,0]
	v_mfma_scale_f32_16x16x128_f8f6f4 v[146:149], v[10:17], v[204:211], v[146:149], v194, v194 op_sel_hi:[0,0,0]
	v_mfma_scale_f32_16x16x128_f8f6f4 v[130:133], v[2:9], v[212:219], v[130:133], v194, v194 op_sel_hi:[0,0,0]
	v_mfma_scale_f32_16x16x128_f8f6f4 v[122:125], v[10:17], v[212:219], v[122:125], v194, v194 op_sel_hi:[0,0,0]
	v_mfma_scale_f32_16x16x128_f8f6f4 v[114:117], v[2:9], v[220:227], v[114:117], v194, v194 op_sel_hi:[0,0,0]
	v_mfma_scale_f32_16x16x128_f8f6f4 v[106:109], v[10:17], v[220:227], v[106:109], v194, v194 op_sel_hi:[0,0,0]
	s_nop 3
	s_setprio 0
	s_setprio 2
	v_mfma_scale_f32_16x16x128_f8f6f4 v[142:145], v[18:25], v[196:203], v[142:145], v194, v194 op_sel_hi:[0,0,0]
	v_mfma_scale_f32_16x16x128_f8f6f4 v[138:141], v[26:33], v[196:203], v[138:141], v194, v194 op_sel_hi:[0,0,0]
	v_mfma_scale_f32_16x16x128_f8f6f4 v[134:137], v[18:25], v[204:211], v[134:137], v194, v194 op_sel_hi:[0,0,0]
	v_mfma_scale_f32_16x16x128_f8f6f4 v[126:129], v[26:33], v[204:211], v[126:129], v194, v194 op_sel_hi:[0,0,0]
	v_mfma_scale_f32_16x16x128_f8f6f4 v[118:121], v[18:25], v[212:219], v[118:121], v194, v194 op_sel_hi:[0,0,0]
	v_mfma_scale_f32_16x16x128_f8f6f4 v[110:113], v[26:33], v[212:219], v[110:113], v194, v194 op_sel_hi:[0,0,0]
	v_mfma_scale_f32_16x16x128_f8f6f4 v[102:105], v[18:25], v[220:227], v[102:105], v194, v194 op_sel_hi:[0,0,0]
	v_mfma_scale_f32_16x16x128_f8f6f4 v[98:101], v[26:33], v[220:227], v[98:101], v194, v194 op_sel_hi:[0,0,0]
	s_nop 3
	s_setprio 0
	s_add_u32 s40, s40, 0x8000
	s_addc_u32 s41, s41, 0
	s_add_i32 s42, s66, s48
	v_lshl_add_u64 v[228:229], s[40:41], 0, v[162:163]
	s_mov_b32 m0, s42
	ds_read_b128 v[196:199], v193 offset:49152
	ds_read_b128 v[200:203], v193 offset:50176
	ds_read_b128 v[204:207], v193 offset:51200
	ds_read_b128 v[208:211], v193 offset:52224
	ds_read_b128 v[212:215], v193 offset:53248
	ds_read_b128 v[216:219], v193 offset:54272
	ds_read_b128 v[220:223], v193 offset:55296
	ds_read_b128 v[224:227], v193 offset:56320
	global_load_lds_dwordx4 v[228:229], off
	v_lshl_add_u64 v[228:229], s[40:41], 0, v[164:165]
	s_add_i32 m0, s42, 0x2000
	s_add_i32 s42, s67, s48
	global_load_lds_dwordx4 v[228:229], off
	v_lshl_add_u64 v[228:229], s[40:41], 0, v[176:177]
	s_mov_b32 m0, s42
	s_nop 0
	global_load_lds_dwordx4 v[228:229], off
	v_lshl_add_u64 v[228:229], s[40:41], 0, v[178:179]
	s_add_i32 m0, s42, 0x2000
	s_nop 0
	global_load_lds_dwordx4 v[228:229], off
	v_lshl_add_u64 v[228:229], s[30:31], 0, v[166:167]
	s_mov_b32 m0, s53
	s_nop 0
	global_load_lds_dwordx4 v[228:229], off
	v_lshl_add_u64 v[228:229], s[30:31], 0, v[168:169]
	s_mov_b32 m0, s58
	s_nop 0
	global_load_lds_dwordx4 v[228:229], off
	s_waitcnt vmcnt(8)
	s_waitcnt lgkmcnt(0)
	s_barrier
	s_setprio 2
	s_waitcnt lgkmcnt(0)
	v_mfma_scale_f32_16x16x128_f8f6f4 v[94:97], v[2:9], v[196:203], v[94:97], v194, v194 op_sel_hi:[0,0,0]
	v_mfma_scale_f32_16x16x128_f8f6f4 v[90:93], v[10:17], v[196:203], v[90:93], v194, v194 op_sel_hi:[0,0,0]
	v_mfma_scale_f32_16x16x128_f8f6f4 v[82:85], v[2:9], v[204:211], v[82:85], v194, v194 op_sel_hi:[0,0,0]
	v_mfma_scale_f32_16x16x128_f8f6f4 v[74:77], v[10:17], v[204:211], v[74:77], v194, v194 op_sel_hi:[0,0,0]
	v_mfma_scale_f32_16x16x128_f8f6f4 v[66:69], v[2:9], v[212:219], v[66:69], v194, v194 op_sel_hi:[0,0,0]
	v_mfma_scale_f32_16x16x128_f8f6f4 v[58:61], v[10:17], v[212:219], v[58:61], v194, v194 op_sel_hi:[0,0,0]
	v_mfma_scale_f32_16x16x128_f8f6f4 v[50:53], v[2:9], v[220:227], v[50:53], v194, v194 op_sel_hi:[0,0,0]
	v_mfma_scale_f32_16x16x128_f8f6f4 v[42:45], v[10:17], v[220:227], v[42:45], v194, v194 op_sel_hi:[0,0,0]
	s_nop 3
	s_setprio 0
	s_setprio 2
	v_mfma_scale_f32_16x16x128_f8f6f4 v[86:89], v[18:25], v[196:203], v[86:89], v194, v194 op_sel_hi:[0,0,0]
	v_mfma_scale_f32_16x16x128_f8f6f4 v[78:81], v[26:33], v[196:203], v[78:81], v194, v194 op_sel_hi:[0,0,0]
	v_mfma_scale_f32_16x16x128_f8f6f4 v[70:73], v[18:25], v[204:211], v[70:73], v194, v194 op_sel_hi:[0,0,0]
	v_mfma_scale_f32_16x16x128_f8f6f4 v[62:65], v[26:33], v[204:211], v[62:65], v194, v194 op_sel_hi:[0,0,0]
	v_mfma_scale_f32_16x16x128_f8f6f4 v[54:57], v[18:25], v[212:219], v[54:57], v194, v194 op_sel_hi:[0,0,0]
	v_mfma_scale_f32_16x16x128_f8f6f4 v[46:49], v[26:33], v[212:219], v[46:49], v194, v194 op_sel_hi:[0,0,0]
	v_mfma_scale_f32_16x16x128_f8f6f4 v[38:41], v[18:25], v[220:227], v[38:41], v194, v194 op_sel_hi:[0,0,0]
	v_mfma_scale_f32_16x16x128_f8f6f4 v[34:37], v[26:33], v[220:227], v[34:37], v194, v194 op_sel_hi:[0,0,0]
	s_nop 3
	s_setprio 0
	s_add_i32 s65, s65, 2
	s_add_u32 s19, s19, 0x10000
	s_addc_u32 s21, s21, 0
	s_add_u32 s28, s28, 0x10000
	s_addc_u32 s29, s29, 0
	s_cmp_gt_u32 s65, 13
	s_cbranch_scc0 .Lh1_911

; __device__ __forceinline__ unsigned pk4_fp8(float a, float b, float c, float d) { int w = 0; w = __builtin_amdgcn_cvt_pk_fp8_f32(clamp8(a), clamp8(b), w, false); w = __builtin_amdgcn_cvt_pk_fp8_f32(clamp8(c), clamp8(d), w, true); return (unsigned)w; }
; #define PG8_BAR __builtin_amdgcn_s_barrier()
; template <class Epi, class Sched, bool ALIGN_EPI = true, bool F8 = false>
; __device__ __forceinline__ void gemm_phase(PG8_LAS unsigned char* lds, const Sched& S, const Epi& E) {
;     ...
;         if constexpr (ALIGN_EPI) { if (wr == 0) PG8_BAR; }
;         if constexpr (F8) {
; #pragma unroll
;             for (int a = 0; a < 2; ++a)
; #pragma unroll
;                 for (int b = 0; b < 2; ++b)
;                     asm volatile("s_nop 15\n\ts_nop 7" : "+v"(acc[a][b][0][0]), "+v"(acc[a][b][0][1]), "+v"(acc[a][b][1][0]), "+v"(acc[a][b][1][1]), "+v"(acc[a][b][2][0]), "+v"(acc[a][b][2][1]), "+v"(acc[a][b][3][0]), "+v"(acc[a][b][3][1]));
;     __device__ __forceinline__ void operator()(AccRef acc, const GUnit& u, int wr, int wc, int fr, int fq) const {
;         const int pm = u.x0, pn = u.x1; const float* gate = modv + (size_t)(pm >> 5) * 12288 + 2 * D;
;         const int col0 = pn * 256 + wc * 64 + 16 * fq;
;         f32x4 gv[4];
; #pragma unroll
;         for (int q = 0; q < 4; ++q) gv[q] = *(const f32x4*)(gate + col0 + 4 * q) * (W8_INV * MG8_SCALE);
; #pragma unroll
;         for (int ai = 0; ai < 2; ++ai)
; #pragma unroll
;             for (int m = 0; m < 4; ++m) { u32x4 w;
; #pragma unroll
;                 for (int q = 0; q < 4; ++q) { const f32x4 v = acc[ai][q >> 1][m][q & 1] * gv[q]; w[q] = pk4_fp8(v[0], v[1], v[2], v[3]); }
;                 *(u32x4*)(MG + (size_t)(pm * 256 + ai * 128 + wr * 64 + m * 16 + fr) * D + col0) = w; }
.LBB0_914:
	s_ashr_i32 s19, s26, 5
	s_mul_hi_i32 s21, s19, 0xc000
	s_mul_i32 s19, s19, 0xc000
	s_add_u32 s28, s36, s19
	v_lshl_or_b32 v2, s64, 8, v190
	s_addc_u32 s29, s37, s21
	v_ashrrev_i32_e32 v3, 31, v2
	v_lshl_add_u64 v[4:5], v[2:3], 2, s[28:29]
	v_add_co_u32_e32 v6, vcc, s62, v4
	s_nop 15
	s_nop 7
	s_nop 15
	s_nop 7
	s_nop 15
	s_nop 7
	s_nop 15
	s_nop 7
	s_nop 1
	v_addc_co_u32_e32 v7, vcc, 0, v5, vcc
	flat_load_dwordx4 v[6:9], v[6:7]
	v_lshl_add_u64 v[4:5], v[4:5], 0, s[14:15]
	flat_load_dwordx4 v[10:13], v[4:5] offset:16
	flat_load_dwordx4 v[22:25], v[4:5] offset:32
	flat_load_dwordx4 v[26:29], v[4:5] offset:48
	v_lshl_add_u32 v4, s26, 8, v188
	v_ashrrev_i32_e32 v5, 31, v4
	v_mov_b32_e32 v30, 0
	v_lshlrev_b64 v[14:15], 11, v[4:5]
	v_lshl_add_u64 v[14:15], s[10:11], 0, v[14:15]
	v_lshl_add_u64 v[200:201], v[14:15], 0, v[2:3]
	v_mov_b32_e32 v199, 0
	v_mov_b32_e32 v196, 0
	v_mov_b32_e32 v197, 0
	v_mov_b32_e32 v198, 0
	v_mov_b32_e32 v31, 0
	v_mov_b32_e32 v32, 0
	v_mov_b32_e32 v33, 0
	s_andn2_b64 vcc, exec, s[0:1]
	s_mov_b64 s[0:1], -1
	s_waitcnt vmcnt(0) lgkmcnt(0)
	v_pk_mul_f32 v[16:17], v[10:11], s[16:17] op_sel_hi:[1,0]
	v_pk_mul_f32 v[20:21], v[6:7], s[16:17] op_sel_hi:[1,0]
	v_pk_mul_f32 v[10:11], v[24:25], s[16:17] op_sel_hi:[1,0]
	v_pk_mul_f32 v[24:25], v[158:159], v[20:21]
	v_pk_mul_f32 v[18:19], v[8:9], s[16:17] op_sel_hi:[1,0]
	v_med3_f32 v5, v24, s63, v195
	v_med3_f32 v24, v25, s63, v195
	v_cvt_pk_fp8_f32 v30, v5, v24
	v_pk_mul_f32 v[14:15], v[12:13], s[16:17] op_sel_hi:[1,0]
	v_pk_mul_f32 v[12:13], v[22:23], s[16:17] op_sel_hi:[1,0]
	v_pk_mul_f32 v[22:23], v[160:161], v[18:19]
	v_pk_mul_f32 v[8:9], v[26:27], s[16:17] op_sel_hi:[1,0]
	v_med3_f32 v22, v22, s63, v195
	v_med3_f32 v23, v23, s63, v195
	v_cvt_pk_fp8_f32 v30, v22, v23 op_sel:[0,0,1]
	v_pk_mul_f32 v[22:23], v[126:127], v[8:9]
	v_pk_mul_f32 v[6:7], v[28:29], s[16:17] op_sel_hi:[1,0]
	v_pk_mul_f32 v[28:29], v[154:155], v[16:17]
	v_pk_mul_f32 v[144:145], v[144:145], v[10:11]
	v_pk_mul_f32 v[142:143], v[142:143], v[12:13]
	v_pk_mul_f32 v[150:151], v[150:151], v[20:21]
	v_pk_mul_f32 v[146:147], v[146:147], v[16:17]
	v_pk_mul_f32 v[134:135], v[134:135], v[12:13]
	v_med3_f32 v5, v22, s63, v195
	v_med3_f32 v22, v23, s63, v195
	v_med3_f32 v25, v28, s63, v195
	v_med3_f32 v28, v29, s63, v195
	v_med3_f32 v29, v142, s63, v195
	v_med3_f32 v142, v143, s63, v195
	v_med3_f32 v143, v144, s63, v195
	v_med3_f32 v144, v145, s63, v195
	v_med3_f32 v145, v150, s63, v195
	v_med3_f32 v150, v151, s63, v195
	v_med3_f32 v146, v146, s63, v195
	v_med3_f32 v147, v147, s63, v195
	v_med3_f32 v134, v134, s63, v195
	v_med3_f32 v135, v135, s63, v195
	v_cvt_pk_fp8_f32 v199, v5, v22
	v_cvt_pk_fp8_f32 v196, v145, v150
	v_cvt_pk_fp8_f32 v197, v146, v147
	v_cvt_pk_fp8_f32 v198, v134, v135
	v_pk_mul_f32 v[22:23], v[128:129], v[6:7]
	v_pk_mul_f32 v[152:153], v[152:153], v[18:19]
	v_pk_mul_f32 v[148:149], v[148:149], v[14:15]
	v_pk_mul_f32 v[136:137], v[136:137], v[10:11]
	v_med3_f32 v5, v22, s63, v195
	v_med3_f32 v22, v23, s63, v195
	v_med3_f32 v151, v152, s63, v195
	v_med3_f32 v152, v153, s63, v195
	v_med3_f32 v148, v148, s63, v195
	v_med3_f32 v149, v149, s63, v195
	v_med3_f32 v136, v136, s63, v195
	v_med3_f32 v137, v137, s63, v195
	v_cvt_pk_fp8_f32 v199, v5, v22 op_sel:[0,0,1]
	v_or_b32_e32 v22, 16, v4
	v_cvt_pk_fp8_f32 v196, v151, v152 op_sel:[0,0,1]
	v_cvt_pk_fp8_f32 v197, v148, v149 op_sel:[0,0,1]
	v_cvt_pk_fp8_f32 v198, v136, v137 op_sel:[0,0,1]
	v_ashrrev_i32_e32 v23, 31, v22
	v_lshlrev_b64 v[22:23], 11, v[22:23]
	v_lshl_add_u64 v[22:23], s[10:11], 0, v[22:23]
	v_lshl_add_u64 v[22:23], v[22:23], 0, v[2:3]
	flat_store_dwordx4 v[22:23], v[196:199]
	v_pk_mul_f32 v[22:23], v[130:131], v[20:21]
	v_cvt_pk_fp8_f32 v31, v25, v28
	v_med3_f32 v5, v22, s63, v195
	v_med3_f32 v23, v23, s63, v195
	v_mov_b32_e32 v22, 0
	v_cvt_pk_fp8_f32 v22, v5, v23
	v_pk_mul_f32 v[24:25], v[132:133], v[18:19]
	v_pk_mul_f32 v[26:27], v[156:157], v[14:15]
	v_med3_f32 v5, v24, s63, v195
	v_med3_f32 v23, v25, s63, v195
	v_pk_mul_f32 v[24:25], v[122:123], v[16:17]
	v_cvt_pk_fp8_f32 v22, v5, v23 op_sel:[0,0,1]
	v_med3_f32 v5, v24, s63, v195
	v_med3_f32 v24, v25, s63, v195
	v_mov_b32_e32 v23, 0
	v_cvt_pk_fp8_f32 v23, v5, v24
	v_pk_mul_f32 v[24:25], v[124:125], v[14:15]
	v_med3_f32 v26, v26, s63, v195
	v_med3_f32 v5, v24, s63, v195
	v_med3_f32 v24, v25, s63, v195
	v_cvt_pk_fp8_f32 v23, v5, v24 op_sel:[0,0,1]
	v_pk_mul_f32 v[24:25], v[118:119], v[12:13]
	v_med3_f32 v27, v27, s63, v195
	v_med3_f32 v5, v24, s63, v195
	v_med3_f32 v25, v25, s63, v195
	v_mov_b32_e32 v24, 0
	v_cvt_pk_fp8_f32 v24, v5, v25
	v_cvt_pk_fp8_f32 v31, v26, v27 op_sel:[0,0,1]
	v_pk_mul_f32 v[26:27], v[120:121], v[10:11]
	v_cvt_pk_fp8_f32 v32, v29, v142
	v_med3_f32 v5, v26, s63, v195
	v_med3_f32 v25, v27, s63, v195
	v_pk_mul_f32 v[26:27], v[110:111], v[8:9]
	v_cvt_pk_fp8_f32 v24, v5, v25 op_sel:[0,0,1]
	v_med3_f32 v5, v26, s63, v195
	v_med3_f32 v26, v27, s63, v195
	v_mov_b32_e32 v25, 0
	v_cvt_pk_fp8_f32 v25, v5, v26
	v_pk_mul_f32 v[26:27], v[112:113], v[6:7]
	v_pk_mul_f32 v[28:29], v[88:89], v[10:11]
	v_med3_f32 v5, v26, s63, v195
	v_med3_f32 v26, v27, s63, v195
	v_cvt_pk_fp8_f32 v25, v5, v26 op_sel:[0,0,1]
	v_or_b32_e32 v26, 32, v4
	v_ashrrev_i32_e32 v27, 31, v26
	v_lshlrev_b64 v[26:27], 11, v[26:27]
	v_lshl_add_u64 v[26:27], s[10:11], 0, v[26:27]
	v_lshl_add_u64 v[26:27], v[26:27], 0, v[2:3]
	flat_store_dwordx4 v[26:27], v[22:25]
	v_pk_mul_f32 v[26:27], v[104:105], v[10:11]
	v_pk_mul_f32 v[138:139], v[138:139], v[8:9]
	v_pk_mul_f32 v[22:23], v[114:115], v[20:21]
	v_pk_mul_f32 v[24:25], v[116:117], v[18:19]
	v_med3_f32 v5, v22, s63, v195
	v_med3_f32 v23, v23, s63, v195
; __device__ __forceinline__ unsigned pk4_fp8(float a, float b, float c, float d) { int w = 0; w = __builtin_amdgcn_cvt_pk_fp8_f32(clamp8(a), clamp8(b), w, false); w = __builtin_amdgcn_cvt_pk_fp8_f32(clamp8(c), clamp8(d), w, true); return (unsigned)w; }
;     __device__ __forceinline__ void operator()(AccRef acc, const GUnit& u, int wr, int wc, int fr, int fq) const {
;     ...
;         for (int q = 0; q < 4; ++q) gv[q] = *(const f32x4*)(gate + col0 + 4 * q) * (W8_INV * MG8_SCALE);
; #pragma unroll
;         for (int ai = 0; ai < 2; ++ai)
; #pragma unroll
;             for (int m = 0; m < 4; ++m) { u32x4 w;
; #pragma unroll
;                 for (int q = 0; q < 4; ++q) { const f32x4 v = acc[ai][q >> 1][m][q & 1] * gv[q]; w[q] = pk4_fp8(v[0], v[1], v[2], v[3]); }
;                 *(u32x4*)(MG + (size_t)(pm * 256 + ai * 128 + wr * 64 + m * 16 + fr) * D + col0) = w; }
	v_mov_b32_e32 v22, 0
	v_cvt_pk_fp8_f32 v22, v5, v23
	v_med3_f32 v5, v24, s63, v195
	v_med3_f32 v23, v25, s63, v195
	v_pk_mul_f32 v[24:25], v[106:107], v[16:17]
	v_cvt_pk_fp8_f32 v22, v5, v23 op_sel:[0,0,1]
	v_med3_f32 v5, v24, s63, v195
	v_med3_f32 v24, v25, s63, v195
	v_mov_b32_e32 v23, 0
	v_cvt_pk_fp8_f32 v23, v5, v24
	v_pk_mul_f32 v[24:25], v[108:109], v[14:15]
	v_med3_f32 v138, v138, s63, v195
	v_med3_f32 v5, v24, s63, v195
	v_med3_f32 v24, v25, s63, v195
	v_cvt_pk_fp8_f32 v23, v5, v24 op_sel:[0,0,1]
	v_pk_mul_f32 v[24:25], v[102:103], v[12:13]
	v_med3_f32 v139, v139, s63, v195
	v_med3_f32 v5, v24, s63, v195
	v_med3_f32 v25, v25, s63, v195
	v_mov_b32_e32 v24, 0
	v_cvt_pk_fp8_f32 v24, v5, v25
	v_med3_f32 v5, v26, s63, v195
	v_med3_f32 v25, v27, s63, v195
	v_pk_mul_f32 v[26:27], v[98:99], v[8:9]
	v_cvt_pk_fp8_f32 v24, v5, v25 op_sel:[0,0,1]
	v_med3_f32 v5, v26, s63, v195
	v_med3_f32 v26, v27, s63, v195
	v_mov_b32_e32 v25, 0
	v_cvt_pk_fp8_f32 v25, v5, v26
	v_pk_mul_f32 v[26:27], v[100:101], v[6:7]
	v_cvt_pk_fp8_f32 v33, v138, v139
	v_med3_f32 v5, v26, s63, v195
	v_med3_f32 v26, v27, s63, v195
	v_cvt_pk_fp8_f32 v25, v5, v26 op_sel:[0,0,1]
	v_or_b32_e32 v26, 48, v4
	v_ashrrev_i32_e32 v27, 31, v26
	v_lshlrev_b64 v[26:27], 11, v[26:27]
	v_lshl_add_u64 v[26:27], s[10:11], 0, v[26:27]
	v_lshl_add_u64 v[26:27], v[26:27], 0, v[2:3]
	flat_store_dwordx4 v[26:27], v[22:25]
	v_add_u32_e32 v26, 0x80, v4
	v_pk_mul_f32 v[140:141], v[140:141], v[6:7]
	v_pk_mul_f32 v[22:23], v[94:95], v[20:21]
	v_pk_mul_f32 v[24:25], v[96:97], v[18:19]
	v_med3_f32 v5, v22, s63, v195
	v_med3_f32 v23, v23, s63, v195
	v_mov_b32_e32 v22, 0
	v_cvt_pk_fp8_f32 v22, v5, v23
	v_med3_f32 v5, v24, s63, v195
	v_med3_f32 v23, v25, s63, v195
	v_pk_mul_f32 v[24:25], v[90:91], v[16:17]
	v_cvt_pk_fp8_f32 v22, v5, v23 op_sel:[0,0,1]
	v_med3_f32 v5, v24, s63, v195
	v_med3_f32 v24, v25, s63, v195
	v_mov_b32_e32 v23, 0
	v_cvt_pk_fp8_f32 v23, v5, v24
	v_pk_mul_f32 v[24:25], v[92:93], v[14:15]
	v_med3_f32 v140, v140, s63, v195
	v_med3_f32 v5, v24, s63, v195
	v_med3_f32 v24, v25, s63, v195
	v_cvt_pk_fp8_f32 v23, v5, v24 op_sel:[0,0,1]
	v_pk_mul_f32 v[24:25], v[86:87], v[12:13]
	v_med3_f32 v141, v141, s63, v195
	v_med3_f32 v5, v24, s63, v195
	v_med3_f32 v25, v25, s63, v195
	v_mov_b32_e32 v24, 0
	v_cvt_pk_fp8_f32 v24, v5, v25
	v_med3_f32 v5, v28, s63, v195
	v_med3_f32 v25, v29, s63, v195
	v_pk_mul_f32 v[28:29], v[78:79], v[8:9]
	v_cvt_pk_fp8_f32 v24, v5, v25 op_sel:[0,0,1]
	v_med3_f32 v5, v28, s63, v195
	v_med3_f32 v27, v29, s63, v195
	v_mov_b32_e32 v25, 0
	v_cvt_pk_fp8_f32 v25, v5, v27
	v_pk_mul_f32 v[28:29], v[80:81], v[6:7]
	v_cvt_pk_fp8_f32 v32, v143, v144 op_sel:[0,0,1]
	v_med3_f32 v5, v28, s63, v195
	v_med3_f32 v27, v29, s63, v195
	v_cvt_pk_fp8_f32 v25, v5, v27 op_sel:[0,0,1]
	v_ashrrev_i32_e32 v27, 31, v26
	v_lshlrev_b64 v[26:27], 11, v[26:27]
	v_lshl_add_u64 v[26:27], s[10:11], 0, v[26:27]
	v_lshl_add_u64 v[26:27], v[26:27], 0, v[2:3]
	flat_store_dwordx4 v[26:27], v[22:25]
	v_pk_mul_f32 v[26:27], v[72:73], v[10:11]
	v_cvt_pk_fp8_f32 v33, v140, v141 op_sel:[0,0,1]
	v_pk_mul_f32 v[22:23], v[82:83], v[20:21]
	v_pk_mul_f32 v[24:25], v[84:85], v[18:19]
	v_med3_f32 v5, v22, s63, v195
	v_med3_f32 v23, v23, s63, v195
	v_mov_b32_e32 v22, 0
	v_cvt_pk_fp8_f32 v22, v5, v23
	v_med3_f32 v5, v24, s63, v195
	v_med3_f32 v23, v25, s63, v195
	v_pk_mul_f32 v[24:25], v[74:75], v[16:17]
	v_cvt_pk_fp8_f32 v22, v5, v23 op_sel:[0,0,1]
	v_med3_f32 v5, v24, s63, v195
	v_med3_f32 v24, v25, s63, v195
	v_mov_b32_e32 v23, 0
	v_cvt_pk_fp8_f32 v23, v5, v24
	v_pk_mul_f32 v[24:25], v[76:77], v[14:15]
	flat_store_dwordx4 v[200:201], v[30:33]
	v_med3_f32 v5, v24, s63, v195
	v_med3_f32 v24, v25, s63, v195
	v_cvt_pk_fp8_f32 v23, v5, v24 op_sel:[0,0,1]
	v_pk_mul_f32 v[24:25], v[70:71], v[12:13]
	s_nop 0
; __device__ __forceinline__ unsigned pk4_fp8(float a, float b, float c, float d) { int w = 0; w = __builtin_amdgcn_cvt_pk_fp8_f32(clamp8(a), clamp8(b), w, false); w = __builtin_amdgcn_cvt_pk_fp8_f32(clamp8(c), clamp8(d), w, true); return (unsigned)w; }
; #define PG8_BAR __builtin_amdgcn_s_barrier()
; template <class Epi, class Sched, bool ALIGN_EPI = true, bool F8 = false>
; __device__ __forceinline__ void gemm_phase(PG8_LAS unsigned char* lds, const Sched& S, const Epi& E) {
;     ...
;         if (!has_next) break;
;         if (!(HasSeg<Epi>::v && cur.x2 == 0)) {
; #pragma unroll
;         for (int a = 0; a < 2; ++a)
; #pragma unroll
;             for (int b = 0; b < 2; ++b)
; #pragma unroll
;                 for (int m = 0; m < 4; ++m)
; #pragma unroll
;                     for (int n = 0; n < 2; ++n) acc[a][b][m][n] = (f32x4){0.f, 0.f, 0.f, 0.f};
;         }
;         cur = nxt; cA = nA; cB = nB; ++ui;
; #pragma unroll
;         for (int h = 0; h < 2; ++h)
; #pragma unroll
;             for (int i = 0; i < 2; ++i) voffA[h][i] = voffAn[h][i];
;         if constexpr (ALIGN_EPI) { if (wr == 1) PG8_BAR; }
;     __device__ __forceinline__ void operator()(AccRef acc, const GUnit& u, int wr, int wc, int fr, int fq) const {
;     ...
;             for (int m = 0; m < 4; ++m) { u32x4 w;
; #pragma unroll
;                 for (int q = 0; q < 4; ++q) { const f32x4 v = acc[ai][q >> 1][m][q & 1] * gv[q]; w[q] = pk4_fp8(v[0], v[1], v[2], v[3]); }
;                 *(u32x4*)(MG + (size_t)(pm * 256 + ai * 128 + wr * 64 + m * 16 + fr) * D + col0) = w; }
	v_med3_f32 v5, v24, s63, v195
	v_med3_f32 v25, v25, s63, v195
	v_mov_b32_e32 v24, 0
	v_cvt_pk_fp8_f32 v24, v5, v25
	v_med3_f32 v5, v26, s63, v195
	v_med3_f32 v25, v27, s63, v195
	v_pk_mul_f32 v[26:27], v[62:63], v[8:9]
	v_cvt_pk_fp8_f32 v24, v5, v25 op_sel:[0,0,1]
	v_med3_f32 v5, v26, s63, v195
	v_med3_f32 v26, v27, s63, v195
	v_mov_b32_e32 v25, 0
	v_cvt_pk_fp8_f32 v25, v5, v26
	v_pk_mul_f32 v[26:27], v[64:65], v[6:7]
	s_nop 0
	v_med3_f32 v5, v26, s63, v195
	v_med3_f32 v26, v27, s63, v195
	v_cvt_pk_fp8_f32 v25, v5, v26 op_sel:[0,0,1]
	v_add_u32_e32 v26, 0x90, v4
	v_ashrrev_i32_e32 v27, 31, v26
	v_lshlrev_b64 v[26:27], 11, v[26:27]
	v_lshl_add_u64 v[26:27], s[10:11], 0, v[26:27]
	v_lshl_add_u64 v[26:27], v[26:27], 0, v[2:3]
	flat_store_dwordx4 v[26:27], v[22:25]
	v_pk_mul_f32 v[26:27], v[56:57], v[10:11]
	v_pk_mul_f32 v[10:11], v[40:41], v[10:11]
	v_pk_mul_f32 v[22:23], v[66:67], v[20:21]
	v_pk_mul_f32 v[24:25], v[68:69], v[18:19]
	v_med3_f32 v5, v22, s63, v195
	v_med3_f32 v23, v23, s63, v195
	v_mov_b32_e32 v22, 0
	v_cvt_pk_fp8_f32 v22, v5, v23
	v_med3_f32 v5, v24, s63, v195
	v_med3_f32 v23, v25, s63, v195
	v_pk_mul_f32 v[24:25], v[58:59], v[16:17]
	v_cvt_pk_fp8_f32 v22, v5, v23 op_sel:[0,0,1]
	v_med3_f32 v5, v24, s63, v195
	v_med3_f32 v24, v25, s63, v195
	v_mov_b32_e32 v23, 0
	v_cvt_pk_fp8_f32 v23, v5, v24
	v_pk_mul_f32 v[24:25], v[60:61], v[14:15]
	v_pk_mul_f32 v[20:21], v[50:51], v[20:21]
	v_med3_f32 v5, v24, s63, v195
	v_med3_f32 v24, v25, s63, v195
	v_cvt_pk_fp8_f32 v23, v5, v24 op_sel:[0,0,1]
	v_pk_mul_f32 v[24:25], v[54:55], v[12:13]
	v_med3_f32 v21, v21, s63, v195
	v_med3_f32 v5, v24, s63, v195
	v_med3_f32 v25, v25, s63, v195
	v_mov_b32_e32 v24, 0
	v_cvt_pk_fp8_f32 v24, v5, v25
	v_med3_f32 v5, v26, s63, v195
	v_med3_f32 v25, v27, s63, v195
	v_pk_mul_f32 v[26:27], v[46:47], v[8:9]
	v_cvt_pk_fp8_f32 v24, v5, v25 op_sel:[0,0,1]
	v_med3_f32 v5, v26, s63, v195
	v_med3_f32 v26, v27, s63, v195
	v_mov_b32_e32 v25, 0
	v_cvt_pk_fp8_f32 v25, v5, v26
	v_pk_mul_f32 v[26:27], v[48:49], v[6:7]
	v_pk_mul_f32 v[18:19], v[52:53], v[18:19]
	v_med3_f32 v5, v26, s63, v195
	v_med3_f32 v26, v27, s63, v195
	v_cvt_pk_fp8_f32 v25, v5, v26 op_sel:[0,0,1]
	v_med3_f32 v5, v20, s63, v195
	v_mov_b32_e32 v20, 0
	v_cvt_pk_fp8_f32 v20, v5, v21
	v_med3_f32 v5, v18, s63, v195
	v_med3_f32 v18, v19, s63, v195
	v_pk_mul_f32 v[16:17], v[42:43], v[16:17]
	v_add_u32_e32 v26, 0xa0, v4
	v_cvt_pk_fp8_f32 v20, v5, v18 op_sel:[0,0,1]
	v_med3_f32 v5, v16, s63, v195
	v_med3_f32 v16, v17, s63, v195
	v_mov_b32_e32 v21, 0
	v_ashrrev_i32_e32 v27, 31, v26
	v_cvt_pk_fp8_f32 v21, v5, v16
	v_lshlrev_b64 v[26:27], 11, v[26:27]
	v_lshl_add_u64 v[26:27], s[10:11], 0, v[26:27]
	v_pk_mul_f32 v[14:15], v[44:45], v[14:15]
	v_lshl_add_u64 v[26:27], v[26:27], 0, v[2:3]
	v_med3_f32 v5, v14, s63, v195
	v_med3_f32 v14, v15, s63, v195
	v_pk_mul_f32 v[12:13], v[38:39], v[12:13]
	flat_store_dwordx4 v[26:27], v[22:25]
	v_cvt_pk_fp8_f32 v21, v5, v14 op_sel:[0,0,1]
	v_med3_f32 v5, v12, s63, v195
	v_med3_f32 v12, v13, s63, v195
	v_mov_b32_e32 v22, 0
	v_cvt_pk_fp8_f32 v22, v5, v12
	v_med3_f32 v5, v10, s63, v195
	v_med3_f32 v10, v11, s63, v195
	v_pk_mul_f32 v[8:9], v[34:35], v[8:9]
	v_cvt_pk_fp8_f32 v22, v5, v10 op_sel:[0,0,1]
	v_med3_f32 v5, v8, s63, v195
	v_med3_f32 v8, v9, s63, v195
	v_mov_b32_e32 v23, 0
	v_cvt_pk_fp8_f32 v23, v5, v8
	v_pk_mul_f32 v[6:7], v[36:37], v[6:7]
	v_add_u32_e32 v4, 0xb0, v4
	v_med3_f32 v5, v6, s63, v195
	v_med3_f32 v6, v7, s63, v195
	v_cvt_pk_fp8_f32 v23, v5, v6 op_sel:[0,0,1]
	v_ashrrev_i32_e32 v5, 31, v4
	v_lshlrev_b64 v[4:5], 11, v[4:5]
	v_lshl_add_u64 v[4:5], s[10:11], 0, v[4:5]
	v_lshl_add_u64 v[2:3], v[4:5], 0, v[2:3]
	flat_store_dwordx4 v[2:3], v[20:23]
	s_cbranch_vccnz .LBB0_903
	s_andn2_b64 vcc, exec, s[8:9]
	s_cbranch_vccnz .LBB0_902
	s_branch .LBB0_902

; #define PG8_STAGE(bufoff, gbase, voff) do { _Pragma("unroll") for (int _i = 0; _i < 2; ++_i) \
;         __builtin_amdgcn_global_load_lds((const unsigned*)((const char*)(gbase) + (voff)[_i]), (PG8_LAS unsigned*)(lds + (bufoff) + ldsw + _i * 8192), 16, 0, 0); } while (0)
;     __device__ __forceinline__ unsigned b_off(int R, int C) const { return (unsigned)(R * ldb + C) * 2u; }
;     __device__ __forceinline__ unsigned b_off(int R, int C) const { return (unsigned)(R * 128 + C * 2); }
;     __device__ __forceinline__ unsigned b_off(int R, int C) const { return (unsigned)(R * ldb + C) * 2u; }
;     __device__ __forceinline__ unsigned b_off(int R, int C) const { return (unsigned)(R * 128 + C * 2); }
;     __device__ __forceinline__ unsigned b_off(int R, int C) const { return (unsigned)(R * 512 + C) * 2u; }
; template <class Epi, class Sched, bool ALIGN_EPI = true, bool F8 = false>
; __device__ __forceinline__ void gemm_phase(PG8_LAS unsigned char* lds, const Sched& S, const Epi& E) {
;     ...
;     const char* cA = cur.A; const char* cB = cur.B;
;     PG8_STAGE(PG8_SB(0, 0), cB, voffB[0]); PG8_STAGE(PG8_SB(0, 1), cB, voffB[1]); PG8_STAGE(PG8_SA(0, 0), cA, voffA[0]); PG8_STAGE(PG8_SA(0, 1), cA, voffA[1]);
;     __device__ __forceinline__ bool next(int i, GUnit& u) const { const int L = i * G + c; const int ti = L >> 3, ct = L & 7; if (ti >= __builtin_amdgcn_readfirstlane(pre[NE])) return false;
;         int e = 0;
; #pragma unroll 1
;         for (int s = 16; s >= 1; s >>= 1) if (pre[e + s] <= ti) e += s;
;         e = __builtin_amdgcn_readfirstlane(e);
;         u.A = Abase; u.B = Bbase + ((size_t)((e * 8 + ct) * NT) << 15); u.nt = NT; u.x0 = e; u.x1 = ti - __builtin_amdgcn_readfirstlane(pre[e]); u.x2 = ct; u.x3 = __builtin_amdgcn_readfirstlane(cnt[e]); return true; }
;     __device__ __forceinline__ unsigned b_off(int R, int C) const { return (unsigned)(R * 128 + C * 2); }
;     __device__ __forceinline__ void a_off(const GUnit& u, const int (&R)[2], const int (&C)[2], unsigned (&v)[2][2]) const {
;         const int* rl = rowlist + (size_t)u.x0 * ECAP; const int base = u.x1 * 256, cm = u.x3 - 1;
; #pragma unroll
;         for (int h = 0; h < 2; ++h)
; #pragma unroll
;             for (int i = 0; i < 2; ++i) { int p = base + h * 128 + R[i]; p = p < cm ? p : cm; const unsigned ent = (unsigned)rl[p]; v[h][i] = (ent >> SHIFT) * (unsigned)PA + (unsigned)C[i] * 2u; } }
.LBB0_1047:
	s_add_i32 s7, s0, s6
	s_lshl_b32 s8, s7, 2
	s_add_i32 s8, s8, 0
	s_add_i32 s8, s8, 0x24100
	v_mov_b32_e32 v2, s8
	ds_read_b32 v2, v2
	s_waitcnt lgkmcnt(0)
	v_readfirstlane_b32 s8, v2
	s_cmp_gt_i32 s8, s1
	s_cselect_b32 s0, s0, s7
	s_lshr_b32 s7, s6, 1
	s_cmp_lt_u32 s6, 2
	s_mov_b32 s6, s7
	s_cbranch_scc0 .LBB0_1047
	s_add_u32 s6, s36, 0x2e000000
	s_addc_u32 s7, s37, 0
	s_add_u32 s44, s36, 0x6000000
	s_addc_u32 s45, s37, 0
	s_add_u32 s46, s36, 0xd00000
	s_addc_u32 s47, s37, 0
	s_and_b32 s49, s2, 7
	s_lshl_b32 s8, s0, 7
	s_lshl_b32 s9, s49, 4
	s_or_b32 s8, s8, s9
	s_lshr_b32 s14, s16, 6
	s_ashr_i32 s9, s8, 31
	s_lshr_b32 s12, s16, 8
	s_lshl_b32 s48, s14, 10
	s_lshl_b64 s[8:9], s[8:9], 15
	s_add_u32 s8, s44, s8
	s_addc_u32 s9, s45, s9
	s_lshl_b32 s11, s0, 2
	s_add_i32 s11, s11, 0
	s_add_i32 s13, s11, 0x24100
	v_mov_b32_e32 v3, s13
	ds_read_b32 v3, v3
	s_add_i32 s11, s11, 0x24200
	v_mov_b32_e32 v4, s11
	v_lshrrev_b32_e32 v2, 3, v0
	s_movk_i32 s10, 0x70
	ds_read_b32 v4, v4
	v_bitop3_b32 v8, v2, s10, 64 bitop3:0xc8
	s_waitcnt lgkmcnt(0)
	v_readfirstlane_b32 s10, v3
	s_sub_i32 s50, s1, s10
	s_ashr_i32 s1, s0, 31
	s_lshl_b64 s[10:11], s[0:1], 17
	v_bfe_u32 v6, v0, 2, 4
	v_and_b32_e32 v7, 48, v2
	s_add_u32 s10, s46, s10
	v_or_b32_e32 v206, v7, v6
	v_readfirstlane_b32 s51, v4
	s_addc_u32 s11, s47, s11
	s_lshl_b32 s1, s50, 8
	v_or_b32_e32 v207, v8, v6
	s_add_i32 s13, s51, -1
	v_or_b32_e32 v2, s1, v206
	v_min_i32_e32 v2, s13, v2
	v_or_b32_e32 v4, s1, v207
	v_ashrrev_i32_e32 v3, 31, v2
	v_min_i32_e32 v4, s13, v4
	v_lshl_add_u64 v[2:3], v[2:3], 2, s[10:11]
	v_ashrrev_i32_e32 v5, 31, v4
	s_bitset1_b32 s1, 7
	v_lshl_add_u64 v[4:5], v[4:5], 2, s[10:11]
	flat_load_dword v9, v[2:3]
	flat_load_dword v10, v[4:5]
	v_or_b32_e32 v2, s1, v206
	v_min_i32_e32 v2, s13, v2
	v_or_b32_e32 v4, s1, v207
	v_ashrrev_i32_e32 v3, 31, v2
	v_min_i32_e32 v4, s13, v4
	v_lshl_add_u64 v[2:3], v[2:3], 2, s[10:11]
	v_ashrrev_i32_e32 v5, 31, v4
	v_lshl_add_u64 v[4:5], v[4:5], 2, s[10:11]
	flat_load_dword v11, v[2:3]
	flat_load_dword v12, v[4:5]
	v_lshlrev_b32_e32 v3, 4, v0
	v_and_b32_e32 v4, 32, v0
	v_lshrrev_b32_e32 v2, 1, v0
	v_lshrrev_b32_e32 v5, 5, v0
	v_bitop3_b32 v3, v3, v4, 48 bitop3:0x6c
	s_movk_i32 s10, 0x63
	v_and_b32_e32 v4, 24, v2
	v_and_b32_e32 v5, 4, v5
	v_and_or_b32 v208, v0, 64, v3
	v_bitop3_b32 v3, v7, 35, v6 bitop3:0xc8
	v_bitop3_b32 v6, v8, s10, v6 bitop3:0xc8
	v_or3_b32 v3, v5, v3, v4
	v_or3_b32 v4, v5, v6, v4
	v_lshlrev_b32_e32 v3, 7, v3
	s_add_i32 s52, s48, 0
	v_lshlrev_b32_e32 v4, 7, v4
	v_or_b32_e32 v162, v3, v208
	s_add_i32 m0, s52, 0x10000
	v_or_b32_e32 v5, 0x4000, v208
	v_or_b32_e32 v164, v4, v208
	global_load_lds_dwordx4 v162, s[8:9]
	s_add_i32 m0, s52, 0x12000
	v_or_b32_e32 v166, v3, v5
	global_load_lds_dwordx4 v164, s[8:9]
	s_add_i32 m0, s52, 0x14000
	s_movk_i32 s1, 0xf800
	v_or_b32_e32 v168, v4, v5
	global_load_lds_dwordx4 v166, s[8:9]
	s_add_i32 m0, s52, 0x16000
	s_add_i32 s53, s52, 0x2000
	global_load_lds_dwordx4 v168, s[8:9]
	s_mov_b32 m0, s52
	s_add_i32 s58, s52, 0x4000
	s_add_i32 s59, s52, 0x6000
	s_cmp_eq_u32 s12, 1
	v_mov_b32_e32 v171, 0
	s_cselect_b64 s[10:11], -1, 0
	s_mov_b32 s13, 0
	v_mov_b32_e32 v163, v171
	v_mov_b32_e32 v165, v171
	v_mov_b32_e32 v167, v171
	v_mov_b32_e32 v169, v171
	v_mov_b32_e32 v173, v171
	s_and_b64 vcc, exec, s[10:11]
	s_waitcnt vmcnt(0) lgkmcnt(0)
	v_lshlrev_b32_e32 v3, 10, v9
	v_lshlrev_b32_e32 v4, 10, v10
	v_and_or_b32 v170, v3, s1, v208
	v_and_or_b32 v172, v4, s1, v208
	global_load_lds_dwordx4 v170, s[6:7]
	s_mov_b32 m0, s53
	v_lshlrev_b32_e32 v3, 10, v11
	v_lshlrev_b32_e32 v4, 10, v12
	v_and_or_b32 v176, v3, s1, v208
	global_load_lds_dwordx4 v172, s[6:7]
	s_mov_b32 m0, s58
	v_and_or_b32 v174, v4, s1, v208
	global_load_lds_dwordx4 v176, s[6:7]
	s_mov_b32 m0, s59
	s_nop 0
	global_load_lds_dwordx4 v174, s[6:7]
	s_cbranch_vccz .LBB0_1050
; #define PG8_STAGE(bufoff, gbase, voff) do { _Pragma("unroll") for (int _i = 0; _i < 2; ++_i) \
;         __builtin_amdgcn_global_load_lds((const unsigned*)((const char*)(gbase) + (voff)[_i]), (PG8_LAS unsigned*)(lds + (bufoff) + ldsw + _i * 8192), 16, 0, 0); } while (0)
; #define PG8_WAIT_V(n) asm volatile("s_waitcnt vmcnt(" #n ")" ::: "memory")
; #define PG8_BAR __builtin_amdgcn_s_barrier()
; template <class Epi, class Sched, bool ALIGN_EPI = true, bool F8 = false>
; __device__ __forceinline__ void gemm_phase(PG8_LAS unsigned char* lds, const Sched& S, const Epi& E) {
;     ...
;     f32x4 acc[2][2][4][2];
; #pragma unroll
;     for (int a = 0; a < 2; ++a)
; #pragma unroll
;         for (int b = 0; b < 2; ++b)
; #pragma unroll
;             for (int m = 0; m < 4; ++m)
; #pragma unroll
;                 for (int n = 0; n < 2; ++n) acc[a][b][m][n] = (f32x4){0.f, 0.f, 0.f, 0.f};
;     ...
;     if (wr == 1) PG8_BAR;
;     PG8_WAIT_V(2); PG8_BAR;
;     PG8_STAGE(PG8_SB(1, 0), cB + kstepB, voffB[0]); PG8_STAGE(PG8_SA(1, 0), cA + kstep, voffA[0]); PG8_STAGE(PG8_SB(1, 1), cB + kstepB, voffB[1]);
;     PG8_WAIT_V(6); PG8_BAR;
.LBB0_1050:
	v_and_b32_e32 v3, 15, v0
	v_bfe_u32 v8, v0, 4, 2
	v_lshlrev_b32_e32 v5, 2, v0
	v_lshl_or_b32 v209, s12, 6, v3
	v_lshlrev_b32_e32 v3, 6, v3
	v_lshlrev_b32_e32 v9, 4, v8
	v_and_b32_e32 v5, 32, v5
	v_lshlrev_b32_e32 v4, 7, v209
	v_bitop3_b32 v3, v3, v5, v9 bitop3:0x36
	s_movk_i32 s12, 0xe000
	v_and_or_b32 v10, v4, s12, v3
	s_lshl_b32 s12, s14, 5
	s_and_b32 s12, s12, 0x60
	v_lshlrev_b32_e32 v3, 6, v0
	s_movk_i32 s14, 0x3c0
	v_and_or_b32 v3, v3, s14, v9
	s_lshl_b32 s14, s12, 7
	s_add_u32 s18, s8, 0x8000
	s_addc_u32 s19, s9, 0
	s_add_i32 m0, s52, 0x18000
	v_lshl_add_u64 v[6:7], s[18:19], 0, v[162:163]
	s_waitcnt vmcnt(2)
	s_barrier
	global_load_lds_dwordx4 v[6:7], off
	s_add_i32 m0, s52, 0x1a000
	v_bitop3_b32 v210, s14, v3, v5 bitop3:0xf6
	s_add_u32 s14, s36, 0x2e000080
	v_lshl_add_u64 v[6:7], s[18:19], 0, v[164:165]
	s_addc_u32 s15, s37, 0
	s_add_i32 s60, s52, 0x8000
	global_load_lds_dwordx4 v[6:7], off
	v_lshl_add_u64 v[6:7], s[14:15], 0, v[170:171]
	s_mov_b32 m0, s60
	s_add_i32 s61, s52, 0xa000
	global_load_lds_dwordx4 v[6:7], off
	v_lshl_add_u64 v[6:7], s[14:15], 0, v[172:173]
	s_mov_b32 m0, s61
	v_ashrrev_i32_e32 v5, 31, v4
	global_load_lds_dwordx4 v[6:7], off
	s_add_i32 m0, s52, 0x1c000
	v_lshl_add_u64 v[6:7], s[18:19], 0, v[166:167]
	global_load_lds_dwordx4 v[6:7], off
	v_lshl_add_u64 v[6:7], s[18:19], 0, v[168:169]
	s_add_i32 m0, s52, 0x1e000
	v_lshl_add_u64 v[4:5], s[36:37], 0, v[4:5]
	global_load_lds_dwordx4 v[6:7], off
	v_lshl_add_u64 v[4:5], v[4:5], 0, s[12:13]
	v_and_b32_e32 v2, 16, v2
	v_mov_b32_e32 v3, v171
	s_waitcnt vmcnt(6)
	s_cmpk_lt_u32 s16, 0x100
	v_lshl_add_u64 v[2:3], v[4:5], 0, v[2:3]
	s_mov_b64 s[18:19], 0x26000000
	s_cselect_b64 s[16:17], -1, 0
	v_bfe_u32 v6, v0, 4, 1
	v_lshl_add_u64 v[178:179], v[2:3], 0, s[18:19]
	v_or_b32_e32 v211, 32, v9
	v_mov_b32_e32 v2, 0x5000
	s_add_i32 s12, 0, 0x24180
	v_lshlrev_b32_e32 v173, 4, v6
	v_lshlrev_b32_e32 v180, 11, v6
	v_mov_b32_e32 v181, v171
	v_lshlrev_b32_e32 v182, 7, v211
	v_mov_b32_e32 v183, v171
	v_lshl_or_b32 v184, v8, 11, v2
	v_mov_b32_e32 v185, v171
	v_mov_b32_e32 v212, s12
	s_add_i32 s12, 0, 0x10000
	s_add_i32 s62, 0, 0x14000
	v_add_u32_e32 v213, 0, v10
	v_mov_b32_e32 v214, 0x7f7f7f7f
	s_mov_b64 s[18:19], 0x80
	s_mov_b32 s63, 0xc3e00000
	v_mov_b32_e32 v215, 0x43e00000
	v_mov_b32_e32 v216, v170
	v_mov_b32_e32 v219, v174
	v_mov_b32_e32 v220, v176
	v_mov_b32_e32 v217, v172
	v_mov_b32_e32 v218, v170
	v_mov_b32_e32 v34, v171
	v_mov_b32_e32 v35, v171
	v_mov_b32_e32 v36, v171
	v_mov_b32_e32 v37, v171
	v_mov_b32_e32 v38, v171
	v_mov_b32_e32 v39, v171
	v_mov_b32_e32 v40, v171
	v_mov_b32_e32 v41, v171
	v_mov_b32_e32 v42, v171
	v_mov_b32_e32 v43, v171
	v_mov_b32_e32 v44, v171
	v_mov_b32_e32 v45, v171
	v_mov_b32_e32 v46, v171
	v_mov_b32_e32 v47, v171
	v_mov_b32_e32 v48, v171
	v_mov_b32_e32 v49, v171
	v_mov_b32_e32 v50, v171
	v_mov_b32_e32 v51, v171
	v_mov_b32_e32 v52, v171
	v_mov_b32_e32 v53, v171
	v_mov_b32_e32 v54, v171
	v_mov_b32_e32 v55, v171
	v_mov_b32_e32 v56, v171
	v_mov_b32_e32 v57, v171
	v_mov_b32_e32 v58, v171
	v_mov_b32_e32 v59, v171
	v_mov_b32_e32 v60, v171
	v_mov_b32_e32 v61, v171
	v_mov_b32_e32 v62, v171
	v_mov_b32_e32 v63, v171
	v_mov_b32_e32 v64, v171
	v_mov_b32_e32 v65, v171
	v_mov_b32_e32 v66, v171
	v_mov_b32_e32 v67, v171
	v_mov_b32_e32 v68, v171
	v_mov_b32_e32 v69, v171
	v_mov_b32_e32 v70, v171
	v_mov_b32_e32 v71, v171
	v_mov_b32_e32 v72, v171
	v_mov_b32_e32 v73, v171
	v_mov_b32_e32 v74, v171
	v_mov_b32_e32 v75, v171
	v_mov_b32_e32 v76, v171
	v_mov_b32_e32 v77, v171
	v_mov_b32_e32 v78, v171
	v_mov_b32_e32 v79, v171
	v_mov_b32_e32 v80, v171
	v_mov_b32_e32 v81, v171
	v_mov_b32_e32 v82, v171
	v_mov_b32_e32 v83, v171
	v_mov_b32_e32 v84, v171
	v_mov_b32_e32 v85, v171
	v_mov_b32_e32 v86, v171
	v_mov_b32_e32 v87, v171
	v_mov_b32_e32 v88, v171
	v_mov_b32_e32 v89, v171
	v_mov_b32_e32 v90, v171
	v_mov_b32_e32 v91, v171
	v_mov_b32_e32 v92, v171
	v_mov_b32_e32 v93, v171
	v_mov_b32_e32 v94, v171
	v_mov_b32_e32 v95, v171
	v_mov_b32_e32 v96, v171
	v_mov_b32_e32 v97, v171
	v_mov_b32_e32 v98, v171
	v_mov_b32_e32 v99, v171
	v_mov_b32_e32 v100, v171
	v_mov_b32_e32 v101, v171
	v_mov_b32_e32 v102, v171
	v_mov_b32_e32 v103, v171
	v_mov_b32_e32 v104, v171
	v_mov_b32_e32 v105, v171
	v_mov_b32_e32 v106, v171
	v_mov_b32_e32 v107, v171
	v_mov_b32_e32 v108, v171
	v_mov_b32_e32 v109, v171
	v_mov_b32_e32 v110, v171
	v_mov_b32_e32 v111, v171
	v_mov_b32_e32 v112, v171
	v_mov_b32_e32 v113, v171
	v_mov_b32_e32 v114, v171
	v_mov_b32_e32 v115, v171
	v_mov_b32_e32 v116, v171
	v_mov_b32_e32 v117, v171
	v_mov_b32_e32 v118, v171
	v_mov_b32_e32 v119, v171
	v_mov_b32_e32 v120, v171
	v_mov_b32_e32 v121, v171
	v_mov_b32_e32 v122, v171
	v_mov_b32_e32 v123, v171
	v_mov_b32_e32 v124, v171
	v_mov_b32_e32 v125, v171
	v_mov_b32_e32 v126, v171
	v_mov_b32_e32 v127, v171
	v_mov_b32_e32 v128, v171
	v_mov_b32_e32 v129, v171
	v_mov_b32_e32 v130, v171
	v_mov_b32_e32 v131, v171
	v_mov_b32_e32 v132, v171
	v_mov_b32_e32 v133, v171
	v_mov_b32_e32 v134, v171
	v_mov_b32_e32 v135, v171
	v_mov_b32_e32 v136, v171
	v_mov_b32_e32 v137, v171
	v_mov_b32_e32 v138, v171
	v_mov_b32_e32 v139, v171
	v_mov_b32_e32 v140, v171
	v_mov_b32_e32 v141, v171
	v_mov_b32_e32 v142, v171
	v_mov_b32_e32 v143, v171
	v_mov_b32_e32 v144, v171
	v_mov_b32_e32 v145, v171
	v_mov_b32_e32 v146, v171
	v_mov_b32_e32 v147, v171
	v_mov_b32_e32 v148, v171
	v_mov_b32_e32 v149, v171
	v_mov_b32_e32 v150, v171
	v_mov_b32_e32 v151, v171
	v_mov_b32_e32 v152, v171
	v_mov_b32_e32 v153, v171
	v_mov_b32_e32 v154, v171
	v_mov_b32_e32 v155, v171
	v_mov_b32_e32 v156, v171
	v_mov_b32_e32 v157, v171
	v_mov_b32_e32 v158, v171
	v_mov_b32_e32 v159, v171
	v_mov_b32_e32 v160, v171
	v_mov_b32_e32 v161, v171
	s_barrier
	s_branch .LBB0_1053

; template <class Epi, class Sched, bool ALIGN_EPI = true, bool F8 = false>
; __device__ __forceinline__ void gemm_phase(PG8_LAS unsigned char* lds, const Sched& S, const Epi& E) {
;     ...
;             if constexpr (Sched::GATHER) { if (last && has_next) S.a_off(nxt, Rs, Cs, voffAn); }
;             const char* a1 = cA + (size_t)(t + 1) * kstep;
;             const char* a2 = last ? nA : cA + (size_t)(t + 2) * kstep; const char* b2 = last ? nB : cB + (size_t)(t + 2) * kstepB;
;             const char* a3 = a2 + kstep; const char* b3 = b2 + kstepB;
;             unsigned vA2[2][2];
; #pragma unroll
;             for (int h = 0; h < 2; ++h)
; #pragma unroll
;                 for (int i = 0; i < 2; ++i) { if constexpr (Sched::GATHER) vA2[h][i] = (last && has_next) ? voffAn[h][i] : voffA[h][i]; else vA2[h][i] = voffA[h][i]; }
.LBB0_1057:
	s_ashr_i32 s21, s20, 31
	s_lshl_b64 s[28:29], s[20:21], 17
	s_lshl_b32 s21, s66, 8
	s_add_i32 s30, s65, -1
	s_or_b32 s31, s21, 0x80
	v_or_b32_e32 v2, s21, v206
	v_or_b32_e32 v4, s21, v207
	v_or_b32_e32 v6, s31, v206
	v_or_b32_e32 v8, s31, v207
	s_add_u32 s28, s46, s28
	v_min_i32_e32 v2, s30, v2
	v_min_i32_e32 v4, s30, v4
	v_min_i32_e32 v6, s30, v6
	v_min_i32_e32 v8, s30, v8
	s_addc_u32 s29, s47, s29
	v_ashrrev_i32_e32 v3, 31, v2
	v_ashrrev_i32_e32 v5, 31, v4
	v_ashrrev_i32_e32 v7, 31, v6
	v_ashrrev_i32_e32 v9, 31, v8
	v_mov_b32_e32 v177, v171
	v_mov_b32_e32 v175, v171
	s_add_u32 s21, s8, 0x10000
	v_lshl_add_u64 v[186:187], v[2:3], 2, s[28:29]
	v_lshl_add_u64 v[188:189], v[4:5], 2, s[28:29]
	v_lshl_add_u64 v[190:191], v[6:7], 2, s[28:29]
	v_lshl_add_u64 v[192:193], v[8:9], 2, s[28:29]
	s_addc_u32 s68, s9, 0
	v_lshl_add_u64 v[194:195], s[14:15], 0, v[174:175]
	v_lshl_add_u64 v[196:197], s[14:15], 0, v[176:177]
	s_mov_b32 s69, -2
	s_mov_b64 s[30:31], 0
	s_bitcmp1_b32 s3, 2
	s_cbranch_scc1 .Lh1_1058

; #define PG8_STAGE(bufoff, gbase, voff) do { _Pragma("unroll") for (int _i = 0; _i < 2; ++_i) \
;         __builtin_amdgcn_global_load_lds((const unsigned*)((const char*)(gbase) + (voff)[_i]), (PG8_LAS unsigned*)(lds + (bufoff) + ldsw + _i * 8192), 16, 0, 0); } while (0)
; #define PG8_WAIT_V(n) asm volatile("s_waitcnt vmcnt(" #n ")" ::: "memory")
; #define PG8_WAIT_L(n) asm volatile("s_waitcnt lgkmcnt(" #n ")" ::: "memory")
; #define PG8_BAR __builtin_amdgcn_s_barrier()
; #define PG8_SCHED __builtin_amdgcn_sched_barrier(0)
; template <class Epi, class Sched, bool ALIGN_EPI = true, bool F8 = false>
; __device__ __forceinline__ void gemm_phase(PG8_LAS unsigned char* lds, const Sched& S, const Epi& E) {
;     ...
;             PG8_LDB(B0, 0, 0); PG8_LDB(B1, 0, 1); PG8_SCHED; PG8_LDA(At, 0, 0); PG8_STAGE(PG8_SA(1, 1), a1, voffA[1]);
;             PG8_WAIT_V(8); PG8_WAIT_L(0); PG8_BAR; PG8_MMA(0, 0, At, B0); PG8_MMA(0, 1, At, B1); PG8_BAR; PG8_SCHED;
;             PG8_LDA(At, 0, 1); PG8_STAGE(PG8_SB(0, 0), b2, voffB[0]); PG8_STAGE(PG8_SB(0, 1), b2, voffB[1]); PG8_STAGE(PG8_SA(0, 0), a2, vA2[0]);
;             PG8_WAIT_V(8); PG8_WAIT_L(0); PG8_BAR; PG8_MMA(1, 0, At, B0); PG8_MMA(1, 1, At, B1); PG8_BAR; PG8_SCHED;
;             PG8_LDB(B0, 1, 0); PG8_LDB(B1, 1, 1); PG8_SCHED; PG8_LDA(At, 1, 0); PG8_STAGE(PG8_SA(0, 1), a2, vA2[1]);
.LBB0_1060:
	v_add_u32_e32 v2, s12, v210
	v_add_u32_e32 v14, s62, v210
	s_add_u32 s28, s30, 0x100
	ds_read_b128 v[18:21], v2
	ds_read_b128 v[22:25], v2 offset:1024
	ds_read_b128 v[26:29], v2 offset:2048
	ds_read_b128 v[30:33], v2 offset:3072
	ds_read_b128 v[2:5], v14
	ds_read_b128 v[6:9], v14 offset:1024
	ds_read_b128 v[10:13], v14 offset:2048
	ds_read_b128 v[14:17], v14 offset:3072
	s_addc_u32 s29, s31, 0
	s_and_b64 s[42:43], s[40:41], exec
	s_cselect_b32 s42, 0, s28
	s_cselect_b32 s43, 0, s29
	s_add_u32 s42, s6, s42
	s_addc_u32 s43, s7, s43
	s_and_b64 s[40:41], s[40:41], exec
	s_cselect_b32 s41, s25, s68
	s_cselect_b32 s40, s24, s21
	v_lshl_add_u64 v[204:205], v[196:197], 0, s[30:31]
	s_add_i32 m0, s52, 0xc000
	ds_read_b128 v[222:225], v213
	ds_read_b128 v[226:229], v213 offset:1024
	ds_read_b128 v[230:233], v213 offset:2048
	ds_read_b128 v[234:237], v213 offset:3072
	ds_read_b128 v[238:241], v213 offset:4096
	ds_read_b128 v[242:245], v213 offset:5120
	ds_read_b128 v[246:249], v213 offset:6144
	ds_read_b128 v[250:253], v213 offset:7168
	global_load_lds_dwordx4 v[204:205], off
	v_lshl_add_u64 v[204:205], v[194:195], 0, s[30:31]
	s_add_i32 m0, s52, 0xe000
	s_nop 0
	global_load_lds_dwordx4 v[204:205], off
	s_waitcnt vmcnt(8)
	s_waitcnt lgkmcnt(0)
	s_setprio 1
	s_waitcnt lgkmcnt(0)
	v_mfma_scale_f32_16x16x128_f8f6f4 v[142:145], v[18:25], v[222:229], v[142:145], v214, v214 op_sel_hi:[0,0,0]
	v_mfma_scale_f32_16x16x128_f8f6f4 v[138:141], v[26:33], v[222:229], v[138:141], v214, v214 op_sel_hi:[0,0,0]
	v_mfma_scale_f32_16x16x128_f8f6f4 v[134:137], v[18:25], v[230:237], v[134:137], v214, v214 op_sel_hi:[0,0,0]
	v_mfma_scale_f32_16x16x128_f8f6f4 v[130:133], v[26:33], v[230:237], v[130:133], v214, v214 op_sel_hi:[0,0,0]
	v_mfma_scale_f32_16x16x128_f8f6f4 v[126:129], v[18:25], v[238:245], v[126:129], v214, v214 op_sel_hi:[0,0,0]
	v_mfma_scale_f32_16x16x128_f8f6f4 v[122:125], v[26:33], v[238:245], v[122:125], v214, v214 op_sel_hi:[0,0,0]
	v_mfma_scale_f32_16x16x128_f8f6f4 v[118:121], v[18:25], v[246:253], v[118:121], v214, v214 op_sel_hi:[0,0,0]
	v_mfma_scale_f32_16x16x128_f8f6f4 v[114:117], v[26:33], v[246:253], v[114:117], v214, v214 op_sel_hi:[0,0,0]
	s_nop 3
	s_setprio 0
	s_setprio 1
	v_mfma_scale_f32_16x16x128_f8f6f4 v[110:113], v[2:9], v[222:229], v[110:113], v214, v214 op_sel_hi:[0,0,0]
	v_mfma_scale_f32_16x16x128_f8f6f4 v[106:109], v[10:17], v[222:229], v[106:109], v214, v214 op_sel_hi:[0,0,0]
	v_mfma_scale_f32_16x16x128_f8f6f4 v[102:105], v[2:9], v[230:237], v[102:105], v214, v214 op_sel_hi:[0,0,0]
	v_mfma_scale_f32_16x16x128_f8f6f4 v[98:101], v[10:17], v[230:237], v[98:101], v214, v214 op_sel_hi:[0,0,0]
	v_mfma_scale_f32_16x16x128_f8f6f4 v[94:97], v[2:9], v[238:245], v[94:97], v214, v214 op_sel_hi:[0,0,0]
	v_mfma_scale_f32_16x16x128_f8f6f4 v[90:93], v[10:17], v[238:245], v[90:93], v214, v214 op_sel_hi:[0,0,0]
	v_mfma_scale_f32_16x16x128_f8f6f4 v[86:89], v[2:9], v[246:253], v[86:89], v214, v214 op_sel_hi:[0,0,0]
	v_mfma_scale_f32_16x16x128_f8f6f4 v[82:85], v[10:17], v[246:253], v[82:85], v214, v214 op_sel_hi:[0,0,0]
	s_nop 3
	s_setprio 0
	s_barrier
	s_add_i32 s30, s12, s48
	v_lshl_add_u64 v[204:205], s[40:41], 0, v[162:163]
	s_mov_b32 m0, s30
	ds_read_b128 v[222:225], v213 offset:16384
	ds_read_b128 v[226:229], v213 offset:17408
	ds_read_b128 v[230:233], v213 offset:18432
	ds_read_b128 v[234:237], v213 offset:19456
	ds_read_b128 v[238:241], v213 offset:20480
	ds_read_b128 v[242:245], v213 offset:21504
	ds_read_b128 v[246:249], v213 offset:22528
	ds_read_b128 v[250:253], v213 offset:23552
	global_load_lds_dwordx4 v[204:205], off
	v_lshl_add_u64 v[204:205], s[40:41], 0, v[164:165]
	s_add_i32 m0, s30, 0x2000
	s_add_i32 s30, s62, s48
	global_load_lds_dwordx4 v[204:205], off
	v_lshl_add_u64 v[204:205], s[40:41], 0, v[166:167]
	s_mov_b32 m0, s30
	v_mov_b32_e32 v203, v171
	global_load_lds_dwordx4 v[204:205], off
	v_lshl_add_u64 v[204:205], s[40:41], 0, v[168:169]
	s_add_i32 m0, s30, 0x2000
	s_nop 0
	global_load_lds_dwordx4 v[204:205], off
	s_mov_b32 m0, s52
	v_lshl_add_u64 v[204:205], s[42:43], 0, v[170:171]
	global_load_lds_dwordx4 v170, s[42:43]
	s_mov_b32 m0, s53
	s_nop 0
	global_load_lds_dwordx4 v202, s[42:43]
	s_waitcnt vmcnt(8)
	s_waitcnt lgkmcnt(0)
	v_lshl_add_u64 v[202:203], s[42:43], 0, v[202:203]
	s_setprio 1
	s_waitcnt lgkmcnt(0)
	v_mfma_scale_f32_16x16x128_f8f6f4 v[78:81], v[18:25], v[222:229], v[78:81], v214, v214 op_sel_hi:[0,0,0]
	v_mfma_scale_f32_16x16x128_f8f6f4 v[74:77], v[26:33], v[222:229], v[74:77], v214, v214 op_sel_hi:[0,0,0]
	v_mfma_scale_f32_16x16x128_f8f6f4 v[70:73], v[18:25], v[230:237], v[70:73], v214, v214 op_sel_hi:[0,0,0]
	v_mfma_scale_f32_16x16x128_f8f6f4 v[66:69], v[26:33], v[230:237], v[66:69], v214, v214 op_sel_hi:[0,0,0]
	v_mfma_scale_f32_16x16x128_f8f6f4 v[62:65], v[18:25], v[238:245], v[62:65], v214, v214 op_sel_hi:[0,0,0]
	v_mfma_scale_f32_16x16x128_f8f6f4 v[58:61], v[26:33], v[238:245], v[58:61], v214, v214 op_sel_hi:[0,0,0]
	v_mfma_scale_f32_16x16x128_f8f6f4 v[54:57], v[18:25], v[246:253], v[54:57], v214, v214 op_sel_hi:[0,0,0]
	v_mfma_scale_f32_16x16x128_f8f6f4 v[50:53], v[26:33], v[246:253], v[50:53], v214, v214 op_sel_hi:[0,0,0]
	s_nop 3
	s_setprio 0
	s_setprio 1
	v_mfma_scale_f32_16x16x128_f8f6f4 v[46:49], v[2:9], v[222:229], v[46:49], v214, v214 op_sel_hi:[0,0,0]
	v_mfma_scale_f32_16x16x128_f8f6f4 v[42:45], v[10:17], v[222:229], v[42:45], v214, v214 op_sel_hi:[0,0,0]
	v_mfma_scale_f32_16x16x128_f8f6f4 v[38:41], v[2:9], v[230:237], v[38:41], v214, v214 op_sel_hi:[0,0,0]
	v_mfma_scale_f32_16x16x128_f8f6f4 v[34:37], v[10:17], v[230:237], v[34:37], v214, v214 op_sel_hi:[0,0,0]
	v_mfma_scale_f32_16x16x128_f8f6f4 v[146:149], v[2:9], v[238:245], v[146:149], v214, v214 op_sel_hi:[0,0,0]
	v_mfma_scale_f32_16x16x128_f8f6f4 v[150:153], v[10:17], v[238:245], v[150:153], v214, v214 op_sel_hi:[0,0,0]
	v_mfma_scale_f32_16x16x128_f8f6f4 v[154:157], v[2:9], v[246:253], v[154:157], v214, v214 op_sel_hi:[0,0,0]
	v_mfma_scale_f32_16x16x128_f8f6f4 v[158:161], v[10:17], v[246:253], v[158:161], v214, v214 op_sel_hi:[0,0,0]
	s_nop 3
	s_setprio 0
	s_barrier
; #define PG8_STAGE(bufoff, gbase, voff) do { _Pragma("unroll") for (int _i = 0; _i < 2; ++_i) \
;         __builtin_amdgcn_global_load_lds((const unsigned*)((const char*)(gbase) + (voff)[_i]), (PG8_LAS unsigned*)(lds + (bufoff) + ldsw + _i * 8192), 16, 0, 0); } while (0)
; #define PG8_WAIT_V(n) asm volatile("s_waitcnt vmcnt(" #n ")" ::: "memory")
; #define PG8_WAIT_L(n) asm volatile("s_waitcnt lgkmcnt(" #n ")" ::: "memory")
; #define PG8_BAR __builtin_amdgcn_s_barrier()
; #define PG8_SCHED __builtin_amdgcn_sched_barrier(0)
; template <class Epi, class Sched, bool ALIGN_EPI = true, bool F8 = false>
; __device__ __forceinline__ void gemm_phase(PG8_LAS unsigned char* lds, const Sched& S, const Epi& E) {
;     ...
;             PG8_LDB(B0, 1, 0); PG8_LDB(B1, 1, 1); PG8_SCHED; PG8_LDA(At, 1, 0); PG8_STAGE(PG8_SA(0, 1), a2, vA2[1]);
;             PG8_WAIT_V(8); PG8_WAIT_L(0); PG8_BAR; PG8_MMA(0, 0, At, B0); PG8_MMA(0, 1, At, B1); PG8_BAR; PG8_SCHED;
;             PG8_LDA(At, 1, 1); PG8_STAGE(PG8_SB(1, 0), b3, voffB[0]); PG8_STAGE(PG8_SB(1, 1), b3, voffB[1]); PG8_STAGE(PG8_SA(1, 0), a3, vA2[0]);
;             PG8_WAIT_V(8); PG8_WAIT_L(0); PG8_BAR; PG8_MMA(1, 0, At, B0); PG8_MMA(1, 1, At, B1); PG8_BAR; PG8_SCHED;
	s_add_i32 s70, 0, 0x18000
	s_add_i32 s71, 0, 0x1c000
	v_add_u32_e32 v14, s70, v210
	v_add_u32_e32 v30, s71, v210
	ds_read_b128 v[2:5], v14
	ds_read_b128 v[6:9], v14 offset:1024
	ds_read_b128 v[10:13], v14 offset:2048
	ds_read_b128 v[14:17], v14 offset:3072
	ds_read_b128 v[18:21], v30
	ds_read_b128 v[22:25], v30 offset:1024
	ds_read_b128 v[26:29], v30 offset:2048
	ds_read_b128 v[30:33], v30 offset:3072
	s_mov_b32 m0, s58
	v_lshl_add_u64 v[200:201], s[42:43], 0, v[200:201]
	ds_read_b128 v[222:225], v213 offset:32768
	ds_read_b128 v[226:229], v213 offset:33792
	ds_read_b128 v[230:233], v213 offset:34816
	ds_read_b128 v[234:237], v213 offset:35840
	ds_read_b128 v[238:241], v213 offset:36864
	ds_read_b128 v[242:245], v213 offset:37888
	ds_read_b128 v[246:249], v213 offset:38912
	ds_read_b128 v[250:253], v213 offset:39936
	global_load_lds_dwordx4 v[200:201], off
	v_lshl_add_u64 v[198:199], s[42:43], 0, v[198:199]
	s_mov_b32 m0, s59
	s_nop 0
	global_load_lds_dwordx4 v[198:199], off
	s_waitcnt vmcnt(8)
	s_waitcnt lgkmcnt(0)
	s_setprio 1
	s_waitcnt lgkmcnt(0)
	v_mfma_scale_f32_16x16x128_f8f6f4 v[142:145], v[2:9], v[222:229], v[142:145], v214, v214 op_sel_hi:[0,0,0]
	v_mfma_scale_f32_16x16x128_f8f6f4 v[138:141], v[10:17], v[222:229], v[138:141], v214, v214 op_sel_hi:[0,0,0]
	v_mfma_scale_f32_16x16x128_f8f6f4 v[134:137], v[2:9], v[230:237], v[134:137], v214, v214 op_sel_hi:[0,0,0]
	v_mfma_scale_f32_16x16x128_f8f6f4 v[130:133], v[10:17], v[230:237], v[130:133], v214, v214 op_sel_hi:[0,0,0]
	v_mfma_scale_f32_16x16x128_f8f6f4 v[126:129], v[2:9], v[238:245], v[126:129], v214, v214 op_sel_hi:[0,0,0]
	v_mfma_scale_f32_16x16x128_f8f6f4 v[122:125], v[10:17], v[238:245], v[122:125], v214, v214 op_sel_hi:[0,0,0]
	v_mfma_scale_f32_16x16x128_f8f6f4 v[118:121], v[2:9], v[246:253], v[118:121], v214, v214 op_sel_hi:[0,0,0]
	v_mfma_scale_f32_16x16x128_f8f6f4 v[114:117], v[10:17], v[246:253], v[114:117], v214, v214 op_sel_hi:[0,0,0]
	s_nop 3
	s_setprio 0
	s_setprio 1
	v_mfma_scale_f32_16x16x128_f8f6f4 v[110:113], v[18:25], v[222:229], v[110:113], v214, v214 op_sel_hi:[0,0,0]
	v_mfma_scale_f32_16x16x128_f8f6f4 v[106:109], v[26:33], v[222:229], v[106:109], v214, v214 op_sel_hi:[0,0,0]
	v_mfma_scale_f32_16x16x128_f8f6f4 v[102:105], v[18:25], v[230:237], v[102:105], v214, v214 op_sel_hi:[0,0,0]
	v_mfma_scale_f32_16x16x128_f8f6f4 v[98:101], v[26:33], v[230:237], v[98:101], v214, v214 op_sel_hi:[0,0,0]
	v_mfma_scale_f32_16x16x128_f8f6f4 v[94:97], v[18:25], v[238:245], v[94:97], v214, v214 op_sel_hi:[0,0,0]
	v_mfma_scale_f32_16x16x128_f8f6f4 v[90:93], v[26:33], v[238:245], v[90:93], v214, v214 op_sel_hi:[0,0,0]
	v_mfma_scale_f32_16x16x128_f8f6f4 v[86:89], v[18:25], v[246:253], v[86:89], v214, v214 op_sel_hi:[0,0,0]
	v_mfma_scale_f32_16x16x128_f8f6f4 v[82:85], v[26:33], v[246:253], v[82:85], v214, v214 op_sel_hi:[0,0,0]
	s_nop 3
	s_setprio 0
	s_barrier
	s_add_u32 s30, s40, 0x8000
	s_addc_u32 s31, s41, 0
	s_add_i32 s40, s70, s48
	v_lshl_add_u64 v[198:199], s[30:31], 0, v[162:163]
	s_mov_b32 m0, s40
	ds_read_b128 v[222:225], v213 offset:49152
	ds_read_b128 v[226:229], v213 offset:50176
	ds_read_b128 v[230:233], v213 offset:51200
	ds_read_b128 v[234:237], v213 offset:52224
	ds_read_b128 v[238:241], v213 offset:53248
	ds_read_b128 v[242:245], v213 offset:54272
	ds_read_b128 v[246:249], v213 offset:55296
	ds_read_b128 v[250:253], v213 offset:56320
	global_load_lds_dwordx4 v[198:199], off
	v_lshl_add_u64 v[198:199], s[30:31], 0, v[164:165]
	s_add_i32 m0, s40, 0x2000
	s_add_i32 s40, s71, s48
	global_load_lds_dwordx4 v[198:199], off
	v_lshl_add_u64 v[198:199], s[30:31], 0, v[166:167]
	s_mov_b32 m0, s40
	s_nop 0
	global_load_lds_dwordx4 v[198:199], off
	v_lshl_add_u64 v[198:199], s[30:31], 0, v[168:169]
	s_add_i32 m0, s40, 0x2000
	s_nop 0
	global_load_lds_dwordx4 v[198:199], off
	v_lshl_add_u64 v[198:199], v[204:205], 0, s[18:19]
	s_mov_b32 m0, s60
	s_nop 0
	global_load_lds_dwordx4 v[198:199], off
	v_lshl_add_u64 v[198:199], v[202:203], 0, s[18:19]
	s_mov_b32 m0, s61
	s_nop 0
	global_load_lds_dwordx4 v[198:199], off
	s_waitcnt vmcnt(8)
	s_waitcnt lgkmcnt(0)
	s_setprio 1
	s_waitcnt lgkmcnt(0)
	v_mfma_scale_f32_16x16x128_f8f6f4 v[78:81], v[2:9], v[222:229], v[78:81], v214, v214 op_sel_hi:[0,0,0]
	v_mfma_scale_f32_16x16x128_f8f6f4 v[74:77], v[10:17], v[222:229], v[74:77], v214, v214 op_sel_hi:[0,0,0]
	v_mfma_scale_f32_16x16x128_f8f6f4 v[70:73], v[2:9], v[230:237], v[70:73], v214, v214 op_sel_hi:[0,0,0]
	v_mfma_scale_f32_16x16x128_f8f6f4 v[66:69], v[10:17], v[230:237], v[66:69], v214, v214 op_sel_hi:[0,0,0]
	v_mfma_scale_f32_16x16x128_f8f6f4 v[62:65], v[2:9], v[238:245], v[62:65], v214, v214 op_sel_hi:[0,0,0]
	v_mfma_scale_f32_16x16x128_f8f6f4 v[58:61], v[10:17], v[238:245], v[58:61], v214, v214 op_sel_hi:[0,0,0]
	v_mfma_scale_f32_16x16x128_f8f6f4 v[54:57], v[2:9], v[246:253], v[54:57], v214, v214 op_sel_hi:[0,0,0]
	v_mfma_scale_f32_16x16x128_f8f6f4 v[50:53], v[10:17], v[246:253], v[50:53], v214, v214 op_sel_hi:[0,0,0]
	s_nop 3
	s_setprio 0
	s_setprio 1
	v_mfma_scale_f32_16x16x128_f8f6f4 v[46:49], v[18:25], v[222:229], v[46:49], v214, v214 op_sel_hi:[0,0,0]
	v_mfma_scale_f32_16x16x128_f8f6f4 v[42:45], v[26:33], v[222:229], v[42:45], v214, v214 op_sel_hi:[0,0,0]
	v_mfma_scale_f32_16x16x128_f8f6f4 v[38:41], v[18:25], v[230:237], v[38:41], v214, v214 op_sel_hi:[0,0,0]
	v_mfma_scale_f32_16x16x128_f8f6f4 v[34:37], v[26:33], v[230:237], v[34:37], v214, v214 op_sel_hi:[0,0,0]
	v_mfma_scale_f32_16x16x128_f8f6f4 v[146:149], v[18:25], v[238:245], v[146:149], v214, v214 op_sel_hi:[0,0,0]
	v_mfma_scale_f32_16x16x128_f8f6f4 v[150:153], v[26:33], v[238:245], v[150:153], v214, v214 op_sel_hi:[0,0,0]
	v_mfma_scale_f32_16x16x128_f8f6f4 v[154:157], v[18:25], v[246:253], v[154:157], v214, v214 op_sel_hi:[0,0,0]
	v_mfma_scale_f32_16x16x128_f8f6f4 v[158:161], v[26:33], v[246:253], v[158:161], v214, v214 op_sel_hi:[0,0,0]
	s_nop 3
	s_setprio 0
	s_barrier
	s_add_i32 s69, s69, 2
	s_add_u32 s21, s21, 0x10000
	s_addc_u32 s68, s68, 0
	s_cmp_gt_u32 s69, 13
	s_cbranch_scc1 .LBB0_1062
	s_mov_b64 s[30:31], s[28:29]
	s_branch .LBB0_1058

; #define PG8_STAGE(bufoff, gbase, voff) do { _Pragma("unroll") for (int _i = 0; _i < 2; ++_i) \
;         __builtin_amdgcn_global_load_lds((const unsigned*)((const char*)(gbase) + (voff)[_i]), (PG8_LAS unsigned*)(lds + (bufoff) + ldsw + _i * 8192), 16, 0, 0); } while (0)
; #define PG8_WAIT_V(n) asm volatile("s_waitcnt vmcnt(" #n ")" ::: "memory")
; #define PG8_WAIT_L(n) asm volatile("s_waitcnt lgkmcnt(" #n ")" ::: "memory")
; #define PG8_BAR __builtin_amdgcn_s_barrier()
; #define PG8_SCHED __builtin_amdgcn_sched_barrier(0)
; template <class Epi, class Sched, bool ALIGN_EPI = true, bool F8 = false>
; __device__ __forceinline__ void gemm_phase(PG8_LAS unsigned char* lds, const Sched& S, const Epi& E) {
;     ...
;             PG8_LDB(B0, 0, 0); PG8_LDB(B1, 0, 1); PG8_SCHED; PG8_LDA(At, 0, 0); PG8_STAGE(PG8_SA(1, 1), a1, voffA[1]);
;             PG8_WAIT_V(8); PG8_WAIT_L(0); PG8_BAR; PG8_MMA(0, 0, At, B0); PG8_MMA(0, 1, At, B1); PG8_BAR; PG8_SCHED;
;             PG8_LDA(At, 0, 1); PG8_STAGE(PG8_SB(0, 0), b2, voffB[0]); PG8_STAGE(PG8_SB(0, 1), b2, voffB[1]); PG8_STAGE(PG8_SA(0, 0), a2, vA2[0]);
;             PG8_WAIT_V(8); PG8_WAIT_L(0); PG8_BAR; PG8_MMA(1, 0, At, B0); PG8_MMA(1, 1, At, B1); PG8_BAR; PG8_SCHED;
.Lh1_1060:
	v_add_u32_e32 v2, s12, v210
	v_add_u32_e32 v14, s62, v210
	s_add_u32 s28, s30, 0x100
	ds_read_b128 v[18:21], v2
	ds_read_b128 v[22:25], v2 offset:1024
	ds_read_b128 v[26:29], v2 offset:2048
	ds_read_b128 v[30:33], v2 offset:3072
	ds_read_b128 v[2:5], v14
	ds_read_b128 v[6:9], v14 offset:1024
	ds_read_b128 v[10:13], v14 offset:2048
	ds_read_b128 v[14:17], v14 offset:3072
	s_addc_u32 s29, s31, 0
	s_and_b64 s[42:43], s[40:41], exec
	s_cselect_b32 s42, 0, s28
	s_cselect_b32 s43, 0, s29
	s_add_u32 s42, s6, s42
	s_addc_u32 s43, s7, s43
	s_and_b64 s[40:41], s[40:41], exec
	s_cselect_b32 s41, s25, s68
	s_cselect_b32 s40, s24, s21
	v_lshl_add_u64 v[204:205], v[196:197], 0, s[30:31]
	s_add_i32 m0, s52, 0xc000
	ds_read_b128 v[222:225], v213
	ds_read_b128 v[226:229], v213 offset:1024
	ds_read_b128 v[230:233], v213 offset:2048
	ds_read_b128 v[234:237], v213 offset:3072
	ds_read_b128 v[238:241], v213 offset:4096
	ds_read_b128 v[242:245], v213 offset:5120
	ds_read_b128 v[246:249], v213 offset:6144
	ds_read_b128 v[250:253], v213 offset:7168
	global_load_lds_dwordx4 v[204:205], off
	v_lshl_add_u64 v[204:205], v[194:195], 0, s[30:31]
	s_add_i32 m0, s52, 0xe000
	s_nop 0
	global_load_lds_dwordx4 v[204:205], off
	s_waitcnt vmcnt(8)
	s_waitcnt lgkmcnt(0)
	s_barrier
	s_setprio 2
	s_waitcnt lgkmcnt(0)
	v_mfma_scale_f32_16x16x128_f8f6f4 v[142:145], v[18:25], v[222:229], v[142:145], v214, v214 op_sel_hi:[0,0,0]
	v_mfma_scale_f32_16x16x128_f8f6f4 v[138:141], v[26:33], v[222:229], v[138:141], v214, v214 op_sel_hi:[0,0,0]
	v_mfma_scale_f32_16x16x128_f8f6f4 v[134:137], v[18:25], v[230:237], v[134:137], v214, v214 op_sel_hi:[0,0,0]
	v_mfma_scale_f32_16x16x128_f8f6f4 v[130:133], v[26:33], v[230:237], v[130:133], v214, v214 op_sel_hi:[0,0,0]
	v_mfma_scale_f32_16x16x128_f8f6f4 v[126:129], v[18:25], v[238:245], v[126:129], v214, v214 op_sel_hi:[0,0,0]
	v_mfma_scale_f32_16x16x128_f8f6f4 v[122:125], v[26:33], v[238:245], v[122:125], v214, v214 op_sel_hi:[0,0,0]
	v_mfma_scale_f32_16x16x128_f8f6f4 v[118:121], v[18:25], v[246:253], v[118:121], v214, v214 op_sel_hi:[0,0,0]
	v_mfma_scale_f32_16x16x128_f8f6f4 v[114:117], v[26:33], v[246:253], v[114:117], v214, v214 op_sel_hi:[0,0,0]
	s_nop 3
	s_setprio 0
	s_setprio 2
	v_mfma_scale_f32_16x16x128_f8f6f4 v[110:113], v[2:9], v[222:229], v[110:113], v214, v214 op_sel_hi:[0,0,0]
	v_mfma_scale_f32_16x16x128_f8f6f4 v[106:109], v[10:17], v[222:229], v[106:109], v214, v214 op_sel_hi:[0,0,0]
	v_mfma_scale_f32_16x16x128_f8f6f4 v[102:105], v[2:9], v[230:237], v[102:105], v214, v214 op_sel_hi:[0,0,0]
	v_mfma_scale_f32_16x16x128_f8f6f4 v[98:101], v[10:17], v[230:237], v[98:101], v214, v214 op_sel_hi:[0,0,0]
	v_mfma_scale_f32_16x16x128_f8f6f4 v[94:97], v[2:9], v[238:245], v[94:97], v214, v214 op_sel_hi:[0,0,0]
	v_mfma_scale_f32_16x16x128_f8f6f4 v[90:93], v[10:17], v[238:245], v[90:93], v214, v214 op_sel_hi:[0,0,0]
	v_mfma_scale_f32_16x16x128_f8f6f4 v[86:89], v[2:9], v[246:253], v[86:89], v214, v214 op_sel_hi:[0,0,0]
	v_mfma_scale_f32_16x16x128_f8f6f4 v[82:85], v[10:17], v[246:253], v[82:85], v214, v214 op_sel_hi:[0,0,0]
	s_nop 3
	s_setprio 0
	s_add_i32 s30, s12, s48
	v_lshl_add_u64 v[204:205], s[40:41], 0, v[162:163]
	s_mov_b32 m0, s30
	ds_read_b128 v[222:225], v213 offset:16384
	ds_read_b128 v[226:229], v213 offset:17408
	ds_read_b128 v[230:233], v213 offset:18432
	ds_read_b128 v[234:237], v213 offset:19456
	ds_read_b128 v[238:241], v213 offset:20480
	ds_read_b128 v[242:245], v213 offset:21504
	ds_read_b128 v[246:249], v213 offset:22528
	ds_read_b128 v[250:253], v213 offset:23552
	global_load_lds_dwordx4 v[204:205], off
	v_lshl_add_u64 v[204:205], s[40:41], 0, v[164:165]
	s_add_i32 m0, s30, 0x2000
	s_add_i32 s30, s62, s48
	global_load_lds_dwordx4 v[204:205], off
	v_lshl_add_u64 v[204:205], s[40:41], 0, v[166:167]
	s_mov_b32 m0, s30
	v_mov_b32_e32 v203, v171
	global_load_lds_dwordx4 v[204:205], off
	v_lshl_add_u64 v[204:205], s[40:41], 0, v[168:169]
	s_add_i32 m0, s30, 0x2000
	s_nop 0
	global_load_lds_dwordx4 v[204:205], off
	s_mov_b32 m0, s52
	v_lshl_add_u64 v[204:205], s[42:43], 0, v[170:171]
	global_load_lds_dwordx4 v170, s[42:43]
	s_mov_b32 m0, s53
	s_nop 0
	global_load_lds_dwordx4 v202, s[42:43]
	s_waitcnt vmcnt(8)
	s_waitcnt lgkmcnt(0)
	v_lshl_add_u64 v[202:203], s[42:43], 0, v[202:203]
	s_barrier
; #define PG8_STAGE(bufoff, gbase, voff) do { _Pragma("unroll") for (int _i = 0; _i < 2; ++_i) \
;         __builtin_amdgcn_global_load_lds((const unsigned*)((const char*)(gbase) + (voff)[_i]), (PG8_LAS unsigned*)(lds + (bufoff) + ldsw + _i * 8192), 16, 0, 0); } while (0)
; #define PG8_WAIT_V(n) asm volatile("s_waitcnt vmcnt(" #n ")" ::: "memory")
; #define PG8_WAIT_L(n) asm volatile("s_waitcnt lgkmcnt(" #n ")" ::: "memory")
; #define PG8_BAR __builtin_amdgcn_s_barrier()
; #define PG8_SCHED __builtin_amdgcn_sched_barrier(0)
; template <class Epi, class Sched, bool ALIGN_EPI = true, bool F8 = false>
; __device__ __forceinline__ void gemm_phase(PG8_LAS unsigned char* lds, const Sched& S, const Epi& E) {
;     ...
;             PG8_WAIT_V(8); PG8_WAIT_L(0); PG8_BAR; PG8_MMA(1, 0, At, B0); PG8_MMA(1, 1, At, B1); PG8_BAR; PG8_SCHED;
;             PG8_LDB(B0, 1, 0); PG8_LDB(B1, 1, 1); PG8_SCHED; PG8_LDA(At, 1, 0); PG8_STAGE(PG8_SA(0, 1), a2, vA2[1]);
;             PG8_WAIT_V(8); PG8_WAIT_L(0); PG8_BAR; PG8_MMA(0, 0, At, B0); PG8_MMA(0, 1, At, B1); PG8_BAR; PG8_SCHED;
;             PG8_LDA(At, 1, 1); PG8_STAGE(PG8_SB(1, 0), b3, voffB[0]); PG8_STAGE(PG8_SB(1, 1), b3, voffB[1]); PG8_STAGE(PG8_SA(1, 0), a3, vA2[0]);
	s_setprio 2
	s_waitcnt lgkmcnt(0)
	v_mfma_scale_f32_16x16x128_f8f6f4 v[78:81], v[18:25], v[222:229], v[78:81], v214, v214 op_sel_hi:[0,0,0]
	v_mfma_scale_f32_16x16x128_f8f6f4 v[74:77], v[26:33], v[222:229], v[74:77], v214, v214 op_sel_hi:[0,0,0]
	v_mfma_scale_f32_16x16x128_f8f6f4 v[70:73], v[18:25], v[230:237], v[70:73], v214, v214 op_sel_hi:[0,0,0]
	v_mfma_scale_f32_16x16x128_f8f6f4 v[66:69], v[26:33], v[230:237], v[66:69], v214, v214 op_sel_hi:[0,0,0]
	v_mfma_scale_f32_16x16x128_f8f6f4 v[62:65], v[18:25], v[238:245], v[62:65], v214, v214 op_sel_hi:[0,0,0]
	v_mfma_scale_f32_16x16x128_f8f6f4 v[58:61], v[26:33], v[238:245], v[58:61], v214, v214 op_sel_hi:[0,0,0]
	v_mfma_scale_f32_16x16x128_f8f6f4 v[54:57], v[18:25], v[246:253], v[54:57], v214, v214 op_sel_hi:[0,0,0]
	v_mfma_scale_f32_16x16x128_f8f6f4 v[50:53], v[26:33], v[246:253], v[50:53], v214, v214 op_sel_hi:[0,0,0]
	s_nop 3
	s_setprio 0
	s_setprio 2
	v_mfma_scale_f32_16x16x128_f8f6f4 v[46:49], v[2:9], v[222:229], v[46:49], v214, v214 op_sel_hi:[0,0,0]
	v_mfma_scale_f32_16x16x128_f8f6f4 v[42:45], v[10:17], v[222:229], v[42:45], v214, v214 op_sel_hi:[0,0,0]
	v_mfma_scale_f32_16x16x128_f8f6f4 v[38:41], v[2:9], v[230:237], v[38:41], v214, v214 op_sel_hi:[0,0,0]
	v_mfma_scale_f32_16x16x128_f8f6f4 v[34:37], v[10:17], v[230:237], v[34:37], v214, v214 op_sel_hi:[0,0,0]
	v_mfma_scale_f32_16x16x128_f8f6f4 v[146:149], v[2:9], v[238:245], v[146:149], v214, v214 op_sel_hi:[0,0,0]
	v_mfma_scale_f32_16x16x128_f8f6f4 v[150:153], v[10:17], v[238:245], v[150:153], v214, v214 op_sel_hi:[0,0,0]
	v_mfma_scale_f32_16x16x128_f8f6f4 v[154:157], v[2:9], v[246:253], v[154:157], v214, v214 op_sel_hi:[0,0,0]
	v_mfma_scale_f32_16x16x128_f8f6f4 v[158:161], v[10:17], v[246:253], v[158:161], v214, v214 op_sel_hi:[0,0,0]
	s_nop 3
	s_setprio 0
	s_add_i32 s70, 0, 0x18000
	s_add_i32 s71, 0, 0x1c000
	v_add_u32_e32 v14, s70, v210
	v_add_u32_e32 v30, s71, v210
	ds_read_b128 v[2:5], v14
	ds_read_b128 v[6:9], v14 offset:1024
	ds_read_b128 v[10:13], v14 offset:2048
	ds_read_b128 v[14:17], v14 offset:3072
	ds_read_b128 v[18:21], v30
	ds_read_b128 v[22:25], v30 offset:1024
	ds_read_b128 v[26:29], v30 offset:2048
	ds_read_b128 v[30:33], v30 offset:3072
	s_mov_b32 m0, s58
	v_lshl_add_u64 v[200:201], s[42:43], 0, v[200:201]
	ds_read_b128 v[222:225], v213 offset:32768
	ds_read_b128 v[226:229], v213 offset:33792
	ds_read_b128 v[230:233], v213 offset:34816
	ds_read_b128 v[234:237], v213 offset:35840
	ds_read_b128 v[238:241], v213 offset:36864
	ds_read_b128 v[242:245], v213 offset:37888
	ds_read_b128 v[246:249], v213 offset:38912
	ds_read_b128 v[250:253], v213 offset:39936
	global_load_lds_dwordx4 v[200:201], off
	v_lshl_add_u64 v[198:199], s[42:43], 0, v[198:199]
	s_mov_b32 m0, s59
	s_nop 0
	global_load_lds_dwordx4 v[198:199], off
	s_waitcnt vmcnt(8)
	s_waitcnt lgkmcnt(0)
	s_barrier
	s_setprio 2
	s_waitcnt lgkmcnt(0)
	v_mfma_scale_f32_16x16x128_f8f6f4 v[142:145], v[2:9], v[222:229], v[142:145], v214, v214 op_sel_hi:[0,0,0]
	v_mfma_scale_f32_16x16x128_f8f6f4 v[138:141], v[10:17], v[222:229], v[138:141], v214, v214 op_sel_hi:[0,0,0]
	v_mfma_scale_f32_16x16x128_f8f6f4 v[134:137], v[2:9], v[230:237], v[134:137], v214, v214 op_sel_hi:[0,0,0]
	v_mfma_scale_f32_16x16x128_f8f6f4 v[130:133], v[10:17], v[230:237], v[130:133], v214, v214 op_sel_hi:[0,0,0]
	v_mfma_scale_f32_16x16x128_f8f6f4 v[126:129], v[2:9], v[238:245], v[126:129], v214, v214 op_sel_hi:[0,0,0]
	v_mfma_scale_f32_16x16x128_f8f6f4 v[122:125], v[10:17], v[238:245], v[122:125], v214, v214 op_sel_hi:[0,0,0]
	v_mfma_scale_f32_16x16x128_f8f6f4 v[118:121], v[2:9], v[246:253], v[118:121], v214, v214 op_sel_hi:[0,0,0]
	v_mfma_scale_f32_16x16x128_f8f6f4 v[114:117], v[10:17], v[246:253], v[114:117], v214, v214 op_sel_hi:[0,0,0]
	s_nop 3
	s_setprio 0
	s_setprio 2
	v_mfma_scale_f32_16x16x128_f8f6f4 v[110:113], v[18:25], v[222:229], v[110:113], v214, v214 op_sel_hi:[0,0,0]
	v_mfma_scale_f32_16x16x128_f8f6f4 v[106:109], v[26:33], v[222:229], v[106:109], v214, v214 op_sel_hi:[0,0,0]
	v_mfma_scale_f32_16x16x128_f8f6f4 v[102:105], v[18:25], v[230:237], v[102:105], v214, v214 op_sel_hi:[0,0,0]
	v_mfma_scale_f32_16x16x128_f8f6f4 v[98:101], v[26:33], v[230:237], v[98:101], v214, v214 op_sel_hi:[0,0,0]
	v_mfma_scale_f32_16x16x128_f8f6f4 v[94:97], v[18:25], v[238:245], v[94:97], v214, v214 op_sel_hi:[0,0,0]
	v_mfma_scale_f32_16x16x128_f8f6f4 v[90:93], v[26:33], v[238:245], v[90:93], v214, v214 op_sel_hi:[0,0,0]
	v_mfma_scale_f32_16x16x128_f8f6f4 v[86:89], v[18:25], v[246:253], v[86:89], v214, v214 op_sel_hi:[0,0,0]
	v_mfma_scale_f32_16x16x128_f8f6f4 v[82:85], v[26:33], v[246:253], v[82:85], v214, v214 op_sel_hi:[0,0,0]
	s_nop 3
	s_setprio 0
	s_add_u32 s30, s40, 0x8000
	s_addc_u32 s31, s41, 0
	s_add_i32 s40, s70, s48
	v_lshl_add_u64 v[198:199], s[30:31], 0, v[162:163]
	s_mov_b32 m0, s40
	ds_read_b128 v[222:225], v213 offset:49152
	ds_read_b128 v[226:229], v213 offset:50176
	ds_read_b128 v[230:233], v213 offset:51200
	ds_read_b128 v[234:237], v213 offset:52224
	ds_read_b128 v[238:241], v213 offset:53248
	ds_read_b128 v[242:245], v213 offset:54272
	ds_read_b128 v[246:249], v213 offset:55296
	ds_read_b128 v[250:253], v213 offset:56320
	global_load_lds_dwordx4 v[198:199], off
	v_lshl_add_u64 v[198:199], s[30:31], 0, v[164:165]
	s_add_i32 m0, s40, 0x2000
	s_add_i32 s40, s71, s48
	global_load_lds_dwordx4 v[198:199], off
	v_lshl_add_u64 v[198:199], s[30:31], 0, v[166:167]
	s_mov_b32 m0, s40
	s_nop 0
	global_load_lds_dwordx4 v[198:199], off
	v_lshl_add_u64 v[198:199], s[30:31], 0, v[168:169]
	s_add_i32 m0, s40, 0x2000
	s_nop 0
	global_load_lds_dwordx4 v[198:199], off
	v_lshl_add_u64 v[198:199], v[204:205], 0, s[18:19]
	s_mov_b32 m0, s60
	s_nop 0
	global_load_lds_dwordx4 v[198:199], off
	v_lshl_add_u64 v[198:199], v[202:203], 0, s[18:19]
	s_mov_b32 m0, s61
	s_nop 0
	global_load_lds_dwordx4 v[198:199], off
	s_waitcnt vmcnt(8)
	s_waitcnt lgkmcnt(0)
	s_barrier
; #define PG8_WAIT_V(n) asm volatile("s_waitcnt vmcnt(" #n ")" ::: "memory")
; #define PG8_WAIT_L(n) asm volatile("s_waitcnt lgkmcnt(" #n ")" ::: "memory")
; #define PG8_BAR __builtin_amdgcn_s_barrier()
; #define PG8_SCHED __builtin_amdgcn_sched_barrier(0)
; template <class Epi, class Sched, bool ALIGN_EPI = true, bool F8 = false>
; __device__ __forceinline__ void gemm_phase(PG8_LAS unsigned char* lds, const Sched& S, const Epi& E) {
;     ...
;             PG8_WAIT_V(8); PG8_WAIT_L(0); PG8_BAR; PG8_MMA(1, 0, At, B0); PG8_MMA(1, 1, At, B1); PG8_BAR; PG8_SCHED;
;         }
;         if constexpr (ALIGN_EPI) { if (wr == 0) PG8_BAR; }
	s_setprio 2
	s_waitcnt lgkmcnt(0)
	v_mfma_scale_f32_16x16x128_f8f6f4 v[78:81], v[2:9], v[222:229], v[78:81], v214, v214 op_sel_hi:[0,0,0]
	v_mfma_scale_f32_16x16x128_f8f6f4 v[74:77], v[10:17], v[222:229], v[74:77], v214, v214 op_sel_hi:[0,0,0]
	v_mfma_scale_f32_16x16x128_f8f6f4 v[70:73], v[2:9], v[230:237], v[70:73], v214, v214 op_sel_hi:[0,0,0]
	v_mfma_scale_f32_16x16x128_f8f6f4 v[66:69], v[10:17], v[230:237], v[66:69], v214, v214 op_sel_hi:[0,0,0]
	v_mfma_scale_f32_16x16x128_f8f6f4 v[62:65], v[2:9], v[238:245], v[62:65], v214, v214 op_sel_hi:[0,0,0]
	v_mfma_scale_f32_16x16x128_f8f6f4 v[58:61], v[10:17], v[238:245], v[58:61], v214, v214 op_sel_hi:[0,0,0]
	v_mfma_scale_f32_16x16x128_f8f6f4 v[54:57], v[2:9], v[246:253], v[54:57], v214, v214 op_sel_hi:[0,0,0]
	v_mfma_scale_f32_16x16x128_f8f6f4 v[50:53], v[10:17], v[246:253], v[50:53], v214, v214 op_sel_hi:[0,0,0]
	s_nop 3
	s_setprio 0
	s_setprio 2
	v_mfma_scale_f32_16x16x128_f8f6f4 v[46:49], v[18:25], v[222:229], v[46:49], v214, v214 op_sel_hi:[0,0,0]
	v_mfma_scale_f32_16x16x128_f8f6f4 v[42:45], v[26:33], v[222:229], v[42:45], v214, v214 op_sel_hi:[0,0,0]
	v_mfma_scale_f32_16x16x128_f8f6f4 v[38:41], v[18:25], v[230:237], v[38:41], v214, v214 op_sel_hi:[0,0,0]
	v_mfma_scale_f32_16x16x128_f8f6f4 v[34:37], v[26:33], v[230:237], v[34:37], v214, v214 op_sel_hi:[0,0,0]
	v_mfma_scale_f32_16x16x128_f8f6f4 v[146:149], v[18:25], v[238:245], v[146:149], v214, v214 op_sel_hi:[0,0,0]
	v_mfma_scale_f32_16x16x128_f8f6f4 v[150:153], v[26:33], v[238:245], v[150:153], v214, v214 op_sel_hi:[0,0,0]
	v_mfma_scale_f32_16x16x128_f8f6f4 v[154:157], v[18:25], v[246:253], v[154:157], v214, v214 op_sel_hi:[0,0,0]
	v_mfma_scale_f32_16x16x128_f8f6f4 v[158:161], v[26:33], v[246:253], v[158:161], v214, v214 op_sel_hi:[0,0,0]
	s_nop 3
	s_setprio 0
	s_add_i32 s69, s69, 2
	s_add_u32 s21, s21, 0x10000
	s_addc_u32 s68, s68, 0
	s_cmp_gt_u32 s69, 13
	s_cbranch_scc1 .LBB0_1062
	s_mov_b64 s[30:31], s[28:29]
	s_branch .Lh1_1058
.LBB0_1062:
	s_and_b64 vcc, exec, s[16:17]
	s_cbranch_vccz .LBB0_1064
; #define PG8_BAR __builtin_amdgcn_s_barrier()
; template <class Epi, class Sched, bool ALIGN_EPI = true, bool F8 = false>
; __device__ __forceinline__ void gemm_phase(PG8_LAS unsigned char* lds, const Sched& S, const Epi& E) {
;     ...
;         if constexpr (ALIGN_EPI) { if (wr == 0) PG8_BAR; }
;         if constexpr (F8) {
; #pragma unroll
;             for (int a = 0; a < 2; ++a)
; #pragma unroll
;                 for (int b = 0; b < 2; ++b)
;                     asm volatile("s_nop 15\n\ts_nop 7" : "+v"(acc[a][b][0][0]), "+v"(acc[a][b][0][1]), "+v"(acc[a][b][1][0]), "+v"(acc[a][b][1][1]), "+v"(acc[a][b][2][0]), "+v"(acc[a][b][2][1]), "+v"(acc[a][b][3][0]), "+v"(acc[a][b][3][1]));
;     __device__ __forceinline__ void operator()(AccRef acc, const GUnit& u, int wr, int wc, int fr, int fq) const {
;         const int e = u.x0, rt = u.x1, ct = u.x2, cnt = u.x3; const int p0 = rt * 256 + wr * 64 + fr;
;         const int odd = fq & 1;
;         unsigned char* blk = HID + ((size_t)((__builtin_amdgcn_readfirstlane(pre[e]) + rt) * (DE / 128) + ct) << 15) + (wr * 64 + fr) * 128 + wc * 32 + 16 * (fq >> 1);
; #pragma unroll
;         for (int ai = 0; ai < 2; ++ai)
; #pragma unroll
;             for (int mp = 0; mp < 4; mp += 2) {
;                 f32x4 v0, v1, w0, w1;
; #pragma unroll
;                 for (int j = 0; j < 4; ++j) { const float a0 = acc[ai][0][mp][0][j] * W8_INV, a1 = acc[ai][0][mp][1][j] * W8_INV; v0[j] = a0 * fsigmoid(a0) * (acc[ai][1][mp][0][j] * W8_INV); v1[j] = a1 * fsigmoid(a1) * (acc[ai][1][mp][1][j] * W8_INV); }
; #pragma unroll
;                 for (int j = 0; j < 4; ++j) { const float a0 = acc[ai][0][mp + 1][0][j] * W8_INV, a1 = acc[ai][0][mp + 1][1][j] * W8_INV; w0[j] = a0 * fsigmoid(a0) * (acc[ai][1][mp + 1][0][j] * W8_INV); w1[j] = a1 * fsigmoid(a1) * (acc[ai][1][mp + 1][1][j] * W8_INV); }
;                 const unsigned lo0 = pk4_fp8(v0[0], v0[1], v0[2], v0[3]), hi0 = pk4_fp8(v1[0], v1[1], v1[2], v1[3]), lo1 = pk4_fp8(w0[0], w0[1], w0[2], w0[3]), hi1 = pk4_fp8(w1[0], w1[1], w1[2], w1[3]);
;                 const auto sl = __builtin_amdgcn_permlane16_swap(lo0, lo1, false, false), sh = __builtin_amdgcn_permlane16_swap(hi0, hi1, false, false);
;                 const int p = p0 + ai * 128 + (mp + odd) * 16;
;                 if (p < cnt) *(u32x4*)(blk + (ai * 128 + (mp + odd) * 16) * 128) = (u32x4){sl[0], sh[0], sl[1], sh[1]}; }
.LBB0_1064:
	s_lshl_b32 s21, s0, 2
	s_add_i32 s21, s21, 0
	s_add_i32 s21, s21, 0x24100
	v_mov_b32_e32 v2, s21
	s_nop 15
	s_nop 7
	s_nop 15
	s_nop 7
	s_nop 15
	s_nop 7
	s_nop 15
	s_nop 7
	ds_read_b32 v2, v2
	v_mul_f32_e32 v4, 0x3c800000, v138
	v_mul_f32_e32 v5, 0xbfb8aa3b, v4
	v_exp_f32_e32 v5, v5
	v_mul_f32_e32 v9, 0x3c800000, v139
	s_waitcnt lgkmcnt(0)
	v_readfirstlane_b32 s21, v2
	v_mul_f32_e32 v2, 0x3c800000, v142
	v_mul_f32_e32 v3, 0xbfb8aa3b, v2
	v_exp_f32_e32 v3, v3
	v_add_f32_e32 v5, 1.0, v5
	v_rcp_f32_e32 v5, v5
	v_mul_f32_e32 v11, 0xbfb8aa3b, v9
	v_add_f32_e32 v3, 1.0, v3
	v_rcp_f32_e32 v3, v3
	v_exp_f32_e32 v11, v11
	v_mul_f32_e32 v12, 0x3c800000, v140
	v_mul_f32_e32 v13, 0xbfb8aa3b, v12
	v_mul_f32_e32 v2, v2, v3
	v_mul_f32_e32 v3, 0x3c800000, v110
	v_mul_f32_e32 v2, v3, v2
	v_mul_f32_e32 v3, v4, v5
	v_mul_f32_e32 v5, 0x3c800000, v143
	v_mul_f32_e32 v8, 0xbfb8aa3b, v5
	v_exp_f32_e32 v8, v8
	v_mul_f32_e32 v4, 0x3c800000, v106
	v_mul_f32_e32 v3, v4, v3
	v_add_f32_e32 v4, 1.0, v11
	v_add_f32_e32 v8, 1.0, v8
	v_rcp_f32_e32 v8, v8
	v_rcp_f32_e32 v4, v4
	v_exp_f32_e32 v13, v13
	v_mul_f32_e32 v14, 0x3c800000, v141
	v_mul_f32_e32 v5, v5, v8
	v_mul_f32_e32 v8, 0x3c800000, v111
	v_mul_f32_e32 v5, v8, v5
	v_mul_f32_e32 v4, v9, v4
	v_mul_f32_e32 v8, 0x3c800000, v107
	v_mul_f32_e32 v9, 0x3c800000, v144
	v_mul_f32_e32 v11, 0xbfb8aa3b, v9
	v_mul_f32_e32 v4, v8, v4
	v_add_f32_e32 v8, 1.0, v13
	v_exp_f32_e32 v11, v11
	v_rcp_f32_e32 v8, v8
	v_mul_f32_e32 v15, 0xbfb8aa3b, v14
	v_exp_f32_e32 v15, v15
	v_add_f32_e32 v11, 1.0, v11
	v_mul_f32_e32 v8, v12, v8
	v_mul_f32_e32 v12, 0x3c800000, v145
	v_rcp_f32_e32 v11, v11
	v_mul_f32_e32 v13, 0xbfb8aa3b, v12
	v_exp_f32_e32 v13, v13
	v_mul_f32_e32 v16, 0x3c800000, v130
	v_mul_f32_e32 v9, v9, v11
	v_mul_f32_e32 v11, 0x3c800000, v112
	v_mul_f32_e32 v9, v11, v9
	v_mul_f32_e32 v11, 0x3c800000, v108
	v_add_f32_e32 v13, 1.0, v13
	v_rcp_f32_e32 v13, v13
	v_mul_f32_e32 v8, v11, v8
	v_add_f32_e32 v11, 1.0, v15
	v_rcp_f32_e32 v11, v11
	v_mul_f32_e32 v17, 0xbfb8aa3b, v16
	v_exp_f32_e32 v17, v17
	v_mul_f32_e32 v12, v12, v13
	v_mul_f32_e32 v13, 0x3c800000, v113
	v_mul_f32_e32 v12, v13, v12
	v_mul_f32_e32 v11, v14, v11
	v_mul_f32_e32 v13, 0x3c800000, v109
	v_mul_f32_e32 v14, 0x3c800000, v134
	v_mul_f32_e32 v15, 0xbfb8aa3b, v14
	v_mul_f32_e32 v11, v13, v11
	v_add_f32_e32 v13, 1.0, v17
	v_exp_f32_e32 v15, v15
	v_rcp_f32_e32 v13, v13
	v_mul_f32_e32 v18, 0x3c800000, v131
	v_mul_f32_e32 v19, 0xbfb8aa3b, v18
	v_add_f32_e32 v15, 1.0, v15
	v_mul_f32_e32 v13, v16, v13
	v_mul_f32_e32 v16, 0x3c800000, v135
	v_rcp_f32_e32 v15, v15
	v_mul_f32_e32 v17, 0xbfb8aa3b, v16
	v_exp_f32_e32 v17, v17
	v_exp_f32_e32 v19, v19
	v_mul_f32_e32 v14, v14, v15
	v_mul_f32_e32 v15, 0x3c800000, v102
	v_mul_f32_e32 v14, v15, v14
	v_mul_f32_e32 v15, 0x3c800000, v98
	v_add_f32_e32 v17, 1.0, v17
	v_rcp_f32_e32 v17, v17
	v_mul_f32_e32 v13, v15, v13
	v_add_f32_e32 v15, 1.0, v19
	v_mul_f32_e32 v20, 0x3c800000, v132
	v_rcp_f32_e32 v15, v15
	v_mul_f32_e32 v21, 0xbfb8aa3b, v20
	v_exp_f32_e32 v21, v21
	v_mul_f32_e32 v16, v16, v17
	v_mul_f32_e32 v17, 0x3c800000, v103
	v_mul_f32_e32 v16, v17, v16
	v_mul_f32_e32 v15, v18, v15
	v_mul_f32_e32 v17, 0x3c800000, v99
	v_mul_f32_e32 v18, 0x3c800000, v136
	v_mul_f32_e32 v19, 0xbfb8aa3b, v18
	v_mul_f32_e32 v15, v17, v15
	v_add_f32_e32 v17, 1.0, v21
	v_exp_f32_e32 v19, v19
	v_rcp_f32_e32 v17, v17
	v_mul_f32_e32 v22, 0x3c800000, v133
	v_mul_f32_e32 v23, 0xbfb8aa3b, v22
	v_add_f32_e32 v19, 1.0, v19
	v_mul_f32_e32 v17, v20, v17
	v_mul_f32_e32 v20, 0x3c800000, v137
	v_rcp_f32_e32 v19, v19
	v_mul_f32_e32 v21, 0xbfb8aa3b, v20
	v_exp_f32_e32 v21, v21
	v_exp_f32_e32 v23, v23
	v_mul_f32_e32 v18, v18, v19
	v_mul_f32_e32 v19, 0x3c800000, v104
	v_mul_f32_e32 v18, v19, v18
	v_mul_f32_e32 v19, 0x3c800000, v100
	v_add_f32_e32 v21, 1.0, v21
	v_rcp_f32_e32 v21, v21
	v_mul_f32_e32 v17, v19, v17
	v_add_f32_e32 v19, 1.0, v23
	v_rcp_f32_e32 v19, v19
	v_mul_f32_e32 v20, v20, v21
	v_mul_f32_e32 v21, 0x3c800000, v105
	v_mul_f32_e32 v20, v21, v20
	v_mul_f32_e32 v19, v22, v19
	v_mul_f32_e32 v21, 0x3c800000, v101
	v_mul_f32_e32 v19, v21, v19
	v_med3_f32 v21, v2, s63, v215
	v_med3_f32 v5, v5, s63, v215
	v_mov_b32_e32 v2, v171
	v_cvt_pk_fp8_f32 v2, v21, v5
	v_med3_f32 v5, v9, s63, v215
	v_med3_f32 v9, v12, s63, v215
	v_med3_f32 v12, v3, s63, v215
	v_med3_f32 v4, v4, s63, v215
	v_mov_b32_e32 v3, v171
	v_cvt_pk_fp8_f32 v3, v12, v4
	v_cvt_pk_fp8_f32 v2, v5, v9 op_sel:[0,0,1]
	v_med3_f32 v4, v8, s63, v215
	v_med3_f32 v5, v11, s63, v215
	v_cvt_pk_fp8_f32 v3, v4, v5 op_sel:[0,0,1]
	v_med3_f32 v5, v14, s63, v215
	v_med3_f32 v8, v16, s63, v215
	v_mov_b32_e32 v4, v171
	v_cvt_pk_fp8_f32 v4, v5, v8
	v_med3_f32 v11, v13, s63, v215
	v_med3_f32 v12, v15, s63, v215
	v_mov_b32_e32 v5, v171
	v_cvt_pk_fp8_f32 v5, v11, v12
	s_add_i32 s21, s21, s50
	v_med3_f32 v8, v18, s63, v215
	v_med3_f32 v9, v20, s63, v215
	s_lshl_b32 s21, s21, 3
	v_cvt_pk_fp8_f32 v4, v8, v9 op_sel:[0,0,1]
	v_med3_f32 v8, v17, s63, v215
	v_med3_f32 v9, v19, s63, v215
	s_add_i32 s28, s21, s49
	v_cvt_pk_fp8_f32 v5, v8, v9 op_sel:[0,0,1]
	s_ashr_i32 s29, s28, 31
	s_lshl_b64 s[28:29], s[28:29], 15
	v_lshl_add_u32 v10, s50, 8, v209
	v_lshl_add_u64 v[6:7], v[178:179], 0, s[28:29]
	v_or_b32_e32 v8, v10, v173
	v_permlane16_swap_b32_e32 v2, v4
	v_permlane16_swap_b32_e32 v3, v5
	v_cmp_gt_i32_e32 vcc, s51, v8
	v_lshl_add_u64 v[8:9], v[6:7], 0, v[180:181]
	s_and_saveexec_b64 s[28:29], vcc
	s_cbranch_execz .LBB0_1066
	flat_store_dwordx4 v[8:9], v[2:5]

; #define PG8_STAGE(bufoff, gbase, voff) do { _Pragma("unroll") for (int _i = 0; _i < 2; ++_i) \
;         __builtin_amdgcn_global_load_lds((const unsigned*)((const char*)(gbase) + (voff)[_i]), (PG8_LAS unsigned*)(lds + (bufoff) + ldsw + _i * 8192), 16, 0, 0); } while (0)
; #define PG8_WAIT_V(n) asm volatile("s_waitcnt vmcnt(" #n ")" ::: "memory")
; #define PG8_BAR __builtin_amdgcn_s_barrier()
; template <class Epi, class Sched, bool ALIGN_EPI = true, bool F8 = false>
; __device__ __forceinline__ void gemm_phase(PG8_LAS unsigned char* lds, const Sched& S, const Epi& E) {
;     ...
;     const char* cA = cur.A; const char* cB = cur.B;
;     PG8_STAGE(PG8_SB(0, 0), cB, voffB[0]); PG8_STAGE(PG8_SB(0, 1), cB, voffB[1]); PG8_STAGE(PG8_SA(0, 0), cA, voffA[0]); PG8_STAGE(PG8_SA(0, 1), cA, voffA[1]);
;     if (wr == 1) PG8_BAR;
;     PG8_WAIT_V(2); PG8_BAR;
;     PG8_STAGE(PG8_SB(1, 0), cB + kstepB, voffB[0]); PG8_STAGE(PG8_SA(1, 0), cA + kstep, voffA[0]); PG8_STAGE(PG8_SB(1, 1), cB + kstepB, voffB[1]);
;     PG8_WAIT_V(6); PG8_BAR;
.LBB0_1128:
	v_lshlrev_b32_e32 v2, 4, v0
	v_and_b32_e32 v3, 32, v0
	v_lshrrev_b32_e32 v7, 2, v0
	v_bfe_u32 v5, v0, 2, 4
	v_lshrrev_b32_e32 v6, 3, v0
	v_and_b32_e32 v162, 48, v0
	v_lshrrev_b32_e32 v11, 5, v0
	v_bitop3_b32 v3, v2, v3, 48 bitop3:0x6c
	v_and_b32_e32 v4, 64, v0
	v_and_or_b32 v9, v6, 48, v5
	v_or_b32_e32 v6, 0x2000, v2
	v_and_b32_e32 v11, 4, v11
	v_bfe_u32 v12, v0, 2, 2
	v_and_or_b32 v7, v7, 64, v162
	s_lshr_b32 s12, s6, 6
	v_or_b32_e32 v8, v3, v4
	v_lshrrev_b32_e32 v10, 7, v6
	s_movk_i32 s4, 0x70
	v_or3_b32 v7, v7, v11, v12
	v_and_or_b32 v10, v10, s4, v5
	v_lshl_or_b32 v164, v7, 7, v8
	v_lshrrev_b32_e32 v7, 6, v6
	s_movk_i32 s4, 0xc0
	s_lshl_b32 s43, s12, 10
	v_and_or_b32 v7, v7, s4, v162
	s_add_i32 s44, s43, 0
	v_mov_b32_e32 v177, 0
	v_or3_b32 v7, v7, v11, v12
	s_add_i32 m0, s44, 0x10000
	v_mov_b32_e32 v165, v177
	v_lshl_or_b32 v166, v7, 7, v8
	v_lshl_or_b32 v168, v9, 7, v8
	v_lshl_or_b32 v170, v10, 7, v8
	v_lshl_add_u64 v[8:9], s[26:27], 0, v[164:165]
	global_load_lds_dwordx4 v164, s[26:27]
	v_mov_b32_e32 v167, v177
	s_add_i32 m0, s44, 0x12000
	s_mov_b64 s[4:5], 0x400
	v_lshl_add_u64 v[10:11], s[26:27], 0, v[166:167]
	global_load_lds_dwordx4 v166, s[26:27]
	s_add_i32 m0, s44, 0x14000
	v_lshl_add_u64 v[8:9], v[8:9], 0, s[4:5]
	global_load_lds_dwordx4 v[8:9], off
	v_lshl_add_u64 v[8:9], v[10:11], 0, s[4:5]
	s_add_i32 m0, s44, 0x16000
	s_add_i32 s45, s44, 0x2000
	global_load_lds_dwordx4 v[8:9], off
	s_mov_b32 m0, s44
	s_add_i32 s46, s44, 0x4000
	global_load_lds_dwordx4 v168, s[24:25]
	s_mov_b32 m0, s45
	v_or_b32_e32 v172, 0x4000, v168
	global_load_lds_dwordx4 v170, s[24:25]
	s_mov_b32 m0, s46
	s_add_i32 s47, s44, 0x6000
	v_or_b32_e32 v174, 0x4000, v170
	global_load_lds_dwordx4 v172, s[24:25]
	s_mov_b32 m0, s47
	s_lshr_b32 s13, s6, 8
	global_load_lds_dwordx4 v174, s[24:25]
	s_cmp_eq_u32 s13, 1
	s_movk_i32 s14, 0x4000
	s_mov_b32 s7, 0
	v_mov_b32_e32 v169, v177
	s_cselect_b64 s[8:9], -1, 0
	s_cmp_lg_u32 s13, 1
	v_mov_b32_e32 v171, v177
	s_cbranch_scc1 .LBB0_1130
.LBB0_1130:
	s_add_u32 s10, s36, 0x2e000000
	s_addc_u32 s11, s37, 0
	s_add_u32 s49, s36, 0xd00000
	s_addc_u32 s50, s37, 0
	s_and_b32 s20, s12, 3
	s_lshl_b32 s12, s13, 13
	s_lshl_b32 s21, s20, 12
	s_add_u32 s16, s26, 0x8000
	s_addc_u32 s17, s27, 0
	s_add_i32 m0, s44, 0x18000
	v_lshl_add_u64 v[8:9], s[16:17], 0, v[164:165]
	s_waitcnt vmcnt(2)
	s_barrier
	global_load_lds_dwordx4 v[8:9], off
	s_add_i32 m0, s44, 0x1a000
	s_add_u32 s18, s24, 0x8000
	v_lshl_add_u64 v[8:9], s[16:17], 0, v[166:167]
	s_addc_u32 s19, s25, 0
	s_add_i32 s51, s44, 0x8000
	global_load_lds_dwordx4 v[8:9], off
	v_lshl_add_u64 v[8:9], s[18:19], 0, v[168:169]
	s_mov_b32 m0, s51
	s_add_i32 s52, s44, 0xa000
	global_load_lds_dwordx4 v[8:9], off
	v_lshl_add_u64 v[8:9], s[18:19], 0, v[170:171]
	s_mov_b32 m0, s52
	v_or_b32_e32 v178, 0x400, v164
	global_load_lds_dwordx4 v[8:9], off
	s_add_i32 m0, s44, 0x1c000
	v_or_b32_e32 v180, 0x400, v166
	global_load_lds_dwordx4 v178, s[16:17]
	s_add_i32 m0, s44, 0x1e000
	v_and_b32_e32 v7, 15, v0
	global_load_lds_dwordx4 v180, s[16:17]
	v_lshlrev_b32_e32 v8, 2, v0
	v_lshl_or_b32 v186, s13, 6, v7
	v_lshl_or_b32 v7, v7, 6, v162
	v_and_b32_e32 v8, 32, v8
	v_bitop3_b32 v7, v7, s12, v8 bitop3:0xde
	v_lshlrev_b32_e32 v9, 6, v0
	s_movk_i32 s12, 0x3c0
	v_and_b32_e32 v6, 0x3800, v6
	v_lshlrev_b32_e32 v5, 7, v5
	v_and_b32_e32 v2, 0x1800, v2
	v_and_or_b32 v9, v9, s12, v162
	s_waitcnt vmcnt(6)
	s_cmpk_lt_u32 s6, 0x100
	v_or3_b32 v6, v3, v6, v5
	v_or3_b32 v2, v3, v2, v5
	v_bitop3_b32 v187, s21, v9, v8 bitop3:0xf6
	s_cselect_b64 s[12:13], -1, 0
	v_add3_u32 v182, v6, v4, s14
	v_add_u32_e32 v2, v2, v4
	s_add_i32 s14, 0, 0x24180
	s_add_i32 s53, 0, 0x10000
	s_add_i32 s58, 0, 0x14000
	v_mov_b32_e32 v173, v177
	v_mov_b32_e32 v175, v177
	v_mov_b32_e32 v179, v177
	v_mov_b32_e32 v181, v177
	s_lshl_b32 s6, s20, 6
	v_mov_b32_e32 v163, v177
	v_mov_b32_e32 v183, v177
	v_or_b32_e32 v184, 0x4000, v2
	v_mov_b32_e32 v185, v177
	v_mov_b32_e32 v188, s14
	v_add_u32_e32 v189, s53, v187
	v_add_u32_e32 v190, s58, v187
	v_add_u32_e32 v191, 0, v7
	v_mov_b32_e32 v192, 0x7f7f7f7f
	s_mov_b32 s14, 0x3e800000
	s_mov_b32 s59, 0xc3e00000
	v_mov_b32_e32 v193, 0x43e00000
	s_mov_b32 s61, s7
	s_mov_b64 s[16:17], s[24:25]
	s_mov_b64 s[18:19], s[26:27]
	s_barrier
	s_branch .LBB0_1133

; #define PG8_STAGE(bufoff, gbase, voff) do { _Pragma("unroll") for (int _i = 0; _i < 2; ++_i) \
;         __builtin_amdgcn_global_load_lds((const unsigned*)((const char*)(gbase) + (voff)[_i]), (PG8_LAS unsigned*)(lds + (bufoff) + ldsw + _i * 8192), 16, 0, 0); } while (0)
; #define PG8_WAIT_V(n) asm volatile("s_waitcnt vmcnt(" #n ")" ::: "memory")
; #define PG8_WAIT_L(n) asm volatile("s_waitcnt lgkmcnt(" #n ")" ::: "memory")
; #define PG8_BAR __builtin_amdgcn_s_barrier()
; #define PG8_SCHED __builtin_amdgcn_sched_barrier(0)
; template <class Epi, class Sched, bool ALIGN_EPI = true, bool F8 = false>
; __device__ __forceinline__ void gemm_phase(PG8_LAS unsigned char* lds, const Sched& S, const Epi& E) {
;     ...
;             PG8_LDB(B0, 0, 0); PG8_LDB(B1, 0, 1); PG8_SCHED; PG8_LDA(At, 0, 0); PG8_STAGE(PG8_SA(1, 1), a1, voffA[1]);
;             PG8_WAIT_V(8); PG8_WAIT_L(0); PG8_BAR; PG8_MMA(0, 0, At, B0); PG8_MMA(0, 1, At, B1); PG8_BAR; PG8_SCHED;
;     ...
;                     for (int n = 0; n < 2; ++n) acc[a][b][m][n] = (f32x4){0.f, 0.f, 0.f, 0.f};
;         }
;         cur = nxt; cA = nA; cB = nB; ++ui;
.LBB0_1137:
	s_add_u32 s23, s26, 0x10000
	s_addc_u32 s67, s27, 0
	s_add_u32 s24, s24, 0x8000
	v_mov_b32_e32 v34, 0
	s_addc_u32 s25, s25, 0
	s_mov_b32 s68, -2
	v_mov_b32_e32 v35, v34
	v_mov_b32_e32 v36, v34
	v_mov_b32_e32 v37, v34
	v_mov_b32_e32 v38, v34
	v_mov_b32_e32 v39, v34
	v_mov_b32_e32 v40, v34
	v_mov_b32_e32 v41, v34
	v_mov_b32_e32 v50, v34
	v_mov_b32_e32 v51, v34
	v_mov_b32_e32 v52, v34
	v_mov_b32_e32 v53, v34
	v_mov_b32_e32 v54, v34
	v_mov_b32_e32 v55, v34
	v_mov_b32_e32 v56, v34
	v_mov_b32_e32 v57, v34
	v_mov_b32_e32 v66, v34
	v_mov_b32_e32 v67, v34
	v_mov_b32_e32 v68, v34
	v_mov_b32_e32 v69, v34
	v_mov_b32_e32 v70, v34
	v_mov_b32_e32 v71, v34
	v_mov_b32_e32 v72, v34
	v_mov_b32_e32 v73, v34
	v_mov_b32_e32 v82, v34
	v_mov_b32_e32 v83, v34
	v_mov_b32_e32 v84, v34
	v_mov_b32_e32 v85, v34
	v_mov_b32_e32 v86, v34
	v_mov_b32_e32 v87, v34
	v_mov_b32_e32 v88, v34
	v_mov_b32_e32 v89, v34
	v_mov_b32_e32 v42, v34
	v_mov_b32_e32 v43, v34
	v_mov_b32_e32 v44, v34
	v_mov_b32_e32 v45, v34
	v_mov_b32_e32 v46, v34
	v_mov_b32_e32 v47, v34
	v_mov_b32_e32 v48, v34
	v_mov_b32_e32 v49, v34
	v_mov_b32_e32 v58, v34
	v_mov_b32_e32 v59, v34
	v_mov_b32_e32 v60, v34
	v_mov_b32_e32 v61, v34
	v_mov_b32_e32 v62, v34
	v_mov_b32_e32 v63, v34
	v_mov_b32_e32 v64, v34
	v_mov_b32_e32 v65, v34
	v_mov_b32_e32 v74, v34
	v_mov_b32_e32 v75, v34
	v_mov_b32_e32 v76, v34
	v_mov_b32_e32 v77, v34
	v_mov_b32_e32 v78, v34
	v_mov_b32_e32 v79, v34
	v_mov_b32_e32 v80, v34
	v_mov_b32_e32 v81, v34
	v_mov_b32_e32 v90, v34
	v_mov_b32_e32 v91, v34
	v_mov_b32_e32 v92, v34
	v_mov_b32_e32 v93, v34
	v_mov_b32_e32 v94, v34
	v_mov_b32_e32 v95, v34
	v_mov_b32_e32 v96, v34
	v_mov_b32_e32 v97, v34
	v_mov_b32_e32 v98, v34
	v_mov_b32_e32 v99, v34
	v_mov_b32_e32 v100, v34
	v_mov_b32_e32 v101, v34
	v_mov_b32_e32 v102, v34
	v_mov_b32_e32 v103, v34
	v_mov_b32_e32 v104, v34
	v_mov_b32_e32 v105, v34
	v_mov_b32_e32 v114, v34
	v_mov_b32_e32 v115, v34
	v_mov_b32_e32 v116, v34
	v_mov_b32_e32 v117, v34
	v_mov_b32_e32 v118, v34
	v_mov_b32_e32 v119, v34
	v_mov_b32_e32 v120, v34
	v_mov_b32_e32 v121, v34
	v_mov_b32_e32 v130, v34
	v_mov_b32_e32 v131, v34
	v_mov_b32_e32 v132, v34
	v_mov_b32_e32 v133, v34
	v_mov_b32_e32 v134, v34
	v_mov_b32_e32 v135, v34
	v_mov_b32_e32 v136, v34
	v_mov_b32_e32 v137, v34
	v_mov_b32_e32 v146, v34
	v_mov_b32_e32 v147, v34
	v_mov_b32_e32 v148, v34
	v_mov_b32_e32 v149, v34
	v_mov_b32_e32 v150, v34
	v_mov_b32_e32 v151, v34
	v_mov_b32_e32 v152, v34
	v_mov_b32_e32 v153, v34
	v_mov_b32_e32 v106, v34
	v_mov_b32_e32 v107, v34
	v_mov_b32_e32 v108, v34
	v_mov_b32_e32 v109, v34
	v_mov_b32_e32 v110, v34
	v_mov_b32_e32 v111, v34
	v_mov_b32_e32 v112, v34
	v_mov_b32_e32 v113, v34
	v_mov_b32_e32 v122, v34
	v_mov_b32_e32 v123, v34
	v_mov_b32_e32 v124, v34
	v_mov_b32_e32 v125, v34
	v_mov_b32_e32 v126, v34
	v_mov_b32_e32 v127, v34
	v_mov_b32_e32 v128, v34
	v_mov_b32_e32 v129, v34
	v_mov_b32_e32 v138, v34
	v_mov_b32_e32 v139, v34
	v_mov_b32_e32 v140, v34
	v_mov_b32_e32 v141, v34
	v_mov_b32_e32 v142, v34
	v_mov_b32_e32 v143, v34
	v_mov_b32_e32 v144, v34
	v_mov_b32_e32 v145, v34
	v_mov_b32_e32 v154, v34
	v_mov_b32_e32 v155, v34
	v_mov_b32_e32 v156, v34
	v_mov_b32_e32 v157, v34
	v_mov_b32_e32 v158, v34
	v_mov_b32_e32 v159, v34
	v_mov_b32_e32 v160, v34
	v_mov_b32_e32 v161, v34
	s_bitcmp1_b32 s3, 2
	s_cbranch_scc1 .Lh1_1138
.LBB0_1138:
	ds_read_b128 v[18:21], v189
	ds_read_b128 v[22:25], v189 offset:1024
	ds_read_b128 v[26:29], v189 offset:2048
	ds_read_b128 v[30:33], v189 offset:3072
	ds_read_b128 v[2:5], v190
	ds_read_b128 v[6:9], v190 offset:1024
	ds_read_b128 v[10:13], v190 offset:2048
	ds_read_b128 v[14:17], v190 offset:3072
	s_add_u32 s26, s24, 0x8000
	s_addc_u32 s27, s25, 0
	s_cmp_eq_u32 s68, 4
	s_cselect_b32 s30, s16, s26
	s_cselect_b32 s31, s17, s27
	s_cselect_b32 s28, s18, s23
	s_cselect_b32 s29, s19, s67
	s_add_u32 s26, s30, 0x8000
	s_addc_u32 s27, s31, 0
	v_lshl_add_u64 v[226:227], s[24:25], 0, v[184:185]
	s_add_i32 m0, s44, 0xc000
	ds_read_b128 v[194:197], v191
	ds_read_b128 v[198:201], v191 offset:1024
	ds_read_b128 v[202:205], v191 offset:2048
	ds_read_b128 v[206:209], v191 offset:3072
	ds_read_b128 v[210:213], v191 offset:4096
	ds_read_b128 v[214:217], v191 offset:5120
	ds_read_b128 v[218:221], v191 offset:6144
	ds_read_b128 v[222:225], v191 offset:7168
	global_load_lds_dwordx4 v[226:227], off
	v_lshl_add_u64 v[226:227], s[24:25], 0, v[182:183]
	s_add_i32 m0, s44, 0xe000
	s_nop 0
	global_load_lds_dwordx4 v[226:227], off
	s_waitcnt vmcnt(8)
	s_waitcnt lgkmcnt(0)
	s_setprio 1
	s_waitcnt lgkmcnt(0)
	v_mfma_scale_f32_16x16x128_f8f6f4 v[158:161], v[18:25], v[194:201], v[158:161], v192, v192 op_sel_hi:[0,0,0]
	v_mfma_scale_f32_16x16x128_f8f6f4 v[154:157], v[26:33], v[194:201], v[154:157], v192, v192 op_sel_hi:[0,0,0]
	v_mfma_scale_f32_16x16x128_f8f6f4 v[142:145], v[18:25], v[202:209], v[142:145], v192, v192 op_sel_hi:[0,0,0]
	v_mfma_scale_f32_16x16x128_f8f6f4 v[138:141], v[26:33], v[202:209], v[138:141], v192, v192 op_sel_hi:[0,0,0]
	v_mfma_scale_f32_16x16x128_f8f6f4 v[126:129], v[18:25], v[210:217], v[126:129], v192, v192 op_sel_hi:[0,0,0]
	v_mfma_scale_f32_16x16x128_f8f6f4 v[122:125], v[26:33], v[210:217], v[122:125], v192, v192 op_sel_hi:[0,0,0]
	v_mfma_scale_f32_16x16x128_f8f6f4 v[110:113], v[18:25], v[218:225], v[110:113], v192, v192 op_sel_hi:[0,0,0]
	v_mfma_scale_f32_16x16x128_f8f6f4 v[106:109], v[26:33], v[218:225], v[106:109], v192, v192 op_sel_hi:[0,0,0]
	s_nop 3
	s_setprio 0
	s_setprio 1
	v_mfma_scale_f32_16x16x128_f8f6f4 v[150:153], v[2:9], v[194:201], v[150:153], v192, v192 op_sel_hi:[0,0,0]
	v_mfma_scale_f32_16x16x128_f8f6f4 v[146:149], v[10:17], v[194:201], v[146:149], v192, v192 op_sel_hi:[0,0,0]
	v_mfma_scale_f32_16x16x128_f8f6f4 v[134:137], v[2:9], v[202:209], v[134:137], v192, v192 op_sel_hi:[0,0,0]
	v_mfma_scale_f32_16x16x128_f8f6f4 v[130:133], v[10:17], v[202:209], v[130:133], v192, v192 op_sel_hi:[0,0,0]
	v_mfma_scale_f32_16x16x128_f8f6f4 v[118:121], v[2:9], v[210:217], v[118:121], v192, v192 op_sel_hi:[0,0,0]
	v_mfma_scale_f32_16x16x128_f8f6f4 v[114:117], v[10:17], v[210:217], v[114:117], v192, v192 op_sel_hi:[0,0,0]
	v_mfma_scale_f32_16x16x128_f8f6f4 v[102:105], v[2:9], v[218:225], v[102:105], v192, v192 op_sel_hi:[0,0,0]
	v_mfma_scale_f32_16x16x128_f8f6f4 v[98:101], v[10:17], v[218:225], v[98:101], v192, v192 op_sel_hi:[0,0,0]
	s_nop 3
	s_setprio 0
	s_barrier
; #define PG8_STAGE(bufoff, gbase, voff) do { _Pragma("unroll") for (int _i = 0; _i < 2; ++_i) \
;         __builtin_amdgcn_global_load_lds((const unsigned*)((const char*)(gbase) + (voff)[_i]), (PG8_LAS unsigned*)(lds + (bufoff) + ldsw + _i * 8192), 16, 0, 0); } while (0)
; #define PG8_WAIT_V(n) asm volatile("s_waitcnt vmcnt(" #n ")" ::: "memory")
; #define PG8_WAIT_L(n) asm volatile("s_waitcnt lgkmcnt(" #n ")" ::: "memory")
; #define PG8_BAR __builtin_amdgcn_s_barrier()
; #define PG8_SCHED __builtin_amdgcn_sched_barrier(0)
; template <class Epi, class Sched, bool ALIGN_EPI = true, bool F8 = false>
; __device__ __forceinline__ void gemm_phase(PG8_LAS unsigned char* lds, const Sched& S, const Epi& E) {
;     ...
;             PG8_LDB(B0, 0, 0); PG8_LDB(B1, 0, 1); PG8_SCHED; PG8_LDA(At, 0, 0); PG8_STAGE(PG8_SA(1, 1), a1, voffA[1]);
;             PG8_WAIT_V(8); PG8_WAIT_L(0); PG8_BAR; PG8_MMA(0, 0, At, B0); PG8_MMA(0, 1, At, B1); PG8_BAR; PG8_SCHED;
;             PG8_LDA(At, 0, 1); PG8_STAGE(PG8_SB(0, 0), b2, voffB[0]); PG8_STAGE(PG8_SB(0, 1), b2, voffB[1]); PG8_STAGE(PG8_SA(0, 0), a2, vA2[0]);
;             PG8_WAIT_V(8); PG8_WAIT_L(0); PG8_BAR; PG8_MMA(1, 0, At, B0); PG8_MMA(1, 1, At, B1); PG8_BAR; PG8_SCHED;
;             PG8_LDB(B0, 1, 0); PG8_LDB(B1, 1, 1); PG8_SCHED; PG8_LDA(At, 1, 0); PG8_STAGE(PG8_SA(0, 1), a2, vA2[1]);
;             PG8_WAIT_V(8); PG8_WAIT_L(0); PG8_BAR; PG8_MMA(0, 0, At, B0); PG8_MMA(0, 1, At, B1); PG8_BAR; PG8_SCHED;
;             PG8_LDA(At, 1, 1); PG8_STAGE(PG8_SB(1, 0), b3, voffB[0]); PG8_STAGE(PG8_SB(1, 1), b3, voffB[1]); PG8_STAGE(PG8_SA(1, 0), a3, vA2[0]);
;             PG8_WAIT_V(8); PG8_WAIT_L(0); PG8_BAR; PG8_MMA(1, 0, At, B0); PG8_MMA(1, 1, At, B1); PG8_BAR; PG8_SCHED;
	s_add_i32 s69, s53, s43
	v_lshl_add_u64 v[226:227], s[28:29], 0, v[164:165]
	s_mov_b32 m0, s69
	ds_read_b128 v[194:197], v191 offset:16384
	ds_read_b128 v[198:201], v191 offset:17408
	ds_read_b128 v[202:205], v191 offset:18432
	ds_read_b128 v[206:209], v191 offset:19456
	ds_read_b128 v[210:213], v191 offset:20480
	ds_read_b128 v[214:217], v191 offset:21504
	ds_read_b128 v[218:221], v191 offset:22528
	ds_read_b128 v[222:225], v191 offset:23552
	global_load_lds_dwordx4 v[226:227], off
	v_lshl_add_u64 v[228:229], s[28:29], 0, v[166:167]
	s_add_i32 m0, s69, 0x2000
	s_add_i32 s69, s58, s43
	global_load_lds_dwordx4 v[228:229], off
	v_lshl_add_u64 v[226:227], v[226:227], 0, s[4:5]
	s_mov_b32 m0, s69
	s_nop 0
	global_load_lds_dwordx4 v[226:227], off
	v_lshl_add_u64 v[226:227], v[228:229], 0, s[4:5]
	s_add_i32 m0, s69, 0x2000
	s_nop 0
	global_load_lds_dwordx4 v[226:227], off
	v_lshl_add_u64 v[226:227], s[30:31], 0, v[168:169]
	s_mov_b32 m0, s44
	s_nop 0
	global_load_lds_dwordx4 v[226:227], off
	v_lshl_add_u64 v[226:227], s[30:31], 0, v[170:171]
	s_mov_b32 m0, s45
	s_nop 0
	global_load_lds_dwordx4 v[226:227], off
	s_waitcnt vmcnt(8)
	s_waitcnt lgkmcnt(0)
	s_setprio 1
	s_waitcnt lgkmcnt(0)
	v_mfma_scale_f32_16x16x128_f8f6f4 v[94:97], v[18:25], v[194:201], v[94:97], v192, v192 op_sel_hi:[0,0,0]
	v_mfma_scale_f32_16x16x128_f8f6f4 v[90:93], v[26:33], v[194:201], v[90:93], v192, v192 op_sel_hi:[0,0,0]
	v_mfma_scale_f32_16x16x128_f8f6f4 v[78:81], v[18:25], v[202:209], v[78:81], v192, v192 op_sel_hi:[0,0,0]
	v_mfma_scale_f32_16x16x128_f8f6f4 v[74:77], v[26:33], v[202:209], v[74:77], v192, v192 op_sel_hi:[0,0,0]
	v_mfma_scale_f32_16x16x128_f8f6f4 v[62:65], v[18:25], v[210:217], v[62:65], v192, v192 op_sel_hi:[0,0,0]
	v_mfma_scale_f32_16x16x128_f8f6f4 v[58:61], v[26:33], v[210:217], v[58:61], v192, v192 op_sel_hi:[0,0,0]
	v_mfma_scale_f32_16x16x128_f8f6f4 v[46:49], v[18:25], v[218:225], v[46:49], v192, v192 op_sel_hi:[0,0,0]
	v_mfma_scale_f32_16x16x128_f8f6f4 v[42:45], v[26:33], v[218:225], v[42:45], v192, v192 op_sel_hi:[0,0,0]
	s_nop 3
	s_setprio 0
	s_setprio 1
	v_mfma_scale_f32_16x16x128_f8f6f4 v[86:89], v[2:9], v[194:201], v[86:89], v192, v192 op_sel_hi:[0,0,0]
	v_mfma_scale_f32_16x16x128_f8f6f4 v[82:85], v[10:17], v[194:201], v[82:85], v192, v192 op_sel_hi:[0,0,0]
	v_mfma_scale_f32_16x16x128_f8f6f4 v[70:73], v[2:9], v[202:209], v[70:73], v192, v192 op_sel_hi:[0,0,0]
	v_mfma_scale_f32_16x16x128_f8f6f4 v[66:69], v[10:17], v[202:209], v[66:69], v192, v192 op_sel_hi:[0,0,0]
	v_mfma_scale_f32_16x16x128_f8f6f4 v[54:57], v[2:9], v[210:217], v[54:57], v192, v192 op_sel_hi:[0,0,0]
	v_mfma_scale_f32_16x16x128_f8f6f4 v[50:53], v[10:17], v[210:217], v[50:53], v192, v192 op_sel_hi:[0,0,0]
	v_mfma_scale_f32_16x16x128_f8f6f4 v[38:41], v[2:9], v[218:225], v[38:41], v192, v192 op_sel_hi:[0,0,0]
	v_mfma_scale_f32_16x16x128_f8f6f4 v[34:37], v[10:17], v[218:225], v[34:37], v192, v192 op_sel_hi:[0,0,0]
	s_nop 3
	s_setprio 0
	s_barrier
	s_add_i32 s69, 0, 0x18000
	s_add_i32 s70, 0, 0x1c000
	v_add_u32_e32 v14, s69, v187
	v_add_u32_e32 v30, s70, v187
	ds_read_b128 v[2:5], v14
	ds_read_b128 v[6:9], v14 offset:1024
	ds_read_b128 v[10:13], v14 offset:2048
	ds_read_b128 v[14:17], v14 offset:3072
	ds_read_b128 v[18:21], v30
	ds_read_b128 v[22:25], v30 offset:1024
	ds_read_b128 v[26:29], v30 offset:2048
	ds_read_b128 v[30:33], v30 offset:3072
	s_mov_b32 m0, s46
	v_lshl_add_u64 v[226:227], s[30:31], 0, v[172:173]
	ds_read_b128 v[194:197], v191 offset:32768
	ds_read_b128 v[198:201], v191 offset:33792
	ds_read_b128 v[202:205], v191 offset:34816
	ds_read_b128 v[206:209], v191 offset:35840
	ds_read_b128 v[210:213], v191 offset:36864
	ds_read_b128 v[214:217], v191 offset:37888
	ds_read_b128 v[218:221], v191 offset:38912
	ds_read_b128 v[222:225], v191 offset:39936
	global_load_lds_dwordx4 v[226:227], off
	v_lshl_add_u64 v[226:227], s[30:31], 0, v[174:175]
	s_mov_b32 m0, s47
	s_nop 0
	global_load_lds_dwordx4 v[226:227], off
	s_waitcnt vmcnt(8)
	s_waitcnt lgkmcnt(0)
	s_setprio 1
	s_waitcnt lgkmcnt(0)
	v_mfma_scale_f32_16x16x128_f8f6f4 v[158:161], v[2:9], v[194:201], v[158:161], v192, v192 op_sel_hi:[0,0,0]
	v_mfma_scale_f32_16x16x128_f8f6f4 v[154:157], v[10:17], v[194:201], v[154:157], v192, v192 op_sel_hi:[0,0,0]
	v_mfma_scale_f32_16x16x128_f8f6f4 v[142:145], v[2:9], v[202:209], v[142:145], v192, v192 op_sel_hi:[0,0,0]
	v_mfma_scale_f32_16x16x128_f8f6f4 v[138:141], v[10:17], v[202:209], v[138:141], v192, v192 op_sel_hi:[0,0,0]
	v_mfma_scale_f32_16x16x128_f8f6f4 v[126:129], v[2:9], v[210:217], v[126:129], v192, v192 op_sel_hi:[0,0,0]
	v_mfma_scale_f32_16x16x128_f8f6f4 v[122:125], v[10:17], v[210:217], v[122:125], v192, v192 op_sel_hi:[0,0,0]
	v_mfma_scale_f32_16x16x128_f8f6f4 v[110:113], v[2:9], v[218:225], v[110:113], v192, v192 op_sel_hi:[0,0,0]
	v_mfma_scale_f32_16x16x128_f8f6f4 v[106:109], v[10:17], v[218:225], v[106:109], v192, v192 op_sel_hi:[0,0,0]
	s_nop 3
	s_setprio 0
	s_setprio 1
	v_mfma_scale_f32_16x16x128_f8f6f4 v[150:153], v[18:25], v[194:201], v[150:153], v192, v192 op_sel_hi:[0,0,0]
	v_mfma_scale_f32_16x16x128_f8f6f4 v[146:149], v[26:33], v[194:201], v[146:149], v192, v192 op_sel_hi:[0,0,0]
	v_mfma_scale_f32_16x16x128_f8f6f4 v[134:137], v[18:25], v[202:209], v[134:137], v192, v192 op_sel_hi:[0,0,0]
	v_mfma_scale_f32_16x16x128_f8f6f4 v[130:133], v[26:33], v[202:209], v[130:133], v192, v192 op_sel_hi:[0,0,0]
	v_mfma_scale_f32_16x16x128_f8f6f4 v[118:121], v[18:25], v[210:217], v[118:121], v192, v192 op_sel_hi:[0,0,0]
	v_mfma_scale_f32_16x16x128_f8f6f4 v[114:117], v[26:33], v[210:217], v[114:117], v192, v192 op_sel_hi:[0,0,0]
	v_mfma_scale_f32_16x16x128_f8f6f4 v[102:105], v[18:25], v[218:225], v[102:105], v192, v192 op_sel_hi:[0,0,0]
	v_mfma_scale_f32_16x16x128_f8f6f4 v[98:101], v[26:33], v[218:225], v[98:101], v192, v192 op_sel_hi:[0,0,0]
	s_nop 3
	s_setprio 0
	s_barrier
; #define PG8_STAGE(bufoff, gbase, voff) do { _Pragma("unroll") for (int _i = 0; _i < 2; ++_i) \
;         __builtin_amdgcn_global_load_lds((const unsigned*)((const char*)(gbase) + (voff)[_i]), (PG8_LAS unsigned*)(lds + (bufoff) + ldsw + _i * 8192), 16, 0, 0); } while (0)
; #define PG8_WAIT_V(n) asm volatile("s_waitcnt vmcnt(" #n ")" ::: "memory")
; #define PG8_WAIT_L(n) asm volatile("s_waitcnt lgkmcnt(" #n ")" ::: "memory")
; #define PG8_BAR __builtin_amdgcn_s_barrier()
; #define PG8_SCHED __builtin_amdgcn_sched_barrier(0)
; template <class Epi, class Sched, bool ALIGN_EPI = true, bool F8 = false>
; __device__ __forceinline__ void gemm_phase(PG8_LAS unsigned char* lds, const Sched& S, const Epi& E) {
;     ...
;         for (int t = 0; t < nt; t += 2) {
;             const bool last = (t == nt - 2);
;             if constexpr (Sched::GATHER) { if (last && has_next) S.a_off(nxt, Rs, Cs, voffAn); }
;             const char* a1 = cA + (size_t)(t + 1) * kstep;
;             const char* a2 = last ? nA : cA + (size_t)(t + 2) * kstep; const char* b2 = last ? nB : cB + (size_t)(t + 2) * kstepB;
;             const char* a3 = a2 + kstep; const char* b3 = b2 + kstepB;
;     ...
;             PG8_LDA(At, 1, 1); PG8_STAGE(PG8_SB(1, 0), b3, voffB[0]); PG8_STAGE(PG8_SB(1, 1), b3, voffB[1]); PG8_STAGE(PG8_SA(1, 0), a3, vA2[0]);
;             PG8_WAIT_V(8); PG8_WAIT_L(0); PG8_BAR; PG8_MMA(1, 0, At, B0); PG8_MMA(1, 1, At, B1); PG8_BAR; PG8_SCHED;
;         }
	s_add_u32 s28, s28, 0x8000
	s_addc_u32 s29, s29, 0
	s_add_i32 s30, s69, s43
	v_lshl_add_u64 v[226:227], s[28:29], 0, v[164:165]
	s_mov_b32 m0, s30
	ds_read_b128 v[194:197], v191 offset:49152
	ds_read_b128 v[198:201], v191 offset:50176
	ds_read_b128 v[202:205], v191 offset:51200
	ds_read_b128 v[206:209], v191 offset:52224
	ds_read_b128 v[210:213], v191 offset:53248
	ds_read_b128 v[214:217], v191 offset:54272
	ds_read_b128 v[218:221], v191 offset:55296
	ds_read_b128 v[222:225], v191 offset:56320
	global_load_lds_dwordx4 v[226:227], off
	v_lshl_add_u64 v[226:227], s[28:29], 0, v[166:167]
	s_add_i32 m0, s30, 0x2000
	s_add_i32 s30, s70, s43
	global_load_lds_dwordx4 v[226:227], off
	v_lshl_add_u64 v[226:227], s[28:29], 0, v[178:179]
	s_mov_b32 m0, s30
	s_nop 0
	global_load_lds_dwordx4 v[226:227], off
	v_lshl_add_u64 v[226:227], s[28:29], 0, v[180:181]
	s_add_i32 m0, s30, 0x2000
	s_nop 0
	global_load_lds_dwordx4 v[226:227], off
	v_lshl_add_u64 v[226:227], s[26:27], 0, v[168:169]
	s_mov_b32 m0, s51
	s_nop 0
	global_load_lds_dwordx4 v[226:227], off
	v_lshl_add_u64 v[226:227], s[26:27], 0, v[170:171]
	s_mov_b32 m0, s52
	s_nop 0
	global_load_lds_dwordx4 v[226:227], off
	s_waitcnt vmcnt(8)
	s_waitcnt lgkmcnt(0)
	s_setprio 1
	s_waitcnt lgkmcnt(0)
	v_mfma_scale_f32_16x16x128_f8f6f4 v[94:97], v[2:9], v[194:201], v[94:97], v192, v192 op_sel_hi:[0,0,0]
	v_mfma_scale_f32_16x16x128_f8f6f4 v[90:93], v[10:17], v[194:201], v[90:93], v192, v192 op_sel_hi:[0,0,0]
	v_mfma_scale_f32_16x16x128_f8f6f4 v[78:81], v[2:9], v[202:209], v[78:81], v192, v192 op_sel_hi:[0,0,0]
	v_mfma_scale_f32_16x16x128_f8f6f4 v[74:77], v[10:17], v[202:209], v[74:77], v192, v192 op_sel_hi:[0,0,0]
	v_mfma_scale_f32_16x16x128_f8f6f4 v[62:65], v[2:9], v[210:217], v[62:65], v192, v192 op_sel_hi:[0,0,0]
	v_mfma_scale_f32_16x16x128_f8f6f4 v[58:61], v[10:17], v[210:217], v[58:61], v192, v192 op_sel_hi:[0,0,0]
	v_mfma_scale_f32_16x16x128_f8f6f4 v[46:49], v[2:9], v[218:225], v[46:49], v192, v192 op_sel_hi:[0,0,0]
	v_mfma_scale_f32_16x16x128_f8f6f4 v[42:45], v[10:17], v[218:225], v[42:45], v192, v192 op_sel_hi:[0,0,0]
	s_nop 3
	s_setprio 0
	s_setprio 1
	v_mfma_scale_f32_16x16x128_f8f6f4 v[86:89], v[18:25], v[194:201], v[86:89], v192, v192 op_sel_hi:[0,0,0]
	v_mfma_scale_f32_16x16x128_f8f6f4 v[82:85], v[26:33], v[194:201], v[82:85], v192, v192 op_sel_hi:[0,0,0]
	v_mfma_scale_f32_16x16x128_f8f6f4 v[70:73], v[18:25], v[202:209], v[70:73], v192, v192 op_sel_hi:[0,0,0]
	v_mfma_scale_f32_16x16x128_f8f6f4 v[66:69], v[26:33], v[202:209], v[66:69], v192, v192 op_sel_hi:[0,0,0]
	v_mfma_scale_f32_16x16x128_f8f6f4 v[54:57], v[18:25], v[210:217], v[54:57], v192, v192 op_sel_hi:[0,0,0]
	v_mfma_scale_f32_16x16x128_f8f6f4 v[50:53], v[26:33], v[210:217], v[50:53], v192, v192 op_sel_hi:[0,0,0]
	v_mfma_scale_f32_16x16x128_f8f6f4 v[38:41], v[18:25], v[218:225], v[38:41], v192, v192 op_sel_hi:[0,0,0]
	v_mfma_scale_f32_16x16x128_f8f6f4 v[34:37], v[26:33], v[218:225], v[34:37], v192, v192 op_sel_hi:[0,0,0]
	s_nop 3
	s_setprio 0
	s_barrier
	s_add_i32 s68, s68, 2
	s_add_u32 s23, s23, 0x10000
	s_addc_u32 s67, s67, 0
	s_add_u32 s24, s24, 0x10000
	s_addc_u32 s25, s25, 0
	s_cmp_gt_u32 s68, 5
	s_cbranch_scc0 .LBB0_1138
	s_branch .Lfx_1138
.Lh1_1138:
	ds_read_b128 v[18:21], v189
	ds_read_b128 v[22:25], v189 offset:1024
	ds_read_b128 v[26:29], v189 offset:2048
	ds_read_b128 v[30:33], v189 offset:3072
	ds_read_b128 v[2:5], v190
	ds_read_b128 v[6:9], v190 offset:1024
	ds_read_b128 v[10:13], v190 offset:2048
	ds_read_b128 v[14:17], v190 offset:3072
	s_add_u32 s26, s24, 0x8000
	s_addc_u32 s27, s25, 0
	s_cmp_eq_u32 s68, 4
	s_cselect_b32 s30, s16, s26
	s_cselect_b32 s31, s17, s27
	s_cselect_b32 s28, s18, s23
	s_cselect_b32 s29, s19, s67
	s_add_u32 s26, s30, 0x8000
	s_addc_u32 s27, s31, 0
	v_lshl_add_u64 v[226:227], s[24:25], 0, v[184:185]
	s_add_i32 m0, s44, 0xc000
	ds_read_b128 v[194:197], v191
	ds_read_b128 v[198:201], v191 offset:1024
	ds_read_b128 v[202:205], v191 offset:2048
	ds_read_b128 v[206:209], v191 offset:3072
	ds_read_b128 v[210:213], v191 offset:4096
	ds_read_b128 v[214:217], v191 offset:5120
	ds_read_b128 v[218:221], v191 offset:6144
	ds_read_b128 v[222:225], v191 offset:7168
	global_load_lds_dwordx4 v[226:227], off
	v_lshl_add_u64 v[226:227], s[24:25], 0, v[182:183]
	s_add_i32 m0, s44, 0xe000
	s_nop 0
	global_load_lds_dwordx4 v[226:227], off
	s_waitcnt vmcnt(8)
	s_waitcnt lgkmcnt(0)
	s_barrier
; #define PG8_STAGE(bufoff, gbase, voff) do { _Pragma("unroll") for (int _i = 0; _i < 2; ++_i) \
;         __builtin_amdgcn_global_load_lds((const unsigned*)((const char*)(gbase) + (voff)[_i]), (PG8_LAS unsigned*)(lds + (bufoff) + ldsw + _i * 8192), 16, 0, 0); } while (0)
; #define PG8_WAIT_V(n) asm volatile("s_waitcnt vmcnt(" #n ")" ::: "memory")
; #define PG8_WAIT_L(n) asm volatile("s_waitcnt lgkmcnt(" #n ")" ::: "memory")
; #define PG8_BAR __builtin_amdgcn_s_barrier()
; #define PG8_SCHED __builtin_amdgcn_sched_barrier(0)
; template <class Epi, class Sched, bool ALIGN_EPI = true, bool F8 = false>
; __device__ __forceinline__ void gemm_phase(PG8_LAS unsigned char* lds, const Sched& S, const Epi& E) {
;     ...
;             PG8_LDB(B0, 0, 0); PG8_LDB(B1, 0, 1); PG8_SCHED; PG8_LDA(At, 0, 0); PG8_STAGE(PG8_SA(1, 1), a1, voffA[1]);
;             PG8_WAIT_V(8); PG8_WAIT_L(0); PG8_BAR; PG8_MMA(0, 0, At, B0); PG8_MMA(0, 1, At, B1); PG8_BAR; PG8_SCHED;
;             PG8_LDA(At, 0, 1); PG8_STAGE(PG8_SB(0, 0), b2, voffB[0]); PG8_STAGE(PG8_SB(0, 1), b2, voffB[1]); PG8_STAGE(PG8_SA(0, 0), a2, vA2[0]);
;             PG8_WAIT_V(8); PG8_WAIT_L(0); PG8_BAR; PG8_MMA(1, 0, At, B0); PG8_MMA(1, 1, At, B1); PG8_BAR; PG8_SCHED;
;             PG8_LDB(B0, 1, 0); PG8_LDB(B1, 1, 1); PG8_SCHED; PG8_LDA(At, 1, 0); PG8_STAGE(PG8_SA(0, 1), a2, vA2[1]);
;             PG8_WAIT_V(8); PG8_WAIT_L(0); PG8_BAR; PG8_MMA(0, 0, At, B0); PG8_MMA(0, 1, At, B1); PG8_BAR; PG8_SCHED;
	s_setprio 2
	s_waitcnt lgkmcnt(0)
	v_mfma_scale_f32_16x16x128_f8f6f4 v[158:161], v[18:25], v[194:201], v[158:161], v192, v192 op_sel_hi:[0,0,0]
	v_mfma_scale_f32_16x16x128_f8f6f4 v[154:157], v[26:33], v[194:201], v[154:157], v192, v192 op_sel_hi:[0,0,0]
	v_mfma_scale_f32_16x16x128_f8f6f4 v[142:145], v[18:25], v[202:209], v[142:145], v192, v192 op_sel_hi:[0,0,0]
	v_mfma_scale_f32_16x16x128_f8f6f4 v[138:141], v[26:33], v[202:209], v[138:141], v192, v192 op_sel_hi:[0,0,0]
	v_mfma_scale_f32_16x16x128_f8f6f4 v[126:129], v[18:25], v[210:217], v[126:129], v192, v192 op_sel_hi:[0,0,0]
	v_mfma_scale_f32_16x16x128_f8f6f4 v[122:125], v[26:33], v[210:217], v[122:125], v192, v192 op_sel_hi:[0,0,0]
	v_mfma_scale_f32_16x16x128_f8f6f4 v[110:113], v[18:25], v[218:225], v[110:113], v192, v192 op_sel_hi:[0,0,0]
	v_mfma_scale_f32_16x16x128_f8f6f4 v[106:109], v[26:33], v[218:225], v[106:109], v192, v192 op_sel_hi:[0,0,0]
	s_nop 3
	s_setprio 0
	s_setprio 2
	v_mfma_scale_f32_16x16x128_f8f6f4 v[150:153], v[2:9], v[194:201], v[150:153], v192, v192 op_sel_hi:[0,0,0]
	v_mfma_scale_f32_16x16x128_f8f6f4 v[146:149], v[10:17], v[194:201], v[146:149], v192, v192 op_sel_hi:[0,0,0]
	v_mfma_scale_f32_16x16x128_f8f6f4 v[134:137], v[2:9], v[202:209], v[134:137], v192, v192 op_sel_hi:[0,0,0]
	v_mfma_scale_f32_16x16x128_f8f6f4 v[130:133], v[10:17], v[202:209], v[130:133], v192, v192 op_sel_hi:[0,0,0]
	v_mfma_scale_f32_16x16x128_f8f6f4 v[118:121], v[2:9], v[210:217], v[118:121], v192, v192 op_sel_hi:[0,0,0]
	v_mfma_scale_f32_16x16x128_f8f6f4 v[114:117], v[10:17], v[210:217], v[114:117], v192, v192 op_sel_hi:[0,0,0]
	v_mfma_scale_f32_16x16x128_f8f6f4 v[102:105], v[2:9], v[218:225], v[102:105], v192, v192 op_sel_hi:[0,0,0]
	v_mfma_scale_f32_16x16x128_f8f6f4 v[98:101], v[10:17], v[218:225], v[98:101], v192, v192 op_sel_hi:[0,0,0]
	s_nop 3
	s_setprio 0
	s_add_i32 s69, s53, s43
	v_lshl_add_u64 v[226:227], s[28:29], 0, v[164:165]
	s_mov_b32 m0, s69
	ds_read_b128 v[194:197], v191 offset:16384
	ds_read_b128 v[198:201], v191 offset:17408
	ds_read_b128 v[202:205], v191 offset:18432
	ds_read_b128 v[206:209], v191 offset:19456
	ds_read_b128 v[210:213], v191 offset:20480
	ds_read_b128 v[214:217], v191 offset:21504
	ds_read_b128 v[218:221], v191 offset:22528
	ds_read_b128 v[222:225], v191 offset:23552
	global_load_lds_dwordx4 v[226:227], off
	v_lshl_add_u64 v[228:229], s[28:29], 0, v[166:167]
	s_add_i32 m0, s69, 0x2000
	s_add_i32 s69, s58, s43
	global_load_lds_dwordx4 v[228:229], off
	v_lshl_add_u64 v[226:227], v[226:227], 0, s[4:5]
	s_mov_b32 m0, s69
	s_nop 0
	global_load_lds_dwordx4 v[226:227], off
	v_lshl_add_u64 v[226:227], v[228:229], 0, s[4:5]
	s_add_i32 m0, s69, 0x2000
	s_nop 0
	global_load_lds_dwordx4 v[226:227], off
	v_lshl_add_u64 v[226:227], s[30:31], 0, v[168:169]
	s_mov_b32 m0, s44
	s_nop 0
	global_load_lds_dwordx4 v[226:227], off
	v_lshl_add_u64 v[226:227], s[30:31], 0, v[170:171]
	s_mov_b32 m0, s45
	s_nop 0
	global_load_lds_dwordx4 v[226:227], off
	s_waitcnt vmcnt(8)
	s_waitcnt lgkmcnt(0)
	s_barrier
	s_setprio 2
	s_waitcnt lgkmcnt(0)
	v_mfma_scale_f32_16x16x128_f8f6f4 v[94:97], v[18:25], v[194:201], v[94:97], v192, v192 op_sel_hi:[0,0,0]
	v_mfma_scale_f32_16x16x128_f8f6f4 v[90:93], v[26:33], v[194:201], v[90:93], v192, v192 op_sel_hi:[0,0,0]
	v_mfma_scale_f32_16x16x128_f8f6f4 v[78:81], v[18:25], v[202:209], v[78:81], v192, v192 op_sel_hi:[0,0,0]
	v_mfma_scale_f32_16x16x128_f8f6f4 v[74:77], v[26:33], v[202:209], v[74:77], v192, v192 op_sel_hi:[0,0,0]
	v_mfma_scale_f32_16x16x128_f8f6f4 v[62:65], v[18:25], v[210:217], v[62:65], v192, v192 op_sel_hi:[0,0,0]
	v_mfma_scale_f32_16x16x128_f8f6f4 v[58:61], v[26:33], v[210:217], v[58:61], v192, v192 op_sel_hi:[0,0,0]
	v_mfma_scale_f32_16x16x128_f8f6f4 v[46:49], v[18:25], v[218:225], v[46:49], v192, v192 op_sel_hi:[0,0,0]
	v_mfma_scale_f32_16x16x128_f8f6f4 v[42:45], v[26:33], v[218:225], v[42:45], v192, v192 op_sel_hi:[0,0,0]
	s_nop 3
	s_setprio 0
	s_setprio 2
	v_mfma_scale_f32_16x16x128_f8f6f4 v[86:89], v[2:9], v[194:201], v[86:89], v192, v192 op_sel_hi:[0,0,0]
	v_mfma_scale_f32_16x16x128_f8f6f4 v[82:85], v[10:17], v[194:201], v[82:85], v192, v192 op_sel_hi:[0,0,0]
	v_mfma_scale_f32_16x16x128_f8f6f4 v[70:73], v[2:9], v[202:209], v[70:73], v192, v192 op_sel_hi:[0,0,0]
	v_mfma_scale_f32_16x16x128_f8f6f4 v[66:69], v[10:17], v[202:209], v[66:69], v192, v192 op_sel_hi:[0,0,0]
	v_mfma_scale_f32_16x16x128_f8f6f4 v[54:57], v[2:9], v[210:217], v[54:57], v192, v192 op_sel_hi:[0,0,0]
	v_mfma_scale_f32_16x16x128_f8f6f4 v[50:53], v[10:17], v[210:217], v[50:53], v192, v192 op_sel_hi:[0,0,0]
	v_mfma_scale_f32_16x16x128_f8f6f4 v[38:41], v[2:9], v[218:225], v[38:41], v192, v192 op_sel_hi:[0,0,0]
	v_mfma_scale_f32_16x16x128_f8f6f4 v[34:37], v[10:17], v[218:225], v[34:37], v192, v192 op_sel_hi:[0,0,0]
	s_nop 3
	s_setprio 0
	s_add_i32 s69, 0, 0x18000
	s_add_i32 s70, 0, 0x1c000
	v_add_u32_e32 v14, s69, v187
	v_add_u32_e32 v30, s70, v187
	ds_read_b128 v[2:5], v14
	ds_read_b128 v[6:9], v14 offset:1024
	ds_read_b128 v[10:13], v14 offset:2048
	ds_read_b128 v[14:17], v14 offset:3072
	ds_read_b128 v[18:21], v30
	ds_read_b128 v[22:25], v30 offset:1024
	ds_read_b128 v[26:29], v30 offset:2048
	ds_read_b128 v[30:33], v30 offset:3072
	s_mov_b32 m0, s46
	v_lshl_add_u64 v[226:227], s[30:31], 0, v[172:173]
	ds_read_b128 v[194:197], v191 offset:32768
	ds_read_b128 v[198:201], v191 offset:33792
	ds_read_b128 v[202:205], v191 offset:34816
	ds_read_b128 v[206:209], v191 offset:35840
	ds_read_b128 v[210:213], v191 offset:36864
	ds_read_b128 v[214:217], v191 offset:37888
	ds_read_b128 v[218:221], v191 offset:38912
	ds_read_b128 v[222:225], v191 offset:39936
	global_load_lds_dwordx4 v[226:227], off
	v_lshl_add_u64 v[226:227], s[30:31], 0, v[174:175]
	s_mov_b32 m0, s47
	s_nop 0
	global_load_lds_dwordx4 v[226:227], off
	s_waitcnt vmcnt(8)
	s_waitcnt lgkmcnt(0)
	s_barrier
; #define PG8_STAGE(bufoff, gbase, voff) do { _Pragma("unroll") for (int _i = 0; _i < 2; ++_i) \
;         __builtin_amdgcn_global_load_lds((const unsigned*)((const char*)(gbase) + (voff)[_i]), (PG8_LAS unsigned*)(lds + (bufoff) + ldsw + _i * 8192), 16, 0, 0); } while (0)
; #define PG8_WAIT_V(n) asm volatile("s_waitcnt vmcnt(" #n ")" ::: "memory")
; #define PG8_WAIT_L(n) asm volatile("s_waitcnt lgkmcnt(" #n ")" ::: "memory")
; #define PG8_BAR __builtin_amdgcn_s_barrier()
; #define PG8_SCHED __builtin_amdgcn_sched_barrier(0)
; template <class Epi, class Sched, bool ALIGN_EPI = true, bool F8 = false>
; __device__ __forceinline__ void gemm_phase(PG8_LAS unsigned char* lds, const Sched& S, const Epi& E) {
;     ...
;         for (int t = 0; t < nt; t += 2) {
;             const bool last = (t == nt - 2);
;             if constexpr (Sched::GATHER) { if (last && has_next) S.a_off(nxt, Rs, Cs, voffAn); }
;             const char* a1 = cA + (size_t)(t + 1) * kstep;
;             const char* a2 = last ? nA : cA + (size_t)(t + 2) * kstep; const char* b2 = last ? nB : cB + (size_t)(t + 2) * kstepB;
;             const char* a3 = a2 + kstep; const char* b3 = b2 + kstepB;
;     ...
;             PG8_WAIT_V(8); PG8_WAIT_L(0); PG8_BAR; PG8_MMA(0, 0, At, B0); PG8_MMA(0, 1, At, B1); PG8_BAR; PG8_SCHED;
;             PG8_LDA(At, 1, 1); PG8_STAGE(PG8_SB(1, 0), b3, voffB[0]); PG8_STAGE(PG8_SB(1, 1), b3, voffB[1]); PG8_STAGE(PG8_SA(1, 0), a3, vA2[0]);
;             PG8_WAIT_V(8); PG8_WAIT_L(0); PG8_BAR; PG8_MMA(1, 0, At, B0); PG8_MMA(1, 1, At, B1); PG8_BAR; PG8_SCHED;
;         }
	s_setprio 2
	s_waitcnt lgkmcnt(0)
	v_mfma_scale_f32_16x16x128_f8f6f4 v[158:161], v[2:9], v[194:201], v[158:161], v192, v192 op_sel_hi:[0,0,0]
	v_mfma_scale_f32_16x16x128_f8f6f4 v[154:157], v[10:17], v[194:201], v[154:157], v192, v192 op_sel_hi:[0,0,0]
	v_mfma_scale_f32_16x16x128_f8f6f4 v[142:145], v[2:9], v[202:209], v[142:145], v192, v192 op_sel_hi:[0,0,0]
	v_mfma_scale_f32_16x16x128_f8f6f4 v[138:141], v[10:17], v[202:209], v[138:141], v192, v192 op_sel_hi:[0,0,0]
	v_mfma_scale_f32_16x16x128_f8f6f4 v[126:129], v[2:9], v[210:217], v[126:129], v192, v192 op_sel_hi:[0,0,0]
	v_mfma_scale_f32_16x16x128_f8f6f4 v[122:125], v[10:17], v[210:217], v[122:125], v192, v192 op_sel_hi:[0,0,0]
	v_mfma_scale_f32_16x16x128_f8f6f4 v[110:113], v[2:9], v[218:225], v[110:113], v192, v192 op_sel_hi:[0,0,0]
	v_mfma_scale_f32_16x16x128_f8f6f4 v[106:109], v[10:17], v[218:225], v[106:109], v192, v192 op_sel_hi:[0,0,0]
	s_nop 3
	s_setprio 0
	s_setprio 2
	v_mfma_scale_f32_16x16x128_f8f6f4 v[150:153], v[18:25], v[194:201], v[150:153], v192, v192 op_sel_hi:[0,0,0]
	v_mfma_scale_f32_16x16x128_f8f6f4 v[146:149], v[26:33], v[194:201], v[146:149], v192, v192 op_sel_hi:[0,0,0]
	v_mfma_scale_f32_16x16x128_f8f6f4 v[134:137], v[18:25], v[202:209], v[134:137], v192, v192 op_sel_hi:[0,0,0]
	v_mfma_scale_f32_16x16x128_f8f6f4 v[130:133], v[26:33], v[202:209], v[130:133], v192, v192 op_sel_hi:[0,0,0]
	v_mfma_scale_f32_16x16x128_f8f6f4 v[118:121], v[18:25], v[210:217], v[118:121], v192, v192 op_sel_hi:[0,0,0]
	v_mfma_scale_f32_16x16x128_f8f6f4 v[114:117], v[26:33], v[210:217], v[114:117], v192, v192 op_sel_hi:[0,0,0]
	v_mfma_scale_f32_16x16x128_f8f6f4 v[102:105], v[18:25], v[218:225], v[102:105], v192, v192 op_sel_hi:[0,0,0]
	v_mfma_scale_f32_16x16x128_f8f6f4 v[98:101], v[26:33], v[218:225], v[98:101], v192, v192 op_sel_hi:[0,0,0]
	s_nop 3
	s_setprio 0
	s_add_u32 s28, s28, 0x8000
	s_addc_u32 s29, s29, 0
	s_add_i32 s30, s69, s43
	v_lshl_add_u64 v[226:227], s[28:29], 0, v[164:165]
	s_mov_b32 m0, s30
	ds_read_b128 v[194:197], v191 offset:49152
	ds_read_b128 v[198:201], v191 offset:50176
	ds_read_b128 v[202:205], v191 offset:51200
	ds_read_b128 v[206:209], v191 offset:52224
	ds_read_b128 v[210:213], v191 offset:53248
	ds_read_b128 v[214:217], v191 offset:54272
	ds_read_b128 v[218:221], v191 offset:55296
	ds_read_b128 v[222:225], v191 offset:56320
	global_load_lds_dwordx4 v[226:227], off
	v_lshl_add_u64 v[226:227], s[28:29], 0, v[166:167]
	s_add_i32 m0, s30, 0x2000
	s_add_i32 s30, s70, s43
	global_load_lds_dwordx4 v[226:227], off
	v_lshl_add_u64 v[226:227], s[28:29], 0, v[178:179]
	s_mov_b32 m0, s30
	s_nop 0
	global_load_lds_dwordx4 v[226:227], off
	v_lshl_add_u64 v[226:227], s[28:29], 0, v[180:181]
	s_add_i32 m0, s30, 0x2000
	s_nop 0
	global_load_lds_dwordx4 v[226:227], off
	v_lshl_add_u64 v[226:227], s[26:27], 0, v[168:169]
	s_mov_b32 m0, s51
	s_nop 0
	global_load_lds_dwordx4 v[226:227], off
	v_lshl_add_u64 v[226:227], s[26:27], 0, v[170:171]
	s_mov_b32 m0, s52
	s_nop 0
	global_load_lds_dwordx4 v[226:227], off
	s_waitcnt vmcnt(8)
	s_waitcnt lgkmcnt(0)
	s_barrier
	s_setprio 2
	s_waitcnt lgkmcnt(0)
	v_mfma_scale_f32_16x16x128_f8f6f4 v[94:97], v[2:9], v[194:201], v[94:97], v192, v192 op_sel_hi:[0,0,0]
	v_mfma_scale_f32_16x16x128_f8f6f4 v[90:93], v[10:17], v[194:201], v[90:93], v192, v192 op_sel_hi:[0,0,0]
	v_mfma_scale_f32_16x16x128_f8f6f4 v[78:81], v[2:9], v[202:209], v[78:81], v192, v192 op_sel_hi:[0,0,0]
	v_mfma_scale_f32_16x16x128_f8f6f4 v[74:77], v[10:17], v[202:209], v[74:77], v192, v192 op_sel_hi:[0,0,0]
	v_mfma_scale_f32_16x16x128_f8f6f4 v[62:65], v[2:9], v[210:217], v[62:65], v192, v192 op_sel_hi:[0,0,0]
	v_mfma_scale_f32_16x16x128_f8f6f4 v[58:61], v[10:17], v[210:217], v[58:61], v192, v192 op_sel_hi:[0,0,0]
	v_mfma_scale_f32_16x16x128_f8f6f4 v[46:49], v[2:9], v[218:225], v[46:49], v192, v192 op_sel_hi:[0,0,0]
	v_mfma_scale_f32_16x16x128_f8f6f4 v[42:45], v[10:17], v[218:225], v[42:45], v192, v192 op_sel_hi:[0,0,0]
	s_nop 3
	s_setprio 0
	s_setprio 2
	v_mfma_scale_f32_16x16x128_f8f6f4 v[86:89], v[18:25], v[194:201], v[86:89], v192, v192 op_sel_hi:[0,0,0]
	v_mfma_scale_f32_16x16x128_f8f6f4 v[82:85], v[26:33], v[194:201], v[82:85], v192, v192 op_sel_hi:[0,0,0]
	v_mfma_scale_f32_16x16x128_f8f6f4 v[70:73], v[18:25], v[202:209], v[70:73], v192, v192 op_sel_hi:[0,0,0]
	v_mfma_scale_f32_16x16x128_f8f6f4 v[66:69], v[26:33], v[202:209], v[66:69], v192, v192 op_sel_hi:[0,0,0]
	v_mfma_scale_f32_16x16x128_f8f6f4 v[54:57], v[18:25], v[210:217], v[54:57], v192, v192 op_sel_hi:[0,0,0]
	v_mfma_scale_f32_16x16x128_f8f6f4 v[50:53], v[26:33], v[210:217], v[50:53], v192, v192 op_sel_hi:[0,0,0]
	v_mfma_scale_f32_16x16x128_f8f6f4 v[38:41], v[18:25], v[218:225], v[38:41], v192, v192 op_sel_hi:[0,0,0]
	v_mfma_scale_f32_16x16x128_f8f6f4 v[34:37], v[26:33], v[218:225], v[34:37], v192, v192 op_sel_hi:[0,0,0]
	s_nop 3
	s_setprio 0
	s_add_i32 s68, s68, 2
	s_add_u32 s23, s23, 0x10000
	s_addc_u32 s67, s67, 0
	s_add_u32 s24, s24, 0x10000
	s_addc_u32 s25, s25, 0
	s_cmp_gt_u32 s68, 5
	s_cbranch_scc0 .Lh1_1138

; #define PG8_BAR __builtin_amdgcn_s_barrier()
; template <class Epi, class Sched, bool ALIGN_EPI = true, bool F8 = false>
; __device__ __forceinline__ void gemm_phase(PG8_LAS unsigned char* lds, const Sched& S, const Epi& E) {
;     ...
;         if constexpr (ALIGN_EPI) { if (wr == 1) PG8_BAR; }
;     }
.LBB0_1158:
	s_andn2_b64 vcc, exec, s[8:9]
	s_cbranch_vccnz .LBB0_1131
	s_branch .LBB0_1131
